# GEMM K loops: the compiler's second lgkmcnt(0) after each pre-MMA barrier (already satisfied by the wait before the barrier) deleted at 104 sites
# baseline (speedup 1.0000x reference)
.Lpeelph1b_0:
	s_add_i32 s73, s60, 2
	s_add_u32 s61, s58, 0xfffc0080
	s_addc_u32 s62, s59, -1
	s_add_i32 s74, 0, 0x10000
	s_cmp_eq_u32 s68, s60
	s_cselect_b32 s63, s39, s62
	s_cselect_b32 s62, s43, s61
	s_cselect_b32 s61, s47, s72
	s_cselect_b32 s60, s55, s71
	s_add_i32 s76, 0, 0x14000
	v_add_u32_e32 v156, s74, v165
	v_add_u32_e32 v166, s76, v165
	ds_read_b128 v[144:147], v156
	ds_read_b128 v[148:151], v156 offset:1024
	ds_read_b128 v[152:155], v156 offset:2048
	ds_read_b128 v[156:159], v156 offset:3072
	ds_read_b128 v[160:163], v166
	ds_read_b128 v[170:173], v166 offset:1024
	ds_read_b128 v[174:177], v166 offset:2048
	ds_read_b128 v[180:183], v166 offset:3072
	v_lshl_add_u64 v[216:217], s[58:59], 0, v[142:143]
	s_add_i32 m0, s8, 0xc000
	ds_read_b128 v[184:187], v178
	ds_read_b128 v[188:191], v178 offset:1024
	ds_read_b128 v[192:195], v178 offset:2048
	ds_read_b128 v[196:199], v178 offset:3072
	ds_read_b128 v[200:203], v178 offset:4096
	ds_read_b128 v[204:207], v178 offset:5120
	ds_read_b128 v[208:211], v178 offset:6144
	ds_read_b128 v[212:215], v178 offset:7168
	global_load_lds_dwordx4 v[216:217], off
	v_lshl_add_u64 v[216:217], s[58:59], 0, v[140:141]
	s_add_i32 m0, s8, 0xe000
	s_nop 0
	global_load_lds_dwordx4 v[216:217], off
	s_waitcnt vmcnt(8)
	s_waitcnt lgkmcnt(0)
	s_barrier
	s_setprio 1
	v_mfma_f32_16x16x32_bf16 v[126:129], v[144:147], v[184:187], 0
	v_mfma_f32_16x16x32_bf16 v[122:125], v[152:155], v[184:187], 0
	v_mfma_f32_16x16x32_bf16 v[110:113], v[144:147], v[192:195], 0
	v_mfma_f32_16x16x32_bf16 v[106:109], v[152:155], v[192:195], 0
	v_mfma_f32_16x16x32_bf16 v[94:97], v[144:147], v[200:203], 0
	v_mfma_f32_16x16x32_bf16 v[90:93], v[152:155], v[200:203], 0
	v_mfma_f32_16x16x32_bf16 v[78:81], v[144:147], v[208:211], 0
	v_mfma_f32_16x16x32_bf16 v[74:77], v[152:155], v[208:211], 0
	v_mfma_f32_16x16x32_bf16 v[126:129], v[148:151], v[188:191], v[126:129]
	v_mfma_f32_16x16x32_bf16 v[122:125], v[156:159], v[188:191], v[122:125]
	v_mfma_f32_16x16x32_bf16 v[110:113], v[148:151], v[196:199], v[110:113]
	v_mfma_f32_16x16x32_bf16 v[106:109], v[156:159], v[196:199], v[106:109]
	v_mfma_f32_16x16x32_bf16 v[94:97], v[148:151], v[204:207], v[94:97]
	v_mfma_f32_16x16x32_bf16 v[90:93], v[156:159], v[204:207], v[90:93]
	v_mfma_f32_16x16x32_bf16 v[78:81], v[148:151], v[212:215], v[78:81]
	v_mfma_f32_16x16x32_bf16 v[74:77], v[156:159], v[212:215], v[74:77]
	s_setprio 0
	s_setprio 1
	v_mfma_f32_16x16x32_bf16 v[118:121], v[160:163], v[184:187], 0
	v_mfma_f32_16x16x32_bf16 v[114:117], v[174:177], v[184:187], 0
	v_mfma_f32_16x16x32_bf16 v[102:105], v[160:163], v[192:195], 0
	v_mfma_f32_16x16x32_bf16 v[98:101], v[174:177], v[192:195], 0
	v_mfma_f32_16x16x32_bf16 v[86:89], v[160:163], v[200:203], 0
	v_mfma_f32_16x16x32_bf16 v[82:85], v[174:177], v[200:203], 0
	v_mfma_f32_16x16x32_bf16 v[70:73], v[160:163], v[208:211], 0
	v_mfma_f32_16x16x32_bf16 v[66:69], v[174:177], v[208:211], 0
	v_mfma_f32_16x16x32_bf16 v[118:121], v[170:173], v[188:191], v[118:121]
	v_mfma_f32_16x16x32_bf16 v[114:117], v[180:183], v[188:191], v[114:117]
	v_mfma_f32_16x16x32_bf16 v[102:105], v[170:173], v[196:199], v[102:105]
	v_mfma_f32_16x16x32_bf16 v[98:101], v[180:183], v[196:199], v[98:101]
	v_mfma_f32_16x16x32_bf16 v[86:89], v[170:173], v[204:207], v[86:89]
	v_mfma_f32_16x16x32_bf16 v[82:85], v[180:183], v[204:207], v[82:85]
	v_mfma_f32_16x16x32_bf16 v[70:73], v[170:173], v[212:215], v[70:73]
	v_mfma_f32_16x16x32_bf16 v[66:69], v[180:183], v[212:215], v[66:69]
	s_setprio 0
	s_barrier
	s_add_i32 s74, s74, s1
	v_lshl_add_u64 v[216:217], s[60:61], 0, v[130:131]
	s_mov_b32 m0, s74
	ds_read_b128 v[184:187], v178 offset:16384
	ds_read_b128 v[188:191], v178 offset:17408
	ds_read_b128 v[192:195], v178 offset:18432
	ds_read_b128 v[196:199], v178 offset:19456
	ds_read_b128 v[200:203], v178 offset:20480
	ds_read_b128 v[204:207], v178 offset:21504
	ds_read_b128 v[208:211], v178 offset:22528
	ds_read_b128 v[212:215], v178 offset:23552
	global_load_lds_dwordx4 v[216:217], off
	s_add_i32 m0, s74, 0x2000
	s_add_u32 s74, s60, 0x40000
	v_lshl_add_u64 v[218:219], s[60:61], 0, v[132:133]
	s_addc_u32 s75, s61, 0
	s_add_i32 s76, s76, s1
	global_load_lds_dwordx4 v[218:219], off
	v_lshl_add_u64 v[220:221], s[74:75], 0, v[130:131]
	s_mov_b32 m0, s76
	v_lshl_add_u64 v[222:223], s[62:63], 0, v[136:137]
	global_load_lds_dwordx4 v[220:221], off
	v_lshl_add_u64 v[220:221], s[74:75], 0, v[132:133]
	s_add_i32 m0, s76, 0x2000
	s_nop 0
	global_load_lds_dwordx4 v[220:221], off
	v_lshl_add_u64 v[220:221], s[62:63], 0, v[134:135]
	s_mov_b32 m0, s8
	s_nop 0
	global_load_lds_dwordx4 v[220:221], off
	s_mov_b32 m0, s11
	s_nop 0
	global_load_lds_dwordx4 v[222:223], off
	s_waitcnt vmcnt(8)
	s_waitcnt lgkmcnt(0)
	s_barrier
	s_setprio 1
	v_mfma_f32_16x16x32_bf16 v[62:65], v[144:147], v[184:187], 0
	v_mfma_f32_16x16x32_bf16 v[58:61], v[152:155], v[184:187], 0
	v_mfma_f32_16x16x32_bf16 v[46:49], v[144:147], v[192:195], 0
	v_mfma_f32_16x16x32_bf16 v[42:45], v[152:155], v[192:195], 0
	v_mfma_f32_16x16x32_bf16 v[30:33], v[144:147], v[200:203], 0
	v_mfma_f32_16x16x32_bf16 v[26:29], v[152:155], v[200:203], 0
	v_mfma_f32_16x16x32_bf16 v[14:17], v[144:147], v[208:211], 0
	v_mfma_f32_16x16x32_bf16 v[10:13], v[152:155], v[208:211], 0
	v_mfma_f32_16x16x32_bf16 v[62:65], v[148:151], v[188:191], v[62:65]
	v_mfma_f32_16x16x32_bf16 v[58:61], v[156:159], v[188:191], v[58:61]
	v_mfma_f32_16x16x32_bf16 v[46:49], v[148:151], v[196:199], v[46:49]
	v_mfma_f32_16x16x32_bf16 v[42:45], v[156:159], v[196:199], v[42:45]
	v_mfma_f32_16x16x32_bf16 v[30:33], v[148:151], v[204:207], v[30:33]
	v_mfma_f32_16x16x32_bf16 v[26:29], v[156:159], v[204:207], v[26:29]
	v_mfma_f32_16x16x32_bf16 v[14:17], v[148:151], v[212:215], v[14:17]
	v_mfma_f32_16x16x32_bf16 v[10:13], v[156:159], v[212:215], v[10:13]
	s_setprio 0
	s_setprio 1
	v_mfma_f32_16x16x32_bf16 v[54:57], v[160:163], v[184:187], 0
	v_mfma_f32_16x16x32_bf16 v[50:53], v[174:177], v[184:187], 0
	v_mfma_f32_16x16x32_bf16 v[38:41], v[160:163], v[192:195], 0
	v_mfma_f32_16x16x32_bf16 v[34:37], v[174:177], v[192:195], 0
	v_mfma_f32_16x16x32_bf16 v[22:25], v[160:163], v[200:203], 0
	v_mfma_f32_16x16x32_bf16 v[18:21], v[174:177], v[200:203], 0
	v_mfma_f32_16x16x32_bf16 v[6:9], v[160:163], v[208:211], 0
	v_mfma_f32_16x16x32_bf16 v[2:5], v[174:177], v[208:211], 0
	v_mfma_f32_16x16x32_bf16 v[54:57], v[170:173], v[188:191], v[54:57]
	v_mfma_f32_16x16x32_bf16 v[50:53], v[180:183], v[188:191], v[50:53]
	v_mfma_f32_16x16x32_bf16 v[38:41], v[170:173], v[196:199], v[38:41]
	v_mfma_f32_16x16x32_bf16 v[34:37], v[180:183], v[196:199], v[34:37]
	v_mfma_f32_16x16x32_bf16 v[22:25], v[170:173], v[204:207], v[22:25]
	v_mfma_f32_16x16x32_bf16 v[18:21], v[180:183], v[204:207], v[18:21]
	v_mfma_f32_16x16x32_bf16 v[6:9], v[170:173], v[212:215], v[6:9]
	v_mfma_f32_16x16x32_bf16 v[2:5], v[180:183], v[212:215], v[2:5]
	s_setprio 0
	s_barrier
	s_add_i32 s74, 0, 0x18000
	s_add_i32 s75, 0, 0x1c000
	v_add_u32_e32 v156, s74, v165
	v_add_u32_e32 v166, s75, v165
	ds_read_b128 v[144:147], v156
	ds_read_b128 v[148:151], v156 offset:1024
	ds_read_b128 v[152:155], v156 offset:2048
	ds_read_b128 v[156:159], v156 offset:3072
	ds_read_b128 v[160:163], v166
	ds_read_b128 v[170:173], v166 offset:1024
	ds_read_b128 v[174:177], v166 offset:2048
	ds_read_b128 v[180:183], v166 offset:3072
	s_add_u32 s62, s62, 0x40000
	s_addc_u32 s63, s63, 0
	s_mov_b32 m0, s16
	v_lshl_add_u64 v[232:233], s[62:63], 0, v[134:135]
	ds_read_b128 v[184:187], v178 offset:32768
	ds_read_b128 v[188:191], v178 offset:33792
	ds_read_b128 v[192:195], v178 offset:34816
	ds_read_b128 v[196:199], v178 offset:35840
	ds_read_b128 v[200:203], v178 offset:36864
	ds_read_b128 v[204:207], v178 offset:37888
	ds_read_b128 v[208:211], v178 offset:38912
	ds_read_b128 v[212:215], v178 offset:39936
	global_load_lds_dwordx4 v[232:233], off
	v_lshl_add_u64 v[232:233], s[62:63], 0, v[136:137]
	s_mov_b32 m0, s25
	s_nop 0
	global_load_lds_dwordx4 v[232:233], off
	s_waitcnt vmcnt(8)
	s_waitcnt lgkmcnt(0)
	s_barrier
	s_setprio 1
	v_mfma_f32_16x16x32_bf16 v[126:129], v[144:147], v[184:187], v[126:129]
	v_mfma_f32_16x16x32_bf16 v[122:125], v[152:155], v[184:187], v[122:125]
	v_mfma_f32_16x16x32_bf16 v[110:113], v[144:147], v[192:195], v[110:113]
	v_mfma_f32_16x16x32_bf16 v[106:109], v[152:155], v[192:195], v[106:109]
	v_mfma_f32_16x16x32_bf16 v[94:97], v[144:147], v[200:203], v[94:97]
	v_mfma_f32_16x16x32_bf16 v[90:93], v[152:155], v[200:203], v[90:93]
	v_mfma_f32_16x16x32_bf16 v[78:81], v[144:147], v[208:211], v[78:81]
	v_mfma_f32_16x16x32_bf16 v[74:77], v[152:155], v[208:211], v[74:77]
	v_mfma_f32_16x16x32_bf16 v[126:129], v[148:151], v[188:191], v[126:129]
	v_mfma_f32_16x16x32_bf16 v[122:125], v[156:159], v[188:191], v[122:125]
	v_mfma_f32_16x16x32_bf16 v[110:113], v[148:151], v[196:199], v[110:113]
	v_mfma_f32_16x16x32_bf16 v[106:109], v[156:159], v[196:199], v[106:109]
	v_mfma_f32_16x16x32_bf16 v[94:97], v[148:151], v[204:207], v[94:97]
	v_mfma_f32_16x16x32_bf16 v[90:93], v[156:159], v[204:207], v[90:93]
	v_mfma_f32_16x16x32_bf16 v[78:81], v[148:151], v[212:215], v[78:81]
	v_mfma_f32_16x16x32_bf16 v[74:77], v[156:159], v[212:215], v[74:77]
	s_setprio 0
	s_setprio 1
	v_mfma_f32_16x16x32_bf16 v[118:121], v[160:163], v[184:187], v[118:121]
	v_mfma_f32_16x16x32_bf16 v[114:117], v[174:177], v[184:187], v[114:117]
	v_mfma_f32_16x16x32_bf16 v[102:105], v[160:163], v[192:195], v[102:105]
	v_mfma_f32_16x16x32_bf16 v[98:101], v[174:177], v[192:195], v[98:101]
	v_mfma_f32_16x16x32_bf16 v[86:89], v[160:163], v[200:203], v[86:89]
	v_mfma_f32_16x16x32_bf16 v[82:85], v[174:177], v[200:203], v[82:85]
	v_mfma_f32_16x16x32_bf16 v[70:73], v[160:163], v[208:211], v[70:73]
	v_mfma_f32_16x16x32_bf16 v[66:69], v[174:177], v[208:211], v[66:69]
	v_mfma_f32_16x16x32_bf16 v[118:121], v[170:173], v[188:191], v[118:121]
	v_mfma_f32_16x16x32_bf16 v[114:117], v[180:183], v[188:191], v[114:117]
	v_mfma_f32_16x16x32_bf16 v[102:105], v[170:173], v[196:199], v[102:105]
	v_mfma_f32_16x16x32_bf16 v[98:101], v[180:183], v[196:199], v[98:101]
	v_mfma_f32_16x16x32_bf16 v[86:89], v[170:173], v[204:207], v[86:89]
	v_mfma_f32_16x16x32_bf16 v[82:85], v[180:183], v[204:207], v[82:85]
	v_mfma_f32_16x16x32_bf16 v[70:73], v[170:173], v[212:215], v[70:73]
	v_mfma_f32_16x16x32_bf16 v[66:69], v[180:183], v[212:215], v[66:69]
	s_setprio 0
	s_barrier
	s_add_i32 s62, s74, s1
	v_lshl_add_u64 v[216:217], v[216:217], 0, s[56:57]
	s_mov_b32 m0, s62
	ds_read_b128 v[184:187], v178 offset:49152
	ds_read_b128 v[188:191], v178 offset:50176
	ds_read_b128 v[192:195], v178 offset:51200
	ds_read_b128 v[196:199], v178 offset:52224
	ds_read_b128 v[200:203], v178 offset:53248
	ds_read_b128 v[204:207], v178 offset:54272
	ds_read_b128 v[208:211], v178 offset:55296
	ds_read_b128 v[212:215], v178 offset:56320
	global_load_lds_dwordx4 v[216:217], off
	s_add_i32 m0, s62, 0x2000
	s_add_u32 s60, s60, 0x40080
	v_lshl_add_u64 v[216:217], v[218:219], 0, s[56:57]
	s_addc_u32 s61, s61, 0
	s_add_i32 s62, s75, s1
	global_load_lds_dwordx4 v[216:217], off
	v_lshl_add_u64 v[216:217], s[60:61], 0, v[130:131]
	s_mov_b32 m0, s62
	s_nop 0
	global_load_lds_dwordx4 v[216:217], off
	v_lshl_add_u64 v[216:217], s[60:61], 0, v[132:133]
	s_add_i32 m0, s62, 0x2000
	s_nop 0
	global_load_lds_dwordx4 v[216:217], off
	v_lshl_add_u64 v[216:217], v[220:221], 0, s[56:57]
	s_mov_b32 m0, s64
	s_nop 0
	global_load_lds_dwordx4 v[216:217], off
	v_lshl_add_u64 v[216:217], v[222:223], 0, s[56:57]
	s_mov_b32 m0, s65
	s_nop 0
	global_load_lds_dwordx4 v[216:217], off
	s_waitcnt vmcnt(8)
	s_waitcnt lgkmcnt(0)
	s_barrier
	s_setprio 1
	v_mfma_f32_16x16x32_bf16 v[62:65], v[144:147], v[184:187], v[62:65]
	v_mfma_f32_16x16x32_bf16 v[58:61], v[152:155], v[184:187], v[58:61]
	v_mfma_f32_16x16x32_bf16 v[46:49], v[144:147], v[192:195], v[46:49]
	v_mfma_f32_16x16x32_bf16 v[42:45], v[152:155], v[192:195], v[42:45]
	v_mfma_f32_16x16x32_bf16 v[30:33], v[144:147], v[200:203], v[30:33]
	v_mfma_f32_16x16x32_bf16 v[26:29], v[152:155], v[200:203], v[26:29]
	v_mfma_f32_16x16x32_bf16 v[14:17], v[144:147], v[208:211], v[14:17]
	v_mfma_f32_16x16x32_bf16 v[10:13], v[152:155], v[208:211], v[10:13]
	v_mfma_f32_16x16x32_bf16 v[62:65], v[148:151], v[188:191], v[62:65]
	v_mfma_f32_16x16x32_bf16 v[58:61], v[156:159], v[188:191], v[58:61]
	v_mfma_f32_16x16x32_bf16 v[46:49], v[148:151], v[196:199], v[46:49]
	v_mfma_f32_16x16x32_bf16 v[42:45], v[156:159], v[196:199], v[42:45]
	v_mfma_f32_16x16x32_bf16 v[30:33], v[148:151], v[204:207], v[30:33]
	v_mfma_f32_16x16x32_bf16 v[26:29], v[156:159], v[204:207], v[26:29]
	v_mfma_f32_16x16x32_bf16 v[14:17], v[148:151], v[212:215], v[14:17]
	v_mfma_f32_16x16x32_bf16 v[10:13], v[156:159], v[212:215], v[10:13]
	s_setprio 0
	s_setprio 1
	v_mfma_f32_16x16x32_bf16 v[54:57], v[160:163], v[184:187], v[54:57]
	v_mfma_f32_16x16x32_bf16 v[50:53], v[174:177], v[184:187], v[50:53]
	v_mfma_f32_16x16x32_bf16 v[38:41], v[160:163], v[192:195], v[38:41]
	v_mfma_f32_16x16x32_bf16 v[34:37], v[174:177], v[192:195], v[34:37]
	v_mfma_f32_16x16x32_bf16 v[22:25], v[160:163], v[200:203], v[22:25]
	v_mfma_f32_16x16x32_bf16 v[18:21], v[174:177], v[200:203], v[18:21]
	v_mfma_f32_16x16x32_bf16 v[6:9], v[160:163], v[208:211], v[6:9]
	v_mfma_f32_16x16x32_bf16 v[2:5], v[174:177], v[208:211], v[2:5]
	v_mfma_f32_16x16x32_bf16 v[54:57], v[170:173], v[188:191], v[54:57]
	v_mfma_f32_16x16x32_bf16 v[50:53], v[180:183], v[188:191], v[50:53]
	v_mfma_f32_16x16x32_bf16 v[38:41], v[170:173], v[196:199], v[38:41]
	v_mfma_f32_16x16x32_bf16 v[34:37], v[180:183], v[196:199], v[34:37]
	v_mfma_f32_16x16x32_bf16 v[22:25], v[170:173], v[204:207], v[22:25]
	v_mfma_f32_16x16x32_bf16 v[18:21], v[180:183], v[204:207], v[18:21]
	v_mfma_f32_16x16x32_bf16 v[6:9], v[170:173], v[212:215], v[6:9]
	v_mfma_f32_16x16x32_bf16 v[2:5], v[180:183], v[212:215], v[2:5]
	s_setprio 0
	s_barrier
	s_add_u32 s71, s71, 0x100
	s_addc_u32 s72, s72, 0
	s_add_u32 s58, s58, 0x100
	s_addc_u32 s59, s59, 0
	s_cmp_ge_i32 s73, s0
	s_mov_b32 s60, s73
	s_cbranch_scc0 .LBB0_229
	s_branch .Lpeelexitph1b
.LBB0_229:
	s_add_i32 s73, s60, 2
	s_add_u32 s61, s58, 0xfffc0080
	s_addc_u32 s62, s59, -1
	s_add_i32 s74, 0, 0x10000
	s_cmp_eq_u32 s68, s60
	s_cselect_b32 s63, s39, s62
	s_cselect_b32 s62, s43, s61
	s_cselect_b32 s61, s47, s72
	s_cselect_b32 s60, s55, s71
	s_add_i32 s76, 0, 0x14000
	v_add_u32_e32 v156, s74, v165
	v_add_u32_e32 v166, s76, v165
	ds_read_b128 v[144:147], v156
	ds_read_b128 v[148:151], v156 offset:1024
	ds_read_b128 v[152:155], v156 offset:2048
	ds_read_b128 v[156:159], v156 offset:3072
	ds_read_b128 v[160:163], v166
	ds_read_b128 v[170:173], v166 offset:1024
	ds_read_b128 v[174:177], v166 offset:2048
	ds_read_b128 v[180:183], v166 offset:3072
	v_lshl_add_u64 v[216:217], s[58:59], 0, v[142:143]
	s_add_i32 m0, s8, 0xc000
	ds_read_b128 v[184:187], v178
	ds_read_b128 v[188:191], v178 offset:1024
	ds_read_b128 v[192:195], v178 offset:2048
	ds_read_b128 v[196:199], v178 offset:3072
	ds_read_b128 v[200:203], v178 offset:4096
	ds_read_b128 v[204:207], v178 offset:5120
	ds_read_b128 v[208:211], v178 offset:6144
	ds_read_b128 v[212:215], v178 offset:7168
	global_load_lds_dwordx4 v[216:217], off
	v_lshl_add_u64 v[216:217], s[58:59], 0, v[140:141]
	s_add_i32 m0, s8, 0xe000
	s_nop 0
	global_load_lds_dwordx4 v[216:217], off
	s_waitcnt vmcnt(8)
	s_waitcnt lgkmcnt(0)
	s_barrier
	s_setprio 1
	v_mfma_f32_16x16x32_bf16 v[126:129], v[144:147], v[184:187], v[126:129]
	v_mfma_f32_16x16x32_bf16 v[122:125], v[152:155], v[184:187], v[122:125]
	v_mfma_f32_16x16x32_bf16 v[110:113], v[144:147], v[192:195], v[110:113]
	v_mfma_f32_16x16x32_bf16 v[106:109], v[152:155], v[192:195], v[106:109]
	v_mfma_f32_16x16x32_bf16 v[94:97], v[144:147], v[200:203], v[94:97]
	v_mfma_f32_16x16x32_bf16 v[90:93], v[152:155], v[200:203], v[90:93]
	v_mfma_f32_16x16x32_bf16 v[78:81], v[144:147], v[208:211], v[78:81]
	v_mfma_f32_16x16x32_bf16 v[74:77], v[152:155], v[208:211], v[74:77]
	v_mfma_f32_16x16x32_bf16 v[126:129], v[148:151], v[188:191], v[126:129]
	v_mfma_f32_16x16x32_bf16 v[122:125], v[156:159], v[188:191], v[122:125]
	v_mfma_f32_16x16x32_bf16 v[110:113], v[148:151], v[196:199], v[110:113]
	v_mfma_f32_16x16x32_bf16 v[106:109], v[156:159], v[196:199], v[106:109]
	v_mfma_f32_16x16x32_bf16 v[94:97], v[148:151], v[204:207], v[94:97]
	v_mfma_f32_16x16x32_bf16 v[90:93], v[156:159], v[204:207], v[90:93]
	v_mfma_f32_16x16x32_bf16 v[78:81], v[148:151], v[212:215], v[78:81]
	v_mfma_f32_16x16x32_bf16 v[74:77], v[156:159], v[212:215], v[74:77]
	s_setprio 0
	s_setprio 1
	v_mfma_f32_16x16x32_bf16 v[118:121], v[160:163], v[184:187], v[118:121]
	v_mfma_f32_16x16x32_bf16 v[114:117], v[174:177], v[184:187], v[114:117]
	v_mfma_f32_16x16x32_bf16 v[102:105], v[160:163], v[192:195], v[102:105]
	v_mfma_f32_16x16x32_bf16 v[98:101], v[174:177], v[192:195], v[98:101]
	v_mfma_f32_16x16x32_bf16 v[86:89], v[160:163], v[200:203], v[86:89]
	v_mfma_f32_16x16x32_bf16 v[82:85], v[174:177], v[200:203], v[82:85]
	v_mfma_f32_16x16x32_bf16 v[70:73], v[160:163], v[208:211], v[70:73]
	v_mfma_f32_16x16x32_bf16 v[66:69], v[174:177], v[208:211], v[66:69]
	v_mfma_f32_16x16x32_bf16 v[118:121], v[170:173], v[188:191], v[118:121]
	v_mfma_f32_16x16x32_bf16 v[114:117], v[180:183], v[188:191], v[114:117]
	v_mfma_f32_16x16x32_bf16 v[102:105], v[170:173], v[196:199], v[102:105]
	v_mfma_f32_16x16x32_bf16 v[98:101], v[180:183], v[196:199], v[98:101]
	v_mfma_f32_16x16x32_bf16 v[86:89], v[170:173], v[204:207], v[86:89]
	v_mfma_f32_16x16x32_bf16 v[82:85], v[180:183], v[204:207], v[82:85]
	v_mfma_f32_16x16x32_bf16 v[70:73], v[170:173], v[212:215], v[70:73]
	v_mfma_f32_16x16x32_bf16 v[66:69], v[180:183], v[212:215], v[66:69]
	s_setprio 0
	s_barrier
	s_add_i32 s74, s74, s1
	v_lshl_add_u64 v[216:217], s[60:61], 0, v[130:131]
	s_mov_b32 m0, s74
	ds_read_b128 v[184:187], v178 offset:16384
	ds_read_b128 v[188:191], v178 offset:17408
	ds_read_b128 v[192:195], v178 offset:18432
	ds_read_b128 v[196:199], v178 offset:19456
	ds_read_b128 v[200:203], v178 offset:20480
	ds_read_b128 v[204:207], v178 offset:21504
	ds_read_b128 v[208:211], v178 offset:22528
	ds_read_b128 v[212:215], v178 offset:23552
	global_load_lds_dwordx4 v[216:217], off
	s_add_i32 m0, s74, 0x2000
	s_add_u32 s74, s60, 0x40000
	v_lshl_add_u64 v[218:219], s[60:61], 0, v[132:133]
	s_addc_u32 s75, s61, 0
	s_add_i32 s76, s76, s1
	global_load_lds_dwordx4 v[218:219], off
	v_lshl_add_u64 v[220:221], s[74:75], 0, v[130:131]
	s_mov_b32 m0, s76
	v_lshl_add_u64 v[222:223], s[62:63], 0, v[136:137]
	global_load_lds_dwordx4 v[220:221], off
	v_lshl_add_u64 v[220:221], s[74:75], 0, v[132:133]
	s_add_i32 m0, s76, 0x2000
	s_nop 0
	global_load_lds_dwordx4 v[220:221], off
	v_lshl_add_u64 v[220:221], s[62:63], 0, v[134:135]
	s_mov_b32 m0, s8
	s_nop 0
	global_load_lds_dwordx4 v[220:221], off
	s_mov_b32 m0, s11
	s_nop 0
	global_load_lds_dwordx4 v[222:223], off
	s_waitcnt vmcnt(8)
	s_waitcnt lgkmcnt(0)
	s_barrier
	s_setprio 1
	v_mfma_f32_16x16x32_bf16 v[62:65], v[144:147], v[184:187], v[62:65]
	v_mfma_f32_16x16x32_bf16 v[58:61], v[152:155], v[184:187], v[58:61]
	v_mfma_f32_16x16x32_bf16 v[46:49], v[144:147], v[192:195], v[46:49]
	v_mfma_f32_16x16x32_bf16 v[42:45], v[152:155], v[192:195], v[42:45]
	v_mfma_f32_16x16x32_bf16 v[30:33], v[144:147], v[200:203], v[30:33]
	v_mfma_f32_16x16x32_bf16 v[26:29], v[152:155], v[200:203], v[26:29]
	v_mfma_f32_16x16x32_bf16 v[14:17], v[144:147], v[208:211], v[14:17]
	v_mfma_f32_16x16x32_bf16 v[10:13], v[152:155], v[208:211], v[10:13]
	v_mfma_f32_16x16x32_bf16 v[62:65], v[148:151], v[188:191], v[62:65]
	v_mfma_f32_16x16x32_bf16 v[58:61], v[156:159], v[188:191], v[58:61]
	v_mfma_f32_16x16x32_bf16 v[46:49], v[148:151], v[196:199], v[46:49]
	v_mfma_f32_16x16x32_bf16 v[42:45], v[156:159], v[196:199], v[42:45]
	v_mfma_f32_16x16x32_bf16 v[30:33], v[148:151], v[204:207], v[30:33]
	v_mfma_f32_16x16x32_bf16 v[26:29], v[156:159], v[204:207], v[26:29]
	v_mfma_f32_16x16x32_bf16 v[14:17], v[148:151], v[212:215], v[14:17]
	v_mfma_f32_16x16x32_bf16 v[10:13], v[156:159], v[212:215], v[10:13]
	s_setprio 0
	s_setprio 1
	v_mfma_f32_16x16x32_bf16 v[54:57], v[160:163], v[184:187], v[54:57]
	v_mfma_f32_16x16x32_bf16 v[50:53], v[174:177], v[184:187], v[50:53]
	v_mfma_f32_16x16x32_bf16 v[38:41], v[160:163], v[192:195], v[38:41]
	v_mfma_f32_16x16x32_bf16 v[34:37], v[174:177], v[192:195], v[34:37]
	v_mfma_f32_16x16x32_bf16 v[22:25], v[160:163], v[200:203], v[22:25]
	v_mfma_f32_16x16x32_bf16 v[18:21], v[174:177], v[200:203], v[18:21]
	v_mfma_f32_16x16x32_bf16 v[6:9], v[160:163], v[208:211], v[6:9]
	v_mfma_f32_16x16x32_bf16 v[2:5], v[174:177], v[208:211], v[2:5]
	v_mfma_f32_16x16x32_bf16 v[54:57], v[170:173], v[188:191], v[54:57]
	v_mfma_f32_16x16x32_bf16 v[50:53], v[180:183], v[188:191], v[50:53]
	v_mfma_f32_16x16x32_bf16 v[38:41], v[170:173], v[196:199], v[38:41]
	v_mfma_f32_16x16x32_bf16 v[34:37], v[180:183], v[196:199], v[34:37]
	v_mfma_f32_16x16x32_bf16 v[22:25], v[170:173], v[204:207], v[22:25]
	v_mfma_f32_16x16x32_bf16 v[18:21], v[180:183], v[204:207], v[18:21]
	v_mfma_f32_16x16x32_bf16 v[6:9], v[170:173], v[212:215], v[6:9]
	v_mfma_f32_16x16x32_bf16 v[2:5], v[180:183], v[212:215], v[2:5]
	s_setprio 0
	s_barrier
	s_add_i32 s74, 0, 0x18000
	s_add_i32 s75, 0, 0x1c000
	v_add_u32_e32 v156, s74, v165
	v_add_u32_e32 v166, s75, v165
	ds_read_b128 v[144:147], v156
	ds_read_b128 v[148:151], v156 offset:1024
	ds_read_b128 v[152:155], v156 offset:2048
	ds_read_b128 v[156:159], v156 offset:3072
	ds_read_b128 v[160:163], v166
	ds_read_b128 v[170:173], v166 offset:1024
	ds_read_b128 v[174:177], v166 offset:2048
	ds_read_b128 v[180:183], v166 offset:3072
	s_add_u32 s62, s62, 0x40000
	s_addc_u32 s63, s63, 0
	s_mov_b32 m0, s16
	v_lshl_add_u64 v[232:233], s[62:63], 0, v[134:135]
	ds_read_b128 v[184:187], v178 offset:32768
	ds_read_b128 v[188:191], v178 offset:33792
	ds_read_b128 v[192:195], v178 offset:34816
	ds_read_b128 v[196:199], v178 offset:35840
	ds_read_b128 v[200:203], v178 offset:36864
	ds_read_b128 v[204:207], v178 offset:37888
	ds_read_b128 v[208:211], v178 offset:38912
	ds_read_b128 v[212:215], v178 offset:39936
	global_load_lds_dwordx4 v[232:233], off
	v_lshl_add_u64 v[232:233], s[62:63], 0, v[136:137]
	s_mov_b32 m0, s25
	s_nop 0
	global_load_lds_dwordx4 v[232:233], off
	s_waitcnt vmcnt(8)
	s_waitcnt lgkmcnt(0)
	s_barrier
	s_setprio 1
	v_mfma_f32_16x16x32_bf16 v[126:129], v[144:147], v[184:187], v[126:129]
	v_mfma_f32_16x16x32_bf16 v[122:125], v[152:155], v[184:187], v[122:125]
	v_mfma_f32_16x16x32_bf16 v[110:113], v[144:147], v[192:195], v[110:113]
	v_mfma_f32_16x16x32_bf16 v[106:109], v[152:155], v[192:195], v[106:109]
	v_mfma_f32_16x16x32_bf16 v[94:97], v[144:147], v[200:203], v[94:97]
	v_mfma_f32_16x16x32_bf16 v[90:93], v[152:155], v[200:203], v[90:93]
	v_mfma_f32_16x16x32_bf16 v[78:81], v[144:147], v[208:211], v[78:81]
	v_mfma_f32_16x16x32_bf16 v[74:77], v[152:155], v[208:211], v[74:77]
	v_mfma_f32_16x16x32_bf16 v[126:129], v[148:151], v[188:191], v[126:129]
	v_mfma_f32_16x16x32_bf16 v[122:125], v[156:159], v[188:191], v[122:125]
	v_mfma_f32_16x16x32_bf16 v[110:113], v[148:151], v[196:199], v[110:113]
	v_mfma_f32_16x16x32_bf16 v[106:109], v[156:159], v[196:199], v[106:109]
	v_mfma_f32_16x16x32_bf16 v[94:97], v[148:151], v[204:207], v[94:97]
	v_mfma_f32_16x16x32_bf16 v[90:93], v[156:159], v[204:207], v[90:93]
	v_mfma_f32_16x16x32_bf16 v[78:81], v[148:151], v[212:215], v[78:81]
	v_mfma_f32_16x16x32_bf16 v[74:77], v[156:159], v[212:215], v[74:77]
	s_setprio 0
	s_setprio 1
	v_mfma_f32_16x16x32_bf16 v[118:121], v[160:163], v[184:187], v[118:121]
	v_mfma_f32_16x16x32_bf16 v[114:117], v[174:177], v[184:187], v[114:117]
	v_mfma_f32_16x16x32_bf16 v[102:105], v[160:163], v[192:195], v[102:105]
	v_mfma_f32_16x16x32_bf16 v[98:101], v[174:177], v[192:195], v[98:101]
	v_mfma_f32_16x16x32_bf16 v[86:89], v[160:163], v[200:203], v[86:89]
	v_mfma_f32_16x16x32_bf16 v[82:85], v[174:177], v[200:203], v[82:85]
	v_mfma_f32_16x16x32_bf16 v[70:73], v[160:163], v[208:211], v[70:73]
	v_mfma_f32_16x16x32_bf16 v[66:69], v[174:177], v[208:211], v[66:69]
	v_mfma_f32_16x16x32_bf16 v[118:121], v[170:173], v[188:191], v[118:121]
	v_mfma_f32_16x16x32_bf16 v[114:117], v[180:183], v[188:191], v[114:117]
	v_mfma_f32_16x16x32_bf16 v[102:105], v[170:173], v[196:199], v[102:105]
	v_mfma_f32_16x16x32_bf16 v[98:101], v[180:183], v[196:199], v[98:101]
	v_mfma_f32_16x16x32_bf16 v[86:89], v[170:173], v[204:207], v[86:89]
	v_mfma_f32_16x16x32_bf16 v[82:85], v[180:183], v[204:207], v[82:85]
	v_mfma_f32_16x16x32_bf16 v[70:73], v[170:173], v[212:215], v[70:73]
	v_mfma_f32_16x16x32_bf16 v[66:69], v[180:183], v[212:215], v[66:69]
	s_setprio 0
	s_barrier
	s_add_i32 s62, s74, s1
	v_lshl_add_u64 v[216:217], v[216:217], 0, s[56:57]
	s_mov_b32 m0, s62
	ds_read_b128 v[184:187], v178 offset:49152
	ds_read_b128 v[188:191], v178 offset:50176
	ds_read_b128 v[192:195], v178 offset:51200
	ds_read_b128 v[196:199], v178 offset:52224
	ds_read_b128 v[200:203], v178 offset:53248
	ds_read_b128 v[204:207], v178 offset:54272
	ds_read_b128 v[208:211], v178 offset:55296
	ds_read_b128 v[212:215], v178 offset:56320
	global_load_lds_dwordx4 v[216:217], off
	s_add_i32 m0, s62, 0x2000
	s_add_u32 s60, s60, 0x40080
	v_lshl_add_u64 v[216:217], v[218:219], 0, s[56:57]
	s_addc_u32 s61, s61, 0
	s_add_i32 s62, s75, s1
	global_load_lds_dwordx4 v[216:217], off
	v_lshl_add_u64 v[216:217], s[60:61], 0, v[130:131]
	s_mov_b32 m0, s62
	s_nop 0
	global_load_lds_dwordx4 v[216:217], off
	v_lshl_add_u64 v[216:217], s[60:61], 0, v[132:133]
	s_add_i32 m0, s62, 0x2000
	s_nop 0
	global_load_lds_dwordx4 v[216:217], off
	v_lshl_add_u64 v[216:217], v[220:221], 0, s[56:57]
	s_mov_b32 m0, s64
	s_nop 0
	global_load_lds_dwordx4 v[216:217], off
	v_lshl_add_u64 v[216:217], v[222:223], 0, s[56:57]
	s_mov_b32 m0, s65
	s_nop 0
	global_load_lds_dwordx4 v[216:217], off
	s_waitcnt vmcnt(8)
	s_waitcnt lgkmcnt(0)
	s_barrier
	s_setprio 1
	v_mfma_f32_16x16x32_bf16 v[62:65], v[144:147], v[184:187], v[62:65]
	v_mfma_f32_16x16x32_bf16 v[58:61], v[152:155], v[184:187], v[58:61]
	v_mfma_f32_16x16x32_bf16 v[46:49], v[144:147], v[192:195], v[46:49]
	v_mfma_f32_16x16x32_bf16 v[42:45], v[152:155], v[192:195], v[42:45]
	v_mfma_f32_16x16x32_bf16 v[30:33], v[144:147], v[200:203], v[30:33]
	v_mfma_f32_16x16x32_bf16 v[26:29], v[152:155], v[200:203], v[26:29]
	v_mfma_f32_16x16x32_bf16 v[14:17], v[144:147], v[208:211], v[14:17]
	v_mfma_f32_16x16x32_bf16 v[10:13], v[152:155], v[208:211], v[10:13]
	v_mfma_f32_16x16x32_bf16 v[62:65], v[148:151], v[188:191], v[62:65]
	v_mfma_f32_16x16x32_bf16 v[58:61], v[156:159], v[188:191], v[58:61]
	v_mfma_f32_16x16x32_bf16 v[46:49], v[148:151], v[196:199], v[46:49]
	v_mfma_f32_16x16x32_bf16 v[42:45], v[156:159], v[196:199], v[42:45]
	v_mfma_f32_16x16x32_bf16 v[30:33], v[148:151], v[204:207], v[30:33]
	v_mfma_f32_16x16x32_bf16 v[26:29], v[156:159], v[204:207], v[26:29]
	v_mfma_f32_16x16x32_bf16 v[14:17], v[148:151], v[212:215], v[14:17]
	v_mfma_f32_16x16x32_bf16 v[10:13], v[156:159], v[212:215], v[10:13]
	s_setprio 0
	s_setprio 1
	v_mfma_f32_16x16x32_bf16 v[54:57], v[160:163], v[184:187], v[54:57]
	v_mfma_f32_16x16x32_bf16 v[50:53], v[174:177], v[184:187], v[50:53]
	v_mfma_f32_16x16x32_bf16 v[38:41], v[160:163], v[192:195], v[38:41]
	v_mfma_f32_16x16x32_bf16 v[34:37], v[174:177], v[192:195], v[34:37]
	v_mfma_f32_16x16x32_bf16 v[22:25], v[160:163], v[200:203], v[22:25]
	v_mfma_f32_16x16x32_bf16 v[18:21], v[174:177], v[200:203], v[18:21]
	v_mfma_f32_16x16x32_bf16 v[6:9], v[160:163], v[208:211], v[6:9]
	v_mfma_f32_16x16x32_bf16 v[2:5], v[174:177], v[208:211], v[2:5]
	v_mfma_f32_16x16x32_bf16 v[54:57], v[170:173], v[188:191], v[54:57]
	v_mfma_f32_16x16x32_bf16 v[50:53], v[180:183], v[188:191], v[50:53]
	v_mfma_f32_16x16x32_bf16 v[38:41], v[170:173], v[196:199], v[38:41]
	v_mfma_f32_16x16x32_bf16 v[34:37], v[180:183], v[196:199], v[34:37]
	v_mfma_f32_16x16x32_bf16 v[22:25], v[170:173], v[204:207], v[22:25]
	v_mfma_f32_16x16x32_bf16 v[18:21], v[180:183], v[204:207], v[18:21]
	v_mfma_f32_16x16x32_bf16 v[6:9], v[170:173], v[212:215], v[6:9]
	v_mfma_f32_16x16x32_bf16 v[2:5], v[180:183], v[212:215], v[2:5]
	s_setprio 0
	s_barrier
	s_add_u32 s71, s71, 0x100
	s_addc_u32 s72, s72, 0
	s_add_u32 s58, s58, 0x100
	s_addc_u32 s59, s59, 0
	s_cmp_ge_i32 s73, s0
	s_mov_b32 s60, s73
	s_cbranch_scc0 .LBB0_229

.Lpeelph1f_0:
	s_add_i32 s71, s58, 2
	s_add_u32 s59, s54, 0xfffe0080
	s_addc_u32 s60, s55, -1
	s_add_i32 s72, 0, 0x10000
	s_cmp_eq_u32 s65, s58
	s_cselect_b32 s61, s39, s60
	s_cselect_b32 s60, s41, s59
	s_cselect_b32 s59, s43, s70
	s_cselect_b32 s58, s53, s69
	s_add_i32 s73, 0, 0x14000
	v_add_u32_e32 v2, s72, v198
	v_add_u32_e32 v6, s73, v198
	ds_read_b128 v[26:29], v2
	ds_read_b128 v[30:33], v2 offset:1024
	ds_read_b128 v[18:21], v2 offset:2048
	ds_read_b128 v[22:25], v2 offset:3072
	ds_read_b128 v[10:13], v6
	ds_read_b128 v[14:17], v6 offset:1024
	ds_read_b128 v[2:5], v6 offset:2048
	ds_read_b128 v[6:9], v6 offset:3072
	v_lshl_add_u64 v[170:171], s[54:55], 0, v[186:187]
	s_add_i32 m0, s8, 0xc000
	ds_read_b128 v[188:191], v200
	ds_read_b128 v[192:195], v200 offset:1024
	ds_read_b128 v[202:205], v200 offset:2048
	ds_read_b128 v[206:209], v200 offset:3072
	ds_read_b128 v[210:213], v200 offset:4096
	ds_read_b128 v[214:217], v200 offset:5120
	ds_read_b128 v[236:239], v200 offset:6144
	ds_read_b128 v[240:243], v200 offset:7168
	global_load_lds_dwordx4 v[170:171], off
	v_lshl_add_u64 v[170:171], s[54:55], 0, v[184:185]
	s_add_i32 m0, s8, 0xe000
	s_nop 0
	global_load_lds_dwordx4 v[170:171], off
	s_waitcnt vmcnt(8)
	s_waitcnt lgkmcnt(0)
	s_barrier
	s_setprio 1
	v_mfma_scale_f32_16x16x128_f8f6f4 v[158:161], v[26:33], v[188:195], 0, v196, v169 op_sel_hi:[0,0,0]
	v_mfma_scale_f32_16x16x128_f8f6f4 v[154:157], v[18:25], v[188:195], 0, v196, v169 op_sel_hi:[0,0,0]
	v_mfma_scale_f32_16x16x128_f8f6f4 v[142:145], v[26:33], v[202:209], 0, v196, v169 op_sel_hi:[0,0,0]
	v_mfma_scale_f32_16x16x128_f8f6f4 v[138:141], v[18:25], v[202:209], 0, v196, v169 op_sel_hi:[0,0,0]
	v_mfma_scale_f32_16x16x128_f8f6f4 v[126:129], v[26:33], v[210:217], 0, v196, v169 op_sel_hi:[0,0,0]
	v_mfma_scale_f32_16x16x128_f8f6f4 v[122:125], v[18:25], v[210:217], 0, v196, v169 op_sel_hi:[0,0,0]
	v_mfma_scale_f32_16x16x128_f8f6f4 v[110:113], v[26:33], v[236:243], 0, v196, v169 op_sel_hi:[0,0,0]
	v_mfma_scale_f32_16x16x128_f8f6f4 v[106:109], v[18:25], v[236:243], 0, v196, v169 op_sel_hi:[0,0,0]
	s_setprio 0
	s_setprio 1
	v_mfma_scale_f32_16x16x128_f8f6f4 v[150:153], v[10:17], v[188:195], 0, v196, v169 op_sel_hi:[0,0,0]
	v_mfma_scale_f32_16x16x128_f8f6f4 v[146:149], v[2:9], v[188:195], 0, v196, v169 op_sel_hi:[0,0,0]
	v_mfma_scale_f32_16x16x128_f8f6f4 v[134:137], v[10:17], v[202:209], 0, v196, v169 op_sel_hi:[0,0,0]
	v_mfma_scale_f32_16x16x128_f8f6f4 v[130:133], v[2:9], v[202:209], 0, v196, v169 op_sel_hi:[0,0,0]
	v_mfma_scale_f32_16x16x128_f8f6f4 v[118:121], v[10:17], v[210:217], 0, v196, v169 op_sel_hi:[0,0,0]
	v_mfma_scale_f32_16x16x128_f8f6f4 v[114:117], v[2:9], v[210:217], 0, v196, v169 op_sel_hi:[0,0,0]
	v_mfma_scale_f32_16x16x128_f8f6f4 v[102:105], v[10:17], v[236:243], 0, v196, v169 op_sel_hi:[0,0,0]
	v_mfma_scale_f32_16x16x128_f8f6f4 v[98:101], v[2:9], v[236:243], 0, v196, v169 op_sel_hi:[0,0,0]
	s_setprio 0
	s_barrier
	s_add_i32 s72, s72, s1
	v_lshl_add_u64 v[188:189], s[58:59], 0, v[162:163]
	s_mov_b32 m0, s72
	ds_read_b128 v[202:205], v200 offset:16384
	ds_read_b128 v[206:209], v200 offset:17408
	ds_read_b128 v[210:213], v200 offset:18432
	ds_read_b128 v[214:217], v200 offset:19456
	ds_read_b128 v[236:239], v200 offset:20480
	ds_read_b128 v[240:243], v200 offset:21504
	ds_read_b128 v[244:247], v200 offset:22528
	ds_read_b128 v[248:251], v200 offset:23552
	global_load_lds_dwordx4 v[188:189], off
	s_add_i32 m0, s72, 0x2000
	s_add_u32 s74, s58, 0x20000
	v_lshl_add_u64 v[190:191], s[58:59], 0, v[164:165]
	s_addc_u32 s75, s59, 0
	s_add_i32 s72, s73, s1
	global_load_lds_dwordx4 v[190:191], off
	v_lshl_add_u64 v[170:171], s[74:75], 0, v[162:163]
	s_mov_b32 m0, s72
	v_lshl_add_u64 v[192:193], s[60:61], 0, v[178:179]
	global_load_lds_dwordx4 v[170:171], off
	v_lshl_add_u64 v[170:171], s[74:75], 0, v[164:165]
	s_add_i32 m0, s72, 0x2000
	v_lshl_add_u64 v[194:195], s[60:61], 0, v[180:181]
	global_load_lds_dwordx4 v[170:171], off
	s_mov_b32 m0, s8
	s_nop 0
	global_load_lds_dwordx4 v[192:193], off
	s_mov_b32 m0, s11
	s_nop 0
	global_load_lds_dwordx4 v[194:195], off
	s_waitcnt vmcnt(8)
	s_waitcnt lgkmcnt(0)
	s_barrier
	s_setprio 1
	v_mfma_scale_f32_16x16x128_f8f6f4 v[94:97], v[26:33], v[202:209], 0, v196, v169 op_sel_hi:[0,0,0]
	v_mfma_scale_f32_16x16x128_f8f6f4 v[90:93], v[18:25], v[202:209], 0, v196, v169 op_sel_hi:[0,0,0]
	v_mfma_scale_f32_16x16x128_f8f6f4 v[78:81], v[26:33], v[210:217], 0, v196, v169 op_sel_hi:[0,0,0]
	v_mfma_scale_f32_16x16x128_f8f6f4 v[74:77], v[18:25], v[210:217], 0, v196, v169 op_sel_hi:[0,0,0]
	v_mfma_scale_f32_16x16x128_f8f6f4 v[62:65], v[26:33], v[236:243], 0, v196, v169 op_sel_hi:[0,0,0]
	v_mfma_scale_f32_16x16x128_f8f6f4 v[58:61], v[18:25], v[236:243], 0, v196, v169 op_sel_hi:[0,0,0]
	v_mfma_scale_f32_16x16x128_f8f6f4 v[46:49], v[26:33], v[244:251], 0, v196, v169 op_sel_hi:[0,0,0]
	v_mfma_scale_f32_16x16x128_f8f6f4 v[42:45], v[18:25], v[244:251], 0, v196, v169 op_sel_hi:[0,0,0]
	s_setprio 0
	s_setprio 1
	v_mfma_scale_f32_16x16x128_f8f6f4 v[86:89], v[10:17], v[202:209], 0, v196, v169 op_sel_hi:[0,0,0]
	v_mfma_scale_f32_16x16x128_f8f6f4 v[82:85], v[2:9], v[202:209], 0, v196, v169 op_sel_hi:[0,0,0]
	v_mfma_scale_f32_16x16x128_f8f6f4 v[70:73], v[10:17], v[210:217], 0, v196, v169 op_sel_hi:[0,0,0]
	v_mfma_scale_f32_16x16x128_f8f6f4 v[66:69], v[2:9], v[210:217], 0, v196, v169 op_sel_hi:[0,0,0]
	v_mfma_scale_f32_16x16x128_f8f6f4 v[54:57], v[10:17], v[236:243], 0, v196, v169 op_sel_hi:[0,0,0]
	v_mfma_scale_f32_16x16x128_f8f6f4 v[50:53], v[2:9], v[236:243], 0, v196, v169 op_sel_hi:[0,0,0]
	v_mfma_scale_f32_16x16x128_f8f6f4 v[38:41], v[10:17], v[244:251], 0, v196, v169 op_sel_hi:[0,0,0]
	v_mfma_scale_f32_16x16x128_f8f6f4 v[34:37], v[2:9], v[244:251], 0, v196, v169 op_sel_hi:[0,0,0]
	s_setprio 0
	s_barrier
	s_add_i32 s72, 0, 0x18000
	s_add_i32 s73, 0, 0x1c000
	v_add_u32_e32 v2, s72, v198
	v_add_u32_e32 v6, s73, v198
	ds_read_b128 v[26:29], v2
	ds_read_b128 v[30:33], v2 offset:1024
	ds_read_b128 v[18:21], v2 offset:2048
	ds_read_b128 v[22:25], v2 offset:3072
	ds_read_b128 v[10:13], v6
	ds_read_b128 v[14:17], v6 offset:1024
	ds_read_b128 v[2:5], v6 offset:2048
	ds_read_b128 v[6:9], v6 offset:3072
	s_add_u32 s60, s60, 0x20000
	s_addc_u32 s61, s61, 0
	s_mov_b32 m0, s16
	v_lshl_add_u64 v[170:171], s[60:61], 0, v[178:179]
	ds_read_b128 v[202:205], v200 offset:32768
	ds_read_b128 v[206:209], v200 offset:33792
	ds_read_b128 v[210:213], v200 offset:34816
	ds_read_b128 v[214:217], v200 offset:35840
	ds_read_b128 v[236:239], v200 offset:36864
	ds_read_b128 v[240:243], v200 offset:37888
	ds_read_b128 v[244:247], v200 offset:38912
	ds_read_b128 v[248:251], v200 offset:39936
	global_load_lds_dwordx4 v[170:171], off
	v_lshl_add_u64 v[170:171], s[60:61], 0, v[180:181]
	s_mov_b32 m0, s25
	s_nop 0
	global_load_lds_dwordx4 v[170:171], off
	s_waitcnt vmcnt(8)
	s_waitcnt lgkmcnt(0)
	s_barrier
	s_setprio 1
	v_mfma_scale_f32_16x16x128_f8f6f4 v[158:161], v[26:33], v[202:209], v[158:161], v196, v169 op_sel_hi:[0,0,0]
	v_mfma_scale_f32_16x16x128_f8f6f4 v[154:157], v[18:25], v[202:209], v[154:157], v196, v169 op_sel_hi:[0,0,0]
	v_mfma_scale_f32_16x16x128_f8f6f4 v[142:145], v[26:33], v[210:217], v[142:145], v196, v169 op_sel_hi:[0,0,0]
	v_mfma_scale_f32_16x16x128_f8f6f4 v[138:141], v[18:25], v[210:217], v[138:141], v196, v169 op_sel_hi:[0,0,0]
	v_mfma_scale_f32_16x16x128_f8f6f4 v[126:129], v[26:33], v[236:243], v[126:129], v196, v169 op_sel_hi:[0,0,0]
	v_mfma_scale_f32_16x16x128_f8f6f4 v[122:125], v[18:25], v[236:243], v[122:125], v196, v169 op_sel_hi:[0,0,0]
	v_mfma_scale_f32_16x16x128_f8f6f4 v[110:113], v[26:33], v[244:251], v[110:113], v196, v169 op_sel_hi:[0,0,0]
	v_mfma_scale_f32_16x16x128_f8f6f4 v[106:109], v[18:25], v[244:251], v[106:109], v196, v169 op_sel_hi:[0,0,0]
	s_setprio 0
	s_setprio 1
	v_mfma_scale_f32_16x16x128_f8f6f4 v[150:153], v[10:17], v[202:209], v[150:153], v196, v169 op_sel_hi:[0,0,0]
	v_mfma_scale_f32_16x16x128_f8f6f4 v[146:149], v[2:9], v[202:209], v[146:149], v196, v169 op_sel_hi:[0,0,0]
	v_mfma_scale_f32_16x16x128_f8f6f4 v[134:137], v[10:17], v[210:217], v[134:137], v196, v169 op_sel_hi:[0,0,0]
	v_mfma_scale_f32_16x16x128_f8f6f4 v[130:133], v[2:9], v[210:217], v[130:133], v196, v169 op_sel_hi:[0,0,0]
	v_mfma_scale_f32_16x16x128_f8f6f4 v[118:121], v[10:17], v[236:243], v[118:121], v196, v169 op_sel_hi:[0,0,0]
	v_mfma_scale_f32_16x16x128_f8f6f4 v[114:117], v[2:9], v[236:243], v[114:117], v196, v169 op_sel_hi:[0,0,0]
	v_mfma_scale_f32_16x16x128_f8f6f4 v[102:105], v[10:17], v[244:251], v[102:105], v196, v169 op_sel_hi:[0,0,0]
	v_mfma_scale_f32_16x16x128_f8f6f4 v[98:101], v[2:9], v[244:251], v[98:101], v196, v169 op_sel_hi:[0,0,0]
	s_setprio 0
	s_barrier
	s_add_i32 s60, s72, s1
	v_lshl_add_u64 v[170:171], v[188:189], 0, s[56:57]
	s_mov_b32 m0, s60
	ds_read_b128 v[202:205], v200 offset:49152
	ds_read_b128 v[206:209], v200 offset:50176
	ds_read_b128 v[210:213], v200 offset:51200
	ds_read_b128 v[214:217], v200 offset:52224
	ds_read_b128 v[236:239], v200 offset:53248
	ds_read_b128 v[240:243], v200 offset:54272
	ds_read_b128 v[244:247], v200 offset:55296
	ds_read_b128 v[248:251], v200 offset:56320
	global_load_lds_dwordx4 v[170:171], off
	s_add_i32 m0, s60, 0x2000
	s_add_u32 s58, s58, 0x20080
	v_lshl_add_u64 v[170:171], v[190:191], 0, s[56:57]
	s_addc_u32 s59, s59, 0
	s_add_i32 s60, s73, s1
	global_load_lds_dwordx4 v[170:171], off
	v_lshl_add_u64 v[170:171], s[58:59], 0, v[162:163]
	s_mov_b32 m0, s60
	s_nop 0
	global_load_lds_dwordx4 v[170:171], off
	v_lshl_add_u64 v[170:171], s[58:59], 0, v[164:165]
	s_add_i32 m0, s60, 0x2000
	s_nop 0
	global_load_lds_dwordx4 v[170:171], off
	v_lshl_add_u64 v[170:171], v[192:193], 0, s[56:57]
	s_mov_b32 m0, s62
	s_nop 0
	global_load_lds_dwordx4 v[170:171], off
	v_lshl_add_u64 v[170:171], v[194:195], 0, s[56:57]
	s_mov_b32 m0, s63
	s_nop 0
	global_load_lds_dwordx4 v[170:171], off
	s_waitcnt vmcnt(8)
	s_waitcnt lgkmcnt(0)
	s_barrier
	s_setprio 1
	v_mfma_scale_f32_16x16x128_f8f6f4 v[94:97], v[26:33], v[202:209], v[94:97], v196, v169 op_sel_hi:[0,0,0]
	v_mfma_scale_f32_16x16x128_f8f6f4 v[90:93], v[18:25], v[202:209], v[90:93], v196, v169 op_sel_hi:[0,0,0]
	v_mfma_scale_f32_16x16x128_f8f6f4 v[78:81], v[26:33], v[210:217], v[78:81], v196, v169 op_sel_hi:[0,0,0]
	v_mfma_scale_f32_16x16x128_f8f6f4 v[74:77], v[18:25], v[210:217], v[74:77], v196, v169 op_sel_hi:[0,0,0]
	v_mfma_scale_f32_16x16x128_f8f6f4 v[62:65], v[26:33], v[236:243], v[62:65], v196, v169 op_sel_hi:[0,0,0]
	v_mfma_scale_f32_16x16x128_f8f6f4 v[58:61], v[18:25], v[236:243], v[58:61], v196, v169 op_sel_hi:[0,0,0]
	v_mfma_scale_f32_16x16x128_f8f6f4 v[46:49], v[26:33], v[244:251], v[46:49], v196, v169 op_sel_hi:[0,0,0]
	v_mfma_scale_f32_16x16x128_f8f6f4 v[42:45], v[18:25], v[244:251], v[42:45], v196, v169 op_sel_hi:[0,0,0]
	s_setprio 0
	s_setprio 1
	v_mfma_scale_f32_16x16x128_f8f6f4 v[86:89], v[10:17], v[202:209], v[86:89], v196, v169 op_sel_hi:[0,0,0]
	v_mfma_scale_f32_16x16x128_f8f6f4 v[82:85], v[2:9], v[202:209], v[82:85], v196, v169 op_sel_hi:[0,0,0]
	v_mfma_scale_f32_16x16x128_f8f6f4 v[70:73], v[10:17], v[210:217], v[70:73], v196, v169 op_sel_hi:[0,0,0]
	v_mfma_scale_f32_16x16x128_f8f6f4 v[66:69], v[2:9], v[210:217], v[66:69], v196, v169 op_sel_hi:[0,0,0]
	v_mfma_scale_f32_16x16x128_f8f6f4 v[54:57], v[10:17], v[236:243], v[54:57], v196, v169 op_sel_hi:[0,0,0]
	v_mfma_scale_f32_16x16x128_f8f6f4 v[50:53], v[2:9], v[236:243], v[50:53], v196, v169 op_sel_hi:[0,0,0]
	v_mfma_scale_f32_16x16x128_f8f6f4 v[38:41], v[10:17], v[244:251], v[38:41], v196, v169 op_sel_hi:[0,0,0]
	v_mfma_scale_f32_16x16x128_f8f6f4 v[34:37], v[2:9], v[244:251], v[34:37], v196, v169 op_sel_hi:[0,0,0]
	s_setprio 0
	s_barrier
	s_add_u32 s69, s69, 0x100
	s_addc_u32 s70, s70, 0
	s_add_u32 s54, s54, 0x100
	s_addc_u32 s55, s55, 0
	s_cmp_ge_i32 s71, s0
	s_mov_b32 s58, s71
	s_cbranch_scc0 .LBB0_298
	s_branch .Lpeelexitph1f
.LBB0_298:
	s_add_i32 s71, s58, 2
	s_add_u32 s59, s54, 0xfffe0080
	s_addc_u32 s60, s55, -1
	s_add_i32 s72, 0, 0x10000
	s_cmp_eq_u32 s65, s58
	s_cselect_b32 s61, s39, s60
	s_cselect_b32 s60, s41, s59
	s_cselect_b32 s59, s43, s70
	s_cselect_b32 s58, s53, s69
	s_add_i32 s73, 0, 0x14000
	v_add_u32_e32 v2, s72, v198
	v_add_u32_e32 v6, s73, v198
	ds_read_b128 v[26:29], v2
	ds_read_b128 v[30:33], v2 offset:1024
	ds_read_b128 v[18:21], v2 offset:2048
	ds_read_b128 v[22:25], v2 offset:3072
	ds_read_b128 v[10:13], v6
	ds_read_b128 v[14:17], v6 offset:1024
	ds_read_b128 v[2:5], v6 offset:2048
	ds_read_b128 v[6:9], v6 offset:3072
	v_lshl_add_u64 v[170:171], s[54:55], 0, v[186:187]
	s_add_i32 m0, s8, 0xc000
	ds_read_b128 v[188:191], v200
	ds_read_b128 v[192:195], v200 offset:1024
	ds_read_b128 v[202:205], v200 offset:2048
	ds_read_b128 v[206:209], v200 offset:3072
	ds_read_b128 v[210:213], v200 offset:4096
	ds_read_b128 v[214:217], v200 offset:5120
	ds_read_b128 v[236:239], v200 offset:6144
	ds_read_b128 v[240:243], v200 offset:7168
	global_load_lds_dwordx4 v[170:171], off
	v_lshl_add_u64 v[170:171], s[54:55], 0, v[184:185]
	s_add_i32 m0, s8, 0xe000
	s_nop 0
	global_load_lds_dwordx4 v[170:171], off
	s_waitcnt vmcnt(8)
	s_waitcnt lgkmcnt(0)
	s_barrier
	s_setprio 1
	v_mfma_scale_f32_16x16x128_f8f6f4 v[158:161], v[26:33], v[188:195], v[158:161], v196, v169 op_sel_hi:[0,0,0]
	v_mfma_scale_f32_16x16x128_f8f6f4 v[154:157], v[18:25], v[188:195], v[154:157], v196, v169 op_sel_hi:[0,0,0]
	v_mfma_scale_f32_16x16x128_f8f6f4 v[142:145], v[26:33], v[202:209], v[142:145], v196, v169 op_sel_hi:[0,0,0]
	v_mfma_scale_f32_16x16x128_f8f6f4 v[138:141], v[18:25], v[202:209], v[138:141], v196, v169 op_sel_hi:[0,0,0]
	v_mfma_scale_f32_16x16x128_f8f6f4 v[126:129], v[26:33], v[210:217], v[126:129], v196, v169 op_sel_hi:[0,0,0]
	v_mfma_scale_f32_16x16x128_f8f6f4 v[122:125], v[18:25], v[210:217], v[122:125], v196, v169 op_sel_hi:[0,0,0]
	v_mfma_scale_f32_16x16x128_f8f6f4 v[110:113], v[26:33], v[236:243], v[110:113], v196, v169 op_sel_hi:[0,0,0]
	v_mfma_scale_f32_16x16x128_f8f6f4 v[106:109], v[18:25], v[236:243], v[106:109], v196, v169 op_sel_hi:[0,0,0]
	s_setprio 0
	s_setprio 1
	v_mfma_scale_f32_16x16x128_f8f6f4 v[150:153], v[10:17], v[188:195], v[150:153], v196, v169 op_sel_hi:[0,0,0]
	v_mfma_scale_f32_16x16x128_f8f6f4 v[146:149], v[2:9], v[188:195], v[146:149], v196, v169 op_sel_hi:[0,0,0]
	v_mfma_scale_f32_16x16x128_f8f6f4 v[134:137], v[10:17], v[202:209], v[134:137], v196, v169 op_sel_hi:[0,0,0]
	v_mfma_scale_f32_16x16x128_f8f6f4 v[130:133], v[2:9], v[202:209], v[130:133], v196, v169 op_sel_hi:[0,0,0]
	v_mfma_scale_f32_16x16x128_f8f6f4 v[118:121], v[10:17], v[210:217], v[118:121], v196, v169 op_sel_hi:[0,0,0]
	v_mfma_scale_f32_16x16x128_f8f6f4 v[114:117], v[2:9], v[210:217], v[114:117], v196, v169 op_sel_hi:[0,0,0]
	v_mfma_scale_f32_16x16x128_f8f6f4 v[102:105], v[10:17], v[236:243], v[102:105], v196, v169 op_sel_hi:[0,0,0]
	v_mfma_scale_f32_16x16x128_f8f6f4 v[98:101], v[2:9], v[236:243], v[98:101], v196, v169 op_sel_hi:[0,0,0]
	s_setprio 0
	s_barrier
	s_add_i32 s72, s72, s1
	v_lshl_add_u64 v[188:189], s[58:59], 0, v[162:163]
	s_mov_b32 m0, s72
	ds_read_b128 v[202:205], v200 offset:16384
	ds_read_b128 v[206:209], v200 offset:17408
	ds_read_b128 v[210:213], v200 offset:18432
	ds_read_b128 v[214:217], v200 offset:19456
	ds_read_b128 v[236:239], v200 offset:20480
	ds_read_b128 v[240:243], v200 offset:21504
	ds_read_b128 v[244:247], v200 offset:22528
	ds_read_b128 v[248:251], v200 offset:23552
	global_load_lds_dwordx4 v[188:189], off
	s_add_i32 m0, s72, 0x2000
	s_add_u32 s74, s58, 0x20000
	v_lshl_add_u64 v[190:191], s[58:59], 0, v[164:165]
	s_addc_u32 s75, s59, 0
	s_add_i32 s72, s73, s1
	global_load_lds_dwordx4 v[190:191], off
	v_lshl_add_u64 v[170:171], s[74:75], 0, v[162:163]
	s_mov_b32 m0, s72
	v_lshl_add_u64 v[192:193], s[60:61], 0, v[178:179]
	global_load_lds_dwordx4 v[170:171], off
	v_lshl_add_u64 v[170:171], s[74:75], 0, v[164:165]
	s_add_i32 m0, s72, 0x2000
	v_lshl_add_u64 v[194:195], s[60:61], 0, v[180:181]
	global_load_lds_dwordx4 v[170:171], off
	s_mov_b32 m0, s8
	s_nop 0
	global_load_lds_dwordx4 v[192:193], off
	s_mov_b32 m0, s11
	s_nop 0
	global_load_lds_dwordx4 v[194:195], off
	s_waitcnt vmcnt(8)
	s_waitcnt lgkmcnt(0)
	s_barrier
	s_setprio 1
	v_mfma_scale_f32_16x16x128_f8f6f4 v[94:97], v[26:33], v[202:209], v[94:97], v196, v169 op_sel_hi:[0,0,0]
	v_mfma_scale_f32_16x16x128_f8f6f4 v[90:93], v[18:25], v[202:209], v[90:93], v196, v169 op_sel_hi:[0,0,0]
	v_mfma_scale_f32_16x16x128_f8f6f4 v[78:81], v[26:33], v[210:217], v[78:81], v196, v169 op_sel_hi:[0,0,0]
	v_mfma_scale_f32_16x16x128_f8f6f4 v[74:77], v[18:25], v[210:217], v[74:77], v196, v169 op_sel_hi:[0,0,0]
	v_mfma_scale_f32_16x16x128_f8f6f4 v[62:65], v[26:33], v[236:243], v[62:65], v196, v169 op_sel_hi:[0,0,0]
	v_mfma_scale_f32_16x16x128_f8f6f4 v[58:61], v[18:25], v[236:243], v[58:61], v196, v169 op_sel_hi:[0,0,0]
	v_mfma_scale_f32_16x16x128_f8f6f4 v[46:49], v[26:33], v[244:251], v[46:49], v196, v169 op_sel_hi:[0,0,0]
	v_mfma_scale_f32_16x16x128_f8f6f4 v[42:45], v[18:25], v[244:251], v[42:45], v196, v169 op_sel_hi:[0,0,0]
	s_setprio 0
	s_setprio 1
	v_mfma_scale_f32_16x16x128_f8f6f4 v[86:89], v[10:17], v[202:209], v[86:89], v196, v169 op_sel_hi:[0,0,0]
	v_mfma_scale_f32_16x16x128_f8f6f4 v[82:85], v[2:9], v[202:209], v[82:85], v196, v169 op_sel_hi:[0,0,0]
	v_mfma_scale_f32_16x16x128_f8f6f4 v[70:73], v[10:17], v[210:217], v[70:73], v196, v169 op_sel_hi:[0,0,0]
	v_mfma_scale_f32_16x16x128_f8f6f4 v[66:69], v[2:9], v[210:217], v[66:69], v196, v169 op_sel_hi:[0,0,0]
	v_mfma_scale_f32_16x16x128_f8f6f4 v[54:57], v[10:17], v[236:243], v[54:57], v196, v169 op_sel_hi:[0,0,0]
	v_mfma_scale_f32_16x16x128_f8f6f4 v[50:53], v[2:9], v[236:243], v[50:53], v196, v169 op_sel_hi:[0,0,0]
	v_mfma_scale_f32_16x16x128_f8f6f4 v[38:41], v[10:17], v[244:251], v[38:41], v196, v169 op_sel_hi:[0,0,0]
	v_mfma_scale_f32_16x16x128_f8f6f4 v[34:37], v[2:9], v[244:251], v[34:37], v196, v169 op_sel_hi:[0,0,0]
	s_setprio 0
	s_barrier
	s_add_i32 s72, 0, 0x18000
	s_add_i32 s73, 0, 0x1c000
	v_add_u32_e32 v2, s72, v198
	v_add_u32_e32 v6, s73, v198
	ds_read_b128 v[26:29], v2
	ds_read_b128 v[30:33], v2 offset:1024
	ds_read_b128 v[18:21], v2 offset:2048
	ds_read_b128 v[22:25], v2 offset:3072
	ds_read_b128 v[10:13], v6
	ds_read_b128 v[14:17], v6 offset:1024
	ds_read_b128 v[2:5], v6 offset:2048
	ds_read_b128 v[6:9], v6 offset:3072
	s_add_u32 s60, s60, 0x20000
	s_addc_u32 s61, s61, 0
	s_mov_b32 m0, s16
	v_lshl_add_u64 v[170:171], s[60:61], 0, v[178:179]
	ds_read_b128 v[202:205], v200 offset:32768
	ds_read_b128 v[206:209], v200 offset:33792
	ds_read_b128 v[210:213], v200 offset:34816
	ds_read_b128 v[214:217], v200 offset:35840
	ds_read_b128 v[236:239], v200 offset:36864
	ds_read_b128 v[240:243], v200 offset:37888
	ds_read_b128 v[244:247], v200 offset:38912
	ds_read_b128 v[248:251], v200 offset:39936
	global_load_lds_dwordx4 v[170:171], off
	v_lshl_add_u64 v[170:171], s[60:61], 0, v[180:181]
	s_mov_b32 m0, s25
	s_nop 0
	global_load_lds_dwordx4 v[170:171], off
	s_waitcnt vmcnt(8)
	s_waitcnt lgkmcnt(0)
	s_barrier
	s_setprio 1
	v_mfma_scale_f32_16x16x128_f8f6f4 v[158:161], v[26:33], v[202:209], v[158:161], v196, v169 op_sel_hi:[0,0,0]
	v_mfma_scale_f32_16x16x128_f8f6f4 v[154:157], v[18:25], v[202:209], v[154:157], v196, v169 op_sel_hi:[0,0,0]
	v_mfma_scale_f32_16x16x128_f8f6f4 v[142:145], v[26:33], v[210:217], v[142:145], v196, v169 op_sel_hi:[0,0,0]
	v_mfma_scale_f32_16x16x128_f8f6f4 v[138:141], v[18:25], v[210:217], v[138:141], v196, v169 op_sel_hi:[0,0,0]
	v_mfma_scale_f32_16x16x128_f8f6f4 v[126:129], v[26:33], v[236:243], v[126:129], v196, v169 op_sel_hi:[0,0,0]
	v_mfma_scale_f32_16x16x128_f8f6f4 v[122:125], v[18:25], v[236:243], v[122:125], v196, v169 op_sel_hi:[0,0,0]
	v_mfma_scale_f32_16x16x128_f8f6f4 v[110:113], v[26:33], v[244:251], v[110:113], v196, v169 op_sel_hi:[0,0,0]
	v_mfma_scale_f32_16x16x128_f8f6f4 v[106:109], v[18:25], v[244:251], v[106:109], v196, v169 op_sel_hi:[0,0,0]
	s_setprio 0
	s_setprio 1
	v_mfma_scale_f32_16x16x128_f8f6f4 v[150:153], v[10:17], v[202:209], v[150:153], v196, v169 op_sel_hi:[0,0,0]
	v_mfma_scale_f32_16x16x128_f8f6f4 v[146:149], v[2:9], v[202:209], v[146:149], v196, v169 op_sel_hi:[0,0,0]
	v_mfma_scale_f32_16x16x128_f8f6f4 v[134:137], v[10:17], v[210:217], v[134:137], v196, v169 op_sel_hi:[0,0,0]
	v_mfma_scale_f32_16x16x128_f8f6f4 v[130:133], v[2:9], v[210:217], v[130:133], v196, v169 op_sel_hi:[0,0,0]
	v_mfma_scale_f32_16x16x128_f8f6f4 v[118:121], v[10:17], v[236:243], v[118:121], v196, v169 op_sel_hi:[0,0,0]
	v_mfma_scale_f32_16x16x128_f8f6f4 v[114:117], v[2:9], v[236:243], v[114:117], v196, v169 op_sel_hi:[0,0,0]
	v_mfma_scale_f32_16x16x128_f8f6f4 v[102:105], v[10:17], v[244:251], v[102:105], v196, v169 op_sel_hi:[0,0,0]
	v_mfma_scale_f32_16x16x128_f8f6f4 v[98:101], v[2:9], v[244:251], v[98:101], v196, v169 op_sel_hi:[0,0,0]
	s_setprio 0
	s_barrier
	s_add_i32 s60, s72, s1
	v_lshl_add_u64 v[170:171], v[188:189], 0, s[56:57]
	s_mov_b32 m0, s60
	ds_read_b128 v[202:205], v200 offset:49152
	ds_read_b128 v[206:209], v200 offset:50176
	ds_read_b128 v[210:213], v200 offset:51200
	ds_read_b128 v[214:217], v200 offset:52224
	ds_read_b128 v[236:239], v200 offset:53248
	ds_read_b128 v[240:243], v200 offset:54272
	ds_read_b128 v[244:247], v200 offset:55296
	ds_read_b128 v[248:251], v200 offset:56320
	global_load_lds_dwordx4 v[170:171], off
	s_add_i32 m0, s60, 0x2000
	s_add_u32 s58, s58, 0x20080
	v_lshl_add_u64 v[170:171], v[190:191], 0, s[56:57]
	s_addc_u32 s59, s59, 0
	s_add_i32 s60, s73, s1
	global_load_lds_dwordx4 v[170:171], off
	v_lshl_add_u64 v[170:171], s[58:59], 0, v[162:163]
	s_mov_b32 m0, s60
	s_nop 0
	global_load_lds_dwordx4 v[170:171], off
	v_lshl_add_u64 v[170:171], s[58:59], 0, v[164:165]
	s_add_i32 m0, s60, 0x2000
	s_nop 0
	global_load_lds_dwordx4 v[170:171], off
	v_lshl_add_u64 v[170:171], v[192:193], 0, s[56:57]
	s_mov_b32 m0, s62
	s_nop 0
	global_load_lds_dwordx4 v[170:171], off
	v_lshl_add_u64 v[170:171], v[194:195], 0, s[56:57]
	s_mov_b32 m0, s63
	s_nop 0
	global_load_lds_dwordx4 v[170:171], off
	s_waitcnt vmcnt(8)
	s_waitcnt lgkmcnt(0)
	s_barrier
	s_setprio 1
	v_mfma_scale_f32_16x16x128_f8f6f4 v[94:97], v[26:33], v[202:209], v[94:97], v196, v169 op_sel_hi:[0,0,0]
	v_mfma_scale_f32_16x16x128_f8f6f4 v[90:93], v[18:25], v[202:209], v[90:93], v196, v169 op_sel_hi:[0,0,0]
	v_mfma_scale_f32_16x16x128_f8f6f4 v[78:81], v[26:33], v[210:217], v[78:81], v196, v169 op_sel_hi:[0,0,0]
	v_mfma_scale_f32_16x16x128_f8f6f4 v[74:77], v[18:25], v[210:217], v[74:77], v196, v169 op_sel_hi:[0,0,0]
	v_mfma_scale_f32_16x16x128_f8f6f4 v[62:65], v[26:33], v[236:243], v[62:65], v196, v169 op_sel_hi:[0,0,0]
	v_mfma_scale_f32_16x16x128_f8f6f4 v[58:61], v[18:25], v[236:243], v[58:61], v196, v169 op_sel_hi:[0,0,0]
	v_mfma_scale_f32_16x16x128_f8f6f4 v[46:49], v[26:33], v[244:251], v[46:49], v196, v169 op_sel_hi:[0,0,0]
	v_mfma_scale_f32_16x16x128_f8f6f4 v[42:45], v[18:25], v[244:251], v[42:45], v196, v169 op_sel_hi:[0,0,0]
	s_setprio 0
	s_setprio 1
	v_mfma_scale_f32_16x16x128_f8f6f4 v[86:89], v[10:17], v[202:209], v[86:89], v196, v169 op_sel_hi:[0,0,0]
	v_mfma_scale_f32_16x16x128_f8f6f4 v[82:85], v[2:9], v[202:209], v[82:85], v196, v169 op_sel_hi:[0,0,0]
	v_mfma_scale_f32_16x16x128_f8f6f4 v[70:73], v[10:17], v[210:217], v[70:73], v196, v169 op_sel_hi:[0,0,0]
	v_mfma_scale_f32_16x16x128_f8f6f4 v[66:69], v[2:9], v[210:217], v[66:69], v196, v169 op_sel_hi:[0,0,0]
	v_mfma_scale_f32_16x16x128_f8f6f4 v[54:57], v[10:17], v[236:243], v[54:57], v196, v169 op_sel_hi:[0,0,0]
	v_mfma_scale_f32_16x16x128_f8f6f4 v[50:53], v[2:9], v[236:243], v[50:53], v196, v169 op_sel_hi:[0,0,0]
	v_mfma_scale_f32_16x16x128_f8f6f4 v[38:41], v[10:17], v[244:251], v[38:41], v196, v169 op_sel_hi:[0,0,0]
	v_mfma_scale_f32_16x16x128_f8f6f4 v[34:37], v[2:9], v[244:251], v[34:37], v196, v169 op_sel_hi:[0,0,0]
	s_setprio 0
	s_barrier
	s_add_u32 s69, s69, 0x100
	s_addc_u32 s70, s70, 0
	s_add_u32 s54, s54, 0x100
	s_addc_u32 s55, s55, 0
	s_cmp_ge_i32 s71, s0
	s_mov_b32 s58, s71
	s_cbranch_scc0 .LBB0_298

.Lpeelph3_0:
	s_add_i32 s73, s68, 2
	s_add_u32 s69, s64, 0xfffc0080
	s_addc_u32 s70, s65, -1
	s_add_i32 s74, 0, 0x10000
	s_cmp_eq_u32 s24, s68
	s_cselect_b32 s71, s59, s70
	s_cselect_b32 s70, s58, s69
	s_cselect_b32 s69, s51, s72
	s_cselect_b32 s68, s53, s66
	s_add_i32 s76, 0, 0x14000
	v_add_u32_e32 v152, s74, v220
	v_add_u32_e32 v164, s76, v220
	ds_read_b128 v[106:109], v152
	ds_read_b128 v[110:113], v152 offset:1024
	ds_read_b128 v[114:117], v152 offset:2048
	ds_read_b128 v[152:155], v152 offset:3072
	ds_read_b128 v[156:159], v164
	ds_read_b128 v[160:163], v164 offset:1024
	ds_read_b128 v[170:173], v164 offset:2048
	ds_read_b128 v[174:177], v164 offset:3072
	v_lshl_add_u64 v[164:165], s[64:65], 0, v[150:151]
	s_add_i32 m0, s14, 0xc000
	ds_read_b128 v[178:181], v222
	ds_read_b128 v[182:185], v222 offset:1024
	ds_read_b128 v[186:189], v222 offset:2048
	ds_read_b128 v[190:193], v222 offset:3072
	ds_read_b128 v[194:197], v222 offset:4096
	ds_read_b128 v[198:201], v222 offset:5120
	ds_read_b128 v[202:205], v222 offset:6144
	ds_read_b128 v[206:209], v222 offset:7168
	global_load_lds_dwordx4 v[164:165], off
	v_lshl_add_u64 v[164:165], s[64:65], 0, v[148:149]
	s_add_i32 m0, s14, 0xe000
	s_nop 0
	global_load_lds_dwordx4 v[164:165], off
	s_waitcnt vmcnt(8)
	s_waitcnt lgkmcnt(0)
	s_barrier
	s_setprio 1
	v_mfma_f32_16x16x32_bf16 v[138:141], v[106:109], v[178:181], 0
	v_mfma_f32_16x16x32_bf16 v[62:65], v[114:117], v[178:181], 0
	v_mfma_f32_16x16x32_bf16 v[130:133], v[106:109], v[186:189], 0
	v_mfma_f32_16x16x32_bf16 v[54:57], v[114:117], v[186:189], 0
	v_mfma_f32_16x16x32_bf16 v[122:125], v[106:109], v[194:197], 0
	v_mfma_f32_16x16x32_bf16 v[46:49], v[114:117], v[194:197], 0
	v_mfma_f32_16x16x32_bf16 v[102:105], v[106:109], v[202:205], 0
	v_mfma_f32_16x16x32_bf16 v[38:41], v[114:117], v[202:205], 0
	v_mfma_f32_16x16x32_bf16 v[138:141], v[110:113], v[182:185], v[138:141]
	v_mfma_f32_16x16x32_bf16 v[62:65], v[152:155], v[182:185], v[62:65]
	v_mfma_f32_16x16x32_bf16 v[130:133], v[110:113], v[190:193], v[130:133]
	v_mfma_f32_16x16x32_bf16 v[54:57], v[152:155], v[190:193], v[54:57]
	v_mfma_f32_16x16x32_bf16 v[122:125], v[110:113], v[198:201], v[122:125]
	v_mfma_f32_16x16x32_bf16 v[46:49], v[152:155], v[198:201], v[46:49]
	v_mfma_f32_16x16x32_bf16 v[102:105], v[110:113], v[206:209], v[102:105]
	v_mfma_f32_16x16x32_bf16 v[38:41], v[152:155], v[206:209], v[38:41]
	s_setprio 0
	s_setprio 1
	v_mfma_f32_16x16x32_bf16 v[134:137], v[156:159], v[178:181], 0
	v_mfma_f32_16x16x32_bf16 v[58:61], v[170:173], v[178:181], 0
	v_mfma_f32_16x16x32_bf16 v[126:129], v[156:159], v[186:189], 0
	v_mfma_f32_16x16x32_bf16 v[50:53], v[170:173], v[186:189], 0
	v_mfma_f32_16x16x32_bf16 v[118:121], v[156:159], v[194:197], 0
	v_mfma_f32_16x16x32_bf16 v[42:45], v[170:173], v[194:197], 0
	v_mfma_f32_16x16x32_bf16 v[98:101], v[156:159], v[202:205], 0
	v_mfma_f32_16x16x32_bf16 v[34:37], v[170:173], v[202:205], 0
	v_mfma_f32_16x16x32_bf16 v[134:137], v[160:163], v[182:185], v[134:137]
	v_mfma_f32_16x16x32_bf16 v[58:61], v[174:177], v[182:185], v[58:61]
	v_mfma_f32_16x16x32_bf16 v[126:129], v[160:163], v[190:193], v[126:129]
	v_mfma_f32_16x16x32_bf16 v[50:53], v[174:177], v[190:193], v[50:53]
	v_mfma_f32_16x16x32_bf16 v[118:121], v[160:163], v[198:201], v[118:121]
	v_mfma_f32_16x16x32_bf16 v[42:45], v[174:177], v[198:201], v[42:45]
	v_mfma_f32_16x16x32_bf16 v[98:101], v[160:163], v[206:209], v[98:101]
	v_mfma_f32_16x16x32_bf16 v[34:37], v[174:177], v[206:209], v[34:37]
	s_setprio 0
	s_barrier
	s_add_i32 s74, s74, s13
	v_lshl_add_u64 v[164:165], s[68:69], 0, v[166:167]
	s_mov_b32 m0, s74
	ds_read_b128 v[178:181], v222 offset:16384
	ds_read_b128 v[182:185], v222 offset:17408
	ds_read_b128 v[186:189], v222 offset:18432
	ds_read_b128 v[190:193], v222 offset:19456
	ds_read_b128 v[194:197], v222 offset:20480
	ds_read_b128 v[198:201], v222 offset:21504
	ds_read_b128 v[202:205], v222 offset:22528
	ds_read_b128 v[206:209], v222 offset:23552
	global_load_lds_dwordx4 v[164:165], off
	s_add_i32 m0, s74, 0x2000
	s_add_u32 s74, s68, 0x8000
	v_lshl_add_u64 v[210:211], s[68:69], 0, v[142:143]
	s_addc_u32 s75, s69, 0
	s_add_i32 s76, s76, s13
	global_load_lds_dwordx4 v[210:211], off
	v_lshl_add_u64 v[212:213], s[74:75], 0, v[166:167]
	s_mov_b32 m0, s76
	v_lshl_add_u64 v[214:215], s[70:71], 0, v[146:147]
	global_load_lds_dwordx4 v[212:213], off
	v_lshl_add_u64 v[212:213], s[74:75], 0, v[142:143]
	s_add_i32 m0, s76, 0x2000
	s_nop 0
	global_load_lds_dwordx4 v[212:213], off
	v_lshl_add_u64 v[212:213], s[70:71], 0, v[144:145]
	s_mov_b32 m0, s14
	s_nop 0
	global_load_lds_dwordx4 v[212:213], off
	s_mov_b32 m0, s15
	s_nop 0
	global_load_lds_dwordx4 v[214:215], off
	s_waitcnt vmcnt(8)
	s_waitcnt lgkmcnt(0)
	s_barrier
	s_setprio 1
	v_mfma_f32_16x16x32_bf16 v[94:97], v[106:109], v[178:181], 0
	v_mfma_f32_16x16x32_bf16 v[30:33], v[114:117], v[178:181], 0
	v_mfma_f32_16x16x32_bf16 v[86:89], v[106:109], v[186:189], 0
	v_mfma_f32_16x16x32_bf16 v[22:25], v[114:117], v[186:189], 0
	v_mfma_f32_16x16x32_bf16 v[78:81], v[106:109], v[194:197], 0
	v_mfma_f32_16x16x32_bf16 v[14:17], v[114:117], v[194:197], 0
	v_mfma_f32_16x16x32_bf16 v[70:73], v[106:109], v[202:205], 0
	v_mfma_f32_16x16x32_bf16 v[6:9], v[114:117], v[202:205], 0
	v_mfma_f32_16x16x32_bf16 v[94:97], v[110:113], v[182:185], v[94:97]
	v_mfma_f32_16x16x32_bf16 v[30:33], v[152:155], v[182:185], v[30:33]
	v_mfma_f32_16x16x32_bf16 v[86:89], v[110:113], v[190:193], v[86:89]
	v_mfma_f32_16x16x32_bf16 v[22:25], v[152:155], v[190:193], v[22:25]
	v_mfma_f32_16x16x32_bf16 v[78:81], v[110:113], v[198:201], v[78:81]
	v_mfma_f32_16x16x32_bf16 v[14:17], v[152:155], v[198:201], v[14:17]
	v_mfma_f32_16x16x32_bf16 v[70:73], v[110:113], v[206:209], v[70:73]
	v_mfma_f32_16x16x32_bf16 v[6:9], v[152:155], v[206:209], v[6:9]
	s_setprio 0
	s_setprio 1
	v_mfma_f32_16x16x32_bf16 v[90:93], v[156:159], v[178:181], 0
	v_mfma_f32_16x16x32_bf16 v[26:29], v[170:173], v[178:181], 0
	v_mfma_f32_16x16x32_bf16 v[82:85], v[156:159], v[186:189], 0
	v_mfma_f32_16x16x32_bf16 v[18:21], v[170:173], v[186:189], 0
	v_mfma_f32_16x16x32_bf16 v[74:77], v[156:159], v[194:197], 0
	v_mfma_f32_16x16x32_bf16 v[10:13], v[170:173], v[194:197], 0
	v_mfma_f32_16x16x32_bf16 v[66:69], v[156:159], v[202:205], 0
	v_mfma_f32_16x16x32_bf16 v[2:5], v[170:173], v[202:205], 0
	v_mfma_f32_16x16x32_bf16 v[90:93], v[160:163], v[182:185], v[90:93]
	v_mfma_f32_16x16x32_bf16 v[26:29], v[174:177], v[182:185], v[26:29]
	v_mfma_f32_16x16x32_bf16 v[82:85], v[160:163], v[190:193], v[82:85]
	v_mfma_f32_16x16x32_bf16 v[18:21], v[174:177], v[190:193], v[18:21]
	v_mfma_f32_16x16x32_bf16 v[74:77], v[160:163], v[198:201], v[74:77]
	v_mfma_f32_16x16x32_bf16 v[10:13], v[174:177], v[198:201], v[10:13]
	v_mfma_f32_16x16x32_bf16 v[66:69], v[160:163], v[206:209], v[66:69]
	v_mfma_f32_16x16x32_bf16 v[2:5], v[174:177], v[206:209], v[2:5]
	s_setprio 0
	s_barrier
	s_add_i32 s74, 0, 0x18000
	s_add_i32 s75, 0, 0x1c000
	v_add_u32_e32 v152, s74, v220
	v_add_u32_e32 v174, s75, v220
	ds_read_b128 v[106:109], v152
	ds_read_b128 v[110:113], v152 offset:1024
	ds_read_b128 v[114:117], v152 offset:2048
	ds_read_b128 v[152:155], v152 offset:3072
	ds_read_b128 v[156:159], v174
	ds_read_b128 v[160:163], v174 offset:1024
	ds_read_b128 v[170:173], v174 offset:2048
	ds_read_b128 v[174:177], v174 offset:3072
	s_add_u32 s70, s70, 0x40000
	s_addc_u32 s71, s71, 0
	s_mov_b32 m0, s16
	v_lshl_add_u64 v[216:217], s[70:71], 0, v[144:145]
	ds_read_b128 v[178:181], v222 offset:32768
	ds_read_b128 v[182:185], v222 offset:33792
	ds_read_b128 v[186:189], v222 offset:34816
	ds_read_b128 v[190:193], v222 offset:35840
	ds_read_b128 v[194:197], v222 offset:36864
	ds_read_b128 v[198:201], v222 offset:37888
	ds_read_b128 v[202:205], v222 offset:38912
	ds_read_b128 v[206:209], v222 offset:39936
	global_load_lds_dwordx4 v[216:217], off
	v_lshl_add_u64 v[216:217], s[70:71], 0, v[146:147]
	s_mov_b32 m0, s20
	s_nop 0
	global_load_lds_dwordx4 v[216:217], off
	s_waitcnt vmcnt(8)
	s_waitcnt lgkmcnt(0)
	s_barrier
	s_setprio 1
	v_mfma_f32_16x16x32_bf16 v[138:141], v[106:109], v[178:181], v[138:141]
	v_mfma_f32_16x16x32_bf16 v[62:65], v[114:117], v[178:181], v[62:65]
	v_mfma_f32_16x16x32_bf16 v[130:133], v[106:109], v[186:189], v[130:133]
	v_mfma_f32_16x16x32_bf16 v[54:57], v[114:117], v[186:189], v[54:57]
	v_mfma_f32_16x16x32_bf16 v[122:125], v[106:109], v[194:197], v[122:125]
	v_mfma_f32_16x16x32_bf16 v[46:49], v[114:117], v[194:197], v[46:49]
	v_mfma_f32_16x16x32_bf16 v[102:105], v[106:109], v[202:205], v[102:105]
	v_mfma_f32_16x16x32_bf16 v[38:41], v[114:117], v[202:205], v[38:41]
	v_mfma_f32_16x16x32_bf16 v[138:141], v[110:113], v[182:185], v[138:141]
	v_mfma_f32_16x16x32_bf16 v[62:65], v[152:155], v[182:185], v[62:65]
	v_mfma_f32_16x16x32_bf16 v[130:133], v[110:113], v[190:193], v[130:133]
	v_mfma_f32_16x16x32_bf16 v[54:57], v[152:155], v[190:193], v[54:57]
	v_mfma_f32_16x16x32_bf16 v[122:125], v[110:113], v[198:201], v[122:125]
	v_mfma_f32_16x16x32_bf16 v[46:49], v[152:155], v[198:201], v[46:49]
	v_mfma_f32_16x16x32_bf16 v[102:105], v[110:113], v[206:209], v[102:105]
	v_mfma_f32_16x16x32_bf16 v[38:41], v[152:155], v[206:209], v[38:41]
	s_setprio 0
	s_setprio 1
	v_mfma_f32_16x16x32_bf16 v[134:137], v[156:159], v[178:181], v[134:137]
	v_mfma_f32_16x16x32_bf16 v[58:61], v[170:173], v[178:181], v[58:61]
	v_mfma_f32_16x16x32_bf16 v[126:129], v[156:159], v[186:189], v[126:129]
	v_mfma_f32_16x16x32_bf16 v[50:53], v[170:173], v[186:189], v[50:53]
	v_mfma_f32_16x16x32_bf16 v[118:121], v[156:159], v[194:197], v[118:121]
	v_mfma_f32_16x16x32_bf16 v[42:45], v[170:173], v[194:197], v[42:45]
	v_mfma_f32_16x16x32_bf16 v[98:101], v[156:159], v[202:205], v[98:101]
	v_mfma_f32_16x16x32_bf16 v[34:37], v[170:173], v[202:205], v[34:37]
	v_mfma_f32_16x16x32_bf16 v[134:137], v[160:163], v[182:185], v[134:137]
	v_mfma_f32_16x16x32_bf16 v[58:61], v[174:177], v[182:185], v[58:61]
	v_mfma_f32_16x16x32_bf16 v[126:129], v[160:163], v[190:193], v[126:129]
	v_mfma_f32_16x16x32_bf16 v[50:53], v[174:177], v[190:193], v[50:53]
	v_mfma_f32_16x16x32_bf16 v[118:121], v[160:163], v[198:201], v[118:121]
	v_mfma_f32_16x16x32_bf16 v[42:45], v[174:177], v[198:201], v[42:45]
	v_mfma_f32_16x16x32_bf16 v[98:101], v[160:163], v[206:209], v[98:101]
	v_mfma_f32_16x16x32_bf16 v[34:37], v[174:177], v[206:209], v[34:37]
	s_setprio 0
	s_barrier
	s_add_i32 s70, s74, s13
	v_lshl_add_u64 v[164:165], v[164:165], 0, s[56:57]
	s_mov_b32 m0, s70
	ds_read_b128 v[178:181], v222 offset:49152
	ds_read_b128 v[182:185], v222 offset:50176
	ds_read_b128 v[186:189], v222 offset:51200
	ds_read_b128 v[190:193], v222 offset:52224
	ds_read_b128 v[194:197], v222 offset:53248
	ds_read_b128 v[198:201], v222 offset:54272
	ds_read_b128 v[202:205], v222 offset:55296
	ds_read_b128 v[206:209], v222 offset:56320
	global_load_lds_dwordx4 v[164:165], off
	s_add_i32 m0, s70, 0x2000
	s_add_u32 s68, s68, 0x8080
	v_lshl_add_u64 v[164:165], v[210:211], 0, s[56:57]
	s_addc_u32 s69, s69, 0
	s_add_i32 s70, s75, s13
	global_load_lds_dwordx4 v[164:165], off
	v_lshl_add_u64 v[164:165], s[68:69], 0, v[166:167]
	s_mov_b32 m0, s70
	s_nop 0
	global_load_lds_dwordx4 v[164:165], off
	v_lshl_add_u64 v[164:165], s[68:69], 0, v[142:143]
	s_add_i32 m0, s70, 0x2000
	s_nop 0
	global_load_lds_dwordx4 v[164:165], off
	v_lshl_add_u64 v[164:165], v[212:213], 0, s[56:57]
	s_mov_b32 m0, s21
	s_nop 0
	global_load_lds_dwordx4 v[164:165], off
	v_lshl_add_u64 v[164:165], v[214:215], 0, s[56:57]
	s_mov_b32 m0, s22
	s_nop 0
	global_load_lds_dwordx4 v[164:165], off
	s_waitcnt vmcnt(8)
	s_waitcnt lgkmcnt(0)
	s_barrier
	s_setprio 1
	v_mfma_f32_16x16x32_bf16 v[94:97], v[106:109], v[178:181], v[94:97]
	v_mfma_f32_16x16x32_bf16 v[30:33], v[114:117], v[178:181], v[30:33]
	v_mfma_f32_16x16x32_bf16 v[86:89], v[106:109], v[186:189], v[86:89]
	v_mfma_f32_16x16x32_bf16 v[22:25], v[114:117], v[186:189], v[22:25]
	v_mfma_f32_16x16x32_bf16 v[78:81], v[106:109], v[194:197], v[78:81]
	v_mfma_f32_16x16x32_bf16 v[14:17], v[114:117], v[194:197], v[14:17]
	v_mfma_f32_16x16x32_bf16 v[70:73], v[106:109], v[202:205], v[70:73]
	v_mfma_f32_16x16x32_bf16 v[6:9], v[114:117], v[202:205], v[6:9]
	v_mfma_f32_16x16x32_bf16 v[94:97], v[110:113], v[182:185], v[94:97]
	v_mfma_f32_16x16x32_bf16 v[30:33], v[152:155], v[182:185], v[30:33]
	v_mfma_f32_16x16x32_bf16 v[86:89], v[110:113], v[190:193], v[86:89]
	v_mfma_f32_16x16x32_bf16 v[22:25], v[152:155], v[190:193], v[22:25]
	v_mfma_f32_16x16x32_bf16 v[78:81], v[110:113], v[198:201], v[78:81]
	v_mfma_f32_16x16x32_bf16 v[14:17], v[152:155], v[198:201], v[14:17]
	v_mfma_f32_16x16x32_bf16 v[70:73], v[110:113], v[206:209], v[70:73]
	v_mfma_f32_16x16x32_bf16 v[6:9], v[152:155], v[206:209], v[6:9]
	s_setprio 0
	s_setprio 1
	v_mfma_f32_16x16x32_bf16 v[90:93], v[156:159], v[178:181], v[90:93]
	v_mfma_f32_16x16x32_bf16 v[26:29], v[170:173], v[178:181], v[26:29]
	v_mfma_f32_16x16x32_bf16 v[82:85], v[156:159], v[186:189], v[82:85]
	v_mfma_f32_16x16x32_bf16 v[18:21], v[170:173], v[186:189], v[18:21]
	v_mfma_f32_16x16x32_bf16 v[74:77], v[156:159], v[194:197], v[74:77]
	v_mfma_f32_16x16x32_bf16 v[10:13], v[170:173], v[194:197], v[10:13]
	v_mfma_f32_16x16x32_bf16 v[66:69], v[156:159], v[202:205], v[66:69]
	v_mfma_f32_16x16x32_bf16 v[2:5], v[170:173], v[202:205], v[2:5]
	v_mfma_f32_16x16x32_bf16 v[90:93], v[160:163], v[182:185], v[90:93]
	v_mfma_f32_16x16x32_bf16 v[26:29], v[174:177], v[182:185], v[26:29]
	v_mfma_f32_16x16x32_bf16 v[82:85], v[160:163], v[190:193], v[82:85]
	v_mfma_f32_16x16x32_bf16 v[18:21], v[174:177], v[190:193], v[18:21]
	v_mfma_f32_16x16x32_bf16 v[74:77], v[160:163], v[198:201], v[74:77]
	v_mfma_f32_16x16x32_bf16 v[10:13], v[174:177], v[198:201], v[10:13]
	v_mfma_f32_16x16x32_bf16 v[66:69], v[160:163], v[206:209], v[66:69]
	v_mfma_f32_16x16x32_bf16 v[2:5], v[174:177], v[206:209], v[2:5]
	s_setprio 0
	s_barrier
	s_add_u32 s66, s66, 0x100
	s_addc_u32 s72, s72, 0
	s_add_u32 s64, s64, 0x100
	s_addc_u32 s65, s65, 0
	s_cmp_ge_i32 s73, s1
	s_mov_b32 s68, s73
	s_cbranch_scc0 .LBB0_469
	s_branch .Lpeelexitph3
.LBB0_469:
	s_add_i32 s73, s68, 2
	s_add_u32 s69, s64, 0xfffc0080
	s_addc_u32 s70, s65, -1
	s_add_i32 s74, 0, 0x10000
	s_cmp_eq_u32 s24, s68
	s_cselect_b32 s71, s59, s70
	s_cselect_b32 s70, s58, s69
	s_cselect_b32 s69, s51, s72
	s_cselect_b32 s68, s53, s66
	s_add_i32 s76, 0, 0x14000
	v_add_u32_e32 v152, s74, v220
	v_add_u32_e32 v164, s76, v220
	ds_read_b128 v[106:109], v152
	ds_read_b128 v[110:113], v152 offset:1024
	ds_read_b128 v[114:117], v152 offset:2048
	ds_read_b128 v[152:155], v152 offset:3072
	ds_read_b128 v[156:159], v164
	ds_read_b128 v[160:163], v164 offset:1024
	ds_read_b128 v[170:173], v164 offset:2048
	ds_read_b128 v[174:177], v164 offset:3072
	v_lshl_add_u64 v[164:165], s[64:65], 0, v[150:151]
	s_add_i32 m0, s14, 0xc000
	ds_read_b128 v[178:181], v222
	ds_read_b128 v[182:185], v222 offset:1024
	ds_read_b128 v[186:189], v222 offset:2048
	ds_read_b128 v[190:193], v222 offset:3072
	ds_read_b128 v[194:197], v222 offset:4096
	ds_read_b128 v[198:201], v222 offset:5120
	ds_read_b128 v[202:205], v222 offset:6144
	ds_read_b128 v[206:209], v222 offset:7168
	global_load_lds_dwordx4 v[164:165], off
	v_lshl_add_u64 v[164:165], s[64:65], 0, v[148:149]
	s_add_i32 m0, s14, 0xe000
	s_nop 0
	global_load_lds_dwordx4 v[164:165], off
	s_waitcnt vmcnt(8)
	s_waitcnt lgkmcnt(0)
	s_barrier
	s_setprio 1
	v_mfma_f32_16x16x32_bf16 v[138:141], v[106:109], v[178:181], v[138:141]
	v_mfma_f32_16x16x32_bf16 v[62:65], v[114:117], v[178:181], v[62:65]
	v_mfma_f32_16x16x32_bf16 v[130:133], v[106:109], v[186:189], v[130:133]
	v_mfma_f32_16x16x32_bf16 v[54:57], v[114:117], v[186:189], v[54:57]
	v_mfma_f32_16x16x32_bf16 v[122:125], v[106:109], v[194:197], v[122:125]
	v_mfma_f32_16x16x32_bf16 v[46:49], v[114:117], v[194:197], v[46:49]
	v_mfma_f32_16x16x32_bf16 v[102:105], v[106:109], v[202:205], v[102:105]
	v_mfma_f32_16x16x32_bf16 v[38:41], v[114:117], v[202:205], v[38:41]
	v_mfma_f32_16x16x32_bf16 v[138:141], v[110:113], v[182:185], v[138:141]
	v_mfma_f32_16x16x32_bf16 v[62:65], v[152:155], v[182:185], v[62:65]
	v_mfma_f32_16x16x32_bf16 v[130:133], v[110:113], v[190:193], v[130:133]
	v_mfma_f32_16x16x32_bf16 v[54:57], v[152:155], v[190:193], v[54:57]
	v_mfma_f32_16x16x32_bf16 v[122:125], v[110:113], v[198:201], v[122:125]
	v_mfma_f32_16x16x32_bf16 v[46:49], v[152:155], v[198:201], v[46:49]
	v_mfma_f32_16x16x32_bf16 v[102:105], v[110:113], v[206:209], v[102:105]
	v_mfma_f32_16x16x32_bf16 v[38:41], v[152:155], v[206:209], v[38:41]
	s_setprio 0
	s_setprio 1
	v_mfma_f32_16x16x32_bf16 v[134:137], v[156:159], v[178:181], v[134:137]
	v_mfma_f32_16x16x32_bf16 v[58:61], v[170:173], v[178:181], v[58:61]
	v_mfma_f32_16x16x32_bf16 v[126:129], v[156:159], v[186:189], v[126:129]
	v_mfma_f32_16x16x32_bf16 v[50:53], v[170:173], v[186:189], v[50:53]
	v_mfma_f32_16x16x32_bf16 v[118:121], v[156:159], v[194:197], v[118:121]
	v_mfma_f32_16x16x32_bf16 v[42:45], v[170:173], v[194:197], v[42:45]
	v_mfma_f32_16x16x32_bf16 v[98:101], v[156:159], v[202:205], v[98:101]
	v_mfma_f32_16x16x32_bf16 v[34:37], v[170:173], v[202:205], v[34:37]
	v_mfma_f32_16x16x32_bf16 v[134:137], v[160:163], v[182:185], v[134:137]
	v_mfma_f32_16x16x32_bf16 v[58:61], v[174:177], v[182:185], v[58:61]
	v_mfma_f32_16x16x32_bf16 v[126:129], v[160:163], v[190:193], v[126:129]
	v_mfma_f32_16x16x32_bf16 v[50:53], v[174:177], v[190:193], v[50:53]
	v_mfma_f32_16x16x32_bf16 v[118:121], v[160:163], v[198:201], v[118:121]
	v_mfma_f32_16x16x32_bf16 v[42:45], v[174:177], v[198:201], v[42:45]
	v_mfma_f32_16x16x32_bf16 v[98:101], v[160:163], v[206:209], v[98:101]
	v_mfma_f32_16x16x32_bf16 v[34:37], v[174:177], v[206:209], v[34:37]
	s_setprio 0
	s_barrier
	s_add_i32 s74, s74, s13
	v_lshl_add_u64 v[164:165], s[68:69], 0, v[166:167]
	s_mov_b32 m0, s74
	ds_read_b128 v[178:181], v222 offset:16384
	ds_read_b128 v[182:185], v222 offset:17408
	ds_read_b128 v[186:189], v222 offset:18432
	ds_read_b128 v[190:193], v222 offset:19456
	ds_read_b128 v[194:197], v222 offset:20480
	ds_read_b128 v[198:201], v222 offset:21504
	ds_read_b128 v[202:205], v222 offset:22528
	ds_read_b128 v[206:209], v222 offset:23552
	global_load_lds_dwordx4 v[164:165], off
	s_add_i32 m0, s74, 0x2000
	s_add_u32 s74, s68, 0x8000
	v_lshl_add_u64 v[210:211], s[68:69], 0, v[142:143]
	s_addc_u32 s75, s69, 0
	s_add_i32 s76, s76, s13
	global_load_lds_dwordx4 v[210:211], off
	v_lshl_add_u64 v[212:213], s[74:75], 0, v[166:167]
	s_mov_b32 m0, s76
	v_lshl_add_u64 v[214:215], s[70:71], 0, v[146:147]
	global_load_lds_dwordx4 v[212:213], off
	v_lshl_add_u64 v[212:213], s[74:75], 0, v[142:143]
	s_add_i32 m0, s76, 0x2000
	s_nop 0
	global_load_lds_dwordx4 v[212:213], off
	v_lshl_add_u64 v[212:213], s[70:71], 0, v[144:145]
	s_mov_b32 m0, s14
	s_nop 0
	global_load_lds_dwordx4 v[212:213], off
	s_mov_b32 m0, s15
	s_nop 0
	global_load_lds_dwordx4 v[214:215], off
	s_waitcnt vmcnt(8)
	s_waitcnt lgkmcnt(0)
	s_barrier
	s_setprio 1
	v_mfma_f32_16x16x32_bf16 v[94:97], v[106:109], v[178:181], v[94:97]
	v_mfma_f32_16x16x32_bf16 v[30:33], v[114:117], v[178:181], v[30:33]
	v_mfma_f32_16x16x32_bf16 v[86:89], v[106:109], v[186:189], v[86:89]
	v_mfma_f32_16x16x32_bf16 v[22:25], v[114:117], v[186:189], v[22:25]
	v_mfma_f32_16x16x32_bf16 v[78:81], v[106:109], v[194:197], v[78:81]
	v_mfma_f32_16x16x32_bf16 v[14:17], v[114:117], v[194:197], v[14:17]
	v_mfma_f32_16x16x32_bf16 v[70:73], v[106:109], v[202:205], v[70:73]
	v_mfma_f32_16x16x32_bf16 v[6:9], v[114:117], v[202:205], v[6:9]
	v_mfma_f32_16x16x32_bf16 v[94:97], v[110:113], v[182:185], v[94:97]
	v_mfma_f32_16x16x32_bf16 v[30:33], v[152:155], v[182:185], v[30:33]
	v_mfma_f32_16x16x32_bf16 v[86:89], v[110:113], v[190:193], v[86:89]
	v_mfma_f32_16x16x32_bf16 v[22:25], v[152:155], v[190:193], v[22:25]
	v_mfma_f32_16x16x32_bf16 v[78:81], v[110:113], v[198:201], v[78:81]
	v_mfma_f32_16x16x32_bf16 v[14:17], v[152:155], v[198:201], v[14:17]
	v_mfma_f32_16x16x32_bf16 v[70:73], v[110:113], v[206:209], v[70:73]
	v_mfma_f32_16x16x32_bf16 v[6:9], v[152:155], v[206:209], v[6:9]
	s_setprio 0
	s_setprio 1
	v_mfma_f32_16x16x32_bf16 v[90:93], v[156:159], v[178:181], v[90:93]
	v_mfma_f32_16x16x32_bf16 v[26:29], v[170:173], v[178:181], v[26:29]
	v_mfma_f32_16x16x32_bf16 v[82:85], v[156:159], v[186:189], v[82:85]
	v_mfma_f32_16x16x32_bf16 v[18:21], v[170:173], v[186:189], v[18:21]
	v_mfma_f32_16x16x32_bf16 v[74:77], v[156:159], v[194:197], v[74:77]
	v_mfma_f32_16x16x32_bf16 v[10:13], v[170:173], v[194:197], v[10:13]
	v_mfma_f32_16x16x32_bf16 v[66:69], v[156:159], v[202:205], v[66:69]
	v_mfma_f32_16x16x32_bf16 v[2:5], v[170:173], v[202:205], v[2:5]
	v_mfma_f32_16x16x32_bf16 v[90:93], v[160:163], v[182:185], v[90:93]
	v_mfma_f32_16x16x32_bf16 v[26:29], v[174:177], v[182:185], v[26:29]
	v_mfma_f32_16x16x32_bf16 v[82:85], v[160:163], v[190:193], v[82:85]
	v_mfma_f32_16x16x32_bf16 v[18:21], v[174:177], v[190:193], v[18:21]
	v_mfma_f32_16x16x32_bf16 v[74:77], v[160:163], v[198:201], v[74:77]
	v_mfma_f32_16x16x32_bf16 v[10:13], v[174:177], v[198:201], v[10:13]
	v_mfma_f32_16x16x32_bf16 v[66:69], v[160:163], v[206:209], v[66:69]
	v_mfma_f32_16x16x32_bf16 v[2:5], v[174:177], v[206:209], v[2:5]
	s_setprio 0
	s_barrier
	s_add_i32 s74, 0, 0x18000
	s_add_i32 s75, 0, 0x1c000
	v_add_u32_e32 v152, s74, v220
	v_add_u32_e32 v174, s75, v220
	ds_read_b128 v[106:109], v152
	ds_read_b128 v[110:113], v152 offset:1024
	ds_read_b128 v[114:117], v152 offset:2048
	ds_read_b128 v[152:155], v152 offset:3072
	ds_read_b128 v[156:159], v174
	ds_read_b128 v[160:163], v174 offset:1024
	ds_read_b128 v[170:173], v174 offset:2048
	ds_read_b128 v[174:177], v174 offset:3072
	s_add_u32 s70, s70, 0x40000
	s_addc_u32 s71, s71, 0
	s_mov_b32 m0, s16
	v_lshl_add_u64 v[216:217], s[70:71], 0, v[144:145]
	ds_read_b128 v[178:181], v222 offset:32768
	ds_read_b128 v[182:185], v222 offset:33792
	ds_read_b128 v[186:189], v222 offset:34816
	ds_read_b128 v[190:193], v222 offset:35840
	ds_read_b128 v[194:197], v222 offset:36864
	ds_read_b128 v[198:201], v222 offset:37888
	ds_read_b128 v[202:205], v222 offset:38912
	ds_read_b128 v[206:209], v222 offset:39936
	global_load_lds_dwordx4 v[216:217], off
	v_lshl_add_u64 v[216:217], s[70:71], 0, v[146:147]
	s_mov_b32 m0, s20
	s_nop 0
	global_load_lds_dwordx4 v[216:217], off
	s_waitcnt vmcnt(8)
	s_waitcnt lgkmcnt(0)
	s_barrier
	s_setprio 1
	v_mfma_f32_16x16x32_bf16 v[138:141], v[106:109], v[178:181], v[138:141]
	v_mfma_f32_16x16x32_bf16 v[62:65], v[114:117], v[178:181], v[62:65]
	v_mfma_f32_16x16x32_bf16 v[130:133], v[106:109], v[186:189], v[130:133]
	v_mfma_f32_16x16x32_bf16 v[54:57], v[114:117], v[186:189], v[54:57]
	v_mfma_f32_16x16x32_bf16 v[122:125], v[106:109], v[194:197], v[122:125]
	v_mfma_f32_16x16x32_bf16 v[46:49], v[114:117], v[194:197], v[46:49]
	v_mfma_f32_16x16x32_bf16 v[102:105], v[106:109], v[202:205], v[102:105]
	v_mfma_f32_16x16x32_bf16 v[38:41], v[114:117], v[202:205], v[38:41]
	v_mfma_f32_16x16x32_bf16 v[138:141], v[110:113], v[182:185], v[138:141]
	v_mfma_f32_16x16x32_bf16 v[62:65], v[152:155], v[182:185], v[62:65]
	v_mfma_f32_16x16x32_bf16 v[130:133], v[110:113], v[190:193], v[130:133]
	v_mfma_f32_16x16x32_bf16 v[54:57], v[152:155], v[190:193], v[54:57]
	v_mfma_f32_16x16x32_bf16 v[122:125], v[110:113], v[198:201], v[122:125]
	v_mfma_f32_16x16x32_bf16 v[46:49], v[152:155], v[198:201], v[46:49]
	v_mfma_f32_16x16x32_bf16 v[102:105], v[110:113], v[206:209], v[102:105]
	v_mfma_f32_16x16x32_bf16 v[38:41], v[152:155], v[206:209], v[38:41]
	s_setprio 0
	s_setprio 1
	v_mfma_f32_16x16x32_bf16 v[134:137], v[156:159], v[178:181], v[134:137]
	v_mfma_f32_16x16x32_bf16 v[58:61], v[170:173], v[178:181], v[58:61]
	v_mfma_f32_16x16x32_bf16 v[126:129], v[156:159], v[186:189], v[126:129]
	v_mfma_f32_16x16x32_bf16 v[50:53], v[170:173], v[186:189], v[50:53]
	v_mfma_f32_16x16x32_bf16 v[118:121], v[156:159], v[194:197], v[118:121]
	v_mfma_f32_16x16x32_bf16 v[42:45], v[170:173], v[194:197], v[42:45]
	v_mfma_f32_16x16x32_bf16 v[98:101], v[156:159], v[202:205], v[98:101]
	v_mfma_f32_16x16x32_bf16 v[34:37], v[170:173], v[202:205], v[34:37]
	v_mfma_f32_16x16x32_bf16 v[134:137], v[160:163], v[182:185], v[134:137]
	v_mfma_f32_16x16x32_bf16 v[58:61], v[174:177], v[182:185], v[58:61]
	v_mfma_f32_16x16x32_bf16 v[126:129], v[160:163], v[190:193], v[126:129]
	v_mfma_f32_16x16x32_bf16 v[50:53], v[174:177], v[190:193], v[50:53]
	v_mfma_f32_16x16x32_bf16 v[118:121], v[160:163], v[198:201], v[118:121]
	v_mfma_f32_16x16x32_bf16 v[42:45], v[174:177], v[198:201], v[42:45]
	v_mfma_f32_16x16x32_bf16 v[98:101], v[160:163], v[206:209], v[98:101]
	v_mfma_f32_16x16x32_bf16 v[34:37], v[174:177], v[206:209], v[34:37]
	s_setprio 0
	s_barrier
	s_add_i32 s70, s74, s13
	v_lshl_add_u64 v[164:165], v[164:165], 0, s[56:57]
	s_mov_b32 m0, s70
	ds_read_b128 v[178:181], v222 offset:49152
	ds_read_b128 v[182:185], v222 offset:50176
	ds_read_b128 v[186:189], v222 offset:51200
	ds_read_b128 v[190:193], v222 offset:52224
	ds_read_b128 v[194:197], v222 offset:53248
	ds_read_b128 v[198:201], v222 offset:54272
	ds_read_b128 v[202:205], v222 offset:55296
	ds_read_b128 v[206:209], v222 offset:56320
	global_load_lds_dwordx4 v[164:165], off
	s_add_i32 m0, s70, 0x2000
	s_add_u32 s68, s68, 0x8080
	v_lshl_add_u64 v[164:165], v[210:211], 0, s[56:57]
	s_addc_u32 s69, s69, 0
	s_add_i32 s70, s75, s13
	global_load_lds_dwordx4 v[164:165], off
	v_lshl_add_u64 v[164:165], s[68:69], 0, v[166:167]
	s_mov_b32 m0, s70
	s_nop 0
	global_load_lds_dwordx4 v[164:165], off
	v_lshl_add_u64 v[164:165], s[68:69], 0, v[142:143]
	s_add_i32 m0, s70, 0x2000
	s_nop 0
	global_load_lds_dwordx4 v[164:165], off
	v_lshl_add_u64 v[164:165], v[212:213], 0, s[56:57]
	s_mov_b32 m0, s21
	s_nop 0
	global_load_lds_dwordx4 v[164:165], off
	v_lshl_add_u64 v[164:165], v[214:215], 0, s[56:57]
	s_mov_b32 m0, s22
	s_nop 0
	global_load_lds_dwordx4 v[164:165], off
	s_waitcnt vmcnt(8)
	s_waitcnt lgkmcnt(0)
	s_barrier
	s_setprio 1
	v_mfma_f32_16x16x32_bf16 v[94:97], v[106:109], v[178:181], v[94:97]
	v_mfma_f32_16x16x32_bf16 v[30:33], v[114:117], v[178:181], v[30:33]
	v_mfma_f32_16x16x32_bf16 v[86:89], v[106:109], v[186:189], v[86:89]
	v_mfma_f32_16x16x32_bf16 v[22:25], v[114:117], v[186:189], v[22:25]
	v_mfma_f32_16x16x32_bf16 v[78:81], v[106:109], v[194:197], v[78:81]
	v_mfma_f32_16x16x32_bf16 v[14:17], v[114:117], v[194:197], v[14:17]
	v_mfma_f32_16x16x32_bf16 v[70:73], v[106:109], v[202:205], v[70:73]
	v_mfma_f32_16x16x32_bf16 v[6:9], v[114:117], v[202:205], v[6:9]
	v_mfma_f32_16x16x32_bf16 v[94:97], v[110:113], v[182:185], v[94:97]
	v_mfma_f32_16x16x32_bf16 v[30:33], v[152:155], v[182:185], v[30:33]
	v_mfma_f32_16x16x32_bf16 v[86:89], v[110:113], v[190:193], v[86:89]
	v_mfma_f32_16x16x32_bf16 v[22:25], v[152:155], v[190:193], v[22:25]
	v_mfma_f32_16x16x32_bf16 v[78:81], v[110:113], v[198:201], v[78:81]
	v_mfma_f32_16x16x32_bf16 v[14:17], v[152:155], v[198:201], v[14:17]
	v_mfma_f32_16x16x32_bf16 v[70:73], v[110:113], v[206:209], v[70:73]
	v_mfma_f32_16x16x32_bf16 v[6:9], v[152:155], v[206:209], v[6:9]
	s_setprio 0
	s_setprio 1
	v_mfma_f32_16x16x32_bf16 v[90:93], v[156:159], v[178:181], v[90:93]
	v_mfma_f32_16x16x32_bf16 v[26:29], v[170:173], v[178:181], v[26:29]
	v_mfma_f32_16x16x32_bf16 v[82:85], v[156:159], v[186:189], v[82:85]
	v_mfma_f32_16x16x32_bf16 v[18:21], v[170:173], v[186:189], v[18:21]
	v_mfma_f32_16x16x32_bf16 v[74:77], v[156:159], v[194:197], v[74:77]
	v_mfma_f32_16x16x32_bf16 v[10:13], v[170:173], v[194:197], v[10:13]
	v_mfma_f32_16x16x32_bf16 v[66:69], v[156:159], v[202:205], v[66:69]
	v_mfma_f32_16x16x32_bf16 v[2:5], v[170:173], v[202:205], v[2:5]
	v_mfma_f32_16x16x32_bf16 v[90:93], v[160:163], v[182:185], v[90:93]
	v_mfma_f32_16x16x32_bf16 v[26:29], v[174:177], v[182:185], v[26:29]
	v_mfma_f32_16x16x32_bf16 v[82:85], v[160:163], v[190:193], v[82:85]
	v_mfma_f32_16x16x32_bf16 v[18:21], v[174:177], v[190:193], v[18:21]
	v_mfma_f32_16x16x32_bf16 v[74:77], v[160:163], v[198:201], v[74:77]
	v_mfma_f32_16x16x32_bf16 v[10:13], v[174:177], v[198:201], v[10:13]
	v_mfma_f32_16x16x32_bf16 v[66:69], v[160:163], v[206:209], v[66:69]
	v_mfma_f32_16x16x32_bf16 v[2:5], v[174:177], v[206:209], v[2:5]
	s_setprio 0
	s_barrier
	s_add_u32 s66, s66, 0x100
	s_addc_u32 s72, s72, 0
	s_add_u32 s64, s64, 0x100
	s_addc_u32 s65, s65, 0
	s_cmp_ge_i32 s73, s1
	s_mov_b32 s68, s73
	s_cbranch_scc0 .LBB0_469

.Lpeelph6_0:
	s_add_i32 s84, s68, 2
	s_add_u32 s69, s74, 0xfffc0080
	s_addc_u32 s70, s75, -1
	s_add_i32 s88, 0, 0x10000
	s_cmp_eq_u32 s72, s68
	s_cselect_b32 s71, s29, s70
	s_cselect_b32 s70, s43, s69
	s_cselect_b32 s69, s55, s79
	s_cselect_b32 s68, s59, s77
	s_add_i32 s92, 0, 0x14000
	v_add_u32_e32 v78, s88, v204
	v_add_u32_e32 v170, s92, v204
	ds_read_b128 v[58:61], v78
	ds_read_b128 v[62:65], v78 offset:1024
	ds_read_b128 v[74:77], v78 offset:2048
	ds_read_b128 v[78:81], v78 offset:3072
	ds_read_b128 v[146:149], v170
	ds_read_b128 v[150:153], v170 offset:1024
	ds_read_b128 v[154:157], v170 offset:2048
	ds_read_b128 v[170:173], v170 offset:3072
	v_lshl_add_u64 v[202:203], s[74:75], 0, v[180:181]
	s_add_i32 m0, s15, 0xc000
	ds_read_b128 v[174:177], v208
	ds_read_b128 v[182:185], v208 offset:1024
	ds_read_b128 v[186:189], v208 offset:2048
	ds_read_b128 v[190:193], v208 offset:3072
	ds_read_b128 v[194:197], v208 offset:4096
	ds_read_b128 v[198:201], v208 offset:5120
	ds_read_b128 v[210:213], v208 offset:6144
	ds_read_b128 v[214:217], v208 offset:7168
	global_load_lds_dwordx4 v[202:203], off
	v_lshl_add_u64 v[202:203], s[74:75], 0, v[178:179]
	s_add_i32 m0, s15, 0xe000
	s_nop 0
	global_load_lds_dwordx4 v[202:203], off
	s_waitcnt vmcnt(8)
	s_waitcnt lgkmcnt(0)
	s_barrier
	s_setprio 1
	v_mfma_f32_16x16x32_bf16 v[142:145], v[58:61], v[174:177], 0
	v_mfma_f32_16x16x32_bf16 v[138:141], v[74:77], v[174:177], 0
	v_mfma_f32_16x16x32_bf16 v[126:129], v[58:61], v[186:189], 0
	v_mfma_f32_16x16x32_bf16 v[122:125], v[74:77], v[186:189], 0
	v_mfma_f32_16x16x32_bf16 v[110:113], v[58:61], v[194:197], 0
	v_mfma_f32_16x16x32_bf16 v[106:109], v[74:77], v[194:197], 0
	v_mfma_f32_16x16x32_bf16 v[94:97], v[58:61], v[210:213], 0
	v_mfma_f32_16x16x32_bf16 v[90:93], v[74:77], v[210:213], 0
	v_mfma_f32_16x16x32_bf16 v[142:145], v[62:65], v[182:185], v[142:145]
	v_mfma_f32_16x16x32_bf16 v[138:141], v[78:81], v[182:185], v[138:141]
	v_mfma_f32_16x16x32_bf16 v[126:129], v[62:65], v[190:193], v[126:129]
	v_mfma_f32_16x16x32_bf16 v[122:125], v[78:81], v[190:193], v[122:125]
	v_mfma_f32_16x16x32_bf16 v[110:113], v[62:65], v[198:201], v[110:113]
	v_mfma_f32_16x16x32_bf16 v[106:109], v[78:81], v[198:201], v[106:109]
	v_mfma_f32_16x16x32_bf16 v[94:97], v[62:65], v[214:217], v[94:97]
	v_mfma_f32_16x16x32_bf16 v[90:93], v[78:81], v[214:217], v[90:93]
	s_setprio 0
	s_setprio 1
	v_mfma_f32_16x16x32_bf16 v[134:137], v[146:149], v[174:177], 0
	v_mfma_f32_16x16x32_bf16 v[130:133], v[154:157], v[174:177], 0
	v_mfma_f32_16x16x32_bf16 v[118:121], v[146:149], v[186:189], 0
	v_mfma_f32_16x16x32_bf16 v[114:117], v[154:157], v[186:189], 0
	v_mfma_f32_16x16x32_bf16 v[102:105], v[146:149], v[194:197], 0
	v_mfma_f32_16x16x32_bf16 v[98:101], v[154:157], v[194:197], 0
	v_mfma_f32_16x16x32_bf16 v[86:89], v[146:149], v[210:213], 0
	v_mfma_f32_16x16x32_bf16 v[82:85], v[154:157], v[210:213], 0
	v_mfma_f32_16x16x32_bf16 v[134:137], v[150:153], v[182:185], v[134:137]
	v_mfma_f32_16x16x32_bf16 v[130:133], v[170:173], v[182:185], v[130:133]
	v_mfma_f32_16x16x32_bf16 v[118:121], v[150:153], v[190:193], v[118:121]
	v_mfma_f32_16x16x32_bf16 v[114:117], v[170:173], v[190:193], v[114:117]
	v_mfma_f32_16x16x32_bf16 v[102:105], v[150:153], v[198:201], v[102:105]
	v_mfma_f32_16x16x32_bf16 v[98:101], v[170:173], v[198:201], v[98:101]
	v_mfma_f32_16x16x32_bf16 v[86:89], v[150:153], v[214:217], v[86:89]
	v_mfma_f32_16x16x32_bf16 v[82:85], v[170:173], v[214:217], v[82:85]
	s_setprio 0
	s_barrier
	s_add_i32 s88, s88, s14
	v_lshl_add_u64 v[202:203], s[68:69], 0, v[166:167]
	s_mov_b32 m0, s88
	ds_read_b128 v[174:177], v208 offset:16384
	ds_read_b128 v[182:185], v208 offset:17408
	ds_read_b128 v[186:189], v208 offset:18432
	ds_read_b128 v[190:193], v208 offset:19456
	ds_read_b128 v[194:197], v208 offset:20480
	ds_read_b128 v[198:201], v208 offset:21504
	ds_read_b128 v[210:213], v208 offset:22528
	ds_read_b128 v[214:217], v208 offset:23552
	global_load_lds_dwordx4 v[202:203], off
	s_add_i32 m0, s88, 0x2000
	s_add_u32 s90, s68, 0x40000
	v_lshl_add_u64 v[218:219], s[68:69], 0, v[158:159]
	s_addc_u32 s91, s69, 0
	s_add_i32 s88, s92, s14
	global_load_lds_dwordx4 v[218:219], off
	v_lshl_add_u64 v[220:221], s[90:91], 0, v[166:167]
	s_mov_b32 m0, s88
	v_lshl_add_u64 v[222:223], s[70:71], 0, v[162:163]
	global_load_lds_dwordx4 v[220:221], off
	v_lshl_add_u64 v[220:221], s[90:91], 0, v[158:159]
	s_add_i32 m0, s88, 0x2000
	s_nop 0
	global_load_lds_dwordx4 v[220:221], off
	v_lshl_add_u64 v[220:221], s[70:71], 0, v[160:161]
	s_mov_b32 m0, s15
	s_nop 0
	global_load_lds_dwordx4 v[220:221], off
	s_mov_b32 m0, s16
	s_nop 0
	global_load_lds_dwordx4 v[222:223], off
	s_waitcnt vmcnt(8)
	s_waitcnt lgkmcnt(0)
	s_barrier
	s_setprio 1
	v_mfma_f32_16x16x32_bf16 v[70:73], v[58:61], v[174:177], 0
	v_mfma_f32_16x16x32_bf16 v[66:69], v[74:77], v[174:177], 0
	v_mfma_f32_16x16x32_bf16 v[46:49], v[58:61], v[186:189], 0
	v_mfma_f32_16x16x32_bf16 v[42:45], v[74:77], v[186:189], 0
	v_mfma_f32_16x16x32_bf16 v[30:33], v[58:61], v[194:197], 0
	v_mfma_f32_16x16x32_bf16 v[26:29], v[74:77], v[194:197], 0
	v_mfma_f32_16x16x32_bf16 v[14:17], v[58:61], v[210:213], 0
	v_mfma_f32_16x16x32_bf16 v[10:13], v[74:77], v[210:213], 0
	v_mfma_f32_16x16x32_bf16 v[70:73], v[62:65], v[182:185], v[70:73]
	v_mfma_f32_16x16x32_bf16 v[66:69], v[78:81], v[182:185], v[66:69]
	v_mfma_f32_16x16x32_bf16 v[46:49], v[62:65], v[190:193], v[46:49]
	v_mfma_f32_16x16x32_bf16 v[42:45], v[78:81], v[190:193], v[42:45]
	v_mfma_f32_16x16x32_bf16 v[30:33], v[62:65], v[198:201], v[30:33]
	v_mfma_f32_16x16x32_bf16 v[26:29], v[78:81], v[198:201], v[26:29]
	v_mfma_f32_16x16x32_bf16 v[14:17], v[62:65], v[214:217], v[14:17]
	v_mfma_f32_16x16x32_bf16 v[10:13], v[78:81], v[214:217], v[10:13]
	s_setprio 0
	s_setprio 1
	v_mfma_f32_16x16x32_bf16 v[54:57], v[146:149], v[174:177], 0
	v_mfma_f32_16x16x32_bf16 v[50:53], v[154:157], v[174:177], 0
	v_mfma_f32_16x16x32_bf16 v[38:41], v[146:149], v[186:189], 0
	v_mfma_f32_16x16x32_bf16 v[34:37], v[154:157], v[186:189], 0
	v_mfma_f32_16x16x32_bf16 v[22:25], v[146:149], v[194:197], 0
	v_mfma_f32_16x16x32_bf16 v[18:21], v[154:157], v[194:197], 0
	v_mfma_f32_16x16x32_bf16 v[6:9], v[146:149], v[210:213], 0
	v_mfma_f32_16x16x32_bf16 v[2:5], v[154:157], v[210:213], 0
	v_mfma_f32_16x16x32_bf16 v[54:57], v[150:153], v[182:185], v[54:57]
	v_mfma_f32_16x16x32_bf16 v[50:53], v[170:173], v[182:185], v[50:53]
	v_mfma_f32_16x16x32_bf16 v[38:41], v[150:153], v[190:193], v[38:41]
	v_mfma_f32_16x16x32_bf16 v[34:37], v[170:173], v[190:193], v[34:37]
	v_mfma_f32_16x16x32_bf16 v[22:25], v[150:153], v[198:201], v[22:25]
	v_mfma_f32_16x16x32_bf16 v[18:21], v[170:173], v[198:201], v[18:21]
	v_mfma_f32_16x16x32_bf16 v[6:9], v[150:153], v[214:217], v[6:9]
	v_mfma_f32_16x16x32_bf16 v[2:5], v[170:173], v[214:217], v[2:5]
	s_setprio 0
	s_barrier
	s_add_i32 s88, 0, 0x18000
	s_add_i32 s90, 0, 0x1c000
	v_add_u32_e32 v78, s88, v204
	v_add_u32_e32 v170, s90, v204
	ds_read_b128 v[58:61], v78
	ds_read_b128 v[62:65], v78 offset:1024
	ds_read_b128 v[74:77], v78 offset:2048
	ds_read_b128 v[78:81], v78 offset:3072
	ds_read_b128 v[146:149], v170
	ds_read_b128 v[150:153], v170 offset:1024
	ds_read_b128 v[154:157], v170 offset:2048
	ds_read_b128 v[170:173], v170 offset:3072
	s_add_u32 s70, s70, 0x40000
	s_addc_u32 s71, s71, 0
	s_mov_b32 m0, s20
	v_lshl_add_u64 v[232:233], s[70:71], 0, v[160:161]
	ds_read_b128 v[174:177], v208 offset:32768
	ds_read_b128 v[182:185], v208 offset:33792
	ds_read_b128 v[186:189], v208 offset:34816
	ds_read_b128 v[190:193], v208 offset:35840
	ds_read_b128 v[194:197], v208 offset:36864
	ds_read_b128 v[198:201], v208 offset:37888
	ds_read_b128 v[210:213], v208 offset:38912
	ds_read_b128 v[214:217], v208 offset:39936
	global_load_lds_dwordx4 v[232:233], off
	v_lshl_add_u64 v[232:233], s[70:71], 0, v[162:163]
	s_mov_b32 m0, s21
	s_nop 0
	global_load_lds_dwordx4 v[232:233], off
	s_waitcnt vmcnt(8)
	s_waitcnt lgkmcnt(0)
	s_barrier
	s_setprio 1
	v_mfma_f32_16x16x32_bf16 v[142:145], v[58:61], v[174:177], v[142:145]
	v_mfma_f32_16x16x32_bf16 v[138:141], v[74:77], v[174:177], v[138:141]
	v_mfma_f32_16x16x32_bf16 v[126:129], v[58:61], v[186:189], v[126:129]
	v_mfma_f32_16x16x32_bf16 v[122:125], v[74:77], v[186:189], v[122:125]
	v_mfma_f32_16x16x32_bf16 v[110:113], v[58:61], v[194:197], v[110:113]
	v_mfma_f32_16x16x32_bf16 v[106:109], v[74:77], v[194:197], v[106:109]
	v_mfma_f32_16x16x32_bf16 v[94:97], v[58:61], v[210:213], v[94:97]
	v_mfma_f32_16x16x32_bf16 v[90:93], v[74:77], v[210:213], v[90:93]
	v_mfma_f32_16x16x32_bf16 v[142:145], v[62:65], v[182:185], v[142:145]
	v_mfma_f32_16x16x32_bf16 v[138:141], v[78:81], v[182:185], v[138:141]
	v_mfma_f32_16x16x32_bf16 v[126:129], v[62:65], v[190:193], v[126:129]
	v_mfma_f32_16x16x32_bf16 v[122:125], v[78:81], v[190:193], v[122:125]
	v_mfma_f32_16x16x32_bf16 v[110:113], v[62:65], v[198:201], v[110:113]
	v_mfma_f32_16x16x32_bf16 v[106:109], v[78:81], v[198:201], v[106:109]
	v_mfma_f32_16x16x32_bf16 v[94:97], v[62:65], v[214:217], v[94:97]
	v_mfma_f32_16x16x32_bf16 v[90:93], v[78:81], v[214:217], v[90:93]
	s_setprio 0
	s_setprio 1
	v_mfma_f32_16x16x32_bf16 v[134:137], v[146:149], v[174:177], v[134:137]
	v_mfma_f32_16x16x32_bf16 v[130:133], v[154:157], v[174:177], v[130:133]
	v_mfma_f32_16x16x32_bf16 v[118:121], v[146:149], v[186:189], v[118:121]
	v_mfma_f32_16x16x32_bf16 v[114:117], v[154:157], v[186:189], v[114:117]
	v_mfma_f32_16x16x32_bf16 v[102:105], v[146:149], v[194:197], v[102:105]
	v_mfma_f32_16x16x32_bf16 v[98:101], v[154:157], v[194:197], v[98:101]
	v_mfma_f32_16x16x32_bf16 v[86:89], v[146:149], v[210:213], v[86:89]
	v_mfma_f32_16x16x32_bf16 v[82:85], v[154:157], v[210:213], v[82:85]
	v_mfma_f32_16x16x32_bf16 v[134:137], v[150:153], v[182:185], v[134:137]
	v_mfma_f32_16x16x32_bf16 v[130:133], v[170:173], v[182:185], v[130:133]
	v_mfma_f32_16x16x32_bf16 v[118:121], v[150:153], v[190:193], v[118:121]
	v_mfma_f32_16x16x32_bf16 v[114:117], v[170:173], v[190:193], v[114:117]
	v_mfma_f32_16x16x32_bf16 v[102:105], v[150:153], v[198:201], v[102:105]
	v_mfma_f32_16x16x32_bf16 v[98:101], v[170:173], v[198:201], v[98:101]
	v_mfma_f32_16x16x32_bf16 v[86:89], v[150:153], v[214:217], v[86:89]
	v_mfma_f32_16x16x32_bf16 v[82:85], v[170:173], v[214:217], v[82:85]
	s_setprio 0
	s_barrier
	s_add_i32 s70, s88, s14
	v_lshl_add_u64 v[202:203], v[202:203], 0, s[56:57]
	s_mov_b32 m0, s70
	ds_read_b128 v[174:177], v208 offset:49152
	ds_read_b128 v[182:185], v208 offset:50176
	ds_read_b128 v[186:189], v208 offset:51200
	ds_read_b128 v[190:193], v208 offset:52224
	ds_read_b128 v[194:197], v208 offset:53248
	ds_read_b128 v[198:201], v208 offset:54272
	ds_read_b128 v[210:213], v208 offset:55296
	ds_read_b128 v[214:217], v208 offset:56320
	global_load_lds_dwordx4 v[202:203], off
	s_add_i32 m0, s70, 0x2000
	s_add_u32 s68, s68, 0x40080
	v_lshl_add_u64 v[202:203], v[218:219], 0, s[56:57]
	s_addc_u32 s69, s69, 0
	s_add_i32 s70, s90, s14
	global_load_lds_dwordx4 v[202:203], off
	v_lshl_add_u64 v[202:203], s[68:69], 0, v[166:167]
	s_mov_b32 m0, s70
	s_nop 0
	global_load_lds_dwordx4 v[202:203], off
	v_lshl_add_u64 v[202:203], s[68:69], 0, v[158:159]
	s_add_i32 m0, s70, 0x2000
	s_nop 0
	global_load_lds_dwordx4 v[202:203], off
	v_lshl_add_u64 v[202:203], v[220:221], 0, s[56:57]
	s_mov_b32 m0, s24
	s_nop 0
	global_load_lds_dwordx4 v[202:203], off
	v_lshl_add_u64 v[202:203], v[222:223], 0, s[56:57]
	s_mov_b32 m0, s25
	s_nop 0
	global_load_lds_dwordx4 v[202:203], off
	s_waitcnt vmcnt(8)
	s_waitcnt lgkmcnt(0)
	s_barrier
	s_setprio 1
	v_mfma_f32_16x16x32_bf16 v[70:73], v[58:61], v[174:177], v[70:73]
	v_mfma_f32_16x16x32_bf16 v[66:69], v[74:77], v[174:177], v[66:69]
	v_mfma_f32_16x16x32_bf16 v[46:49], v[58:61], v[186:189], v[46:49]
	v_mfma_f32_16x16x32_bf16 v[42:45], v[74:77], v[186:189], v[42:45]
	v_mfma_f32_16x16x32_bf16 v[30:33], v[58:61], v[194:197], v[30:33]
	v_mfma_f32_16x16x32_bf16 v[26:29], v[74:77], v[194:197], v[26:29]
	v_mfma_f32_16x16x32_bf16 v[14:17], v[58:61], v[210:213], v[14:17]
	v_mfma_f32_16x16x32_bf16 v[10:13], v[74:77], v[210:213], v[10:13]
	v_mfma_f32_16x16x32_bf16 v[70:73], v[62:65], v[182:185], v[70:73]
	v_mfma_f32_16x16x32_bf16 v[66:69], v[78:81], v[182:185], v[66:69]
	v_mfma_f32_16x16x32_bf16 v[46:49], v[62:65], v[190:193], v[46:49]
	v_mfma_f32_16x16x32_bf16 v[42:45], v[78:81], v[190:193], v[42:45]
	v_mfma_f32_16x16x32_bf16 v[30:33], v[62:65], v[198:201], v[30:33]
	v_mfma_f32_16x16x32_bf16 v[26:29], v[78:81], v[198:201], v[26:29]
	v_mfma_f32_16x16x32_bf16 v[14:17], v[62:65], v[214:217], v[14:17]
	v_mfma_f32_16x16x32_bf16 v[10:13], v[78:81], v[214:217], v[10:13]
	s_setprio 0
	s_setprio 1
	v_mfma_f32_16x16x32_bf16 v[54:57], v[146:149], v[174:177], v[54:57]
	v_mfma_f32_16x16x32_bf16 v[50:53], v[154:157], v[174:177], v[50:53]
	v_mfma_f32_16x16x32_bf16 v[38:41], v[146:149], v[186:189], v[38:41]
	v_mfma_f32_16x16x32_bf16 v[34:37], v[154:157], v[186:189], v[34:37]
	v_mfma_f32_16x16x32_bf16 v[22:25], v[146:149], v[194:197], v[22:25]
	v_mfma_f32_16x16x32_bf16 v[18:21], v[154:157], v[194:197], v[18:21]
	v_mfma_f32_16x16x32_bf16 v[6:9], v[146:149], v[210:213], v[6:9]
	v_mfma_f32_16x16x32_bf16 v[2:5], v[154:157], v[210:213], v[2:5]
	v_mfma_f32_16x16x32_bf16 v[54:57], v[150:153], v[182:185], v[54:57]
	v_mfma_f32_16x16x32_bf16 v[50:53], v[170:173], v[182:185], v[50:53]
	v_mfma_f32_16x16x32_bf16 v[38:41], v[150:153], v[190:193], v[38:41]
	v_mfma_f32_16x16x32_bf16 v[34:37], v[170:173], v[190:193], v[34:37]
	v_mfma_f32_16x16x32_bf16 v[22:25], v[150:153], v[198:201], v[22:25]
	v_mfma_f32_16x16x32_bf16 v[18:21], v[170:173], v[198:201], v[18:21]
	v_mfma_f32_16x16x32_bf16 v[6:9], v[150:153], v[214:217], v[6:9]
	v_mfma_f32_16x16x32_bf16 v[2:5], v[170:173], v[214:217], v[2:5]
	s_setprio 0
	s_barrier
	s_add_u32 s77, s77, 0x100
	s_addc_u32 s79, s79, 0
	s_add_u32 s74, s74, 0x100
	s_addc_u32 s75, s75, 0
	s_cmp_ge_i32 s84, s1
	s_mov_b32 s68, s84
	s_cbranch_scc0 .LBB0_664
	s_branch .Lpeelexitph6
.LBB0_664:
	s_add_i32 s84, s68, 2
	s_add_u32 s69, s74, 0xfffc0080
	s_addc_u32 s70, s75, -1
	s_add_i32 s88, 0, 0x10000
	s_cmp_eq_u32 s72, s68
	s_cselect_b32 s71, s29, s70
	s_cselect_b32 s70, s43, s69
	s_cselect_b32 s69, s55, s79
	s_cselect_b32 s68, s59, s77
	s_add_i32 s92, 0, 0x14000
	v_add_u32_e32 v78, s88, v204
	v_add_u32_e32 v170, s92, v204
	ds_read_b128 v[58:61], v78
	ds_read_b128 v[62:65], v78 offset:1024
	ds_read_b128 v[74:77], v78 offset:2048
	ds_read_b128 v[78:81], v78 offset:3072
	ds_read_b128 v[146:149], v170
	ds_read_b128 v[150:153], v170 offset:1024
	ds_read_b128 v[154:157], v170 offset:2048
	ds_read_b128 v[170:173], v170 offset:3072
	v_lshl_add_u64 v[202:203], s[74:75], 0, v[180:181]
	s_add_i32 m0, s15, 0xc000
	ds_read_b128 v[174:177], v208
	ds_read_b128 v[182:185], v208 offset:1024
	ds_read_b128 v[186:189], v208 offset:2048
	ds_read_b128 v[190:193], v208 offset:3072
	ds_read_b128 v[194:197], v208 offset:4096
	ds_read_b128 v[198:201], v208 offset:5120
	ds_read_b128 v[210:213], v208 offset:6144
	ds_read_b128 v[214:217], v208 offset:7168
	global_load_lds_dwordx4 v[202:203], off
	v_lshl_add_u64 v[202:203], s[74:75], 0, v[178:179]
	s_add_i32 m0, s15, 0xe000
	s_nop 0
	global_load_lds_dwordx4 v[202:203], off
	s_waitcnt vmcnt(8)
	s_waitcnt lgkmcnt(0)
	s_barrier
	s_setprio 1
	v_mfma_f32_16x16x32_bf16 v[142:145], v[58:61], v[174:177], v[142:145]
	v_mfma_f32_16x16x32_bf16 v[138:141], v[74:77], v[174:177], v[138:141]
	v_mfma_f32_16x16x32_bf16 v[126:129], v[58:61], v[186:189], v[126:129]
	v_mfma_f32_16x16x32_bf16 v[122:125], v[74:77], v[186:189], v[122:125]
	v_mfma_f32_16x16x32_bf16 v[110:113], v[58:61], v[194:197], v[110:113]
	v_mfma_f32_16x16x32_bf16 v[106:109], v[74:77], v[194:197], v[106:109]
	v_mfma_f32_16x16x32_bf16 v[94:97], v[58:61], v[210:213], v[94:97]
	v_mfma_f32_16x16x32_bf16 v[90:93], v[74:77], v[210:213], v[90:93]
	v_mfma_f32_16x16x32_bf16 v[142:145], v[62:65], v[182:185], v[142:145]
	v_mfma_f32_16x16x32_bf16 v[138:141], v[78:81], v[182:185], v[138:141]
	v_mfma_f32_16x16x32_bf16 v[126:129], v[62:65], v[190:193], v[126:129]
	v_mfma_f32_16x16x32_bf16 v[122:125], v[78:81], v[190:193], v[122:125]
	v_mfma_f32_16x16x32_bf16 v[110:113], v[62:65], v[198:201], v[110:113]
	v_mfma_f32_16x16x32_bf16 v[106:109], v[78:81], v[198:201], v[106:109]
	v_mfma_f32_16x16x32_bf16 v[94:97], v[62:65], v[214:217], v[94:97]
	v_mfma_f32_16x16x32_bf16 v[90:93], v[78:81], v[214:217], v[90:93]
	s_setprio 0
	s_setprio 1
	v_mfma_f32_16x16x32_bf16 v[134:137], v[146:149], v[174:177], v[134:137]
	v_mfma_f32_16x16x32_bf16 v[130:133], v[154:157], v[174:177], v[130:133]
	v_mfma_f32_16x16x32_bf16 v[118:121], v[146:149], v[186:189], v[118:121]
	v_mfma_f32_16x16x32_bf16 v[114:117], v[154:157], v[186:189], v[114:117]
	v_mfma_f32_16x16x32_bf16 v[102:105], v[146:149], v[194:197], v[102:105]
	v_mfma_f32_16x16x32_bf16 v[98:101], v[154:157], v[194:197], v[98:101]
	v_mfma_f32_16x16x32_bf16 v[86:89], v[146:149], v[210:213], v[86:89]
	v_mfma_f32_16x16x32_bf16 v[82:85], v[154:157], v[210:213], v[82:85]
	v_mfma_f32_16x16x32_bf16 v[134:137], v[150:153], v[182:185], v[134:137]
	v_mfma_f32_16x16x32_bf16 v[130:133], v[170:173], v[182:185], v[130:133]
	v_mfma_f32_16x16x32_bf16 v[118:121], v[150:153], v[190:193], v[118:121]
	v_mfma_f32_16x16x32_bf16 v[114:117], v[170:173], v[190:193], v[114:117]
	v_mfma_f32_16x16x32_bf16 v[102:105], v[150:153], v[198:201], v[102:105]
	v_mfma_f32_16x16x32_bf16 v[98:101], v[170:173], v[198:201], v[98:101]
	v_mfma_f32_16x16x32_bf16 v[86:89], v[150:153], v[214:217], v[86:89]
	v_mfma_f32_16x16x32_bf16 v[82:85], v[170:173], v[214:217], v[82:85]
	s_setprio 0
	s_barrier
	s_add_i32 s88, s88, s14
	v_lshl_add_u64 v[202:203], s[68:69], 0, v[166:167]
	s_mov_b32 m0, s88
	ds_read_b128 v[174:177], v208 offset:16384
	ds_read_b128 v[182:185], v208 offset:17408
	ds_read_b128 v[186:189], v208 offset:18432
	ds_read_b128 v[190:193], v208 offset:19456
	ds_read_b128 v[194:197], v208 offset:20480
	ds_read_b128 v[198:201], v208 offset:21504
	ds_read_b128 v[210:213], v208 offset:22528
	ds_read_b128 v[214:217], v208 offset:23552
	global_load_lds_dwordx4 v[202:203], off
	s_add_i32 m0, s88, 0x2000
	s_add_u32 s90, s68, 0x40000
	v_lshl_add_u64 v[218:219], s[68:69], 0, v[158:159]
	s_addc_u32 s91, s69, 0
	s_add_i32 s88, s92, s14
	global_load_lds_dwordx4 v[218:219], off
	v_lshl_add_u64 v[220:221], s[90:91], 0, v[166:167]
	s_mov_b32 m0, s88
	v_lshl_add_u64 v[222:223], s[70:71], 0, v[162:163]
	global_load_lds_dwordx4 v[220:221], off
	v_lshl_add_u64 v[220:221], s[90:91], 0, v[158:159]
	s_add_i32 m0, s88, 0x2000
	s_nop 0
	global_load_lds_dwordx4 v[220:221], off
	v_lshl_add_u64 v[220:221], s[70:71], 0, v[160:161]
	s_mov_b32 m0, s15
	s_nop 0
	global_load_lds_dwordx4 v[220:221], off
	s_mov_b32 m0, s16
	s_nop 0
	global_load_lds_dwordx4 v[222:223], off
	s_waitcnt vmcnt(8)
	s_waitcnt lgkmcnt(0)
	s_barrier
	s_setprio 1
	v_mfma_f32_16x16x32_bf16 v[70:73], v[58:61], v[174:177], v[70:73]
	v_mfma_f32_16x16x32_bf16 v[66:69], v[74:77], v[174:177], v[66:69]
	v_mfma_f32_16x16x32_bf16 v[46:49], v[58:61], v[186:189], v[46:49]
	v_mfma_f32_16x16x32_bf16 v[42:45], v[74:77], v[186:189], v[42:45]
	v_mfma_f32_16x16x32_bf16 v[30:33], v[58:61], v[194:197], v[30:33]
	v_mfma_f32_16x16x32_bf16 v[26:29], v[74:77], v[194:197], v[26:29]
	v_mfma_f32_16x16x32_bf16 v[14:17], v[58:61], v[210:213], v[14:17]
	v_mfma_f32_16x16x32_bf16 v[10:13], v[74:77], v[210:213], v[10:13]
	v_mfma_f32_16x16x32_bf16 v[70:73], v[62:65], v[182:185], v[70:73]
	v_mfma_f32_16x16x32_bf16 v[66:69], v[78:81], v[182:185], v[66:69]
	v_mfma_f32_16x16x32_bf16 v[46:49], v[62:65], v[190:193], v[46:49]
	v_mfma_f32_16x16x32_bf16 v[42:45], v[78:81], v[190:193], v[42:45]
	v_mfma_f32_16x16x32_bf16 v[30:33], v[62:65], v[198:201], v[30:33]
	v_mfma_f32_16x16x32_bf16 v[26:29], v[78:81], v[198:201], v[26:29]
	v_mfma_f32_16x16x32_bf16 v[14:17], v[62:65], v[214:217], v[14:17]
	v_mfma_f32_16x16x32_bf16 v[10:13], v[78:81], v[214:217], v[10:13]
	s_setprio 0
	s_setprio 1
	v_mfma_f32_16x16x32_bf16 v[54:57], v[146:149], v[174:177], v[54:57]
	v_mfma_f32_16x16x32_bf16 v[50:53], v[154:157], v[174:177], v[50:53]
	v_mfma_f32_16x16x32_bf16 v[38:41], v[146:149], v[186:189], v[38:41]
	v_mfma_f32_16x16x32_bf16 v[34:37], v[154:157], v[186:189], v[34:37]
	v_mfma_f32_16x16x32_bf16 v[22:25], v[146:149], v[194:197], v[22:25]
	v_mfma_f32_16x16x32_bf16 v[18:21], v[154:157], v[194:197], v[18:21]
	v_mfma_f32_16x16x32_bf16 v[6:9], v[146:149], v[210:213], v[6:9]
	v_mfma_f32_16x16x32_bf16 v[2:5], v[154:157], v[210:213], v[2:5]
	v_mfma_f32_16x16x32_bf16 v[54:57], v[150:153], v[182:185], v[54:57]
	v_mfma_f32_16x16x32_bf16 v[50:53], v[170:173], v[182:185], v[50:53]
	v_mfma_f32_16x16x32_bf16 v[38:41], v[150:153], v[190:193], v[38:41]
	v_mfma_f32_16x16x32_bf16 v[34:37], v[170:173], v[190:193], v[34:37]
	v_mfma_f32_16x16x32_bf16 v[22:25], v[150:153], v[198:201], v[22:25]
	v_mfma_f32_16x16x32_bf16 v[18:21], v[170:173], v[198:201], v[18:21]
	v_mfma_f32_16x16x32_bf16 v[6:9], v[150:153], v[214:217], v[6:9]
	v_mfma_f32_16x16x32_bf16 v[2:5], v[170:173], v[214:217], v[2:5]
	s_setprio 0
	s_barrier
	s_add_i32 s88, 0, 0x18000
	s_add_i32 s90, 0, 0x1c000
	v_add_u32_e32 v78, s88, v204
	v_add_u32_e32 v170, s90, v204
	ds_read_b128 v[58:61], v78
	ds_read_b128 v[62:65], v78 offset:1024
	ds_read_b128 v[74:77], v78 offset:2048
	ds_read_b128 v[78:81], v78 offset:3072
	ds_read_b128 v[146:149], v170
	ds_read_b128 v[150:153], v170 offset:1024
	ds_read_b128 v[154:157], v170 offset:2048
	ds_read_b128 v[170:173], v170 offset:3072
	s_add_u32 s70, s70, 0x40000
	s_addc_u32 s71, s71, 0
	s_mov_b32 m0, s20
	v_lshl_add_u64 v[232:233], s[70:71], 0, v[160:161]
	ds_read_b128 v[174:177], v208 offset:32768
	ds_read_b128 v[182:185], v208 offset:33792
	ds_read_b128 v[186:189], v208 offset:34816
	ds_read_b128 v[190:193], v208 offset:35840
	ds_read_b128 v[194:197], v208 offset:36864
	ds_read_b128 v[198:201], v208 offset:37888
	ds_read_b128 v[210:213], v208 offset:38912
	ds_read_b128 v[214:217], v208 offset:39936
	global_load_lds_dwordx4 v[232:233], off
	v_lshl_add_u64 v[232:233], s[70:71], 0, v[162:163]
	s_mov_b32 m0, s21
	s_nop 0
	global_load_lds_dwordx4 v[232:233], off
	s_waitcnt vmcnt(8)
	s_waitcnt lgkmcnt(0)
	s_barrier
	s_setprio 1
	v_mfma_f32_16x16x32_bf16 v[142:145], v[58:61], v[174:177], v[142:145]
	v_mfma_f32_16x16x32_bf16 v[138:141], v[74:77], v[174:177], v[138:141]
	v_mfma_f32_16x16x32_bf16 v[126:129], v[58:61], v[186:189], v[126:129]
	v_mfma_f32_16x16x32_bf16 v[122:125], v[74:77], v[186:189], v[122:125]
	v_mfma_f32_16x16x32_bf16 v[110:113], v[58:61], v[194:197], v[110:113]
	v_mfma_f32_16x16x32_bf16 v[106:109], v[74:77], v[194:197], v[106:109]
	v_mfma_f32_16x16x32_bf16 v[94:97], v[58:61], v[210:213], v[94:97]
	v_mfma_f32_16x16x32_bf16 v[90:93], v[74:77], v[210:213], v[90:93]
	v_mfma_f32_16x16x32_bf16 v[142:145], v[62:65], v[182:185], v[142:145]
	v_mfma_f32_16x16x32_bf16 v[138:141], v[78:81], v[182:185], v[138:141]
	v_mfma_f32_16x16x32_bf16 v[126:129], v[62:65], v[190:193], v[126:129]
	v_mfma_f32_16x16x32_bf16 v[122:125], v[78:81], v[190:193], v[122:125]
	v_mfma_f32_16x16x32_bf16 v[110:113], v[62:65], v[198:201], v[110:113]
	v_mfma_f32_16x16x32_bf16 v[106:109], v[78:81], v[198:201], v[106:109]
	v_mfma_f32_16x16x32_bf16 v[94:97], v[62:65], v[214:217], v[94:97]
	v_mfma_f32_16x16x32_bf16 v[90:93], v[78:81], v[214:217], v[90:93]
	s_setprio 0
	s_setprio 1
	v_mfma_f32_16x16x32_bf16 v[134:137], v[146:149], v[174:177], v[134:137]
	v_mfma_f32_16x16x32_bf16 v[130:133], v[154:157], v[174:177], v[130:133]
	v_mfma_f32_16x16x32_bf16 v[118:121], v[146:149], v[186:189], v[118:121]
	v_mfma_f32_16x16x32_bf16 v[114:117], v[154:157], v[186:189], v[114:117]
	v_mfma_f32_16x16x32_bf16 v[102:105], v[146:149], v[194:197], v[102:105]
	v_mfma_f32_16x16x32_bf16 v[98:101], v[154:157], v[194:197], v[98:101]
	v_mfma_f32_16x16x32_bf16 v[86:89], v[146:149], v[210:213], v[86:89]
	v_mfma_f32_16x16x32_bf16 v[82:85], v[154:157], v[210:213], v[82:85]
	v_mfma_f32_16x16x32_bf16 v[134:137], v[150:153], v[182:185], v[134:137]
	v_mfma_f32_16x16x32_bf16 v[130:133], v[170:173], v[182:185], v[130:133]
	v_mfma_f32_16x16x32_bf16 v[118:121], v[150:153], v[190:193], v[118:121]
	v_mfma_f32_16x16x32_bf16 v[114:117], v[170:173], v[190:193], v[114:117]
	v_mfma_f32_16x16x32_bf16 v[102:105], v[150:153], v[198:201], v[102:105]
	v_mfma_f32_16x16x32_bf16 v[98:101], v[170:173], v[198:201], v[98:101]
	v_mfma_f32_16x16x32_bf16 v[86:89], v[150:153], v[214:217], v[86:89]
	v_mfma_f32_16x16x32_bf16 v[82:85], v[170:173], v[214:217], v[82:85]
	s_setprio 0
	s_barrier
	s_add_i32 s70, s88, s14
	v_lshl_add_u64 v[202:203], v[202:203], 0, s[56:57]
	s_mov_b32 m0, s70
	ds_read_b128 v[174:177], v208 offset:49152
	ds_read_b128 v[182:185], v208 offset:50176
	ds_read_b128 v[186:189], v208 offset:51200
	ds_read_b128 v[190:193], v208 offset:52224
	ds_read_b128 v[194:197], v208 offset:53248
	ds_read_b128 v[198:201], v208 offset:54272
	ds_read_b128 v[210:213], v208 offset:55296
	ds_read_b128 v[214:217], v208 offset:56320
	global_load_lds_dwordx4 v[202:203], off
	s_add_i32 m0, s70, 0x2000
	s_add_u32 s68, s68, 0x40080
	v_lshl_add_u64 v[202:203], v[218:219], 0, s[56:57]
	s_addc_u32 s69, s69, 0
	s_add_i32 s70, s90, s14
	global_load_lds_dwordx4 v[202:203], off
	v_lshl_add_u64 v[202:203], s[68:69], 0, v[166:167]
	s_mov_b32 m0, s70
	s_nop 0
	global_load_lds_dwordx4 v[202:203], off
	v_lshl_add_u64 v[202:203], s[68:69], 0, v[158:159]
	s_add_i32 m0, s70, 0x2000
	s_nop 0
	global_load_lds_dwordx4 v[202:203], off
	v_lshl_add_u64 v[202:203], v[220:221], 0, s[56:57]
	s_mov_b32 m0, s24
	s_nop 0
	global_load_lds_dwordx4 v[202:203], off
	v_lshl_add_u64 v[202:203], v[222:223], 0, s[56:57]
	s_mov_b32 m0, s25
	s_nop 0
	global_load_lds_dwordx4 v[202:203], off
	s_waitcnt vmcnt(8)
	s_waitcnt lgkmcnt(0)
	s_barrier
	s_setprio 1
	v_mfma_f32_16x16x32_bf16 v[70:73], v[58:61], v[174:177], v[70:73]
	v_mfma_f32_16x16x32_bf16 v[66:69], v[74:77], v[174:177], v[66:69]
	v_mfma_f32_16x16x32_bf16 v[46:49], v[58:61], v[186:189], v[46:49]
	v_mfma_f32_16x16x32_bf16 v[42:45], v[74:77], v[186:189], v[42:45]
	v_mfma_f32_16x16x32_bf16 v[30:33], v[58:61], v[194:197], v[30:33]
	v_mfma_f32_16x16x32_bf16 v[26:29], v[74:77], v[194:197], v[26:29]
	v_mfma_f32_16x16x32_bf16 v[14:17], v[58:61], v[210:213], v[14:17]
	v_mfma_f32_16x16x32_bf16 v[10:13], v[74:77], v[210:213], v[10:13]
	v_mfma_f32_16x16x32_bf16 v[70:73], v[62:65], v[182:185], v[70:73]
	v_mfma_f32_16x16x32_bf16 v[66:69], v[78:81], v[182:185], v[66:69]
	v_mfma_f32_16x16x32_bf16 v[46:49], v[62:65], v[190:193], v[46:49]
	v_mfma_f32_16x16x32_bf16 v[42:45], v[78:81], v[190:193], v[42:45]
	v_mfma_f32_16x16x32_bf16 v[30:33], v[62:65], v[198:201], v[30:33]
	v_mfma_f32_16x16x32_bf16 v[26:29], v[78:81], v[198:201], v[26:29]
	v_mfma_f32_16x16x32_bf16 v[14:17], v[62:65], v[214:217], v[14:17]
	v_mfma_f32_16x16x32_bf16 v[10:13], v[78:81], v[214:217], v[10:13]
	s_setprio 0
	s_setprio 1
	v_mfma_f32_16x16x32_bf16 v[54:57], v[146:149], v[174:177], v[54:57]
	v_mfma_f32_16x16x32_bf16 v[50:53], v[154:157], v[174:177], v[50:53]
	v_mfma_f32_16x16x32_bf16 v[38:41], v[146:149], v[186:189], v[38:41]
	v_mfma_f32_16x16x32_bf16 v[34:37], v[154:157], v[186:189], v[34:37]
	v_mfma_f32_16x16x32_bf16 v[22:25], v[146:149], v[194:197], v[22:25]
	v_mfma_f32_16x16x32_bf16 v[18:21], v[154:157], v[194:197], v[18:21]
	v_mfma_f32_16x16x32_bf16 v[6:9], v[146:149], v[210:213], v[6:9]
	v_mfma_f32_16x16x32_bf16 v[2:5], v[154:157], v[210:213], v[2:5]
	v_mfma_f32_16x16x32_bf16 v[54:57], v[150:153], v[182:185], v[54:57]
	v_mfma_f32_16x16x32_bf16 v[50:53], v[170:173], v[182:185], v[50:53]
	v_mfma_f32_16x16x32_bf16 v[38:41], v[150:153], v[190:193], v[38:41]
	v_mfma_f32_16x16x32_bf16 v[34:37], v[170:173], v[190:193], v[34:37]
	v_mfma_f32_16x16x32_bf16 v[22:25], v[150:153], v[198:201], v[22:25]
	v_mfma_f32_16x16x32_bf16 v[18:21], v[170:173], v[198:201], v[18:21]
	v_mfma_f32_16x16x32_bf16 v[6:9], v[150:153], v[214:217], v[6:9]
	v_mfma_f32_16x16x32_bf16 v[2:5], v[170:173], v[214:217], v[2:5]
	s_setprio 0
	s_barrier
	s_add_u32 s77, s77, 0x100
	s_addc_u32 s79, s79, 0
	s_add_u32 s74, s74, 0x100
	s_addc_u32 s75, s75, 0
	s_cmp_ge_i32 s84, s1
	s_mov_b32 s68, s84
	s_cbranch_scc0 .LBB0_664

.Lpeelph7b_0:
	s_add_i32 s69, s58, 2
	s_add_u32 s59, s54, 0xfffc0080
	s_addc_u32 s60, s55, -1
	s_add_i32 s70, 0, 0x10000
	s_cmp_eq_u32 s53, s58
	s_cselect_b32 s61, s43, s60
	s_cselect_b32 s60, s45, s59
	v_add_u32_e32 v146, s70, v151
	s_cselect_b32 s59, s64, s68
	s_cselect_b32 s58, s65, s66
	s_add_i32 s72, 0, 0x14000
	ds_read_b128 v[142:145], v146
	ds_read_b128 v[156:159], v146 offset:1024
	ds_read_b128 v[160:163], v146 offset:2048
	ds_read_b128 v[170:173], v146 offset:3072
	v_add_u32_e32 v146, s72, v151
	ds_read_b128 v[174:177], v146
	ds_read_b128 v[178:181], v146 offset:1024
	ds_read_b128 v[182:185], v146 offset:2048
	ds_read_b128 v[186:189], v146 offset:3072
	v_lshl_add_u64 v[146:147], s[54:55], 0, v[140:141]
	s_add_i32 m0, s16, 0xc000
	ds_read_b128 v[190:193], v154
	ds_read_b128 v[194:197], v154 offset:1024
	ds_read_b128 v[198:201], v154 offset:2048
	ds_read_b128 v[202:205], v154 offset:3072
	ds_read_b128 v[206:209], v154 offset:4096
	ds_read_b128 v[210:213], v154 offset:5120
	ds_read_b128 v[214:217], v154 offset:6144
	ds_read_b128 v[218:221], v154 offset:7168
	global_load_lds_dwordx4 v[146:147], off
	v_lshl_add_u64 v[146:147], s[54:55], 0, v[138:139]
	s_add_i32 m0, s16, 0xe000
	s_nop 0
	global_load_lds_dwordx4 v[146:147], off
	s_waitcnt vmcnt(8)
	s_waitcnt lgkmcnt(0)
	s_barrier
	s_setprio 1
	v_mfma_f32_16x16x32_bf16 v[126:129], v[142:145], v[190:193], 0
	v_mfma_f32_16x16x32_bf16 v[118:121], v[160:163], v[190:193], 0
	v_mfma_f32_16x16x32_bf16 v[110:113], v[142:145], v[198:201], 0
	v_mfma_f32_16x16x32_bf16 v[102:105], v[160:163], v[198:201], 0
	v_mfma_f32_16x16x32_bf16 v[94:97], v[142:145], v[206:209], 0
	v_mfma_f32_16x16x32_bf16 v[86:89], v[160:163], v[206:209], 0
	v_mfma_f32_16x16x32_bf16 v[78:81], v[142:145], v[214:217], 0
	v_mfma_f32_16x16x32_bf16 v[70:73], v[160:163], v[214:217], 0
	v_mfma_f32_16x16x32_bf16 v[126:129], v[156:159], v[194:197], v[126:129]
	v_mfma_f32_16x16x32_bf16 v[118:121], v[170:173], v[194:197], v[118:121]
	v_mfma_f32_16x16x32_bf16 v[110:113], v[156:159], v[202:205], v[110:113]
	v_mfma_f32_16x16x32_bf16 v[102:105], v[170:173], v[202:205], v[102:105]
	v_mfma_f32_16x16x32_bf16 v[94:97], v[156:159], v[210:213], v[94:97]
	v_mfma_f32_16x16x32_bf16 v[86:89], v[170:173], v[210:213], v[86:89]
	v_mfma_f32_16x16x32_bf16 v[78:81], v[156:159], v[218:221], v[78:81]
	v_mfma_f32_16x16x32_bf16 v[70:73], v[170:173], v[218:221], v[70:73]
	s_setprio 0
	s_setprio 1
	v_mfma_f32_16x16x32_bf16 v[122:125], v[174:177], v[190:193], 0
	v_mfma_f32_16x16x32_bf16 v[114:117], v[182:185], v[190:193], 0
	v_mfma_f32_16x16x32_bf16 v[106:109], v[174:177], v[198:201], 0
	v_mfma_f32_16x16x32_bf16 v[98:101], v[182:185], v[198:201], 0
	v_mfma_f32_16x16x32_bf16 v[90:93], v[174:177], v[206:209], 0
	v_mfma_f32_16x16x32_bf16 v[82:85], v[182:185], v[206:209], 0
	v_mfma_f32_16x16x32_bf16 v[74:77], v[174:177], v[214:217], 0
	v_mfma_f32_16x16x32_bf16 v[66:69], v[182:185], v[214:217], 0
	v_mfma_f32_16x16x32_bf16 v[122:125], v[178:181], v[194:197], v[122:125]
	v_mfma_f32_16x16x32_bf16 v[114:117], v[186:189], v[194:197], v[114:117]
	v_mfma_f32_16x16x32_bf16 v[106:109], v[178:181], v[202:205], v[106:109]
	v_mfma_f32_16x16x32_bf16 v[98:101], v[186:189], v[202:205], v[98:101]
	v_mfma_f32_16x16x32_bf16 v[90:93], v[178:181], v[210:213], v[90:93]
	v_mfma_f32_16x16x32_bf16 v[82:85], v[186:189], v[210:213], v[82:85]
	v_mfma_f32_16x16x32_bf16 v[74:77], v[178:181], v[218:221], v[74:77]
	v_mfma_f32_16x16x32_bf16 v[66:69], v[186:189], v[218:221], v[66:69]
	s_setprio 0
	s_barrier
	s_add_i32 s70, s70, s14
	v_lshl_add_u64 v[146:147], s[58:59], 0, v[166:167]
	s_mov_b32 m0, s70
	ds_read_b128 v[190:193], v154 offset:16384
	ds_read_b128 v[194:197], v154 offset:17408
	ds_read_b128 v[198:201], v154 offset:18432
	ds_read_b128 v[202:205], v154 offset:19456
	ds_read_b128 v[206:209], v154 offset:20480
	ds_read_b128 v[210:213], v154 offset:21504
	ds_read_b128 v[214:217], v154 offset:22528
	ds_read_b128 v[218:221], v154 offset:23552
	global_load_lds_dwordx4 v[146:147], off
	s_add_i32 m0, s70, 0x2000
	s_add_u32 s70, s58, 0x40000
	v_lshl_add_u64 v[164:165], s[58:59], 0, v[134:135]
	s_addc_u32 s71, s59, 0
	s_add_i32 s72, s72, s14
	global_load_lds_dwordx4 v[164:165], off
	v_lshl_add_u64 v[222:223], s[70:71], 0, v[166:167]
	s_mov_b32 m0, s72
	v_lshl_add_u64 v[232:233], s[60:61], 0, v[130:131]
	global_load_lds_dwordx4 v[222:223], off
	v_lshl_add_u64 v[222:223], s[70:71], 0, v[134:135]
	s_add_i32 m0, s72, 0x2000
	s_nop 0
	global_load_lds_dwordx4 v[222:223], off
	v_lshl_add_u64 v[222:223], s[60:61], 0, v[132:133]
	s_mov_b32 m0, s16
	s_nop 0
	global_load_lds_dwordx4 v[222:223], off
	s_mov_b32 m0, s20
	s_nop 0
	global_load_lds_dwordx4 v[232:233], off
	s_waitcnt vmcnt(8)
	s_waitcnt lgkmcnt(0)
	s_barrier
	s_setprio 1
	v_mfma_f32_16x16x32_bf16 v[62:65], v[142:145], v[190:193], 0
	v_mfma_f32_16x16x32_bf16 v[54:57], v[160:163], v[190:193], 0
	v_mfma_f32_16x16x32_bf16 v[46:49], v[142:145], v[198:201], 0
	v_mfma_f32_16x16x32_bf16 v[38:41], v[160:163], v[198:201], 0
	v_mfma_f32_16x16x32_bf16 v[30:33], v[142:145], v[206:209], 0
	v_mfma_f32_16x16x32_bf16 v[22:25], v[160:163], v[206:209], 0
	v_mfma_f32_16x16x32_bf16 v[14:17], v[142:145], v[214:217], 0
	v_mfma_f32_16x16x32_bf16 v[6:9], v[160:163], v[214:217], 0
	v_mfma_f32_16x16x32_bf16 v[62:65], v[156:159], v[194:197], v[62:65]
	v_mfma_f32_16x16x32_bf16 v[54:57], v[170:173], v[194:197], v[54:57]
	v_mfma_f32_16x16x32_bf16 v[46:49], v[156:159], v[202:205], v[46:49]
	v_mfma_f32_16x16x32_bf16 v[38:41], v[170:173], v[202:205], v[38:41]
	v_mfma_f32_16x16x32_bf16 v[30:33], v[156:159], v[210:213], v[30:33]
	v_mfma_f32_16x16x32_bf16 v[22:25], v[170:173], v[210:213], v[22:25]
	v_mfma_f32_16x16x32_bf16 v[14:17], v[156:159], v[218:221], v[14:17]
	v_mfma_f32_16x16x32_bf16 v[6:9], v[170:173], v[218:221], v[6:9]
	s_setprio 0
	s_setprio 1
	v_mfma_f32_16x16x32_bf16 v[58:61], v[174:177], v[190:193], 0
	v_mfma_f32_16x16x32_bf16 v[50:53], v[182:185], v[190:193], 0
	v_mfma_f32_16x16x32_bf16 v[42:45], v[174:177], v[198:201], 0
	v_mfma_f32_16x16x32_bf16 v[34:37], v[182:185], v[198:201], 0
	v_mfma_f32_16x16x32_bf16 v[26:29], v[174:177], v[206:209], 0
	v_mfma_f32_16x16x32_bf16 v[18:21], v[182:185], v[206:209], 0
	v_mfma_f32_16x16x32_bf16 v[10:13], v[174:177], v[214:217], 0
	v_mfma_f32_16x16x32_bf16 v[2:5], v[182:185], v[214:217], 0
	v_mfma_f32_16x16x32_bf16 v[58:61], v[178:181], v[194:197], v[58:61]
	v_mfma_f32_16x16x32_bf16 v[50:53], v[186:189], v[194:197], v[50:53]
	v_mfma_f32_16x16x32_bf16 v[42:45], v[178:181], v[202:205], v[42:45]
	v_mfma_f32_16x16x32_bf16 v[34:37], v[186:189], v[202:205], v[34:37]
	v_mfma_f32_16x16x32_bf16 v[26:29], v[178:181], v[210:213], v[26:29]
	v_mfma_f32_16x16x32_bf16 v[18:21], v[186:189], v[210:213], v[18:21]
	v_mfma_f32_16x16x32_bf16 v[10:13], v[178:181], v[218:221], v[10:13]
	v_mfma_f32_16x16x32_bf16 v[2:5], v[186:189], v[218:221], v[2:5]
	s_setprio 0
	s_barrier
	s_add_i32 s70, 0, 0x18000
	v_add_u32_e32 v148, s70, v151
	s_add_i32 s71, 0, 0x1c000
	ds_read_b128 v[142:145], v148
	ds_read_b128 v[156:159], v148 offset:1024
	ds_read_b128 v[160:163], v148 offset:2048
	ds_read_b128 v[170:173], v148 offset:3072
	v_add_u32_e32 v148, s71, v151
	ds_read_b128 v[174:177], v148
	ds_read_b128 v[178:181], v148 offset:1024
	ds_read_b128 v[182:185], v148 offset:2048
	ds_read_b128 v[186:189], v148 offset:3072
	s_add_u32 s60, s60, 0x40000
	s_addc_u32 s61, s61, 0
	s_mov_b32 m0, s21
	v_lshl_add_u64 v[234:235], s[60:61], 0, v[132:133]
	ds_read_b128 v[190:193], v154 offset:32768
	ds_read_b128 v[194:197], v154 offset:33792
	ds_read_b128 v[198:201], v154 offset:34816
	ds_read_b128 v[202:205], v154 offset:35840
	ds_read_b128 v[206:209], v154 offset:36864
	ds_read_b128 v[210:213], v154 offset:37888
	ds_read_b128 v[214:217], v154 offset:38912
	ds_read_b128 v[218:221], v154 offset:39936
	global_load_lds_dwordx4 v[234:235], off
	v_lshl_add_u64 v[234:235], s[60:61], 0, v[130:131]
	s_mov_b32 m0, s22
	s_nop 0
	global_load_lds_dwordx4 v[234:235], off
	s_waitcnt vmcnt(8)
	s_waitcnt lgkmcnt(0)
	s_barrier
	s_setprio 1
	v_mfma_f32_16x16x32_bf16 v[126:129], v[142:145], v[190:193], v[126:129]
	v_mfma_f32_16x16x32_bf16 v[118:121], v[160:163], v[190:193], v[118:121]
	v_mfma_f32_16x16x32_bf16 v[110:113], v[142:145], v[198:201], v[110:113]
	v_mfma_f32_16x16x32_bf16 v[102:105], v[160:163], v[198:201], v[102:105]
	v_mfma_f32_16x16x32_bf16 v[94:97], v[142:145], v[206:209], v[94:97]
	v_mfma_f32_16x16x32_bf16 v[86:89], v[160:163], v[206:209], v[86:89]
	v_mfma_f32_16x16x32_bf16 v[78:81], v[142:145], v[214:217], v[78:81]
	v_mfma_f32_16x16x32_bf16 v[70:73], v[160:163], v[214:217], v[70:73]
	v_mfma_f32_16x16x32_bf16 v[126:129], v[156:159], v[194:197], v[126:129]
	v_mfma_f32_16x16x32_bf16 v[118:121], v[170:173], v[194:197], v[118:121]
	v_mfma_f32_16x16x32_bf16 v[110:113], v[156:159], v[202:205], v[110:113]
	v_mfma_f32_16x16x32_bf16 v[102:105], v[170:173], v[202:205], v[102:105]
	v_mfma_f32_16x16x32_bf16 v[94:97], v[156:159], v[210:213], v[94:97]
	v_mfma_f32_16x16x32_bf16 v[86:89], v[170:173], v[210:213], v[86:89]
	v_mfma_f32_16x16x32_bf16 v[78:81], v[156:159], v[218:221], v[78:81]
	v_mfma_f32_16x16x32_bf16 v[70:73], v[170:173], v[218:221], v[70:73]
	s_setprio 0
	s_setprio 1
	v_mfma_f32_16x16x32_bf16 v[122:125], v[174:177], v[190:193], v[122:125]
	v_mfma_f32_16x16x32_bf16 v[114:117], v[182:185], v[190:193], v[114:117]
	v_mfma_f32_16x16x32_bf16 v[106:109], v[174:177], v[198:201], v[106:109]
	v_mfma_f32_16x16x32_bf16 v[98:101], v[182:185], v[198:201], v[98:101]
	v_mfma_f32_16x16x32_bf16 v[90:93], v[174:177], v[206:209], v[90:93]
	v_mfma_f32_16x16x32_bf16 v[82:85], v[182:185], v[206:209], v[82:85]
	v_mfma_f32_16x16x32_bf16 v[74:77], v[174:177], v[214:217], v[74:77]
	v_mfma_f32_16x16x32_bf16 v[66:69], v[182:185], v[214:217], v[66:69]
	v_mfma_f32_16x16x32_bf16 v[122:125], v[178:181], v[194:197], v[122:125]
	v_mfma_f32_16x16x32_bf16 v[114:117], v[186:189], v[194:197], v[114:117]
	v_mfma_f32_16x16x32_bf16 v[106:109], v[178:181], v[202:205], v[106:109]
	v_mfma_f32_16x16x32_bf16 v[98:101], v[186:189], v[202:205], v[98:101]
	v_mfma_f32_16x16x32_bf16 v[90:93], v[178:181], v[210:213], v[90:93]
	v_mfma_f32_16x16x32_bf16 v[82:85], v[186:189], v[210:213], v[82:85]
	v_mfma_f32_16x16x32_bf16 v[74:77], v[178:181], v[218:221], v[74:77]
	v_mfma_f32_16x16x32_bf16 v[66:69], v[186:189], v[218:221], v[66:69]
	s_setprio 0
	s_barrier
	s_add_i32 s60, s70, s14
	v_lshl_add_u64 v[146:147], v[146:147], 0, s[56:57]
	s_mov_b32 m0, s60
	ds_read_b128 v[190:193], v154 offset:49152
	ds_read_b128 v[194:197], v154 offset:50176
	ds_read_b128 v[198:201], v154 offset:51200
	ds_read_b128 v[202:205], v154 offset:52224
	ds_read_b128 v[206:209], v154 offset:53248
	ds_read_b128 v[210:213], v154 offset:54272
	ds_read_b128 v[214:217], v154 offset:55296
	ds_read_b128 v[218:221], v154 offset:56320
	global_load_lds_dwordx4 v[146:147], off
	s_add_i32 m0, s60, 0x2000
	s_add_u32 s58, s58, 0x40080
	v_lshl_add_u64 v[146:147], v[164:165], 0, s[56:57]
	s_addc_u32 s59, s59, 0
	s_add_i32 s60, s71, s14
	global_load_lds_dwordx4 v[146:147], off
	v_lshl_add_u64 v[146:147], s[58:59], 0, v[166:167]
	s_mov_b32 m0, s60
	s_nop 0
	global_load_lds_dwordx4 v[146:147], off
	v_lshl_add_u64 v[146:147], s[58:59], 0, v[134:135]
	s_add_i32 m0, s60, 0x2000
	s_nop 0
	global_load_lds_dwordx4 v[146:147], off
	v_lshl_add_u64 v[146:147], v[222:223], 0, s[56:57]
	s_mov_b32 m0, s23
	s_nop 0
	global_load_lds_dwordx4 v[146:147], off
	v_lshl_add_u64 v[146:147], v[232:233], 0, s[56:57]
	s_mov_b32 m0, s24
	s_nop 0
	global_load_lds_dwordx4 v[146:147], off
	s_waitcnt vmcnt(8)
	s_waitcnt lgkmcnt(0)
	s_barrier
	s_setprio 1
	v_mfma_f32_16x16x32_bf16 v[62:65], v[142:145], v[190:193], v[62:65]
	v_mfma_f32_16x16x32_bf16 v[54:57], v[160:163], v[190:193], v[54:57]
	v_mfma_f32_16x16x32_bf16 v[46:49], v[142:145], v[198:201], v[46:49]
	v_mfma_f32_16x16x32_bf16 v[38:41], v[160:163], v[198:201], v[38:41]
	v_mfma_f32_16x16x32_bf16 v[30:33], v[142:145], v[206:209], v[30:33]
	v_mfma_f32_16x16x32_bf16 v[22:25], v[160:163], v[206:209], v[22:25]
	v_mfma_f32_16x16x32_bf16 v[14:17], v[142:145], v[214:217], v[14:17]
	v_mfma_f32_16x16x32_bf16 v[6:9], v[160:163], v[214:217], v[6:9]
	v_mfma_f32_16x16x32_bf16 v[62:65], v[156:159], v[194:197], v[62:65]
	v_mfma_f32_16x16x32_bf16 v[54:57], v[170:173], v[194:197], v[54:57]
	v_mfma_f32_16x16x32_bf16 v[46:49], v[156:159], v[202:205], v[46:49]
	v_mfma_f32_16x16x32_bf16 v[38:41], v[170:173], v[202:205], v[38:41]
	v_mfma_f32_16x16x32_bf16 v[30:33], v[156:159], v[210:213], v[30:33]
	v_mfma_f32_16x16x32_bf16 v[22:25], v[170:173], v[210:213], v[22:25]
	v_mfma_f32_16x16x32_bf16 v[14:17], v[156:159], v[218:221], v[14:17]
	v_mfma_f32_16x16x32_bf16 v[6:9], v[170:173], v[218:221], v[6:9]
	s_setprio 0
	s_setprio 1
	v_mfma_f32_16x16x32_bf16 v[58:61], v[174:177], v[190:193], v[58:61]
	v_mfma_f32_16x16x32_bf16 v[50:53], v[182:185], v[190:193], v[50:53]
	v_mfma_f32_16x16x32_bf16 v[42:45], v[174:177], v[198:201], v[42:45]
	v_mfma_f32_16x16x32_bf16 v[34:37], v[182:185], v[198:201], v[34:37]
	v_mfma_f32_16x16x32_bf16 v[26:29], v[174:177], v[206:209], v[26:29]
	v_mfma_f32_16x16x32_bf16 v[18:21], v[182:185], v[206:209], v[18:21]
	v_mfma_f32_16x16x32_bf16 v[10:13], v[174:177], v[214:217], v[10:13]
	v_mfma_f32_16x16x32_bf16 v[2:5], v[182:185], v[214:217], v[2:5]
	v_mfma_f32_16x16x32_bf16 v[58:61], v[178:181], v[194:197], v[58:61]
	v_mfma_f32_16x16x32_bf16 v[50:53], v[186:189], v[194:197], v[50:53]
	v_mfma_f32_16x16x32_bf16 v[42:45], v[178:181], v[202:205], v[42:45]
	v_mfma_f32_16x16x32_bf16 v[34:37], v[186:189], v[202:205], v[34:37]
	v_mfma_f32_16x16x32_bf16 v[26:29], v[178:181], v[210:213], v[26:29]
	v_mfma_f32_16x16x32_bf16 v[18:21], v[186:189], v[210:213], v[18:21]
	v_mfma_f32_16x16x32_bf16 v[10:13], v[178:181], v[218:221], v[10:13]
	v_mfma_f32_16x16x32_bf16 v[2:5], v[186:189], v[218:221], v[2:5]
	s_setprio 0
	s_barrier
	s_add_u32 s66, s66, 0x100
	s_addc_u32 s68, s68, 0
	s_add_u32 s54, s54, 0x100
	s_addc_u32 s55, s55, 0
	s_cmp_ge_i32 s69, s13
	s_mov_b32 s58, s69
	s_cbranch_scc0 .LBB0_817
	s_branch .Lpeelexitph7b
.LBB0_817:
	s_add_i32 s69, s58, 2
	s_add_u32 s59, s54, 0xfffc0080
	s_addc_u32 s60, s55, -1
	s_add_i32 s70, 0, 0x10000
	s_cmp_eq_u32 s53, s58
	s_cselect_b32 s61, s43, s60
	s_cselect_b32 s60, s45, s59
	v_add_u32_e32 v146, s70, v151
	s_cselect_b32 s59, s64, s68
	s_cselect_b32 s58, s65, s66
	s_add_i32 s72, 0, 0x14000
	ds_read_b128 v[142:145], v146
	ds_read_b128 v[156:159], v146 offset:1024
	ds_read_b128 v[160:163], v146 offset:2048
	ds_read_b128 v[170:173], v146 offset:3072
	v_add_u32_e32 v146, s72, v151
	ds_read_b128 v[174:177], v146
	ds_read_b128 v[178:181], v146 offset:1024
	ds_read_b128 v[182:185], v146 offset:2048
	ds_read_b128 v[186:189], v146 offset:3072
	v_lshl_add_u64 v[146:147], s[54:55], 0, v[140:141]
	s_add_i32 m0, s16, 0xc000
	ds_read_b128 v[190:193], v154
	ds_read_b128 v[194:197], v154 offset:1024
	ds_read_b128 v[198:201], v154 offset:2048
	ds_read_b128 v[202:205], v154 offset:3072
	ds_read_b128 v[206:209], v154 offset:4096
	ds_read_b128 v[210:213], v154 offset:5120
	ds_read_b128 v[214:217], v154 offset:6144
	ds_read_b128 v[218:221], v154 offset:7168
	global_load_lds_dwordx4 v[146:147], off
	v_lshl_add_u64 v[146:147], s[54:55], 0, v[138:139]
	s_add_i32 m0, s16, 0xe000
	s_nop 0
	global_load_lds_dwordx4 v[146:147], off
	s_waitcnt vmcnt(8)
	s_waitcnt lgkmcnt(0)
	s_barrier
	s_setprio 1
	v_mfma_f32_16x16x32_bf16 v[126:129], v[142:145], v[190:193], v[126:129]
	v_mfma_f32_16x16x32_bf16 v[118:121], v[160:163], v[190:193], v[118:121]
	v_mfma_f32_16x16x32_bf16 v[110:113], v[142:145], v[198:201], v[110:113]
	v_mfma_f32_16x16x32_bf16 v[102:105], v[160:163], v[198:201], v[102:105]
	v_mfma_f32_16x16x32_bf16 v[94:97], v[142:145], v[206:209], v[94:97]
	v_mfma_f32_16x16x32_bf16 v[86:89], v[160:163], v[206:209], v[86:89]
	v_mfma_f32_16x16x32_bf16 v[78:81], v[142:145], v[214:217], v[78:81]
	v_mfma_f32_16x16x32_bf16 v[70:73], v[160:163], v[214:217], v[70:73]
	v_mfma_f32_16x16x32_bf16 v[126:129], v[156:159], v[194:197], v[126:129]
	v_mfma_f32_16x16x32_bf16 v[118:121], v[170:173], v[194:197], v[118:121]
	v_mfma_f32_16x16x32_bf16 v[110:113], v[156:159], v[202:205], v[110:113]
	v_mfma_f32_16x16x32_bf16 v[102:105], v[170:173], v[202:205], v[102:105]
	v_mfma_f32_16x16x32_bf16 v[94:97], v[156:159], v[210:213], v[94:97]
	v_mfma_f32_16x16x32_bf16 v[86:89], v[170:173], v[210:213], v[86:89]
	v_mfma_f32_16x16x32_bf16 v[78:81], v[156:159], v[218:221], v[78:81]
	v_mfma_f32_16x16x32_bf16 v[70:73], v[170:173], v[218:221], v[70:73]
	s_setprio 0
	s_setprio 1
	v_mfma_f32_16x16x32_bf16 v[122:125], v[174:177], v[190:193], v[122:125]
	v_mfma_f32_16x16x32_bf16 v[114:117], v[182:185], v[190:193], v[114:117]
	v_mfma_f32_16x16x32_bf16 v[106:109], v[174:177], v[198:201], v[106:109]
	v_mfma_f32_16x16x32_bf16 v[98:101], v[182:185], v[198:201], v[98:101]
	v_mfma_f32_16x16x32_bf16 v[90:93], v[174:177], v[206:209], v[90:93]
	v_mfma_f32_16x16x32_bf16 v[82:85], v[182:185], v[206:209], v[82:85]
	v_mfma_f32_16x16x32_bf16 v[74:77], v[174:177], v[214:217], v[74:77]
	v_mfma_f32_16x16x32_bf16 v[66:69], v[182:185], v[214:217], v[66:69]
	v_mfma_f32_16x16x32_bf16 v[122:125], v[178:181], v[194:197], v[122:125]
	v_mfma_f32_16x16x32_bf16 v[114:117], v[186:189], v[194:197], v[114:117]
	v_mfma_f32_16x16x32_bf16 v[106:109], v[178:181], v[202:205], v[106:109]
	v_mfma_f32_16x16x32_bf16 v[98:101], v[186:189], v[202:205], v[98:101]
	v_mfma_f32_16x16x32_bf16 v[90:93], v[178:181], v[210:213], v[90:93]
	v_mfma_f32_16x16x32_bf16 v[82:85], v[186:189], v[210:213], v[82:85]
	v_mfma_f32_16x16x32_bf16 v[74:77], v[178:181], v[218:221], v[74:77]
	v_mfma_f32_16x16x32_bf16 v[66:69], v[186:189], v[218:221], v[66:69]
	s_setprio 0
	s_barrier
	s_add_i32 s70, s70, s14
	v_lshl_add_u64 v[146:147], s[58:59], 0, v[166:167]
	s_mov_b32 m0, s70
	ds_read_b128 v[190:193], v154 offset:16384
	ds_read_b128 v[194:197], v154 offset:17408
	ds_read_b128 v[198:201], v154 offset:18432
	ds_read_b128 v[202:205], v154 offset:19456
	ds_read_b128 v[206:209], v154 offset:20480
	ds_read_b128 v[210:213], v154 offset:21504
	ds_read_b128 v[214:217], v154 offset:22528
	ds_read_b128 v[218:221], v154 offset:23552
	global_load_lds_dwordx4 v[146:147], off
	s_add_i32 m0, s70, 0x2000
	s_add_u32 s70, s58, 0x40000
	v_lshl_add_u64 v[164:165], s[58:59], 0, v[134:135]
	s_addc_u32 s71, s59, 0
	s_add_i32 s72, s72, s14
	global_load_lds_dwordx4 v[164:165], off
	v_lshl_add_u64 v[222:223], s[70:71], 0, v[166:167]
	s_mov_b32 m0, s72
	v_lshl_add_u64 v[232:233], s[60:61], 0, v[130:131]
	global_load_lds_dwordx4 v[222:223], off
	v_lshl_add_u64 v[222:223], s[70:71], 0, v[134:135]
	s_add_i32 m0, s72, 0x2000
	s_nop 0
	global_load_lds_dwordx4 v[222:223], off
	v_lshl_add_u64 v[222:223], s[60:61], 0, v[132:133]
	s_mov_b32 m0, s16
	s_nop 0
	global_load_lds_dwordx4 v[222:223], off
	s_mov_b32 m0, s20
	s_nop 0
	global_load_lds_dwordx4 v[232:233], off
	s_waitcnt vmcnt(8)
	s_waitcnt lgkmcnt(0)
	s_barrier
	s_setprio 1
	v_mfma_f32_16x16x32_bf16 v[62:65], v[142:145], v[190:193], v[62:65]
	v_mfma_f32_16x16x32_bf16 v[54:57], v[160:163], v[190:193], v[54:57]
	v_mfma_f32_16x16x32_bf16 v[46:49], v[142:145], v[198:201], v[46:49]
	v_mfma_f32_16x16x32_bf16 v[38:41], v[160:163], v[198:201], v[38:41]
	v_mfma_f32_16x16x32_bf16 v[30:33], v[142:145], v[206:209], v[30:33]
	v_mfma_f32_16x16x32_bf16 v[22:25], v[160:163], v[206:209], v[22:25]
	v_mfma_f32_16x16x32_bf16 v[14:17], v[142:145], v[214:217], v[14:17]
	v_mfma_f32_16x16x32_bf16 v[6:9], v[160:163], v[214:217], v[6:9]
	v_mfma_f32_16x16x32_bf16 v[62:65], v[156:159], v[194:197], v[62:65]
	v_mfma_f32_16x16x32_bf16 v[54:57], v[170:173], v[194:197], v[54:57]
	v_mfma_f32_16x16x32_bf16 v[46:49], v[156:159], v[202:205], v[46:49]
	v_mfma_f32_16x16x32_bf16 v[38:41], v[170:173], v[202:205], v[38:41]
	v_mfma_f32_16x16x32_bf16 v[30:33], v[156:159], v[210:213], v[30:33]
	v_mfma_f32_16x16x32_bf16 v[22:25], v[170:173], v[210:213], v[22:25]
	v_mfma_f32_16x16x32_bf16 v[14:17], v[156:159], v[218:221], v[14:17]
	v_mfma_f32_16x16x32_bf16 v[6:9], v[170:173], v[218:221], v[6:9]
	s_setprio 0
	s_setprio 1
	v_mfma_f32_16x16x32_bf16 v[58:61], v[174:177], v[190:193], v[58:61]
	v_mfma_f32_16x16x32_bf16 v[50:53], v[182:185], v[190:193], v[50:53]
	v_mfma_f32_16x16x32_bf16 v[42:45], v[174:177], v[198:201], v[42:45]
	v_mfma_f32_16x16x32_bf16 v[34:37], v[182:185], v[198:201], v[34:37]
	v_mfma_f32_16x16x32_bf16 v[26:29], v[174:177], v[206:209], v[26:29]
	v_mfma_f32_16x16x32_bf16 v[18:21], v[182:185], v[206:209], v[18:21]
	v_mfma_f32_16x16x32_bf16 v[10:13], v[174:177], v[214:217], v[10:13]
	v_mfma_f32_16x16x32_bf16 v[2:5], v[182:185], v[214:217], v[2:5]
	v_mfma_f32_16x16x32_bf16 v[58:61], v[178:181], v[194:197], v[58:61]
	v_mfma_f32_16x16x32_bf16 v[50:53], v[186:189], v[194:197], v[50:53]
	v_mfma_f32_16x16x32_bf16 v[42:45], v[178:181], v[202:205], v[42:45]
	v_mfma_f32_16x16x32_bf16 v[34:37], v[186:189], v[202:205], v[34:37]
	v_mfma_f32_16x16x32_bf16 v[26:29], v[178:181], v[210:213], v[26:29]
	v_mfma_f32_16x16x32_bf16 v[18:21], v[186:189], v[210:213], v[18:21]
	v_mfma_f32_16x16x32_bf16 v[10:13], v[178:181], v[218:221], v[10:13]
	v_mfma_f32_16x16x32_bf16 v[2:5], v[186:189], v[218:221], v[2:5]
	s_setprio 0
	s_barrier
	s_add_i32 s70, 0, 0x18000
	v_add_u32_e32 v148, s70, v151
	s_add_i32 s71, 0, 0x1c000
	ds_read_b128 v[142:145], v148
	ds_read_b128 v[156:159], v148 offset:1024
	ds_read_b128 v[160:163], v148 offset:2048
	ds_read_b128 v[170:173], v148 offset:3072
	v_add_u32_e32 v148, s71, v151
	ds_read_b128 v[174:177], v148
	ds_read_b128 v[178:181], v148 offset:1024
	ds_read_b128 v[182:185], v148 offset:2048
	ds_read_b128 v[186:189], v148 offset:3072
	s_add_u32 s60, s60, 0x40000
	s_addc_u32 s61, s61, 0
	s_mov_b32 m0, s21
	v_lshl_add_u64 v[234:235], s[60:61], 0, v[132:133]
	ds_read_b128 v[190:193], v154 offset:32768
	ds_read_b128 v[194:197], v154 offset:33792
	ds_read_b128 v[198:201], v154 offset:34816
	ds_read_b128 v[202:205], v154 offset:35840
	ds_read_b128 v[206:209], v154 offset:36864
	ds_read_b128 v[210:213], v154 offset:37888
	ds_read_b128 v[214:217], v154 offset:38912
	ds_read_b128 v[218:221], v154 offset:39936
	global_load_lds_dwordx4 v[234:235], off
	v_lshl_add_u64 v[234:235], s[60:61], 0, v[130:131]
	s_mov_b32 m0, s22
	s_nop 0
	global_load_lds_dwordx4 v[234:235], off
	s_waitcnt vmcnt(8)
	s_waitcnt lgkmcnt(0)
	s_barrier
	s_setprio 1
	v_mfma_f32_16x16x32_bf16 v[126:129], v[142:145], v[190:193], v[126:129]
	v_mfma_f32_16x16x32_bf16 v[118:121], v[160:163], v[190:193], v[118:121]
	v_mfma_f32_16x16x32_bf16 v[110:113], v[142:145], v[198:201], v[110:113]
	v_mfma_f32_16x16x32_bf16 v[102:105], v[160:163], v[198:201], v[102:105]
	v_mfma_f32_16x16x32_bf16 v[94:97], v[142:145], v[206:209], v[94:97]
	v_mfma_f32_16x16x32_bf16 v[86:89], v[160:163], v[206:209], v[86:89]
	v_mfma_f32_16x16x32_bf16 v[78:81], v[142:145], v[214:217], v[78:81]
	v_mfma_f32_16x16x32_bf16 v[70:73], v[160:163], v[214:217], v[70:73]
	v_mfma_f32_16x16x32_bf16 v[126:129], v[156:159], v[194:197], v[126:129]
	v_mfma_f32_16x16x32_bf16 v[118:121], v[170:173], v[194:197], v[118:121]
	v_mfma_f32_16x16x32_bf16 v[110:113], v[156:159], v[202:205], v[110:113]
	v_mfma_f32_16x16x32_bf16 v[102:105], v[170:173], v[202:205], v[102:105]
	v_mfma_f32_16x16x32_bf16 v[94:97], v[156:159], v[210:213], v[94:97]
	v_mfma_f32_16x16x32_bf16 v[86:89], v[170:173], v[210:213], v[86:89]
	v_mfma_f32_16x16x32_bf16 v[78:81], v[156:159], v[218:221], v[78:81]
	v_mfma_f32_16x16x32_bf16 v[70:73], v[170:173], v[218:221], v[70:73]
	s_setprio 0
	s_setprio 1
	v_mfma_f32_16x16x32_bf16 v[122:125], v[174:177], v[190:193], v[122:125]
	v_mfma_f32_16x16x32_bf16 v[114:117], v[182:185], v[190:193], v[114:117]
	v_mfma_f32_16x16x32_bf16 v[106:109], v[174:177], v[198:201], v[106:109]
	v_mfma_f32_16x16x32_bf16 v[98:101], v[182:185], v[198:201], v[98:101]
	v_mfma_f32_16x16x32_bf16 v[90:93], v[174:177], v[206:209], v[90:93]
	v_mfma_f32_16x16x32_bf16 v[82:85], v[182:185], v[206:209], v[82:85]
	v_mfma_f32_16x16x32_bf16 v[74:77], v[174:177], v[214:217], v[74:77]
	v_mfma_f32_16x16x32_bf16 v[66:69], v[182:185], v[214:217], v[66:69]
	v_mfma_f32_16x16x32_bf16 v[122:125], v[178:181], v[194:197], v[122:125]
	v_mfma_f32_16x16x32_bf16 v[114:117], v[186:189], v[194:197], v[114:117]
	v_mfma_f32_16x16x32_bf16 v[106:109], v[178:181], v[202:205], v[106:109]
	v_mfma_f32_16x16x32_bf16 v[98:101], v[186:189], v[202:205], v[98:101]
	v_mfma_f32_16x16x32_bf16 v[90:93], v[178:181], v[210:213], v[90:93]
	v_mfma_f32_16x16x32_bf16 v[82:85], v[186:189], v[210:213], v[82:85]
	v_mfma_f32_16x16x32_bf16 v[74:77], v[178:181], v[218:221], v[74:77]
	v_mfma_f32_16x16x32_bf16 v[66:69], v[186:189], v[218:221], v[66:69]
	s_setprio 0
	s_barrier
	s_add_i32 s60, s70, s14
	v_lshl_add_u64 v[146:147], v[146:147], 0, s[56:57]
	s_mov_b32 m0, s60
	ds_read_b128 v[190:193], v154 offset:49152
	ds_read_b128 v[194:197], v154 offset:50176
	ds_read_b128 v[198:201], v154 offset:51200
	ds_read_b128 v[202:205], v154 offset:52224
	ds_read_b128 v[206:209], v154 offset:53248
	ds_read_b128 v[210:213], v154 offset:54272
	ds_read_b128 v[214:217], v154 offset:55296
	ds_read_b128 v[218:221], v154 offset:56320
	global_load_lds_dwordx4 v[146:147], off
	s_add_i32 m0, s60, 0x2000
	s_add_u32 s58, s58, 0x40080
	v_lshl_add_u64 v[146:147], v[164:165], 0, s[56:57]
	s_addc_u32 s59, s59, 0
	s_add_i32 s60, s71, s14
	global_load_lds_dwordx4 v[146:147], off
	v_lshl_add_u64 v[146:147], s[58:59], 0, v[166:167]
	s_mov_b32 m0, s60
	s_nop 0
	global_load_lds_dwordx4 v[146:147], off
	v_lshl_add_u64 v[146:147], s[58:59], 0, v[134:135]
	s_add_i32 m0, s60, 0x2000
	s_nop 0
	global_load_lds_dwordx4 v[146:147], off
	v_lshl_add_u64 v[146:147], v[222:223], 0, s[56:57]
	s_mov_b32 m0, s23
	s_nop 0
	global_load_lds_dwordx4 v[146:147], off
	v_lshl_add_u64 v[146:147], v[232:233], 0, s[56:57]
	s_mov_b32 m0, s24
	s_nop 0
	global_load_lds_dwordx4 v[146:147], off
	s_waitcnt vmcnt(8)
	s_waitcnt lgkmcnt(0)
	s_barrier
	s_setprio 1
	v_mfma_f32_16x16x32_bf16 v[62:65], v[142:145], v[190:193], v[62:65]
	v_mfma_f32_16x16x32_bf16 v[54:57], v[160:163], v[190:193], v[54:57]
	v_mfma_f32_16x16x32_bf16 v[46:49], v[142:145], v[198:201], v[46:49]
	v_mfma_f32_16x16x32_bf16 v[38:41], v[160:163], v[198:201], v[38:41]
	v_mfma_f32_16x16x32_bf16 v[30:33], v[142:145], v[206:209], v[30:33]
	v_mfma_f32_16x16x32_bf16 v[22:25], v[160:163], v[206:209], v[22:25]
	v_mfma_f32_16x16x32_bf16 v[14:17], v[142:145], v[214:217], v[14:17]
	v_mfma_f32_16x16x32_bf16 v[6:9], v[160:163], v[214:217], v[6:9]
	v_mfma_f32_16x16x32_bf16 v[62:65], v[156:159], v[194:197], v[62:65]
	v_mfma_f32_16x16x32_bf16 v[54:57], v[170:173], v[194:197], v[54:57]
	v_mfma_f32_16x16x32_bf16 v[46:49], v[156:159], v[202:205], v[46:49]
	v_mfma_f32_16x16x32_bf16 v[38:41], v[170:173], v[202:205], v[38:41]
	v_mfma_f32_16x16x32_bf16 v[30:33], v[156:159], v[210:213], v[30:33]
	v_mfma_f32_16x16x32_bf16 v[22:25], v[170:173], v[210:213], v[22:25]
	v_mfma_f32_16x16x32_bf16 v[14:17], v[156:159], v[218:221], v[14:17]
	v_mfma_f32_16x16x32_bf16 v[6:9], v[170:173], v[218:221], v[6:9]
	s_setprio 0
	s_setprio 1
	v_mfma_f32_16x16x32_bf16 v[58:61], v[174:177], v[190:193], v[58:61]
	v_mfma_f32_16x16x32_bf16 v[50:53], v[182:185], v[190:193], v[50:53]
	v_mfma_f32_16x16x32_bf16 v[42:45], v[174:177], v[198:201], v[42:45]
	v_mfma_f32_16x16x32_bf16 v[34:37], v[182:185], v[198:201], v[34:37]
	v_mfma_f32_16x16x32_bf16 v[26:29], v[174:177], v[206:209], v[26:29]
	v_mfma_f32_16x16x32_bf16 v[18:21], v[182:185], v[206:209], v[18:21]
	v_mfma_f32_16x16x32_bf16 v[10:13], v[174:177], v[214:217], v[10:13]
	v_mfma_f32_16x16x32_bf16 v[2:5], v[182:185], v[214:217], v[2:5]
	v_mfma_f32_16x16x32_bf16 v[58:61], v[178:181], v[194:197], v[58:61]
	v_mfma_f32_16x16x32_bf16 v[50:53], v[186:189], v[194:197], v[50:53]
	v_mfma_f32_16x16x32_bf16 v[42:45], v[178:181], v[202:205], v[42:45]
	v_mfma_f32_16x16x32_bf16 v[34:37], v[186:189], v[202:205], v[34:37]
	v_mfma_f32_16x16x32_bf16 v[26:29], v[178:181], v[210:213], v[26:29]
	v_mfma_f32_16x16x32_bf16 v[18:21], v[186:189], v[210:213], v[18:21]
	v_mfma_f32_16x16x32_bf16 v[10:13], v[178:181], v[218:221], v[10:13]
	v_mfma_f32_16x16x32_bf16 v[2:5], v[186:189], v[218:221], v[2:5]
	s_setprio 0
	s_barrier
	s_add_u32 s66, s66, 0x100
	s_addc_u32 s68, s68, 0
	s_add_u32 s54, s54, 0x100
	s_addc_u32 s55, s55, 0
	s_cmp_ge_i32 s69, s13
	s_mov_b32 s58, s69
	s_cbranch_scc0 .LBB0_817

.Lpeelph7f_0:
	s_add_i32 s66, s54, 2
	s_add_u32 s55, s52, 0xfffe0080
	s_addc_u32 s58, s53, -1
	s_add_i32 s68, 0, 0x10000
	s_cmp_eq_u32 s51, s54
	s_cselect_b32 s59, s41, s58
	s_cselect_b32 s58, s43, s55
	s_cselect_b32 s55, s62, s65
	s_cselect_b32 s54, s63, s64
	s_add_i32 s69, 0, 0x14000
	v_add_u32_e32 v2, s68, v196
	v_add_u32_e32 v6, s69, v196
	ds_read_b128 v[26:29], v2
	ds_read_b128 v[30:33], v2 offset:1024
	ds_read_b128 v[18:21], v2 offset:2048
	ds_read_b128 v[22:25], v2 offset:3072
	ds_read_b128 v[10:13], v6
	ds_read_b128 v[14:17], v6 offset:1024
	ds_read_b128 v[2:5], v6 offset:2048
	ds_read_b128 v[6:9], v6 offset:3072
	v_lshl_add_u64 v[170:171], s[52:53], 0, v[184:185]
	s_add_i32 m0, s16, 0xc000
	ds_read_b128 v[186:189], v198
	ds_read_b128 v[190:193], v198 offset:1024
	ds_read_b128 v[200:203], v198 offset:2048
	ds_read_b128 v[204:207], v198 offset:3072
	ds_read_b128 v[208:211], v198 offset:4096
	ds_read_b128 v[212:215], v198 offset:5120
	ds_read_b128 v[216:219], v198 offset:6144
	ds_read_b128 v[220:223], v198 offset:7168
	global_load_lds_dwordx4 v[170:171], off
	v_lshl_add_u64 v[170:171], s[52:53], 0, v[182:183]
	s_add_i32 m0, s16, 0xe000
	s_nop 0
	global_load_lds_dwordx4 v[170:171], off
	s_waitcnt vmcnt(8)
	s_waitcnt lgkmcnt(0)
	s_barrier
	s_setprio 1
	v_mfma_scale_f32_16x16x128_f8f6f4 v[158:161], v[26:33], v[186:193], 0, v194, v169 op_sel_hi:[0,0,0]
	v_mfma_scale_f32_16x16x128_f8f6f4 v[150:153], v[18:25], v[186:193], 0, v194, v169 op_sel_hi:[0,0,0]
	v_mfma_scale_f32_16x16x128_f8f6f4 v[142:145], v[26:33], v[200:207], 0, v194, v169 op_sel_hi:[0,0,0]
	v_mfma_scale_f32_16x16x128_f8f6f4 v[134:137], v[18:25], v[200:207], 0, v194, v169 op_sel_hi:[0,0,0]
	v_mfma_scale_f32_16x16x128_f8f6f4 v[126:129], v[26:33], v[208:215], 0, v194, v169 op_sel_hi:[0,0,0]
	v_mfma_scale_f32_16x16x128_f8f6f4 v[118:121], v[18:25], v[208:215], 0, v194, v169 op_sel_hi:[0,0,0]
	v_mfma_scale_f32_16x16x128_f8f6f4 v[110:113], v[26:33], v[216:223], 0, v194, v169 op_sel_hi:[0,0,0]
	v_mfma_scale_f32_16x16x128_f8f6f4 v[102:105], v[18:25], v[216:223], 0, v194, v169 op_sel_hi:[0,0,0]
	s_setprio 0
	s_setprio 1
	v_mfma_scale_f32_16x16x128_f8f6f4 v[154:157], v[10:17], v[186:193], 0, v194, v169 op_sel_hi:[0,0,0]
	v_mfma_scale_f32_16x16x128_f8f6f4 v[146:149], v[2:9], v[186:193], 0, v194, v169 op_sel_hi:[0,0,0]
	v_mfma_scale_f32_16x16x128_f8f6f4 v[138:141], v[10:17], v[200:207], 0, v194, v169 op_sel_hi:[0,0,0]
	v_mfma_scale_f32_16x16x128_f8f6f4 v[130:133], v[2:9], v[200:207], 0, v194, v169 op_sel_hi:[0,0,0]
	v_mfma_scale_f32_16x16x128_f8f6f4 v[122:125], v[10:17], v[208:215], 0, v194, v169 op_sel_hi:[0,0,0]
	v_mfma_scale_f32_16x16x128_f8f6f4 v[114:117], v[2:9], v[208:215], 0, v194, v169 op_sel_hi:[0,0,0]
	v_mfma_scale_f32_16x16x128_f8f6f4 v[106:109], v[10:17], v[216:223], 0, v194, v169 op_sel_hi:[0,0,0]
	v_mfma_scale_f32_16x16x128_f8f6f4 v[98:101], v[2:9], v[216:223], 0, v194, v169 op_sel_hi:[0,0,0]
	s_setprio 0
	s_barrier
	s_add_i32 s68, s68, s14
	v_lshl_add_u64 v[186:187], s[54:55], 0, v[166:167]
	s_mov_b32 m0, s68
	ds_read_b128 v[200:203], v198 offset:16384
	ds_read_b128 v[204:207], v198 offset:17408
	ds_read_b128 v[208:211], v198 offset:18432
	ds_read_b128 v[212:215], v198 offset:19456
	ds_read_b128 v[216:219], v198 offset:20480
	ds_read_b128 v[220:223], v198 offset:21504
	ds_read_b128 v[236:239], v198 offset:22528
	ds_read_b128 v[240:243], v198 offset:23552
	global_load_lds_dwordx4 v[186:187], off
	s_add_i32 m0, s68, 0x2000
	s_add_u32 s70, s54, 0x20000
	v_lshl_add_u64 v[188:189], s[54:55], 0, v[178:179]
	s_addc_u32 s71, s55, 0
	s_add_i32 s68, s69, s14
	global_load_lds_dwordx4 v[188:189], off
	v_lshl_add_u64 v[170:171], s[70:71], 0, v[166:167]
	s_mov_b32 m0, s68
	v_lshl_add_u64 v[190:191], s[58:59], 0, v[164:165]
	global_load_lds_dwordx4 v[170:171], off
	v_lshl_add_u64 v[170:171], s[70:71], 0, v[178:179]
	s_add_i32 m0, s68, 0x2000
	v_lshl_add_u64 v[192:193], s[58:59], 0, v[162:163]
	global_load_lds_dwordx4 v[170:171], off
	s_mov_b32 m0, s16
	s_nop 0
	global_load_lds_dwordx4 v[190:191], off
	s_mov_b32 m0, s20
	s_nop 0
	global_load_lds_dwordx4 v[192:193], off
	s_waitcnt vmcnt(8)
	s_waitcnt lgkmcnt(0)
	s_barrier
	s_setprio 1
	v_mfma_scale_f32_16x16x128_f8f6f4 v[94:97], v[26:33], v[200:207], 0, v194, v169 op_sel_hi:[0,0,0]
	v_mfma_scale_f32_16x16x128_f8f6f4 v[86:89], v[18:25], v[200:207], 0, v194, v169 op_sel_hi:[0,0,0]
	v_mfma_scale_f32_16x16x128_f8f6f4 v[78:81], v[26:33], v[208:215], 0, v194, v169 op_sel_hi:[0,0,0]
	v_mfma_scale_f32_16x16x128_f8f6f4 v[70:73], v[18:25], v[208:215], 0, v194, v169 op_sel_hi:[0,0,0]
	v_mfma_scale_f32_16x16x128_f8f6f4 v[62:65], v[26:33], v[216:223], 0, v194, v169 op_sel_hi:[0,0,0]
	v_mfma_scale_f32_16x16x128_f8f6f4 v[54:57], v[18:25], v[216:223], 0, v194, v169 op_sel_hi:[0,0,0]
	v_mfma_scale_f32_16x16x128_f8f6f4 v[46:49], v[26:33], v[236:243], 0, v194, v169 op_sel_hi:[0,0,0]
	v_mfma_scale_f32_16x16x128_f8f6f4 v[38:41], v[18:25], v[236:243], 0, v194, v169 op_sel_hi:[0,0,0]
	s_setprio 0
	s_setprio 1
	v_mfma_scale_f32_16x16x128_f8f6f4 v[90:93], v[10:17], v[200:207], 0, v194, v169 op_sel_hi:[0,0,0]
	v_mfma_scale_f32_16x16x128_f8f6f4 v[82:85], v[2:9], v[200:207], 0, v194, v169 op_sel_hi:[0,0,0]
	v_mfma_scale_f32_16x16x128_f8f6f4 v[74:77], v[10:17], v[208:215], 0, v194, v169 op_sel_hi:[0,0,0]
	v_mfma_scale_f32_16x16x128_f8f6f4 v[66:69], v[2:9], v[208:215], 0, v194, v169 op_sel_hi:[0,0,0]
	v_mfma_scale_f32_16x16x128_f8f6f4 v[58:61], v[10:17], v[216:223], 0, v194, v169 op_sel_hi:[0,0,0]
	v_mfma_scale_f32_16x16x128_f8f6f4 v[50:53], v[2:9], v[216:223], 0, v194, v169 op_sel_hi:[0,0,0]
	v_mfma_scale_f32_16x16x128_f8f6f4 v[42:45], v[10:17], v[236:243], 0, v194, v169 op_sel_hi:[0,0,0]
	v_mfma_scale_f32_16x16x128_f8f6f4 v[34:37], v[2:9], v[236:243], 0, v194, v169 op_sel_hi:[0,0,0]
	s_setprio 0
	s_barrier
	s_add_i32 s68, 0, 0x18000
	s_add_i32 s69, 0, 0x1c000
	v_add_u32_e32 v2, s68, v196
	v_add_u32_e32 v6, s69, v196
	ds_read_b128 v[26:29], v2
	ds_read_b128 v[30:33], v2 offset:1024
	ds_read_b128 v[18:21], v2 offset:2048
	ds_read_b128 v[22:25], v2 offset:3072
	ds_read_b128 v[10:13], v6
	ds_read_b128 v[14:17], v6 offset:1024
	ds_read_b128 v[2:5], v6 offset:2048
	ds_read_b128 v[6:9], v6 offset:3072
	s_add_u32 s58, s58, 0x20000
	s_addc_u32 s59, s59, 0
	s_mov_b32 m0, s21
	v_lshl_add_u64 v[170:171], s[58:59], 0, v[164:165]
	ds_read_b128 v[200:203], v198 offset:32768
	ds_read_b128 v[204:207], v198 offset:33792
	ds_read_b128 v[208:211], v198 offset:34816
	ds_read_b128 v[212:215], v198 offset:35840
	ds_read_b128 v[216:219], v198 offset:36864
	ds_read_b128 v[220:223], v198 offset:37888
	ds_read_b128 v[236:239], v198 offset:38912
	ds_read_b128 v[240:243], v198 offset:39936
	global_load_lds_dwordx4 v[170:171], off
	v_lshl_add_u64 v[170:171], s[58:59], 0, v[162:163]
	s_mov_b32 m0, s22
	s_nop 0
	global_load_lds_dwordx4 v[170:171], off
	s_waitcnt vmcnt(8)
	s_waitcnt lgkmcnt(0)
	s_barrier
	s_setprio 1
	v_mfma_scale_f32_16x16x128_f8f6f4 v[158:161], v[26:33], v[200:207], v[158:161], v194, v169 op_sel_hi:[0,0,0]
	v_mfma_scale_f32_16x16x128_f8f6f4 v[150:153], v[18:25], v[200:207], v[150:153], v194, v169 op_sel_hi:[0,0,0]
	v_mfma_scale_f32_16x16x128_f8f6f4 v[142:145], v[26:33], v[208:215], v[142:145], v194, v169 op_sel_hi:[0,0,0]
	v_mfma_scale_f32_16x16x128_f8f6f4 v[134:137], v[18:25], v[208:215], v[134:137], v194, v169 op_sel_hi:[0,0,0]
	v_mfma_scale_f32_16x16x128_f8f6f4 v[126:129], v[26:33], v[216:223], v[126:129], v194, v169 op_sel_hi:[0,0,0]
	v_mfma_scale_f32_16x16x128_f8f6f4 v[118:121], v[18:25], v[216:223], v[118:121], v194, v169 op_sel_hi:[0,0,0]
	v_mfma_scale_f32_16x16x128_f8f6f4 v[110:113], v[26:33], v[236:243], v[110:113], v194, v169 op_sel_hi:[0,0,0]
	v_mfma_scale_f32_16x16x128_f8f6f4 v[102:105], v[18:25], v[236:243], v[102:105], v194, v169 op_sel_hi:[0,0,0]
	s_setprio 0
	s_setprio 1
	v_mfma_scale_f32_16x16x128_f8f6f4 v[154:157], v[10:17], v[200:207], v[154:157], v194, v169 op_sel_hi:[0,0,0]
	v_mfma_scale_f32_16x16x128_f8f6f4 v[146:149], v[2:9], v[200:207], v[146:149], v194, v169 op_sel_hi:[0,0,0]
	v_mfma_scale_f32_16x16x128_f8f6f4 v[138:141], v[10:17], v[208:215], v[138:141], v194, v169 op_sel_hi:[0,0,0]
	v_mfma_scale_f32_16x16x128_f8f6f4 v[130:133], v[2:9], v[208:215], v[130:133], v194, v169 op_sel_hi:[0,0,0]
	v_mfma_scale_f32_16x16x128_f8f6f4 v[122:125], v[10:17], v[216:223], v[122:125], v194, v169 op_sel_hi:[0,0,0]
	v_mfma_scale_f32_16x16x128_f8f6f4 v[114:117], v[2:9], v[216:223], v[114:117], v194, v169 op_sel_hi:[0,0,0]
	v_mfma_scale_f32_16x16x128_f8f6f4 v[106:109], v[10:17], v[236:243], v[106:109], v194, v169 op_sel_hi:[0,0,0]
	v_mfma_scale_f32_16x16x128_f8f6f4 v[98:101], v[2:9], v[236:243], v[98:101], v194, v169 op_sel_hi:[0,0,0]
	s_setprio 0
	s_barrier
	s_add_i32 s58, s68, s14
	v_lshl_add_u64 v[170:171], v[186:187], 0, s[56:57]
	s_mov_b32 m0, s58
	ds_read_b128 v[200:203], v198 offset:49152
	ds_read_b128 v[204:207], v198 offset:50176
	ds_read_b128 v[208:211], v198 offset:51200
	ds_read_b128 v[212:215], v198 offset:52224
	ds_read_b128 v[216:219], v198 offset:53248
	ds_read_b128 v[220:223], v198 offset:54272
	ds_read_b128 v[236:239], v198 offset:55296
	ds_read_b128 v[240:243], v198 offset:56320
	global_load_lds_dwordx4 v[170:171], off
	s_add_i32 m0, s58, 0x2000
	s_add_u32 s54, s54, 0x20080
	v_lshl_add_u64 v[170:171], v[188:189], 0, s[56:57]
	s_addc_u32 s55, s55, 0
	s_add_i32 s58, s69, s14
	global_load_lds_dwordx4 v[170:171], off
	v_lshl_add_u64 v[170:171], s[54:55], 0, v[166:167]
	s_mov_b32 m0, s58
	s_nop 0
	global_load_lds_dwordx4 v[170:171], off
	v_lshl_add_u64 v[170:171], s[54:55], 0, v[178:179]
	s_add_i32 m0, s58, 0x2000
	s_nop 0
	global_load_lds_dwordx4 v[170:171], off
	v_lshl_add_u64 v[170:171], v[190:191], 0, s[56:57]
	s_mov_b32 m0, s23
	s_nop 0
	global_load_lds_dwordx4 v[170:171], off
	v_lshl_add_u64 v[170:171], v[192:193], 0, s[56:57]
	s_mov_b32 m0, s24
	s_nop 0
	global_load_lds_dwordx4 v[170:171], off
	s_waitcnt vmcnt(8)
	s_waitcnt lgkmcnt(0)
	s_barrier
	s_setprio 1
	v_mfma_scale_f32_16x16x128_f8f6f4 v[94:97], v[26:33], v[200:207], v[94:97], v194, v169 op_sel_hi:[0,0,0]
	v_mfma_scale_f32_16x16x128_f8f6f4 v[86:89], v[18:25], v[200:207], v[86:89], v194, v169 op_sel_hi:[0,0,0]
	v_mfma_scale_f32_16x16x128_f8f6f4 v[78:81], v[26:33], v[208:215], v[78:81], v194, v169 op_sel_hi:[0,0,0]
	v_mfma_scale_f32_16x16x128_f8f6f4 v[70:73], v[18:25], v[208:215], v[70:73], v194, v169 op_sel_hi:[0,0,0]
	v_mfma_scale_f32_16x16x128_f8f6f4 v[62:65], v[26:33], v[216:223], v[62:65], v194, v169 op_sel_hi:[0,0,0]
	v_mfma_scale_f32_16x16x128_f8f6f4 v[54:57], v[18:25], v[216:223], v[54:57], v194, v169 op_sel_hi:[0,0,0]
	v_mfma_scale_f32_16x16x128_f8f6f4 v[46:49], v[26:33], v[236:243], v[46:49], v194, v169 op_sel_hi:[0,0,0]
	v_mfma_scale_f32_16x16x128_f8f6f4 v[38:41], v[18:25], v[236:243], v[38:41], v194, v169 op_sel_hi:[0,0,0]
	s_setprio 0
	s_setprio 1
	v_mfma_scale_f32_16x16x128_f8f6f4 v[90:93], v[10:17], v[200:207], v[90:93], v194, v169 op_sel_hi:[0,0,0]
	v_mfma_scale_f32_16x16x128_f8f6f4 v[82:85], v[2:9], v[200:207], v[82:85], v194, v169 op_sel_hi:[0,0,0]
	v_mfma_scale_f32_16x16x128_f8f6f4 v[74:77], v[10:17], v[208:215], v[74:77], v194, v169 op_sel_hi:[0,0,0]
	v_mfma_scale_f32_16x16x128_f8f6f4 v[66:69], v[2:9], v[208:215], v[66:69], v194, v169 op_sel_hi:[0,0,0]
	v_mfma_scale_f32_16x16x128_f8f6f4 v[58:61], v[10:17], v[216:223], v[58:61], v194, v169 op_sel_hi:[0,0,0]
	v_mfma_scale_f32_16x16x128_f8f6f4 v[50:53], v[2:9], v[216:223], v[50:53], v194, v169 op_sel_hi:[0,0,0]
	v_mfma_scale_f32_16x16x128_f8f6f4 v[42:45], v[10:17], v[236:243], v[42:45], v194, v169 op_sel_hi:[0,0,0]
	v_mfma_scale_f32_16x16x128_f8f6f4 v[34:37], v[2:9], v[236:243], v[34:37], v194, v169 op_sel_hi:[0,0,0]
	s_setprio 0
	s_barrier
	s_add_u32 s64, s64, 0x100
	s_addc_u32 s65, s65, 0
	s_add_u32 s52, s52, 0x100
	s_addc_u32 s53, s53, 0
	s_cmp_ge_i32 s66, s13
	s_mov_b32 s54, s66
	s_cbranch_scc0 .LBB0_842
	s_branch .Lpeelexitph7f
.LBB0_842:
	s_add_i32 s66, s54, 2
	s_add_u32 s55, s52, 0xfffe0080
	s_addc_u32 s58, s53, -1
	s_add_i32 s68, 0, 0x10000
	s_cmp_eq_u32 s51, s54
	s_cselect_b32 s59, s41, s58
	s_cselect_b32 s58, s43, s55
	s_cselect_b32 s55, s62, s65
	s_cselect_b32 s54, s63, s64
	s_add_i32 s69, 0, 0x14000
	v_add_u32_e32 v2, s68, v196
	v_add_u32_e32 v6, s69, v196
	ds_read_b128 v[26:29], v2
	ds_read_b128 v[30:33], v2 offset:1024
	ds_read_b128 v[18:21], v2 offset:2048
	ds_read_b128 v[22:25], v2 offset:3072
	ds_read_b128 v[10:13], v6
	ds_read_b128 v[14:17], v6 offset:1024
	ds_read_b128 v[2:5], v6 offset:2048
	ds_read_b128 v[6:9], v6 offset:3072
	v_lshl_add_u64 v[170:171], s[52:53], 0, v[184:185]
	s_add_i32 m0, s16, 0xc000
	ds_read_b128 v[186:189], v198
	ds_read_b128 v[190:193], v198 offset:1024
	ds_read_b128 v[200:203], v198 offset:2048
	ds_read_b128 v[204:207], v198 offset:3072
	ds_read_b128 v[208:211], v198 offset:4096
	ds_read_b128 v[212:215], v198 offset:5120
	ds_read_b128 v[216:219], v198 offset:6144
	ds_read_b128 v[220:223], v198 offset:7168
	global_load_lds_dwordx4 v[170:171], off
	v_lshl_add_u64 v[170:171], s[52:53], 0, v[182:183]
	s_add_i32 m0, s16, 0xe000
	s_nop 0
	global_load_lds_dwordx4 v[170:171], off
	s_waitcnt vmcnt(8)
	s_waitcnt lgkmcnt(0)
	s_barrier
	s_setprio 1
	v_mfma_scale_f32_16x16x128_f8f6f4 v[158:161], v[26:33], v[186:193], v[158:161], v194, v169 op_sel_hi:[0,0,0]
	v_mfma_scale_f32_16x16x128_f8f6f4 v[150:153], v[18:25], v[186:193], v[150:153], v194, v169 op_sel_hi:[0,0,0]
	v_mfma_scale_f32_16x16x128_f8f6f4 v[142:145], v[26:33], v[200:207], v[142:145], v194, v169 op_sel_hi:[0,0,0]
	v_mfma_scale_f32_16x16x128_f8f6f4 v[134:137], v[18:25], v[200:207], v[134:137], v194, v169 op_sel_hi:[0,0,0]
	v_mfma_scale_f32_16x16x128_f8f6f4 v[126:129], v[26:33], v[208:215], v[126:129], v194, v169 op_sel_hi:[0,0,0]
	v_mfma_scale_f32_16x16x128_f8f6f4 v[118:121], v[18:25], v[208:215], v[118:121], v194, v169 op_sel_hi:[0,0,0]
	v_mfma_scale_f32_16x16x128_f8f6f4 v[110:113], v[26:33], v[216:223], v[110:113], v194, v169 op_sel_hi:[0,0,0]
	v_mfma_scale_f32_16x16x128_f8f6f4 v[102:105], v[18:25], v[216:223], v[102:105], v194, v169 op_sel_hi:[0,0,0]
	s_setprio 0
	s_setprio 1
	v_mfma_scale_f32_16x16x128_f8f6f4 v[154:157], v[10:17], v[186:193], v[154:157], v194, v169 op_sel_hi:[0,0,0]
	v_mfma_scale_f32_16x16x128_f8f6f4 v[146:149], v[2:9], v[186:193], v[146:149], v194, v169 op_sel_hi:[0,0,0]
	v_mfma_scale_f32_16x16x128_f8f6f4 v[138:141], v[10:17], v[200:207], v[138:141], v194, v169 op_sel_hi:[0,0,0]
	v_mfma_scale_f32_16x16x128_f8f6f4 v[130:133], v[2:9], v[200:207], v[130:133], v194, v169 op_sel_hi:[0,0,0]
	v_mfma_scale_f32_16x16x128_f8f6f4 v[122:125], v[10:17], v[208:215], v[122:125], v194, v169 op_sel_hi:[0,0,0]
	v_mfma_scale_f32_16x16x128_f8f6f4 v[114:117], v[2:9], v[208:215], v[114:117], v194, v169 op_sel_hi:[0,0,0]
	v_mfma_scale_f32_16x16x128_f8f6f4 v[106:109], v[10:17], v[216:223], v[106:109], v194, v169 op_sel_hi:[0,0,0]
	v_mfma_scale_f32_16x16x128_f8f6f4 v[98:101], v[2:9], v[216:223], v[98:101], v194, v169 op_sel_hi:[0,0,0]
	s_setprio 0
	s_barrier
	s_add_i32 s68, s68, s14
	v_lshl_add_u64 v[186:187], s[54:55], 0, v[166:167]
	s_mov_b32 m0, s68
	ds_read_b128 v[200:203], v198 offset:16384
	ds_read_b128 v[204:207], v198 offset:17408
	ds_read_b128 v[208:211], v198 offset:18432
	ds_read_b128 v[212:215], v198 offset:19456
	ds_read_b128 v[216:219], v198 offset:20480
	ds_read_b128 v[220:223], v198 offset:21504
	ds_read_b128 v[236:239], v198 offset:22528
	ds_read_b128 v[240:243], v198 offset:23552
	global_load_lds_dwordx4 v[186:187], off
	s_add_i32 m0, s68, 0x2000
	s_add_u32 s70, s54, 0x20000
	v_lshl_add_u64 v[188:189], s[54:55], 0, v[178:179]
	s_addc_u32 s71, s55, 0
	s_add_i32 s68, s69, s14
	global_load_lds_dwordx4 v[188:189], off
	v_lshl_add_u64 v[170:171], s[70:71], 0, v[166:167]
	s_mov_b32 m0, s68
	v_lshl_add_u64 v[190:191], s[58:59], 0, v[164:165]
	global_load_lds_dwordx4 v[170:171], off
	v_lshl_add_u64 v[170:171], s[70:71], 0, v[178:179]
	s_add_i32 m0, s68, 0x2000
	v_lshl_add_u64 v[192:193], s[58:59], 0, v[162:163]
	global_load_lds_dwordx4 v[170:171], off
	s_mov_b32 m0, s16
	s_nop 0
	global_load_lds_dwordx4 v[190:191], off
	s_mov_b32 m0, s20
	s_nop 0
	global_load_lds_dwordx4 v[192:193], off
	s_waitcnt vmcnt(8)
	s_waitcnt lgkmcnt(0)
	s_barrier
	s_setprio 1
	v_mfma_scale_f32_16x16x128_f8f6f4 v[94:97], v[26:33], v[200:207], v[94:97], v194, v169 op_sel_hi:[0,0,0]
	v_mfma_scale_f32_16x16x128_f8f6f4 v[86:89], v[18:25], v[200:207], v[86:89], v194, v169 op_sel_hi:[0,0,0]
	v_mfma_scale_f32_16x16x128_f8f6f4 v[78:81], v[26:33], v[208:215], v[78:81], v194, v169 op_sel_hi:[0,0,0]
	v_mfma_scale_f32_16x16x128_f8f6f4 v[70:73], v[18:25], v[208:215], v[70:73], v194, v169 op_sel_hi:[0,0,0]
	v_mfma_scale_f32_16x16x128_f8f6f4 v[62:65], v[26:33], v[216:223], v[62:65], v194, v169 op_sel_hi:[0,0,0]
	v_mfma_scale_f32_16x16x128_f8f6f4 v[54:57], v[18:25], v[216:223], v[54:57], v194, v169 op_sel_hi:[0,0,0]
	v_mfma_scale_f32_16x16x128_f8f6f4 v[46:49], v[26:33], v[236:243], v[46:49], v194, v169 op_sel_hi:[0,0,0]
	v_mfma_scale_f32_16x16x128_f8f6f4 v[38:41], v[18:25], v[236:243], v[38:41], v194, v169 op_sel_hi:[0,0,0]
	s_setprio 0
	s_setprio 1
	v_mfma_scale_f32_16x16x128_f8f6f4 v[90:93], v[10:17], v[200:207], v[90:93], v194, v169 op_sel_hi:[0,0,0]
	v_mfma_scale_f32_16x16x128_f8f6f4 v[82:85], v[2:9], v[200:207], v[82:85], v194, v169 op_sel_hi:[0,0,0]
	v_mfma_scale_f32_16x16x128_f8f6f4 v[74:77], v[10:17], v[208:215], v[74:77], v194, v169 op_sel_hi:[0,0,0]
	v_mfma_scale_f32_16x16x128_f8f6f4 v[66:69], v[2:9], v[208:215], v[66:69], v194, v169 op_sel_hi:[0,0,0]
	v_mfma_scale_f32_16x16x128_f8f6f4 v[58:61], v[10:17], v[216:223], v[58:61], v194, v169 op_sel_hi:[0,0,0]
	v_mfma_scale_f32_16x16x128_f8f6f4 v[50:53], v[2:9], v[216:223], v[50:53], v194, v169 op_sel_hi:[0,0,0]
	v_mfma_scale_f32_16x16x128_f8f6f4 v[42:45], v[10:17], v[236:243], v[42:45], v194, v169 op_sel_hi:[0,0,0]
	v_mfma_scale_f32_16x16x128_f8f6f4 v[34:37], v[2:9], v[236:243], v[34:37], v194, v169 op_sel_hi:[0,0,0]
	s_setprio 0
	s_barrier
	s_add_i32 s68, 0, 0x18000
	s_add_i32 s69, 0, 0x1c000
	v_add_u32_e32 v2, s68, v196
	v_add_u32_e32 v6, s69, v196
	ds_read_b128 v[26:29], v2
	ds_read_b128 v[30:33], v2 offset:1024
	ds_read_b128 v[18:21], v2 offset:2048
	ds_read_b128 v[22:25], v2 offset:3072
	ds_read_b128 v[10:13], v6
	ds_read_b128 v[14:17], v6 offset:1024
	ds_read_b128 v[2:5], v6 offset:2048
	ds_read_b128 v[6:9], v6 offset:3072
	s_add_u32 s58, s58, 0x20000
	s_addc_u32 s59, s59, 0
	s_mov_b32 m0, s21
	v_lshl_add_u64 v[170:171], s[58:59], 0, v[164:165]
	ds_read_b128 v[200:203], v198 offset:32768
	ds_read_b128 v[204:207], v198 offset:33792
	ds_read_b128 v[208:211], v198 offset:34816
	ds_read_b128 v[212:215], v198 offset:35840
	ds_read_b128 v[216:219], v198 offset:36864
	ds_read_b128 v[220:223], v198 offset:37888
	ds_read_b128 v[236:239], v198 offset:38912
	ds_read_b128 v[240:243], v198 offset:39936
	global_load_lds_dwordx4 v[170:171], off
	v_lshl_add_u64 v[170:171], s[58:59], 0, v[162:163]
	s_mov_b32 m0, s22
	s_nop 0
	global_load_lds_dwordx4 v[170:171], off
	s_waitcnt vmcnt(8)
	s_waitcnt lgkmcnt(0)
	s_barrier
	s_setprio 1
	v_mfma_scale_f32_16x16x128_f8f6f4 v[158:161], v[26:33], v[200:207], v[158:161], v194, v169 op_sel_hi:[0,0,0]
	v_mfma_scale_f32_16x16x128_f8f6f4 v[150:153], v[18:25], v[200:207], v[150:153], v194, v169 op_sel_hi:[0,0,0]
	v_mfma_scale_f32_16x16x128_f8f6f4 v[142:145], v[26:33], v[208:215], v[142:145], v194, v169 op_sel_hi:[0,0,0]
	v_mfma_scale_f32_16x16x128_f8f6f4 v[134:137], v[18:25], v[208:215], v[134:137], v194, v169 op_sel_hi:[0,0,0]
	v_mfma_scale_f32_16x16x128_f8f6f4 v[126:129], v[26:33], v[216:223], v[126:129], v194, v169 op_sel_hi:[0,0,0]
	v_mfma_scale_f32_16x16x128_f8f6f4 v[118:121], v[18:25], v[216:223], v[118:121], v194, v169 op_sel_hi:[0,0,0]
	v_mfma_scale_f32_16x16x128_f8f6f4 v[110:113], v[26:33], v[236:243], v[110:113], v194, v169 op_sel_hi:[0,0,0]
	v_mfma_scale_f32_16x16x128_f8f6f4 v[102:105], v[18:25], v[236:243], v[102:105], v194, v169 op_sel_hi:[0,0,0]
	s_setprio 0
	s_setprio 1
	v_mfma_scale_f32_16x16x128_f8f6f4 v[154:157], v[10:17], v[200:207], v[154:157], v194, v169 op_sel_hi:[0,0,0]
	v_mfma_scale_f32_16x16x128_f8f6f4 v[146:149], v[2:9], v[200:207], v[146:149], v194, v169 op_sel_hi:[0,0,0]
	v_mfma_scale_f32_16x16x128_f8f6f4 v[138:141], v[10:17], v[208:215], v[138:141], v194, v169 op_sel_hi:[0,0,0]
	v_mfma_scale_f32_16x16x128_f8f6f4 v[130:133], v[2:9], v[208:215], v[130:133], v194, v169 op_sel_hi:[0,0,0]
	v_mfma_scale_f32_16x16x128_f8f6f4 v[122:125], v[10:17], v[216:223], v[122:125], v194, v169 op_sel_hi:[0,0,0]
	v_mfma_scale_f32_16x16x128_f8f6f4 v[114:117], v[2:9], v[216:223], v[114:117], v194, v169 op_sel_hi:[0,0,0]
	v_mfma_scale_f32_16x16x128_f8f6f4 v[106:109], v[10:17], v[236:243], v[106:109], v194, v169 op_sel_hi:[0,0,0]
	v_mfma_scale_f32_16x16x128_f8f6f4 v[98:101], v[2:9], v[236:243], v[98:101], v194, v169 op_sel_hi:[0,0,0]
	s_setprio 0
	s_barrier
	s_add_i32 s58, s68, s14
	v_lshl_add_u64 v[170:171], v[186:187], 0, s[56:57]
	s_mov_b32 m0, s58
	ds_read_b128 v[200:203], v198 offset:49152
	ds_read_b128 v[204:207], v198 offset:50176
	ds_read_b128 v[208:211], v198 offset:51200
	ds_read_b128 v[212:215], v198 offset:52224
	ds_read_b128 v[216:219], v198 offset:53248
	ds_read_b128 v[220:223], v198 offset:54272
	ds_read_b128 v[236:239], v198 offset:55296
	ds_read_b128 v[240:243], v198 offset:56320
	global_load_lds_dwordx4 v[170:171], off
	s_add_i32 m0, s58, 0x2000
	s_add_u32 s54, s54, 0x20080
	v_lshl_add_u64 v[170:171], v[188:189], 0, s[56:57]
	s_addc_u32 s55, s55, 0
	s_add_i32 s58, s69, s14
	global_load_lds_dwordx4 v[170:171], off
	v_lshl_add_u64 v[170:171], s[54:55], 0, v[166:167]
	s_mov_b32 m0, s58
	s_nop 0
	global_load_lds_dwordx4 v[170:171], off
	v_lshl_add_u64 v[170:171], s[54:55], 0, v[178:179]
	s_add_i32 m0, s58, 0x2000
	s_nop 0
	global_load_lds_dwordx4 v[170:171], off
	v_lshl_add_u64 v[170:171], v[190:191], 0, s[56:57]
	s_mov_b32 m0, s23
	s_nop 0
	global_load_lds_dwordx4 v[170:171], off
	v_lshl_add_u64 v[170:171], v[192:193], 0, s[56:57]
	s_mov_b32 m0, s24
	s_nop 0
	global_load_lds_dwordx4 v[170:171], off
	s_waitcnt vmcnt(8)
	s_waitcnt lgkmcnt(0)
	s_barrier
	s_setprio 1
	v_mfma_scale_f32_16x16x128_f8f6f4 v[94:97], v[26:33], v[200:207], v[94:97], v194, v169 op_sel_hi:[0,0,0]
	v_mfma_scale_f32_16x16x128_f8f6f4 v[86:89], v[18:25], v[200:207], v[86:89], v194, v169 op_sel_hi:[0,0,0]
	v_mfma_scale_f32_16x16x128_f8f6f4 v[78:81], v[26:33], v[208:215], v[78:81], v194, v169 op_sel_hi:[0,0,0]
	v_mfma_scale_f32_16x16x128_f8f6f4 v[70:73], v[18:25], v[208:215], v[70:73], v194, v169 op_sel_hi:[0,0,0]
	v_mfma_scale_f32_16x16x128_f8f6f4 v[62:65], v[26:33], v[216:223], v[62:65], v194, v169 op_sel_hi:[0,0,0]
	v_mfma_scale_f32_16x16x128_f8f6f4 v[54:57], v[18:25], v[216:223], v[54:57], v194, v169 op_sel_hi:[0,0,0]
	v_mfma_scale_f32_16x16x128_f8f6f4 v[46:49], v[26:33], v[236:243], v[46:49], v194, v169 op_sel_hi:[0,0,0]
	v_mfma_scale_f32_16x16x128_f8f6f4 v[38:41], v[18:25], v[236:243], v[38:41], v194, v169 op_sel_hi:[0,0,0]
	s_setprio 0
	s_setprio 1
	v_mfma_scale_f32_16x16x128_f8f6f4 v[90:93], v[10:17], v[200:207], v[90:93], v194, v169 op_sel_hi:[0,0,0]
	v_mfma_scale_f32_16x16x128_f8f6f4 v[82:85], v[2:9], v[200:207], v[82:85], v194, v169 op_sel_hi:[0,0,0]
	v_mfma_scale_f32_16x16x128_f8f6f4 v[74:77], v[10:17], v[208:215], v[74:77], v194, v169 op_sel_hi:[0,0,0]
	v_mfma_scale_f32_16x16x128_f8f6f4 v[66:69], v[2:9], v[208:215], v[66:69], v194, v169 op_sel_hi:[0,0,0]
	v_mfma_scale_f32_16x16x128_f8f6f4 v[58:61], v[10:17], v[216:223], v[58:61], v194, v169 op_sel_hi:[0,0,0]
	v_mfma_scale_f32_16x16x128_f8f6f4 v[50:53], v[2:9], v[216:223], v[50:53], v194, v169 op_sel_hi:[0,0,0]
	v_mfma_scale_f32_16x16x128_f8f6f4 v[42:45], v[10:17], v[236:243], v[42:45], v194, v169 op_sel_hi:[0,0,0]
	v_mfma_scale_f32_16x16x128_f8f6f4 v[34:37], v[2:9], v[236:243], v[34:37], v194, v169 op_sel_hi:[0,0,0]
	s_setprio 0
	s_barrier
	s_add_u32 s64, s64, 0x100
	s_addc_u32 s65, s65, 0
	s_add_u32 s52, s52, 0x100
	s_addc_u32 s53, s53, 0
	s_cmp_ge_i32 s66, s13
	s_mov_b32 s54, s66
	s_cbranch_scc0 .LBB0_842

.Lpeelph8_0:
	s_add_i32 s75, s62, 2
	s_add_u32 s60, s58, 0x100
	s_addc_u32 s61, s59, 0
	s_add_i32 s76, 0, 0x10000
	s_cmp_eq_u32 s68, s62
	s_cselect_b32 s65, s53, s61
	s_cselect_b32 s64, s52, s60
	s_cselect_b32 s63, s55, s74
	s_cselect_b32 s62, s54, s73
	s_add_i32 s77, 0, 0x14000
	v_add_u32_e32 v2, s76, v200
	v_add_u32_e32 v6, s77, v200
	ds_read_b128 v[26:29], v2
	ds_read_b128 v[30:33], v2 offset:1024
	ds_read_b128 v[18:21], v2 offset:2048
	ds_read_b128 v[22:25], v2 offset:3072
	ds_read_b128 v[10:13], v6
	ds_read_b128 v[14:17], v6 offset:1024
	s_waitcnt lgkmcnt(0)
	ds_read_b128 v[2:5], v6 offset:2048
	ds_read_b128 v[6:9], v6 offset:3072
	v_lshl_add_u64 v[170:171], s[58:59], 0, v[184:185]
	s_add_i32 m0, s15, 0xc000
	ds_read_b128 v[186:189], v204
	ds_read_b128 v[190:193], v204 offset:1024
	ds_read_b128 v[206:209], v204 offset:2048
	ds_read_b128 v[210:213], v204 offset:3072
	ds_read_b128 v[214:217], v204 offset:4096
	ds_read_b128 v[218:221], v204 offset:5120
	ds_read_b128 v[236:239], v204 offset:6144
	ds_read_b128 v[240:243], v204 offset:7168
	global_load_lds_dwordx4 v[170:171], off
	v_lshl_add_u64 v[170:171], s[58:59], 0, v[182:183]
	s_add_i32 m0, s15, 0xe000
	s_nop 0
	global_load_lds_dwordx4 v[170:171], off
	s_waitcnt vmcnt(8)
	s_waitcnt lgkmcnt(0)
	s_barrier
	s_setprio 1
	v_mfma_scale_f32_16x16x128_f8f6f4 v[158:161], v[26:33], v[186:193], 0, v198, v169 op_sel_hi:[0,0,0]
	v_mfma_scale_f32_16x16x128_f8f6f4 v[154:157], v[18:25], v[186:193], 0, v198, v169 op_sel_hi:[0,0,0]
	v_mfma_scale_f32_16x16x128_f8f6f4 v[142:145], v[26:33], v[206:213], 0, v198, v169 op_sel_hi:[0,0,0]
	v_mfma_scale_f32_16x16x128_f8f6f4 v[138:141], v[18:25], v[206:213], 0, v198, v169 op_sel_hi:[0,0,0]
	v_mfma_scale_f32_16x16x128_f8f6f4 v[126:129], v[26:33], v[214:221], 0, v198, v169 op_sel_hi:[0,0,0]
	v_mfma_scale_f32_16x16x128_f8f6f4 v[122:125], v[18:25], v[214:221], 0, v198, v169 op_sel_hi:[0,0,0]
	v_mfma_scale_f32_16x16x128_f8f6f4 v[110:113], v[26:33], v[236:243], 0, v198, v169 op_sel_hi:[0,0,0]
	v_mfma_scale_f32_16x16x128_f8f6f4 v[106:109], v[18:25], v[236:243], 0, v198, v169 op_sel_hi:[0,0,0]
	s_setprio 0
	s_setprio 1
	v_mfma_scale_f32_16x16x128_f8f6f4 v[150:153], v[10:17], v[186:193], 0, v198, v169 op_sel_hi:[0,0,0]
	v_mfma_scale_f32_16x16x128_f8f6f4 v[146:149], v[2:9], v[186:193], 0, v198, v169 op_sel_hi:[0,0,0]
	v_mfma_scale_f32_16x16x128_f8f6f4 v[134:137], v[10:17], v[206:213], 0, v198, v169 op_sel_hi:[0,0,0]
	v_mfma_scale_f32_16x16x128_f8f6f4 v[130:133], v[2:9], v[206:213], 0, v198, v169 op_sel_hi:[0,0,0]
	v_mfma_scale_f32_16x16x128_f8f6f4 v[118:121], v[10:17], v[214:221], 0, v198, v169 op_sel_hi:[0,0,0]
	v_mfma_scale_f32_16x16x128_f8f6f4 v[114:117], v[2:9], v[214:221], 0, v198, v169 op_sel_hi:[0,0,0]
	v_mfma_scale_f32_16x16x128_f8f6f4 v[102:105], v[10:17], v[236:243], 0, v198, v169 op_sel_hi:[0,0,0]
	v_mfma_scale_f32_16x16x128_f8f6f4 v[98:101], v[2:9], v[236:243], 0, v198, v169 op_sel_hi:[0,0,0]
	s_setprio 0
	s_barrier
	s_add_i32 s58, s76, s14
	v_lshl_add_u64 v[186:187], s[62:63], 0, v[166:167]
	s_mov_b32 m0, s58
	ds_read_b128 v[206:209], v204 offset:16384
	ds_read_b128 v[210:213], v204 offset:17408
	ds_read_b128 v[214:217], v204 offset:18432
	ds_read_b128 v[218:221], v204 offset:19456
	ds_read_b128 v[236:239], v204 offset:20480
	ds_read_b128 v[240:243], v204 offset:21504
	ds_read_b128 v[244:247], v204 offset:22528
	ds_read_b128 v[248:251], v204 offset:23552
	global_load_lds_dwordx4 v[186:187], off
	s_add_i32 m0, s58, 0x2000
	s_add_u32 s58, s62, 0x70000
	v_lshl_add_u64 v[188:189], s[62:63], 0, v[162:163]
	s_addc_u32 s59, s63, 0
	s_add_i32 s76, s77, s14
	global_load_lds_dwordx4 v[188:189], off
	v_lshl_add_u64 v[170:171], s[58:59], 0, v[166:167]
	s_mov_b32 m0, s76
	v_lshl_add_u64 v[190:191], s[64:65], 0, v[164:165]
	global_load_lds_dwordx4 v[170:171], off
	v_lshl_add_u64 v[170:171], s[58:59], 0, v[162:163]
	s_add_i32 m0, s76, 0x2000
	v_lshl_add_u64 v[192:193], s[64:65], 0, v[178:179]
	global_load_lds_dwordx4 v[170:171], off
	s_mov_b32 m0, s15
	s_nop 0
	global_load_lds_dwordx4 v[190:191], off
	s_mov_b32 m0, s16
	s_nop 0
	global_load_lds_dwordx4 v[192:193], off
	s_waitcnt vmcnt(8)
	s_waitcnt lgkmcnt(0)
	s_barrier
	s_setprio 1
	v_mfma_scale_f32_16x16x128_f8f6f4 v[94:97], v[26:33], v[206:213], 0, v198, v169 op_sel_hi:[0,0,0]
	v_mfma_scale_f32_16x16x128_f8f6f4 v[90:93], v[18:25], v[206:213], 0, v198, v169 op_sel_hi:[0,0,0]
	v_mfma_scale_f32_16x16x128_f8f6f4 v[78:81], v[26:33], v[214:221], 0, v198, v169 op_sel_hi:[0,0,0]
	v_mfma_scale_f32_16x16x128_f8f6f4 v[74:77], v[18:25], v[214:221], 0, v198, v169 op_sel_hi:[0,0,0]
	v_mfma_scale_f32_16x16x128_f8f6f4 v[62:65], v[26:33], v[236:243], 0, v198, v169 op_sel_hi:[0,0,0]
	v_mfma_scale_f32_16x16x128_f8f6f4 v[58:61], v[18:25], v[236:243], 0, v198, v169 op_sel_hi:[0,0,0]
	v_mfma_scale_f32_16x16x128_f8f6f4 v[46:49], v[26:33], v[244:251], 0, v198, v169 op_sel_hi:[0,0,0]
	v_mfma_scale_f32_16x16x128_f8f6f4 v[42:45], v[18:25], v[244:251], 0, v198, v169 op_sel_hi:[0,0,0]
	s_setprio 0
	s_setprio 1
	v_mfma_scale_f32_16x16x128_f8f6f4 v[86:89], v[10:17], v[206:213], 0, v198, v169 op_sel_hi:[0,0,0]
	v_mfma_scale_f32_16x16x128_f8f6f4 v[82:85], v[2:9], v[206:213], 0, v198, v169 op_sel_hi:[0,0,0]
	v_mfma_scale_f32_16x16x128_f8f6f4 v[70:73], v[10:17], v[214:221], 0, v198, v169 op_sel_hi:[0,0,0]
	v_mfma_scale_f32_16x16x128_f8f6f4 v[66:69], v[2:9], v[214:221], 0, v198, v169 op_sel_hi:[0,0,0]
	v_mfma_scale_f32_16x16x128_f8f6f4 v[54:57], v[10:17], v[236:243], 0, v198, v169 op_sel_hi:[0,0,0]
	v_mfma_scale_f32_16x16x128_f8f6f4 v[50:53], v[2:9], v[236:243], 0, v198, v169 op_sel_hi:[0,0,0]
	v_mfma_scale_f32_16x16x128_f8f6f4 v[38:41], v[10:17], v[244:251], 0, v198, v169 op_sel_hi:[0,0,0]
	v_mfma_scale_f32_16x16x128_f8f6f4 v[34:37], v[2:9], v[244:251], 0, v198, v169 op_sel_hi:[0,0,0]
	s_setprio 0
	s_barrier
	s_add_i32 s76, 0, 0x18000
	s_add_i32 s77, 0, 0x1c000
	v_add_u32_e32 v2, s76, v200
	v_add_u32_e32 v6, s77, v200
	ds_read_b128 v[26:29], v2
	ds_read_b128 v[30:33], v2 offset:1024
	ds_read_b128 v[18:21], v2 offset:2048
	ds_read_b128 v[22:25], v2 offset:3072
	ds_read_b128 v[10:13], v6
	ds_read_b128 v[14:17], v6 offset:1024
	ds_read_b128 v[2:5], v6 offset:2048
	ds_read_b128 v[6:9], v6 offset:3072
	s_add_u32 s58, s64, 0x70000
	s_addc_u32 s59, s65, 0
	s_mov_b32 m0, s20
	v_lshl_add_u64 v[170:171], s[58:59], 0, v[164:165]
	ds_read_b128 v[206:209], v204 offset:32768
	ds_read_b128 v[210:213], v204 offset:33792
	ds_read_b128 v[214:217], v204 offset:34816
	ds_read_b128 v[218:221], v204 offset:35840
	ds_read_b128 v[236:239], v204 offset:36864
	ds_read_b128 v[240:243], v204 offset:37888
	ds_read_b128 v[244:247], v204 offset:38912
	ds_read_b128 v[248:251], v204 offset:39936
	global_load_lds_dwordx4 v[170:171], off
	v_lshl_add_u64 v[170:171], s[58:59], 0, v[178:179]
	s_mov_b32 m0, s21
	s_nop 0
	global_load_lds_dwordx4 v[170:171], off
	s_waitcnt vmcnt(8)
	s_waitcnt lgkmcnt(0)
	s_barrier
	s_setprio 1
	v_mfma_scale_f32_16x16x128_f8f6f4 v[158:161], v[26:33], v[206:213], v[158:161], v198, v169 op_sel_hi:[0,0,0]
	v_mfma_scale_f32_16x16x128_f8f6f4 v[154:157], v[18:25], v[206:213], v[154:157], v198, v169 op_sel_hi:[0,0,0]
	v_mfma_scale_f32_16x16x128_f8f6f4 v[142:145], v[26:33], v[214:221], v[142:145], v198, v169 op_sel_hi:[0,0,0]
	v_mfma_scale_f32_16x16x128_f8f6f4 v[138:141], v[18:25], v[214:221], v[138:141], v198, v169 op_sel_hi:[0,0,0]
	v_mfma_scale_f32_16x16x128_f8f6f4 v[126:129], v[26:33], v[236:243], v[126:129], v198, v169 op_sel_hi:[0,0,0]
	v_mfma_scale_f32_16x16x128_f8f6f4 v[122:125], v[18:25], v[236:243], v[122:125], v198, v169 op_sel_hi:[0,0,0]
	v_mfma_scale_f32_16x16x128_f8f6f4 v[110:113], v[26:33], v[244:251], v[110:113], v198, v169 op_sel_hi:[0,0,0]
	v_mfma_scale_f32_16x16x128_f8f6f4 v[106:109], v[18:25], v[244:251], v[106:109], v198, v169 op_sel_hi:[0,0,0]
	s_setprio 0
	s_setprio 1
	v_mfma_scale_f32_16x16x128_f8f6f4 v[150:153], v[10:17], v[206:213], v[150:153], v198, v169 op_sel_hi:[0,0,0]
	v_mfma_scale_f32_16x16x128_f8f6f4 v[146:149], v[2:9], v[206:213], v[146:149], v198, v169 op_sel_hi:[0,0,0]
	v_mfma_scale_f32_16x16x128_f8f6f4 v[134:137], v[10:17], v[214:221], v[134:137], v198, v169 op_sel_hi:[0,0,0]
	v_mfma_scale_f32_16x16x128_f8f6f4 v[130:133], v[2:9], v[214:221], v[130:133], v198, v169 op_sel_hi:[0,0,0]
	v_mfma_scale_f32_16x16x128_f8f6f4 v[118:121], v[10:17], v[236:243], v[118:121], v198, v169 op_sel_hi:[0,0,0]
	v_mfma_scale_f32_16x16x128_f8f6f4 v[114:117], v[2:9], v[236:243], v[114:117], v198, v169 op_sel_hi:[0,0,0]
	v_mfma_scale_f32_16x16x128_f8f6f4 v[102:105], v[10:17], v[244:251], v[102:105], v198, v169 op_sel_hi:[0,0,0]
	v_mfma_scale_f32_16x16x128_f8f6f4 v[98:101], v[2:9], v[244:251], v[98:101], v198, v169 op_sel_hi:[0,0,0]
	s_setprio 0
	s_barrier
	s_add_i32 s58, s76, s14
	v_lshl_add_u64 v[170:171], v[186:187], 0, s[56:57]
	s_mov_b32 m0, s58
	ds_read_b128 v[206:209], v204 offset:49152
	ds_read_b128 v[210:213], v204 offset:50176
	ds_read_b128 v[214:217], v204 offset:51200
	ds_read_b128 v[218:221], v204 offset:52224
	ds_read_b128 v[236:239], v204 offset:53248
	ds_read_b128 v[240:243], v204 offset:54272
	ds_read_b128 v[244:247], v204 offset:55296
	ds_read_b128 v[248:251], v204 offset:56320
	global_load_lds_dwordx4 v[170:171], off
	s_add_i32 m0, s58, 0x2000
	s_add_u32 s58, s62, 0x70080
	v_lshl_add_u64 v[170:171], v[188:189], 0, s[56:57]
	s_addc_u32 s59, s63, 0
	s_add_i32 s62, s77, s14
	global_load_lds_dwordx4 v[170:171], off
	v_lshl_add_u64 v[170:171], s[58:59], 0, v[166:167]
	s_mov_b32 m0, s62
	s_nop 0
	global_load_lds_dwordx4 v[170:171], off
	v_lshl_add_u64 v[170:171], s[58:59], 0, v[162:163]
	s_add_i32 m0, s62, 0x2000
	s_nop 0
	global_load_lds_dwordx4 v[170:171], off
	v_lshl_add_u64 v[170:171], v[190:191], 0, s[56:57]
	s_mov_b32 m0, s24
	s_nop 0
	global_load_lds_dwordx4 v[170:171], off
	v_lshl_add_u64 v[170:171], v[192:193], 0, s[56:57]
	s_mov_b32 m0, s25
	s_nop 0
	global_load_lds_dwordx4 v[170:171], off
	s_waitcnt vmcnt(8)
	s_waitcnt lgkmcnt(0)
	s_barrier
	s_setprio 1
	v_mfma_scale_f32_16x16x128_f8f6f4 v[94:97], v[26:33], v[206:213], v[94:97], v198, v169 op_sel_hi:[0,0,0]
	v_mfma_scale_f32_16x16x128_f8f6f4 v[90:93], v[18:25], v[206:213], v[90:93], v198, v169 op_sel_hi:[0,0,0]
	v_mfma_scale_f32_16x16x128_f8f6f4 v[78:81], v[26:33], v[214:221], v[78:81], v198, v169 op_sel_hi:[0,0,0]
	v_mfma_scale_f32_16x16x128_f8f6f4 v[74:77], v[18:25], v[214:221], v[74:77], v198, v169 op_sel_hi:[0,0,0]
	v_mfma_scale_f32_16x16x128_f8f6f4 v[62:65], v[26:33], v[236:243], v[62:65], v198, v169 op_sel_hi:[0,0,0]
	v_mfma_scale_f32_16x16x128_f8f6f4 v[58:61], v[18:25], v[236:243], v[58:61], v198, v169 op_sel_hi:[0,0,0]
	v_mfma_scale_f32_16x16x128_f8f6f4 v[46:49], v[26:33], v[244:251], v[46:49], v198, v169 op_sel_hi:[0,0,0]
	v_mfma_scale_f32_16x16x128_f8f6f4 v[42:45], v[18:25], v[244:251], v[42:45], v198, v169 op_sel_hi:[0,0,0]
	s_setprio 0
	s_setprio 1
	v_mfma_scale_f32_16x16x128_f8f6f4 v[86:89], v[10:17], v[206:213], v[86:89], v198, v169 op_sel_hi:[0,0,0]
	v_mfma_scale_f32_16x16x128_f8f6f4 v[82:85], v[2:9], v[206:213], v[82:85], v198, v169 op_sel_hi:[0,0,0]
	v_mfma_scale_f32_16x16x128_f8f6f4 v[70:73], v[10:17], v[214:221], v[70:73], v198, v169 op_sel_hi:[0,0,0]
	v_mfma_scale_f32_16x16x128_f8f6f4 v[66:69], v[2:9], v[214:221], v[66:69], v198, v169 op_sel_hi:[0,0,0]
	v_mfma_scale_f32_16x16x128_f8f6f4 v[54:57], v[10:17], v[236:243], v[54:57], v198, v169 op_sel_hi:[0,0,0]
	v_mfma_scale_f32_16x16x128_f8f6f4 v[50:53], v[2:9], v[236:243], v[50:53], v198, v169 op_sel_hi:[0,0,0]
	v_mfma_scale_f32_16x16x128_f8f6f4 v[38:41], v[10:17], v[244:251], v[38:41], v198, v169 op_sel_hi:[0,0,0]
	v_mfma_scale_f32_16x16x128_f8f6f4 v[34:37], v[2:9], v[244:251], v[34:37], v198, v169 op_sel_hi:[0,0,0]
	s_setprio 0
	s_barrier
	s_add_u32 s73, s73, 0x100
	s_addc_u32 s74, s74, 0
	s_cmp_ge_i32 s75, s1
	s_mov_b64 s[58:59], s[60:61]
	s_mov_b32 s62, s75
	s_cbranch_scc0 .LBB0_924
	s_branch .Lpeelexitph8
.LBB0_924:
	s_add_i32 s75, s62, 2
	s_add_u32 s60, s58, 0x100
	s_addc_u32 s61, s59, 0
	s_add_i32 s76, 0, 0x10000
	s_cmp_eq_u32 s68, s62
	s_cselect_b32 s65, s53, s61
	s_cselect_b32 s64, s52, s60
	s_cselect_b32 s63, s55, s74
	s_cselect_b32 s62, s54, s73
	s_add_i32 s77, 0, 0x14000
	v_add_u32_e32 v2, s76, v200
	v_add_u32_e32 v6, s77, v200
	ds_read_b128 v[26:29], v2
	ds_read_b128 v[30:33], v2 offset:1024
	ds_read_b128 v[18:21], v2 offset:2048
	ds_read_b128 v[22:25], v2 offset:3072
	ds_read_b128 v[10:13], v6
	ds_read_b128 v[14:17], v6 offset:1024
	s_waitcnt lgkmcnt(0)
	ds_read_b128 v[2:5], v6 offset:2048
	ds_read_b128 v[6:9], v6 offset:3072
	v_lshl_add_u64 v[170:171], s[58:59], 0, v[184:185]
	s_add_i32 m0, s15, 0xc000
	ds_read_b128 v[186:189], v204
	ds_read_b128 v[190:193], v204 offset:1024
	ds_read_b128 v[206:209], v204 offset:2048
	ds_read_b128 v[210:213], v204 offset:3072
	ds_read_b128 v[214:217], v204 offset:4096
	ds_read_b128 v[218:221], v204 offset:5120
	ds_read_b128 v[236:239], v204 offset:6144
	ds_read_b128 v[240:243], v204 offset:7168
	global_load_lds_dwordx4 v[170:171], off
	v_lshl_add_u64 v[170:171], s[58:59], 0, v[182:183]
	s_add_i32 m0, s15, 0xe000
	s_nop 0
	global_load_lds_dwordx4 v[170:171], off
	s_waitcnt vmcnt(8)
	s_waitcnt lgkmcnt(0)
	s_barrier
	s_setprio 1
	v_mfma_scale_f32_16x16x128_f8f6f4 v[158:161], v[26:33], v[186:193], v[158:161], v198, v169 op_sel_hi:[0,0,0]
	v_mfma_scale_f32_16x16x128_f8f6f4 v[154:157], v[18:25], v[186:193], v[154:157], v198, v169 op_sel_hi:[0,0,0]
	v_mfma_scale_f32_16x16x128_f8f6f4 v[142:145], v[26:33], v[206:213], v[142:145], v198, v169 op_sel_hi:[0,0,0]
	v_mfma_scale_f32_16x16x128_f8f6f4 v[138:141], v[18:25], v[206:213], v[138:141], v198, v169 op_sel_hi:[0,0,0]
	v_mfma_scale_f32_16x16x128_f8f6f4 v[126:129], v[26:33], v[214:221], v[126:129], v198, v169 op_sel_hi:[0,0,0]
	v_mfma_scale_f32_16x16x128_f8f6f4 v[122:125], v[18:25], v[214:221], v[122:125], v198, v169 op_sel_hi:[0,0,0]
	v_mfma_scale_f32_16x16x128_f8f6f4 v[110:113], v[26:33], v[236:243], v[110:113], v198, v169 op_sel_hi:[0,0,0]
	v_mfma_scale_f32_16x16x128_f8f6f4 v[106:109], v[18:25], v[236:243], v[106:109], v198, v169 op_sel_hi:[0,0,0]
	s_setprio 0
	s_setprio 1
	v_mfma_scale_f32_16x16x128_f8f6f4 v[150:153], v[10:17], v[186:193], v[150:153], v198, v169 op_sel_hi:[0,0,0]
	v_mfma_scale_f32_16x16x128_f8f6f4 v[146:149], v[2:9], v[186:193], v[146:149], v198, v169 op_sel_hi:[0,0,0]
	v_mfma_scale_f32_16x16x128_f8f6f4 v[134:137], v[10:17], v[206:213], v[134:137], v198, v169 op_sel_hi:[0,0,0]
	v_mfma_scale_f32_16x16x128_f8f6f4 v[130:133], v[2:9], v[206:213], v[130:133], v198, v169 op_sel_hi:[0,0,0]
	v_mfma_scale_f32_16x16x128_f8f6f4 v[118:121], v[10:17], v[214:221], v[118:121], v198, v169 op_sel_hi:[0,0,0]
	v_mfma_scale_f32_16x16x128_f8f6f4 v[114:117], v[2:9], v[214:221], v[114:117], v198, v169 op_sel_hi:[0,0,0]
	v_mfma_scale_f32_16x16x128_f8f6f4 v[102:105], v[10:17], v[236:243], v[102:105], v198, v169 op_sel_hi:[0,0,0]
	v_mfma_scale_f32_16x16x128_f8f6f4 v[98:101], v[2:9], v[236:243], v[98:101], v198, v169 op_sel_hi:[0,0,0]
	s_setprio 0
	s_barrier
	s_add_i32 s58, s76, s14
	v_lshl_add_u64 v[186:187], s[62:63], 0, v[166:167]
	s_mov_b32 m0, s58
	ds_read_b128 v[206:209], v204 offset:16384
	ds_read_b128 v[210:213], v204 offset:17408
	ds_read_b128 v[214:217], v204 offset:18432
	ds_read_b128 v[218:221], v204 offset:19456
	ds_read_b128 v[236:239], v204 offset:20480
	ds_read_b128 v[240:243], v204 offset:21504
	ds_read_b128 v[244:247], v204 offset:22528
	ds_read_b128 v[248:251], v204 offset:23552
	global_load_lds_dwordx4 v[186:187], off
	s_add_i32 m0, s58, 0x2000
	s_add_u32 s58, s62, 0x70000
	v_lshl_add_u64 v[188:189], s[62:63], 0, v[162:163]
	s_addc_u32 s59, s63, 0
	s_add_i32 s76, s77, s14
	global_load_lds_dwordx4 v[188:189], off
	v_lshl_add_u64 v[170:171], s[58:59], 0, v[166:167]
	s_mov_b32 m0, s76
	v_lshl_add_u64 v[190:191], s[64:65], 0, v[164:165]
	global_load_lds_dwordx4 v[170:171], off
	v_lshl_add_u64 v[170:171], s[58:59], 0, v[162:163]
	s_add_i32 m0, s76, 0x2000
	v_lshl_add_u64 v[192:193], s[64:65], 0, v[178:179]
	global_load_lds_dwordx4 v[170:171], off
	s_mov_b32 m0, s15
	s_nop 0
	global_load_lds_dwordx4 v[190:191], off
	s_mov_b32 m0, s16
	s_nop 0
	global_load_lds_dwordx4 v[192:193], off
	s_waitcnt vmcnt(8)
	s_waitcnt lgkmcnt(0)
	s_barrier
	s_setprio 1
	v_mfma_scale_f32_16x16x128_f8f6f4 v[94:97], v[26:33], v[206:213], v[94:97], v198, v169 op_sel_hi:[0,0,0]
	v_mfma_scale_f32_16x16x128_f8f6f4 v[90:93], v[18:25], v[206:213], v[90:93], v198, v169 op_sel_hi:[0,0,0]
	v_mfma_scale_f32_16x16x128_f8f6f4 v[78:81], v[26:33], v[214:221], v[78:81], v198, v169 op_sel_hi:[0,0,0]
	v_mfma_scale_f32_16x16x128_f8f6f4 v[74:77], v[18:25], v[214:221], v[74:77], v198, v169 op_sel_hi:[0,0,0]
	v_mfma_scale_f32_16x16x128_f8f6f4 v[62:65], v[26:33], v[236:243], v[62:65], v198, v169 op_sel_hi:[0,0,0]
	v_mfma_scale_f32_16x16x128_f8f6f4 v[58:61], v[18:25], v[236:243], v[58:61], v198, v169 op_sel_hi:[0,0,0]
	v_mfma_scale_f32_16x16x128_f8f6f4 v[46:49], v[26:33], v[244:251], v[46:49], v198, v169 op_sel_hi:[0,0,0]
	v_mfma_scale_f32_16x16x128_f8f6f4 v[42:45], v[18:25], v[244:251], v[42:45], v198, v169 op_sel_hi:[0,0,0]
	s_setprio 0
	s_setprio 1
	v_mfma_scale_f32_16x16x128_f8f6f4 v[86:89], v[10:17], v[206:213], v[86:89], v198, v169 op_sel_hi:[0,0,0]
	v_mfma_scale_f32_16x16x128_f8f6f4 v[82:85], v[2:9], v[206:213], v[82:85], v198, v169 op_sel_hi:[0,0,0]
	v_mfma_scale_f32_16x16x128_f8f6f4 v[70:73], v[10:17], v[214:221], v[70:73], v198, v169 op_sel_hi:[0,0,0]
	v_mfma_scale_f32_16x16x128_f8f6f4 v[66:69], v[2:9], v[214:221], v[66:69], v198, v169 op_sel_hi:[0,0,0]
	v_mfma_scale_f32_16x16x128_f8f6f4 v[54:57], v[10:17], v[236:243], v[54:57], v198, v169 op_sel_hi:[0,0,0]
	v_mfma_scale_f32_16x16x128_f8f6f4 v[50:53], v[2:9], v[236:243], v[50:53], v198, v169 op_sel_hi:[0,0,0]
	v_mfma_scale_f32_16x16x128_f8f6f4 v[38:41], v[10:17], v[244:251], v[38:41], v198, v169 op_sel_hi:[0,0,0]
	v_mfma_scale_f32_16x16x128_f8f6f4 v[34:37], v[2:9], v[244:251], v[34:37], v198, v169 op_sel_hi:[0,0,0]
	s_setprio 0
	s_barrier
	s_add_i32 s76, 0, 0x18000
	s_add_i32 s77, 0, 0x1c000
	v_add_u32_e32 v2, s76, v200
	v_add_u32_e32 v6, s77, v200
	ds_read_b128 v[26:29], v2
	ds_read_b128 v[30:33], v2 offset:1024
	ds_read_b128 v[18:21], v2 offset:2048
	ds_read_b128 v[22:25], v2 offset:3072
	ds_read_b128 v[10:13], v6
	ds_read_b128 v[14:17], v6 offset:1024
	ds_read_b128 v[2:5], v6 offset:2048
	ds_read_b128 v[6:9], v6 offset:3072
	s_add_u32 s58, s64, 0x70000
	s_addc_u32 s59, s65, 0
	s_mov_b32 m0, s20
	v_lshl_add_u64 v[170:171], s[58:59], 0, v[164:165]
	ds_read_b128 v[206:209], v204 offset:32768
	ds_read_b128 v[210:213], v204 offset:33792
	ds_read_b128 v[214:217], v204 offset:34816
	ds_read_b128 v[218:221], v204 offset:35840
	ds_read_b128 v[236:239], v204 offset:36864
	ds_read_b128 v[240:243], v204 offset:37888
	ds_read_b128 v[244:247], v204 offset:38912
	ds_read_b128 v[248:251], v204 offset:39936
	global_load_lds_dwordx4 v[170:171], off
	v_lshl_add_u64 v[170:171], s[58:59], 0, v[178:179]
	s_mov_b32 m0, s21
	s_nop 0
	global_load_lds_dwordx4 v[170:171], off
	s_waitcnt vmcnt(8)
	s_waitcnt lgkmcnt(0)
	s_barrier
	s_setprio 1
	v_mfma_scale_f32_16x16x128_f8f6f4 v[158:161], v[26:33], v[206:213], v[158:161], v198, v169 op_sel_hi:[0,0,0]
	v_mfma_scale_f32_16x16x128_f8f6f4 v[154:157], v[18:25], v[206:213], v[154:157], v198, v169 op_sel_hi:[0,0,0]
	v_mfma_scale_f32_16x16x128_f8f6f4 v[142:145], v[26:33], v[214:221], v[142:145], v198, v169 op_sel_hi:[0,0,0]
	v_mfma_scale_f32_16x16x128_f8f6f4 v[138:141], v[18:25], v[214:221], v[138:141], v198, v169 op_sel_hi:[0,0,0]
	v_mfma_scale_f32_16x16x128_f8f6f4 v[126:129], v[26:33], v[236:243], v[126:129], v198, v169 op_sel_hi:[0,0,0]
	v_mfma_scale_f32_16x16x128_f8f6f4 v[122:125], v[18:25], v[236:243], v[122:125], v198, v169 op_sel_hi:[0,0,0]
	v_mfma_scale_f32_16x16x128_f8f6f4 v[110:113], v[26:33], v[244:251], v[110:113], v198, v169 op_sel_hi:[0,0,0]
	v_mfma_scale_f32_16x16x128_f8f6f4 v[106:109], v[18:25], v[244:251], v[106:109], v198, v169 op_sel_hi:[0,0,0]
	s_setprio 0
	s_setprio 1
	v_mfma_scale_f32_16x16x128_f8f6f4 v[150:153], v[10:17], v[206:213], v[150:153], v198, v169 op_sel_hi:[0,0,0]
	v_mfma_scale_f32_16x16x128_f8f6f4 v[146:149], v[2:9], v[206:213], v[146:149], v198, v169 op_sel_hi:[0,0,0]
	v_mfma_scale_f32_16x16x128_f8f6f4 v[134:137], v[10:17], v[214:221], v[134:137], v198, v169 op_sel_hi:[0,0,0]
	v_mfma_scale_f32_16x16x128_f8f6f4 v[130:133], v[2:9], v[214:221], v[130:133], v198, v169 op_sel_hi:[0,0,0]
	v_mfma_scale_f32_16x16x128_f8f6f4 v[118:121], v[10:17], v[236:243], v[118:121], v198, v169 op_sel_hi:[0,0,0]
	v_mfma_scale_f32_16x16x128_f8f6f4 v[114:117], v[2:9], v[236:243], v[114:117], v198, v169 op_sel_hi:[0,0,0]
	v_mfma_scale_f32_16x16x128_f8f6f4 v[102:105], v[10:17], v[244:251], v[102:105], v198, v169 op_sel_hi:[0,0,0]
	v_mfma_scale_f32_16x16x128_f8f6f4 v[98:101], v[2:9], v[244:251], v[98:101], v198, v169 op_sel_hi:[0,0,0]
	s_setprio 0
	s_barrier
	s_add_i32 s58, s76, s14
	v_lshl_add_u64 v[170:171], v[186:187], 0, s[56:57]
	s_mov_b32 m0, s58
	ds_read_b128 v[206:209], v204 offset:49152
	ds_read_b128 v[210:213], v204 offset:50176
	ds_read_b128 v[214:217], v204 offset:51200
	ds_read_b128 v[218:221], v204 offset:52224
	ds_read_b128 v[236:239], v204 offset:53248
	ds_read_b128 v[240:243], v204 offset:54272
	ds_read_b128 v[244:247], v204 offset:55296
	ds_read_b128 v[248:251], v204 offset:56320
	global_load_lds_dwordx4 v[170:171], off
	s_add_i32 m0, s58, 0x2000
	s_add_u32 s58, s62, 0x70080
	v_lshl_add_u64 v[170:171], v[188:189], 0, s[56:57]
	s_addc_u32 s59, s63, 0
	s_add_i32 s62, s77, s14
	global_load_lds_dwordx4 v[170:171], off
	v_lshl_add_u64 v[170:171], s[58:59], 0, v[166:167]
	s_mov_b32 m0, s62
	s_nop 0
	global_load_lds_dwordx4 v[170:171], off
	v_lshl_add_u64 v[170:171], s[58:59], 0, v[162:163]
	s_add_i32 m0, s62, 0x2000
	s_nop 0
	global_load_lds_dwordx4 v[170:171], off
	v_lshl_add_u64 v[170:171], v[190:191], 0, s[56:57]
	s_mov_b32 m0, s24
	s_nop 0
	global_load_lds_dwordx4 v[170:171], off
	v_lshl_add_u64 v[170:171], v[192:193], 0, s[56:57]
	s_mov_b32 m0, s25
	s_nop 0
	global_load_lds_dwordx4 v[170:171], off
	s_waitcnt vmcnt(8)
	s_waitcnt lgkmcnt(0)
	s_barrier
	s_setprio 1
	v_mfma_scale_f32_16x16x128_f8f6f4 v[94:97], v[26:33], v[206:213], v[94:97], v198, v169 op_sel_hi:[0,0,0]
	v_mfma_scale_f32_16x16x128_f8f6f4 v[90:93], v[18:25], v[206:213], v[90:93], v198, v169 op_sel_hi:[0,0,0]
	v_mfma_scale_f32_16x16x128_f8f6f4 v[78:81], v[26:33], v[214:221], v[78:81], v198, v169 op_sel_hi:[0,0,0]
	v_mfma_scale_f32_16x16x128_f8f6f4 v[74:77], v[18:25], v[214:221], v[74:77], v198, v169 op_sel_hi:[0,0,0]
	v_mfma_scale_f32_16x16x128_f8f6f4 v[62:65], v[26:33], v[236:243], v[62:65], v198, v169 op_sel_hi:[0,0,0]
	v_mfma_scale_f32_16x16x128_f8f6f4 v[58:61], v[18:25], v[236:243], v[58:61], v198, v169 op_sel_hi:[0,0,0]
	v_mfma_scale_f32_16x16x128_f8f6f4 v[46:49], v[26:33], v[244:251], v[46:49], v198, v169 op_sel_hi:[0,0,0]
	v_mfma_scale_f32_16x16x128_f8f6f4 v[42:45], v[18:25], v[244:251], v[42:45], v198, v169 op_sel_hi:[0,0,0]
	s_setprio 0
	s_setprio 1
	v_mfma_scale_f32_16x16x128_f8f6f4 v[86:89], v[10:17], v[206:213], v[86:89], v198, v169 op_sel_hi:[0,0,0]
	v_mfma_scale_f32_16x16x128_f8f6f4 v[82:85], v[2:9], v[206:213], v[82:85], v198, v169 op_sel_hi:[0,0,0]
	v_mfma_scale_f32_16x16x128_f8f6f4 v[70:73], v[10:17], v[214:221], v[70:73], v198, v169 op_sel_hi:[0,0,0]
	v_mfma_scale_f32_16x16x128_f8f6f4 v[66:69], v[2:9], v[214:221], v[66:69], v198, v169 op_sel_hi:[0,0,0]
	v_mfma_scale_f32_16x16x128_f8f6f4 v[54:57], v[10:17], v[236:243], v[54:57], v198, v169 op_sel_hi:[0,0,0]
	v_mfma_scale_f32_16x16x128_f8f6f4 v[50:53], v[2:9], v[236:243], v[50:53], v198, v169 op_sel_hi:[0,0,0]
	v_mfma_scale_f32_16x16x128_f8f6f4 v[38:41], v[10:17], v[244:251], v[38:41], v198, v169 op_sel_hi:[0,0,0]
	v_mfma_scale_f32_16x16x128_f8f6f4 v[34:37], v[2:9], v[244:251], v[34:37], v198, v169 op_sel_hi:[0,0,0]
	s_setprio 0
	s_barrier
	s_add_u32 s73, s73, 0x100
	s_addc_u32 s74, s74, 0
	s_cmp_ge_i32 s75, s1
	s_mov_b64 s[58:59], s[60:61]
	s_mov_b32 s62, s75
	s_cbranch_scc0 .LBB0_924

.Lpeelph9_0:
	s_add_i32 s27, s37, 2
	s_add_u32 s40, s38, 0xfffe0080
	s_addc_u32 s41, s39, -1
	s_add_i32 s65, 0, 0x10000
	s_cmp_eq_u32 s95, s37
	s_cselect_b32 s69, s0, s41
	s_cselect_b32 s68, s1, s40
	s_cselect_b32 s41, s8, s19
	s_cselect_b32 s40, s11, s16
	s_add_i32 s37, 0, 0x14000
	v_add_u32_e32 v2, s65, v221
	v_add_u32_e32 v6, s37, v221
	ds_read_b128 v[26:29], v2
	ds_read_b128 v[30:33], v2 offset:1024
	ds_read_b128 v[18:21], v2 offset:2048
	ds_read_b128 v[22:25], v2 offset:3072
	ds_read_b128 v[10:13], v6
	ds_read_b128 v[14:17], v6 offset:1024
	ds_read_b128 v[2:5], v6 offset:2048
	ds_read_b128 v[6:9], v6 offset:3072
	v_lshl_add_u64 v[170:171], s[38:39], 0, v[192:193]
	s_add_i32 m0, s21, 0xc000
	ds_read_b128 v[194:197], v222
	ds_read_b128 v[198:201], v222 offset:1024
	ds_read_b128 v[202:205], v222 offset:2048
	ds_read_b128 v[206:209], v222 offset:3072
	ds_read_b128 v[210:213], v222 offset:4096
	ds_read_b128 v[214:217], v222 offset:5120
	ds_read_b128 v[236:239], v222 offset:6144
	ds_read_b128 v[240:243], v222 offset:7168
	global_load_lds_dwordx4 v[170:171], off
	v_lshl_add_u64 v[170:171], s[38:39], 0, v[190:191]
	s_add_i32 m0, s21, 0xe000
	s_nop 0
	global_load_lds_dwordx4 v[170:171], off
	s_waitcnt vmcnt(8)
	s_waitcnt lgkmcnt(0)
	s_barrier
	s_setprio 1
	v_mfma_scale_f32_16x16x128_f8f6f4 v[94:97], v[26:33], v[194:201], 0, v183, v169 op_sel_hi:[0,0,0]
	v_mfma_scale_f32_16x16x128_f8f6f4 v[90:93], v[18:25], v[194:201], 0, v183, v169 op_sel_hi:[0,0,0]
	v_mfma_scale_f32_16x16x128_f8f6f4 v[86:89], v[26:33], v[202:209], 0, v183, v169 op_sel_hi:[0,0,0]
	v_mfma_scale_f32_16x16x128_f8f6f4 v[82:85], v[18:25], v[202:209], 0, v183, v169 op_sel_hi:[0,0,0]
	v_mfma_scale_f32_16x16x128_f8f6f4 v[78:81], v[26:33], v[210:217], 0, v183, v169 op_sel_hi:[0,0,0]
	v_mfma_scale_f32_16x16x128_f8f6f4 v[74:77], v[18:25], v[210:217], 0, v183, v169 op_sel_hi:[0,0,0]
	v_mfma_scale_f32_16x16x128_f8f6f4 v[70:73], v[26:33], v[236:243], 0, v183, v169 op_sel_hi:[0,0,0]
	v_mfma_scale_f32_16x16x128_f8f6f4 v[66:69], v[18:25], v[236:243], 0, v183, v169 op_sel_hi:[0,0,0]
	s_setprio 0
	s_setprio 1
	v_mfma_scale_f32_16x16x128_f8f6f4 v[158:161], v[10:17], v[194:201], 0, v183, v169 op_sel_hi:[0,0,0]
	v_mfma_scale_f32_16x16x128_f8f6f4 v[154:157], v[2:9], v[194:201], 0, v183, v169 op_sel_hi:[0,0,0]
	v_mfma_scale_f32_16x16x128_f8f6f4 v[150:153], v[10:17], v[202:209], 0, v183, v169 op_sel_hi:[0,0,0]
	v_mfma_scale_f32_16x16x128_f8f6f4 v[146:149], v[2:9], v[202:209], 0, v183, v169 op_sel_hi:[0,0,0]
	v_mfma_scale_f32_16x16x128_f8f6f4 v[142:145], v[10:17], v[210:217], 0, v183, v169 op_sel_hi:[0,0,0]
	v_mfma_scale_f32_16x16x128_f8f6f4 v[138:141], v[2:9], v[210:217], 0, v183, v169 op_sel_hi:[0,0,0]
	v_mfma_scale_f32_16x16x128_f8f6f4 v[134:137], v[10:17], v[236:243], 0, v183, v169 op_sel_hi:[0,0,0]
	v_mfma_scale_f32_16x16x128_f8f6f4 v[130:133], v[2:9], v[236:243], 0, v183, v169 op_sel_hi:[0,0,0]
	s_setprio 0
	s_barrier
	s_add_i32 s65, s65, s20
	v_lshl_add_u64 v[194:195], s[40:41], 0, v[162:163]
	s_mov_b32 m0, s65
	ds_read_b128 v[202:205], v222 offset:16384
	ds_read_b128 v[206:209], v222 offset:17408
	ds_read_b128 v[210:213], v222 offset:18432
	ds_read_b128 v[214:217], v222 offset:19456
	ds_read_b128 v[236:239], v222 offset:20480
	ds_read_b128 v[240:243], v222 offset:21504
	ds_read_b128 v[244:247], v222 offset:22528
	ds_read_b128 v[248:251], v222 offset:23552
	global_load_lds_dwordx4 v[194:195], off
	s_add_i32 m0, s65, 0x2000
	s_add_u32 s70, s40, 0x20000
	v_lshl_add_u64 v[196:197], s[40:41], 0, v[164:165]
	s_addc_u32 s71, s41, 0
	s_add_i32 s37, s37, s20
	global_load_lds_dwordx4 v[196:197], off
	v_lshl_add_u64 v[170:171], s[70:71], 0, v[162:163]
	s_mov_b32 m0, s37
	v_lshl_add_u64 v[198:199], s[68:69], 0, v[178:179]
	global_load_lds_dwordx4 v[170:171], off
	v_lshl_add_u64 v[170:171], s[70:71], 0, v[164:165]
	s_add_i32 m0, s37, 0x2000
	v_lshl_add_u64 v[200:201], s[68:69], 0, v[180:181]
	global_load_lds_dwordx4 v[170:171], off
	s_mov_b32 m0, s21
	s_nop 0
	global_load_lds_dwordx4 v[198:199], off
	s_mov_b32 m0, s22
	s_nop 0
	global_load_lds_dwordx4 v[200:201], off
	s_waitcnt vmcnt(8)
	s_waitcnt lgkmcnt(0)
	s_barrier
	s_setprio 1
	v_mfma_scale_f32_16x16x128_f8f6f4 v[62:65], v[26:33], v[202:209], 0, v183, v169 op_sel_hi:[0,0,0]
	v_mfma_scale_f32_16x16x128_f8f6f4 v[58:61], v[18:25], v[202:209], 0, v183, v169 op_sel_hi:[0,0,0]
	v_mfma_scale_f32_16x16x128_f8f6f4 v[54:57], v[26:33], v[210:217], 0, v183, v169 op_sel_hi:[0,0,0]
	v_mfma_scale_f32_16x16x128_f8f6f4 v[50:53], v[18:25], v[210:217], 0, v183, v169 op_sel_hi:[0,0,0]
	v_mfma_scale_f32_16x16x128_f8f6f4 v[46:49], v[26:33], v[236:243], 0, v183, v169 op_sel_hi:[0,0,0]
	v_mfma_scale_f32_16x16x128_f8f6f4 v[42:45], v[18:25], v[236:243], 0, v183, v169 op_sel_hi:[0,0,0]
	v_mfma_scale_f32_16x16x128_f8f6f4 v[38:41], v[26:33], v[244:251], 0, v183, v169 op_sel_hi:[0,0,0]
	v_mfma_scale_f32_16x16x128_f8f6f4 v[34:37], v[18:25], v[244:251], 0, v183, v169 op_sel_hi:[0,0,0]
	s_setprio 0
	s_setprio 1
	v_mfma_scale_f32_16x16x128_f8f6f4 v[126:129], v[10:17], v[202:209], 0, v183, v169 op_sel_hi:[0,0,0]
	v_mfma_scale_f32_16x16x128_f8f6f4 v[122:125], v[2:9], v[202:209], 0, v183, v169 op_sel_hi:[0,0,0]
	v_mfma_scale_f32_16x16x128_f8f6f4 v[118:121], v[10:17], v[210:217], 0, v183, v169 op_sel_hi:[0,0,0]
	v_mfma_scale_f32_16x16x128_f8f6f4 v[114:117], v[2:9], v[210:217], 0, v183, v169 op_sel_hi:[0,0,0]
	v_mfma_scale_f32_16x16x128_f8f6f4 v[110:113], v[10:17], v[236:243], 0, v183, v169 op_sel_hi:[0,0,0]
	v_mfma_scale_f32_16x16x128_f8f6f4 v[106:109], v[2:9], v[236:243], 0, v183, v169 op_sel_hi:[0,0,0]
	v_mfma_scale_f32_16x16x128_f8f6f4 v[102:105], v[10:17], v[244:251], 0, v183, v169 op_sel_hi:[0,0,0]
	v_mfma_scale_f32_16x16x128_f8f6f4 v[98:101], v[2:9], v[244:251], 0, v183, v169 op_sel_hi:[0,0,0]
	s_setprio 0
	s_barrier
	s_add_i32 s37, 0, 0x18000
	s_add_i32 s65, 0, 0x1c000
	v_add_u32_e32 v2, s37, v221
	v_add_u32_e32 v6, s65, v221
	ds_read_b128 v[26:29], v2
	ds_read_b128 v[30:33], v2 offset:1024
	ds_read_b128 v[18:21], v2 offset:2048
	ds_read_b128 v[22:25], v2 offset:3072
	ds_read_b128 v[10:13], v6
	ds_read_b128 v[14:17], v6 offset:1024
	ds_read_b128 v[2:5], v6 offset:2048
	ds_read_b128 v[6:9], v6 offset:3072
	s_add_u32 s68, s68, 0x20000
	s_addc_u32 s69, s69, 0
	s_mov_b32 m0, s23
	v_lshl_add_u64 v[170:171], s[68:69], 0, v[178:179]
	ds_read_b128 v[202:205], v222 offset:32768
	ds_read_b128 v[206:209], v222 offset:33792
	ds_read_b128 v[210:213], v222 offset:34816
	ds_read_b128 v[214:217], v222 offset:35840
	ds_read_b128 v[236:239], v222 offset:36864
	ds_read_b128 v[240:243], v222 offset:37888
	ds_read_b128 v[244:247], v222 offset:38912
	ds_read_b128 v[248:251], v222 offset:39936
	global_load_lds_dwordx4 v[170:171], off
	v_lshl_add_u64 v[170:171], s[68:69], 0, v[180:181]
	s_mov_b32 m0, s12
	s_nop 0
	global_load_lds_dwordx4 v[170:171], off
	s_waitcnt vmcnt(8)
	s_waitcnt lgkmcnt(0)
	s_barrier
	s_setprio 1
	v_mfma_scale_f32_16x16x128_f8f6f4 v[94:97], v[26:33], v[202:209], v[94:97], v183, v169 op_sel_hi:[0,0,0]
	v_mfma_scale_f32_16x16x128_f8f6f4 v[90:93], v[18:25], v[202:209], v[90:93], v183, v169 op_sel_hi:[0,0,0]
	v_mfma_scale_f32_16x16x128_f8f6f4 v[86:89], v[26:33], v[210:217], v[86:89], v183, v169 op_sel_hi:[0,0,0]
	v_mfma_scale_f32_16x16x128_f8f6f4 v[82:85], v[18:25], v[210:217], v[82:85], v183, v169 op_sel_hi:[0,0,0]
	v_mfma_scale_f32_16x16x128_f8f6f4 v[78:81], v[26:33], v[236:243], v[78:81], v183, v169 op_sel_hi:[0,0,0]
	v_mfma_scale_f32_16x16x128_f8f6f4 v[74:77], v[18:25], v[236:243], v[74:77], v183, v169 op_sel_hi:[0,0,0]
	v_mfma_scale_f32_16x16x128_f8f6f4 v[70:73], v[26:33], v[244:251], v[70:73], v183, v169 op_sel_hi:[0,0,0]
	v_mfma_scale_f32_16x16x128_f8f6f4 v[66:69], v[18:25], v[244:251], v[66:69], v183, v169 op_sel_hi:[0,0,0]
	s_setprio 0
	s_setprio 1
	v_mfma_scale_f32_16x16x128_f8f6f4 v[158:161], v[10:17], v[202:209], v[158:161], v183, v169 op_sel_hi:[0,0,0]
	v_mfma_scale_f32_16x16x128_f8f6f4 v[154:157], v[2:9], v[202:209], v[154:157], v183, v169 op_sel_hi:[0,0,0]
	v_mfma_scale_f32_16x16x128_f8f6f4 v[150:153], v[10:17], v[210:217], v[150:153], v183, v169 op_sel_hi:[0,0,0]
	v_mfma_scale_f32_16x16x128_f8f6f4 v[146:149], v[2:9], v[210:217], v[146:149], v183, v169 op_sel_hi:[0,0,0]
	v_mfma_scale_f32_16x16x128_f8f6f4 v[142:145], v[10:17], v[236:243], v[142:145], v183, v169 op_sel_hi:[0,0,0]
	v_mfma_scale_f32_16x16x128_f8f6f4 v[138:141], v[2:9], v[236:243], v[138:141], v183, v169 op_sel_hi:[0,0,0]
	v_mfma_scale_f32_16x16x128_f8f6f4 v[134:137], v[10:17], v[244:251], v[134:137], v183, v169 op_sel_hi:[0,0,0]
	v_mfma_scale_f32_16x16x128_f8f6f4 v[130:133], v[2:9], v[244:251], v[130:133], v183, v169 op_sel_hi:[0,0,0]
	s_setprio 0
	s_barrier
	s_add_i32 s37, s37, s20
	v_lshl_add_u64 v[170:171], v[194:195], 0, s[56:57]
	s_mov_b32 m0, s37
	ds_read_b128 v[202:205], v222 offset:49152
	ds_read_b128 v[206:209], v222 offset:50176
	ds_read_b128 v[210:213], v222 offset:51200
	ds_read_b128 v[214:217], v222 offset:52224
	ds_read_b128 v[236:239], v222 offset:53248
	ds_read_b128 v[240:243], v222 offset:54272
	ds_read_b128 v[244:247], v222 offset:55296
	ds_read_b128 v[248:251], v222 offset:56320
	global_load_lds_dwordx4 v[170:171], off
	s_add_i32 m0, s37, 0x2000
	s_add_u32 s40, s40, 0x20080
	v_lshl_add_u64 v[170:171], v[196:197], 0, s[56:57]
	s_addc_u32 s41, s41, 0
	s_add_i32 s37, s65, s20
	global_load_lds_dwordx4 v[170:171], off
	v_lshl_add_u64 v[170:171], s[40:41], 0, v[162:163]
	s_mov_b32 m0, s37
	s_nop 0
	global_load_lds_dwordx4 v[170:171], off
	v_lshl_add_u64 v[170:171], s[40:41], 0, v[164:165]
	s_add_i32 m0, s37, 0x2000
	s_nop 0
	global_load_lds_dwordx4 v[170:171], off
	v_lshl_add_u64 v[170:171], v[198:199], 0, s[56:57]
	s_mov_b32 m0, s92
	s_nop 0
	global_load_lds_dwordx4 v[170:171], off
	v_lshl_add_u64 v[170:171], v[200:201], 0, s[56:57]
	s_mov_b32 m0, s93
	s_nop 0
	global_load_lds_dwordx4 v[170:171], off
	s_waitcnt vmcnt(8)
	s_waitcnt lgkmcnt(0)
	s_barrier
	s_setprio 1
	v_mfma_scale_f32_16x16x128_f8f6f4 v[62:65], v[26:33], v[202:209], v[62:65], v183, v169 op_sel_hi:[0,0,0]
	v_mfma_scale_f32_16x16x128_f8f6f4 v[58:61], v[18:25], v[202:209], v[58:61], v183, v169 op_sel_hi:[0,0,0]
	v_mfma_scale_f32_16x16x128_f8f6f4 v[54:57], v[26:33], v[210:217], v[54:57], v183, v169 op_sel_hi:[0,0,0]
	v_mfma_scale_f32_16x16x128_f8f6f4 v[50:53], v[18:25], v[210:217], v[50:53], v183, v169 op_sel_hi:[0,0,0]
	v_mfma_scale_f32_16x16x128_f8f6f4 v[46:49], v[26:33], v[236:243], v[46:49], v183, v169 op_sel_hi:[0,0,0]
	v_mfma_scale_f32_16x16x128_f8f6f4 v[42:45], v[18:25], v[236:243], v[42:45], v183, v169 op_sel_hi:[0,0,0]
	v_mfma_scale_f32_16x16x128_f8f6f4 v[38:41], v[26:33], v[244:251], v[38:41], v183, v169 op_sel_hi:[0,0,0]
	v_mfma_scale_f32_16x16x128_f8f6f4 v[34:37], v[18:25], v[244:251], v[34:37], v183, v169 op_sel_hi:[0,0,0]
	s_setprio 0
	s_setprio 1
	v_mfma_scale_f32_16x16x128_f8f6f4 v[126:129], v[10:17], v[202:209], v[126:129], v183, v169 op_sel_hi:[0,0,0]
	v_mfma_scale_f32_16x16x128_f8f6f4 v[122:125], v[2:9], v[202:209], v[122:125], v183, v169 op_sel_hi:[0,0,0]
	v_mfma_scale_f32_16x16x128_f8f6f4 v[118:121], v[10:17], v[210:217], v[118:121], v183, v169 op_sel_hi:[0,0,0]
	v_mfma_scale_f32_16x16x128_f8f6f4 v[114:117], v[2:9], v[210:217], v[114:117], v183, v169 op_sel_hi:[0,0,0]
	v_mfma_scale_f32_16x16x128_f8f6f4 v[110:113], v[10:17], v[236:243], v[110:113], v183, v169 op_sel_hi:[0,0,0]
	v_mfma_scale_f32_16x16x128_f8f6f4 v[106:109], v[2:9], v[236:243], v[106:109], v183, v169 op_sel_hi:[0,0,0]
	v_mfma_scale_f32_16x16x128_f8f6f4 v[102:105], v[10:17], v[244:251], v[102:105], v183, v169 op_sel_hi:[0,0,0]
	v_mfma_scale_f32_16x16x128_f8f6f4 v[98:101], v[2:9], v[244:251], v[98:101], v183, v169 op_sel_hi:[0,0,0]
	s_setprio 0
	s_barrier
	s_add_u32 s16, s16, 0x100
	s_addc_u32 s19, s19, 0
	s_add_u32 s38, s38, 0x100
	s_addc_u32 s39, s39, 0
	s_cmp_ge_i32 s27, s74
	s_mov_b32 s37, s27
	s_cbranch_scc0 .LBB0_1016
	s_branch .Lpeelexitph9
.LBB0_1016:
	s_add_i32 s27, s37, 2
	s_add_u32 s40, s38, 0xfffe0080
	s_addc_u32 s41, s39, -1
	s_add_i32 s65, 0, 0x10000
	s_cmp_eq_u32 s95, s37
	s_cselect_b32 s69, s0, s41
	s_cselect_b32 s68, s1, s40
	s_cselect_b32 s41, s8, s19
	s_cselect_b32 s40, s11, s16
	s_add_i32 s37, 0, 0x14000
	v_add_u32_e32 v2, s65, v221
	v_add_u32_e32 v6, s37, v221
	ds_read_b128 v[26:29], v2
	ds_read_b128 v[30:33], v2 offset:1024
	ds_read_b128 v[18:21], v2 offset:2048
	ds_read_b128 v[22:25], v2 offset:3072
	ds_read_b128 v[10:13], v6
	ds_read_b128 v[14:17], v6 offset:1024
	ds_read_b128 v[2:5], v6 offset:2048
	ds_read_b128 v[6:9], v6 offset:3072
	v_lshl_add_u64 v[170:171], s[38:39], 0, v[192:193]
	s_add_i32 m0, s21, 0xc000
	ds_read_b128 v[194:197], v222
	ds_read_b128 v[198:201], v222 offset:1024
	ds_read_b128 v[202:205], v222 offset:2048
	ds_read_b128 v[206:209], v222 offset:3072
	ds_read_b128 v[210:213], v222 offset:4096
	ds_read_b128 v[214:217], v222 offset:5120
	ds_read_b128 v[236:239], v222 offset:6144
	ds_read_b128 v[240:243], v222 offset:7168
	global_load_lds_dwordx4 v[170:171], off
	v_lshl_add_u64 v[170:171], s[38:39], 0, v[190:191]
	s_add_i32 m0, s21, 0xe000
	s_nop 0
	global_load_lds_dwordx4 v[170:171], off
	s_waitcnt vmcnt(8)
	s_waitcnt lgkmcnt(0)
	s_barrier
	s_setprio 1
	v_mfma_scale_f32_16x16x128_f8f6f4 v[94:97], v[26:33], v[194:201], v[94:97], v183, v169 op_sel_hi:[0,0,0]
	v_mfma_scale_f32_16x16x128_f8f6f4 v[90:93], v[18:25], v[194:201], v[90:93], v183, v169 op_sel_hi:[0,0,0]
	v_mfma_scale_f32_16x16x128_f8f6f4 v[86:89], v[26:33], v[202:209], v[86:89], v183, v169 op_sel_hi:[0,0,0]
	v_mfma_scale_f32_16x16x128_f8f6f4 v[82:85], v[18:25], v[202:209], v[82:85], v183, v169 op_sel_hi:[0,0,0]
	v_mfma_scale_f32_16x16x128_f8f6f4 v[78:81], v[26:33], v[210:217], v[78:81], v183, v169 op_sel_hi:[0,0,0]
	v_mfma_scale_f32_16x16x128_f8f6f4 v[74:77], v[18:25], v[210:217], v[74:77], v183, v169 op_sel_hi:[0,0,0]
	v_mfma_scale_f32_16x16x128_f8f6f4 v[70:73], v[26:33], v[236:243], v[70:73], v183, v169 op_sel_hi:[0,0,0]
	v_mfma_scale_f32_16x16x128_f8f6f4 v[66:69], v[18:25], v[236:243], v[66:69], v183, v169 op_sel_hi:[0,0,0]
	s_setprio 0
	s_setprio 1
	v_mfma_scale_f32_16x16x128_f8f6f4 v[158:161], v[10:17], v[194:201], v[158:161], v183, v169 op_sel_hi:[0,0,0]
	v_mfma_scale_f32_16x16x128_f8f6f4 v[154:157], v[2:9], v[194:201], v[154:157], v183, v169 op_sel_hi:[0,0,0]
	v_mfma_scale_f32_16x16x128_f8f6f4 v[150:153], v[10:17], v[202:209], v[150:153], v183, v169 op_sel_hi:[0,0,0]
	v_mfma_scale_f32_16x16x128_f8f6f4 v[146:149], v[2:9], v[202:209], v[146:149], v183, v169 op_sel_hi:[0,0,0]
	v_mfma_scale_f32_16x16x128_f8f6f4 v[142:145], v[10:17], v[210:217], v[142:145], v183, v169 op_sel_hi:[0,0,0]
	v_mfma_scale_f32_16x16x128_f8f6f4 v[138:141], v[2:9], v[210:217], v[138:141], v183, v169 op_sel_hi:[0,0,0]
	v_mfma_scale_f32_16x16x128_f8f6f4 v[134:137], v[10:17], v[236:243], v[134:137], v183, v169 op_sel_hi:[0,0,0]
	v_mfma_scale_f32_16x16x128_f8f6f4 v[130:133], v[2:9], v[236:243], v[130:133], v183, v169 op_sel_hi:[0,0,0]
	s_setprio 0
	s_barrier
	s_add_i32 s65, s65, s20
	v_lshl_add_u64 v[194:195], s[40:41], 0, v[162:163]
	s_mov_b32 m0, s65
	ds_read_b128 v[202:205], v222 offset:16384
	ds_read_b128 v[206:209], v222 offset:17408
	ds_read_b128 v[210:213], v222 offset:18432
	ds_read_b128 v[214:217], v222 offset:19456
	ds_read_b128 v[236:239], v222 offset:20480
	ds_read_b128 v[240:243], v222 offset:21504
	ds_read_b128 v[244:247], v222 offset:22528
	ds_read_b128 v[248:251], v222 offset:23552
	global_load_lds_dwordx4 v[194:195], off
	s_add_i32 m0, s65, 0x2000
	s_add_u32 s70, s40, 0x20000
	v_lshl_add_u64 v[196:197], s[40:41], 0, v[164:165]
	s_addc_u32 s71, s41, 0
	s_add_i32 s37, s37, s20
	global_load_lds_dwordx4 v[196:197], off
	v_lshl_add_u64 v[170:171], s[70:71], 0, v[162:163]
	s_mov_b32 m0, s37
	v_lshl_add_u64 v[198:199], s[68:69], 0, v[178:179]
	global_load_lds_dwordx4 v[170:171], off
	v_lshl_add_u64 v[170:171], s[70:71], 0, v[164:165]
	s_add_i32 m0, s37, 0x2000
	v_lshl_add_u64 v[200:201], s[68:69], 0, v[180:181]
	global_load_lds_dwordx4 v[170:171], off
	s_mov_b32 m0, s21
	s_nop 0
	global_load_lds_dwordx4 v[198:199], off
	s_mov_b32 m0, s22
	s_nop 0
	global_load_lds_dwordx4 v[200:201], off
	s_waitcnt vmcnt(8)
	s_waitcnt lgkmcnt(0)
	s_barrier
	s_setprio 1
	v_mfma_scale_f32_16x16x128_f8f6f4 v[62:65], v[26:33], v[202:209], v[62:65], v183, v169 op_sel_hi:[0,0,0]
	v_mfma_scale_f32_16x16x128_f8f6f4 v[58:61], v[18:25], v[202:209], v[58:61], v183, v169 op_sel_hi:[0,0,0]
	v_mfma_scale_f32_16x16x128_f8f6f4 v[54:57], v[26:33], v[210:217], v[54:57], v183, v169 op_sel_hi:[0,0,0]
	v_mfma_scale_f32_16x16x128_f8f6f4 v[50:53], v[18:25], v[210:217], v[50:53], v183, v169 op_sel_hi:[0,0,0]
	v_mfma_scale_f32_16x16x128_f8f6f4 v[46:49], v[26:33], v[236:243], v[46:49], v183, v169 op_sel_hi:[0,0,0]
	v_mfma_scale_f32_16x16x128_f8f6f4 v[42:45], v[18:25], v[236:243], v[42:45], v183, v169 op_sel_hi:[0,0,0]
	v_mfma_scale_f32_16x16x128_f8f6f4 v[38:41], v[26:33], v[244:251], v[38:41], v183, v169 op_sel_hi:[0,0,0]
	v_mfma_scale_f32_16x16x128_f8f6f4 v[34:37], v[18:25], v[244:251], v[34:37], v183, v169 op_sel_hi:[0,0,0]
	s_setprio 0
	s_setprio 1
	v_mfma_scale_f32_16x16x128_f8f6f4 v[126:129], v[10:17], v[202:209], v[126:129], v183, v169 op_sel_hi:[0,0,0]
	v_mfma_scale_f32_16x16x128_f8f6f4 v[122:125], v[2:9], v[202:209], v[122:125], v183, v169 op_sel_hi:[0,0,0]
	v_mfma_scale_f32_16x16x128_f8f6f4 v[118:121], v[10:17], v[210:217], v[118:121], v183, v169 op_sel_hi:[0,0,0]
	v_mfma_scale_f32_16x16x128_f8f6f4 v[114:117], v[2:9], v[210:217], v[114:117], v183, v169 op_sel_hi:[0,0,0]
	v_mfma_scale_f32_16x16x128_f8f6f4 v[110:113], v[10:17], v[236:243], v[110:113], v183, v169 op_sel_hi:[0,0,0]
	v_mfma_scale_f32_16x16x128_f8f6f4 v[106:109], v[2:9], v[236:243], v[106:109], v183, v169 op_sel_hi:[0,0,0]
	v_mfma_scale_f32_16x16x128_f8f6f4 v[102:105], v[10:17], v[244:251], v[102:105], v183, v169 op_sel_hi:[0,0,0]
	v_mfma_scale_f32_16x16x128_f8f6f4 v[98:101], v[2:9], v[244:251], v[98:101], v183, v169 op_sel_hi:[0,0,0]
	s_setprio 0
	s_barrier
	s_add_i32 s37, 0, 0x18000
	s_add_i32 s65, 0, 0x1c000
	v_add_u32_e32 v2, s37, v221
	v_add_u32_e32 v6, s65, v221
	ds_read_b128 v[26:29], v2
	ds_read_b128 v[30:33], v2 offset:1024
	ds_read_b128 v[18:21], v2 offset:2048
	ds_read_b128 v[22:25], v2 offset:3072
	ds_read_b128 v[10:13], v6
	ds_read_b128 v[14:17], v6 offset:1024
	ds_read_b128 v[2:5], v6 offset:2048
	ds_read_b128 v[6:9], v6 offset:3072
	s_add_u32 s68, s68, 0x20000
	s_addc_u32 s69, s69, 0
	s_mov_b32 m0, s23
	v_lshl_add_u64 v[170:171], s[68:69], 0, v[178:179]
	ds_read_b128 v[202:205], v222 offset:32768
	ds_read_b128 v[206:209], v222 offset:33792
	ds_read_b128 v[210:213], v222 offset:34816
	ds_read_b128 v[214:217], v222 offset:35840
	ds_read_b128 v[236:239], v222 offset:36864
	ds_read_b128 v[240:243], v222 offset:37888
	ds_read_b128 v[244:247], v222 offset:38912
	ds_read_b128 v[248:251], v222 offset:39936
	global_load_lds_dwordx4 v[170:171], off
	v_lshl_add_u64 v[170:171], s[68:69], 0, v[180:181]
	s_mov_b32 m0, s12
	s_nop 0
	global_load_lds_dwordx4 v[170:171], off
	s_waitcnt vmcnt(8)
	s_waitcnt lgkmcnt(0)
	s_barrier
	s_setprio 1
	v_mfma_scale_f32_16x16x128_f8f6f4 v[94:97], v[26:33], v[202:209], v[94:97], v183, v169 op_sel_hi:[0,0,0]
	v_mfma_scale_f32_16x16x128_f8f6f4 v[90:93], v[18:25], v[202:209], v[90:93], v183, v169 op_sel_hi:[0,0,0]
	v_mfma_scale_f32_16x16x128_f8f6f4 v[86:89], v[26:33], v[210:217], v[86:89], v183, v169 op_sel_hi:[0,0,0]
	v_mfma_scale_f32_16x16x128_f8f6f4 v[82:85], v[18:25], v[210:217], v[82:85], v183, v169 op_sel_hi:[0,0,0]
	v_mfma_scale_f32_16x16x128_f8f6f4 v[78:81], v[26:33], v[236:243], v[78:81], v183, v169 op_sel_hi:[0,0,0]
	v_mfma_scale_f32_16x16x128_f8f6f4 v[74:77], v[18:25], v[236:243], v[74:77], v183, v169 op_sel_hi:[0,0,0]
	v_mfma_scale_f32_16x16x128_f8f6f4 v[70:73], v[26:33], v[244:251], v[70:73], v183, v169 op_sel_hi:[0,0,0]
	v_mfma_scale_f32_16x16x128_f8f6f4 v[66:69], v[18:25], v[244:251], v[66:69], v183, v169 op_sel_hi:[0,0,0]
	s_setprio 0
	s_setprio 1
	v_mfma_scale_f32_16x16x128_f8f6f4 v[158:161], v[10:17], v[202:209], v[158:161], v183, v169 op_sel_hi:[0,0,0]
	v_mfma_scale_f32_16x16x128_f8f6f4 v[154:157], v[2:9], v[202:209], v[154:157], v183, v169 op_sel_hi:[0,0,0]
	v_mfma_scale_f32_16x16x128_f8f6f4 v[150:153], v[10:17], v[210:217], v[150:153], v183, v169 op_sel_hi:[0,0,0]
	v_mfma_scale_f32_16x16x128_f8f6f4 v[146:149], v[2:9], v[210:217], v[146:149], v183, v169 op_sel_hi:[0,0,0]
	v_mfma_scale_f32_16x16x128_f8f6f4 v[142:145], v[10:17], v[236:243], v[142:145], v183, v169 op_sel_hi:[0,0,0]
	v_mfma_scale_f32_16x16x128_f8f6f4 v[138:141], v[2:9], v[236:243], v[138:141], v183, v169 op_sel_hi:[0,0,0]
	v_mfma_scale_f32_16x16x128_f8f6f4 v[134:137], v[10:17], v[244:251], v[134:137], v183, v169 op_sel_hi:[0,0,0]
	v_mfma_scale_f32_16x16x128_f8f6f4 v[130:133], v[2:9], v[244:251], v[130:133], v183, v169 op_sel_hi:[0,0,0]
	s_setprio 0
	s_barrier
	s_add_i32 s37, s37, s20
	v_lshl_add_u64 v[170:171], v[194:195], 0, s[56:57]
	s_mov_b32 m0, s37
	ds_read_b128 v[202:205], v222 offset:49152
	ds_read_b128 v[206:209], v222 offset:50176
	ds_read_b128 v[210:213], v222 offset:51200
	ds_read_b128 v[214:217], v222 offset:52224
	ds_read_b128 v[236:239], v222 offset:53248
	ds_read_b128 v[240:243], v222 offset:54272
	ds_read_b128 v[244:247], v222 offset:55296
	ds_read_b128 v[248:251], v222 offset:56320
	global_load_lds_dwordx4 v[170:171], off
	s_add_i32 m0, s37, 0x2000
	s_add_u32 s40, s40, 0x20080
	v_lshl_add_u64 v[170:171], v[196:197], 0, s[56:57]
	s_addc_u32 s41, s41, 0
	s_add_i32 s37, s65, s20
	global_load_lds_dwordx4 v[170:171], off
	v_lshl_add_u64 v[170:171], s[40:41], 0, v[162:163]
	s_mov_b32 m0, s37
	s_nop 0
	global_load_lds_dwordx4 v[170:171], off
	v_lshl_add_u64 v[170:171], s[40:41], 0, v[164:165]
	s_add_i32 m0, s37, 0x2000
	s_nop 0
	global_load_lds_dwordx4 v[170:171], off
	v_lshl_add_u64 v[170:171], v[198:199], 0, s[56:57]
	s_mov_b32 m0, s92
	s_nop 0
	global_load_lds_dwordx4 v[170:171], off
	v_lshl_add_u64 v[170:171], v[200:201], 0, s[56:57]
	s_mov_b32 m0, s93
	s_nop 0
	global_load_lds_dwordx4 v[170:171], off
	s_waitcnt vmcnt(8)
	s_waitcnt lgkmcnt(0)
	s_barrier
	s_setprio 1
	v_mfma_scale_f32_16x16x128_f8f6f4 v[62:65], v[26:33], v[202:209], v[62:65], v183, v169 op_sel_hi:[0,0,0]
	v_mfma_scale_f32_16x16x128_f8f6f4 v[58:61], v[18:25], v[202:209], v[58:61], v183, v169 op_sel_hi:[0,0,0]
	v_mfma_scale_f32_16x16x128_f8f6f4 v[54:57], v[26:33], v[210:217], v[54:57], v183, v169 op_sel_hi:[0,0,0]
	v_mfma_scale_f32_16x16x128_f8f6f4 v[50:53], v[18:25], v[210:217], v[50:53], v183, v169 op_sel_hi:[0,0,0]
	v_mfma_scale_f32_16x16x128_f8f6f4 v[46:49], v[26:33], v[236:243], v[46:49], v183, v169 op_sel_hi:[0,0,0]
	v_mfma_scale_f32_16x16x128_f8f6f4 v[42:45], v[18:25], v[236:243], v[42:45], v183, v169 op_sel_hi:[0,0,0]
	v_mfma_scale_f32_16x16x128_f8f6f4 v[38:41], v[26:33], v[244:251], v[38:41], v183, v169 op_sel_hi:[0,0,0]
	v_mfma_scale_f32_16x16x128_f8f6f4 v[34:37], v[18:25], v[244:251], v[34:37], v183, v169 op_sel_hi:[0,0,0]
	s_setprio 0
	s_setprio 1
	v_mfma_scale_f32_16x16x128_f8f6f4 v[126:129], v[10:17], v[202:209], v[126:129], v183, v169 op_sel_hi:[0,0,0]
	v_mfma_scale_f32_16x16x128_f8f6f4 v[122:125], v[2:9], v[202:209], v[122:125], v183, v169 op_sel_hi:[0,0,0]
	v_mfma_scale_f32_16x16x128_f8f6f4 v[118:121], v[10:17], v[210:217], v[118:121], v183, v169 op_sel_hi:[0,0,0]
	v_mfma_scale_f32_16x16x128_f8f6f4 v[114:117], v[2:9], v[210:217], v[114:117], v183, v169 op_sel_hi:[0,0,0]
	v_mfma_scale_f32_16x16x128_f8f6f4 v[110:113], v[10:17], v[236:243], v[110:113], v183, v169 op_sel_hi:[0,0,0]
	v_mfma_scale_f32_16x16x128_f8f6f4 v[106:109], v[2:9], v[236:243], v[106:109], v183, v169 op_sel_hi:[0,0,0]
	v_mfma_scale_f32_16x16x128_f8f6f4 v[102:105], v[10:17], v[244:251], v[102:105], v183, v169 op_sel_hi:[0,0,0]
	v_mfma_scale_f32_16x16x128_f8f6f4 v[98:101], v[2:9], v[244:251], v[98:101], v183, v169 op_sel_hi:[0,0,0]
	s_setprio 0
	s_barrier
	s_add_u32 s16, s16, 0x100
	s_addc_u32 s19, s19, 0
	s_add_u32 s38, s38, 0x100
	s_addc_u32 s39, s39, 0
	s_cmp_ge_i32 s27, s74
	s_mov_b32 s37, s27
	s_cbranch_scc0 .LBB0_1016

.Lpeelph12_0:
	s_add_i32 s66, s54, 2
	s_add_u32 s55, s52, 0xfffc0080
	s_addc_u32 s58, s53, -1
	s_add_i32 s68, 0, 0x10000
	s_cmp_eq_u32 s60, s54
	s_cselect_b32 s59, s41, s58
	s_cselect_b32 s58, s43, s55
	v_add_u32_e32 v144, s68, v147
	s_cselect_b32 s55, s62, s65
	s_cselect_b32 s54, s63, s64
	s_add_i32 s70, 0, 0x14000
	ds_read_b128 v[140:143], v144
	ds_read_b128 v[150:153], v144 offset:1024
	ds_read_b128 v[154:157], v144 offset:2048
	ds_read_b128 v[158:161], v144 offset:3072
	v_add_u32_e32 v144, s70, v147
	ds_read_b128 v[162:165], v144
	ds_read_b128 v[170:173], v144 offset:1024
	ds_read_b128 v[174:177], v144 offset:2048
	ds_read_b128 v[178:181], v144 offset:3072
	v_lshl_add_u64 v[144:145], s[52:53], 0, v[138:139]
	s_add_i32 m0, s16, 0xc000
	ds_read_b128 v[182:185], v149
	ds_read_b128 v[186:189], v149 offset:1024
	ds_read_b128 v[190:193], v149 offset:2048
	ds_read_b128 v[194:197], v149 offset:3072
	ds_read_b128 v[198:201], v149 offset:4096
	ds_read_b128 v[202:205], v149 offset:5120
	ds_read_b128 v[206:209], v149 offset:6144
	ds_read_b128 v[210:213], v149 offset:7168
	global_load_lds_dwordx4 v[144:145], off
	v_lshl_add_u64 v[144:145], s[52:53], 0, v[136:137]
	s_add_i32 m0, s16, 0xe000
	s_nop 0
	global_load_lds_dwordx4 v[144:145], off
	s_waitcnt vmcnt(8)
	s_waitcnt lgkmcnt(0)
	s_barrier
	s_setprio 1
	v_mfma_f32_16x16x32_bf16 v[126:129], v[140:143], v[182:185], 0
	v_mfma_f32_16x16x32_bf16 v[122:125], v[154:157], v[182:185], 0
	v_mfma_f32_16x16x32_bf16 v[110:113], v[140:143], v[190:193], 0
	v_mfma_f32_16x16x32_bf16 v[106:109], v[154:157], v[190:193], 0
	v_mfma_f32_16x16x32_bf16 v[94:97], v[140:143], v[198:201], 0
	v_mfma_f32_16x16x32_bf16 v[90:93], v[154:157], v[198:201], 0
	v_mfma_f32_16x16x32_bf16 v[78:81], v[140:143], v[206:209], 0
	v_mfma_f32_16x16x32_bf16 v[74:77], v[154:157], v[206:209], 0
	v_mfma_f32_16x16x32_bf16 v[126:129], v[150:153], v[186:189], v[126:129]
	v_mfma_f32_16x16x32_bf16 v[122:125], v[158:161], v[186:189], v[122:125]
	v_mfma_f32_16x16x32_bf16 v[110:113], v[150:153], v[194:197], v[110:113]
	v_mfma_f32_16x16x32_bf16 v[106:109], v[158:161], v[194:197], v[106:109]
	v_mfma_f32_16x16x32_bf16 v[94:97], v[150:153], v[202:205], v[94:97]
	v_mfma_f32_16x16x32_bf16 v[90:93], v[158:161], v[202:205], v[90:93]
	v_mfma_f32_16x16x32_bf16 v[78:81], v[150:153], v[210:213], v[78:81]
	v_mfma_f32_16x16x32_bf16 v[74:77], v[158:161], v[210:213], v[74:77]
	s_setprio 0
	s_setprio 1
	v_mfma_f32_16x16x32_bf16 v[118:121], v[162:165], v[182:185], 0
	v_mfma_f32_16x16x32_bf16 v[114:117], v[174:177], v[182:185], 0
	v_mfma_f32_16x16x32_bf16 v[102:105], v[162:165], v[190:193], 0
	v_mfma_f32_16x16x32_bf16 v[98:101], v[174:177], v[190:193], 0
	v_mfma_f32_16x16x32_bf16 v[86:89], v[162:165], v[198:201], 0
	v_mfma_f32_16x16x32_bf16 v[82:85], v[174:177], v[198:201], 0
	v_mfma_f32_16x16x32_bf16 v[70:73], v[162:165], v[206:209], 0
	v_mfma_f32_16x16x32_bf16 v[66:69], v[174:177], v[206:209], 0
	v_mfma_f32_16x16x32_bf16 v[118:121], v[170:173], v[186:189], v[118:121]
	v_mfma_f32_16x16x32_bf16 v[114:117], v[178:181], v[186:189], v[114:117]
	v_mfma_f32_16x16x32_bf16 v[102:105], v[170:173], v[194:197], v[102:105]
	v_mfma_f32_16x16x32_bf16 v[98:101], v[178:181], v[194:197], v[98:101]
	v_mfma_f32_16x16x32_bf16 v[86:89], v[170:173], v[202:205], v[86:89]
	v_mfma_f32_16x16x32_bf16 v[82:85], v[178:181], v[202:205], v[82:85]
	v_mfma_f32_16x16x32_bf16 v[70:73], v[170:173], v[210:213], v[70:73]
	v_mfma_f32_16x16x32_bf16 v[66:69], v[178:181], v[210:213], v[66:69]
	s_setprio 0
	s_barrier
	s_add_i32 s68, s68, s15
	v_lshl_add_u64 v[144:145], s[54:55], 0, v[166:167]
	s_mov_b32 m0, s68
	ds_read_b128 v[182:185], v149 offset:16384
	ds_read_b128 v[186:189], v149 offset:17408
	ds_read_b128 v[190:193], v149 offset:18432
	ds_read_b128 v[194:197], v149 offset:19456
	ds_read_b128 v[198:201], v149 offset:20480
	ds_read_b128 v[202:205], v149 offset:21504
	ds_read_b128 v[206:209], v149 offset:22528
	ds_read_b128 v[210:213], v149 offset:23552
	global_load_lds_dwordx4 v[144:145], off
	s_add_i32 m0, s68, 0x2000
	s_add_u32 s68, s54, 0x40000
	v_lshl_add_u64 v[214:215], s[54:55], 0, v[130:131]
	s_addc_u32 s69, s55, 0
	s_add_i32 s70, s70, s15
	global_load_lds_dwordx4 v[214:215], off
	v_lshl_add_u64 v[216:217], s[68:69], 0, v[166:167]
	s_mov_b32 m0, s70
	v_lshl_add_u64 v[218:219], s[58:59], 0, v[134:135]
	global_load_lds_dwordx4 v[216:217], off
	v_lshl_add_u64 v[216:217], s[68:69], 0, v[130:131]
	s_add_i32 m0, s70, 0x2000
	s_nop 0
	global_load_lds_dwordx4 v[216:217], off
	v_lshl_add_u64 v[216:217], s[58:59], 0, v[132:133]
	s_mov_b32 m0, s16
	s_nop 0
	global_load_lds_dwordx4 v[216:217], off
	s_mov_b32 m0, s20
	s_nop 0
	global_load_lds_dwordx4 v[218:219], off
	s_waitcnt vmcnt(8)
	s_waitcnt lgkmcnt(0)
	s_barrier
	s_setprio 1
	v_mfma_f32_16x16x32_bf16 v[62:65], v[140:143], v[182:185], 0
	v_mfma_f32_16x16x32_bf16 v[58:61], v[154:157], v[182:185], 0
	v_mfma_f32_16x16x32_bf16 v[46:49], v[140:143], v[190:193], 0
	v_mfma_f32_16x16x32_bf16 v[42:45], v[154:157], v[190:193], 0
	v_mfma_f32_16x16x32_bf16 v[30:33], v[140:143], v[198:201], 0
	v_mfma_f32_16x16x32_bf16 v[26:29], v[154:157], v[198:201], 0
	v_mfma_f32_16x16x32_bf16 v[14:17], v[140:143], v[206:209], 0
	v_mfma_f32_16x16x32_bf16 v[10:13], v[154:157], v[206:209], 0
	v_mfma_f32_16x16x32_bf16 v[62:65], v[150:153], v[186:189], v[62:65]
	v_mfma_f32_16x16x32_bf16 v[58:61], v[158:161], v[186:189], v[58:61]
	v_mfma_f32_16x16x32_bf16 v[46:49], v[150:153], v[194:197], v[46:49]
	v_mfma_f32_16x16x32_bf16 v[42:45], v[158:161], v[194:197], v[42:45]
	v_mfma_f32_16x16x32_bf16 v[30:33], v[150:153], v[202:205], v[30:33]
	v_mfma_f32_16x16x32_bf16 v[26:29], v[158:161], v[202:205], v[26:29]
	v_mfma_f32_16x16x32_bf16 v[14:17], v[150:153], v[210:213], v[14:17]
	v_mfma_f32_16x16x32_bf16 v[10:13], v[158:161], v[210:213], v[10:13]
	s_setprio 0
	s_setprio 1
	v_mfma_f32_16x16x32_bf16 v[54:57], v[162:165], v[182:185], 0
	v_mfma_f32_16x16x32_bf16 v[50:53], v[174:177], v[182:185], 0
	v_mfma_f32_16x16x32_bf16 v[38:41], v[162:165], v[190:193], 0
	v_mfma_f32_16x16x32_bf16 v[34:37], v[174:177], v[190:193], 0
	v_mfma_f32_16x16x32_bf16 v[22:25], v[162:165], v[198:201], 0
	v_mfma_f32_16x16x32_bf16 v[18:21], v[174:177], v[198:201], 0
	v_mfma_f32_16x16x32_bf16 v[6:9], v[162:165], v[206:209], 0
	v_mfma_f32_16x16x32_bf16 v[2:5], v[174:177], v[206:209], 0
	v_mfma_f32_16x16x32_bf16 v[54:57], v[170:173], v[186:189], v[54:57]
	v_mfma_f32_16x16x32_bf16 v[50:53], v[178:181], v[186:189], v[50:53]
	v_mfma_f32_16x16x32_bf16 v[38:41], v[170:173], v[194:197], v[38:41]
	v_mfma_f32_16x16x32_bf16 v[34:37], v[178:181], v[194:197], v[34:37]
	v_mfma_f32_16x16x32_bf16 v[22:25], v[170:173], v[202:205], v[22:25]
	v_mfma_f32_16x16x32_bf16 v[18:21], v[178:181], v[202:205], v[18:21]
	v_mfma_f32_16x16x32_bf16 v[6:9], v[170:173], v[210:213], v[6:9]
	v_mfma_f32_16x16x32_bf16 v[2:5], v[178:181], v[210:213], v[2:5]
	s_setprio 0
	s_barrier
	s_add_i32 s68, 0, 0x18000
	s_add_i32 s69, 0, 0x1c000
	v_add_u32_e32 v158, s68, v147
	v_add_u32_e32 v169, s69, v147
	ds_read_b128 v[140:143], v158
	ds_read_b128 v[150:153], v158 offset:1024
	ds_read_b128 v[154:157], v158 offset:2048
	ds_read_b128 v[158:161], v158 offset:3072
	ds_read_b128 v[162:165], v169
	ds_read_b128 v[170:173], v169 offset:1024
	ds_read_b128 v[174:177], v169 offset:2048
	ds_read_b128 v[178:181], v169 offset:3072
	s_add_u32 s58, s58, 0x40000
	s_addc_u32 s59, s59, 0
	s_mov_b32 m0, s21
	v_lshl_add_u64 v[220:221], s[58:59], 0, v[132:133]
	ds_read_b128 v[182:185], v149 offset:32768
	ds_read_b128 v[186:189], v149 offset:33792
	ds_read_b128 v[190:193], v149 offset:34816
	ds_read_b128 v[194:197], v149 offset:35840
	ds_read_b128 v[198:201], v149 offset:36864
	ds_read_b128 v[202:205], v149 offset:37888
	ds_read_b128 v[206:209], v149 offset:38912
	ds_read_b128 v[210:213], v149 offset:39936
	global_load_lds_dwordx4 v[220:221], off
	v_lshl_add_u64 v[220:221], s[58:59], 0, v[134:135]
	s_mov_b32 m0, s22
	s_nop 0
	global_load_lds_dwordx4 v[220:221], off
	s_waitcnt vmcnt(8)
	s_waitcnt lgkmcnt(0)
	s_barrier
	s_setprio 1
	v_mfma_f32_16x16x32_bf16 v[126:129], v[140:143], v[182:185], v[126:129]
	v_mfma_f32_16x16x32_bf16 v[122:125], v[154:157], v[182:185], v[122:125]
	v_mfma_f32_16x16x32_bf16 v[110:113], v[140:143], v[190:193], v[110:113]
	v_mfma_f32_16x16x32_bf16 v[106:109], v[154:157], v[190:193], v[106:109]
	v_mfma_f32_16x16x32_bf16 v[94:97], v[140:143], v[198:201], v[94:97]
	v_mfma_f32_16x16x32_bf16 v[90:93], v[154:157], v[198:201], v[90:93]
	v_mfma_f32_16x16x32_bf16 v[78:81], v[140:143], v[206:209], v[78:81]
	v_mfma_f32_16x16x32_bf16 v[74:77], v[154:157], v[206:209], v[74:77]
	v_mfma_f32_16x16x32_bf16 v[126:129], v[150:153], v[186:189], v[126:129]
	v_mfma_f32_16x16x32_bf16 v[122:125], v[158:161], v[186:189], v[122:125]
	v_mfma_f32_16x16x32_bf16 v[110:113], v[150:153], v[194:197], v[110:113]
	v_mfma_f32_16x16x32_bf16 v[106:109], v[158:161], v[194:197], v[106:109]
	v_mfma_f32_16x16x32_bf16 v[94:97], v[150:153], v[202:205], v[94:97]
	v_mfma_f32_16x16x32_bf16 v[90:93], v[158:161], v[202:205], v[90:93]
	v_mfma_f32_16x16x32_bf16 v[78:81], v[150:153], v[210:213], v[78:81]
	v_mfma_f32_16x16x32_bf16 v[74:77], v[158:161], v[210:213], v[74:77]
	s_setprio 0
	s_setprio 1
	v_mfma_f32_16x16x32_bf16 v[118:121], v[162:165], v[182:185], v[118:121]
	v_mfma_f32_16x16x32_bf16 v[114:117], v[174:177], v[182:185], v[114:117]
	v_mfma_f32_16x16x32_bf16 v[102:105], v[162:165], v[190:193], v[102:105]
	v_mfma_f32_16x16x32_bf16 v[98:101], v[174:177], v[190:193], v[98:101]
	v_mfma_f32_16x16x32_bf16 v[86:89], v[162:165], v[198:201], v[86:89]
	v_mfma_f32_16x16x32_bf16 v[82:85], v[174:177], v[198:201], v[82:85]
	v_mfma_f32_16x16x32_bf16 v[70:73], v[162:165], v[206:209], v[70:73]
	v_mfma_f32_16x16x32_bf16 v[66:69], v[174:177], v[206:209], v[66:69]
	v_mfma_f32_16x16x32_bf16 v[118:121], v[170:173], v[186:189], v[118:121]
	v_mfma_f32_16x16x32_bf16 v[114:117], v[178:181], v[186:189], v[114:117]
	v_mfma_f32_16x16x32_bf16 v[102:105], v[170:173], v[194:197], v[102:105]
	v_mfma_f32_16x16x32_bf16 v[98:101], v[178:181], v[194:197], v[98:101]
	v_mfma_f32_16x16x32_bf16 v[86:89], v[170:173], v[202:205], v[86:89]
	v_mfma_f32_16x16x32_bf16 v[82:85], v[178:181], v[202:205], v[82:85]
	v_mfma_f32_16x16x32_bf16 v[70:73], v[170:173], v[210:213], v[70:73]
	v_mfma_f32_16x16x32_bf16 v[66:69], v[178:181], v[210:213], v[66:69]
	s_setprio 0
	s_barrier
	s_add_i32 s58, s68, s15
	v_lshl_add_u64 v[144:145], v[144:145], 0, s[56:57]
	s_mov_b32 m0, s58
	ds_read_b128 v[182:185], v149 offset:49152
	ds_read_b128 v[186:189], v149 offset:50176
	ds_read_b128 v[190:193], v149 offset:51200
	ds_read_b128 v[194:197], v149 offset:52224
	ds_read_b128 v[198:201], v149 offset:53248
	ds_read_b128 v[202:205], v149 offset:54272
	ds_read_b128 v[206:209], v149 offset:55296
	ds_read_b128 v[210:213], v149 offset:56320
	global_load_lds_dwordx4 v[144:145], off
	s_add_i32 m0, s58, 0x2000
	s_add_u32 s54, s54, 0x40080
	v_lshl_add_u64 v[144:145], v[214:215], 0, s[56:57]
	s_addc_u32 s55, s55, 0
	s_add_i32 s58, s69, s15
	global_load_lds_dwordx4 v[144:145], off
	v_lshl_add_u64 v[144:145], s[54:55], 0, v[166:167]
	s_mov_b32 m0, s58
	s_nop 0
	global_load_lds_dwordx4 v[144:145], off
	v_lshl_add_u64 v[144:145], s[54:55], 0, v[130:131]
	s_add_i32 m0, s58, 0x2000
	s_nop 0
	global_load_lds_dwordx4 v[144:145], off
	v_lshl_add_u64 v[144:145], v[216:217], 0, s[56:57]
	s_mov_b32 m0, s23
	s_nop 0
	global_load_lds_dwordx4 v[144:145], off
	v_lshl_add_u64 v[144:145], v[218:219], 0, s[56:57]
	s_mov_b32 m0, s24
	s_nop 0
	global_load_lds_dwordx4 v[144:145], off
	s_waitcnt vmcnt(8)
	s_waitcnt lgkmcnt(0)
	s_barrier
	s_setprio 1
	v_mfma_f32_16x16x32_bf16 v[62:65], v[140:143], v[182:185], v[62:65]
	v_mfma_f32_16x16x32_bf16 v[58:61], v[154:157], v[182:185], v[58:61]
	v_mfma_f32_16x16x32_bf16 v[46:49], v[140:143], v[190:193], v[46:49]
	v_mfma_f32_16x16x32_bf16 v[42:45], v[154:157], v[190:193], v[42:45]
	v_mfma_f32_16x16x32_bf16 v[30:33], v[140:143], v[198:201], v[30:33]
	v_mfma_f32_16x16x32_bf16 v[26:29], v[154:157], v[198:201], v[26:29]
	v_mfma_f32_16x16x32_bf16 v[14:17], v[140:143], v[206:209], v[14:17]
	v_mfma_f32_16x16x32_bf16 v[10:13], v[154:157], v[206:209], v[10:13]
	v_mfma_f32_16x16x32_bf16 v[62:65], v[150:153], v[186:189], v[62:65]
	v_mfma_f32_16x16x32_bf16 v[58:61], v[158:161], v[186:189], v[58:61]
	v_mfma_f32_16x16x32_bf16 v[46:49], v[150:153], v[194:197], v[46:49]
	v_mfma_f32_16x16x32_bf16 v[42:45], v[158:161], v[194:197], v[42:45]
	v_mfma_f32_16x16x32_bf16 v[30:33], v[150:153], v[202:205], v[30:33]
	v_mfma_f32_16x16x32_bf16 v[26:29], v[158:161], v[202:205], v[26:29]
	v_mfma_f32_16x16x32_bf16 v[14:17], v[150:153], v[210:213], v[14:17]
	v_mfma_f32_16x16x32_bf16 v[10:13], v[158:161], v[210:213], v[10:13]
	s_setprio 0
	s_setprio 1
	v_mfma_f32_16x16x32_bf16 v[54:57], v[162:165], v[182:185], v[54:57]
	v_mfma_f32_16x16x32_bf16 v[50:53], v[174:177], v[182:185], v[50:53]
	v_mfma_f32_16x16x32_bf16 v[38:41], v[162:165], v[190:193], v[38:41]
	v_mfma_f32_16x16x32_bf16 v[34:37], v[174:177], v[190:193], v[34:37]
	v_mfma_f32_16x16x32_bf16 v[22:25], v[162:165], v[198:201], v[22:25]
	v_mfma_f32_16x16x32_bf16 v[18:21], v[174:177], v[198:201], v[18:21]
	v_mfma_f32_16x16x32_bf16 v[6:9], v[162:165], v[206:209], v[6:9]
	v_mfma_f32_16x16x32_bf16 v[2:5], v[174:177], v[206:209], v[2:5]
	v_mfma_f32_16x16x32_bf16 v[54:57], v[170:173], v[186:189], v[54:57]
	v_mfma_f32_16x16x32_bf16 v[50:53], v[178:181], v[186:189], v[50:53]
	v_mfma_f32_16x16x32_bf16 v[38:41], v[170:173], v[194:197], v[38:41]
	v_mfma_f32_16x16x32_bf16 v[34:37], v[178:181], v[194:197], v[34:37]
	v_mfma_f32_16x16x32_bf16 v[22:25], v[170:173], v[202:205], v[22:25]
	v_mfma_f32_16x16x32_bf16 v[18:21], v[178:181], v[202:205], v[18:21]
	v_mfma_f32_16x16x32_bf16 v[6:9], v[170:173], v[210:213], v[6:9]
	v_mfma_f32_16x16x32_bf16 v[2:5], v[178:181], v[210:213], v[2:5]
	s_setprio 0
	s_barrier
	s_add_u32 s64, s64, 0x100
	s_addc_u32 s65, s65, 0
	s_add_u32 s52, s52, 0x100
	s_addc_u32 s53, s53, 0
	s_cmp_ge_i32 s66, s1
	s_mov_b32 s54, s66
	s_cbranch_scc0 .LBB0_1438
	s_branch .Lpeelexitph12
.LBB0_1438:
	s_add_i32 s66, s54, 2
	s_add_u32 s55, s52, 0xfffc0080
	s_addc_u32 s58, s53, -1
	s_add_i32 s68, 0, 0x10000
	s_cmp_eq_u32 s60, s54
	s_cselect_b32 s59, s41, s58
	s_cselect_b32 s58, s43, s55
	v_add_u32_e32 v144, s68, v147
	s_cselect_b32 s55, s62, s65
	s_cselect_b32 s54, s63, s64
	s_add_i32 s70, 0, 0x14000
	ds_read_b128 v[140:143], v144
	ds_read_b128 v[150:153], v144 offset:1024
	ds_read_b128 v[154:157], v144 offset:2048
	ds_read_b128 v[158:161], v144 offset:3072
	v_add_u32_e32 v144, s70, v147
	ds_read_b128 v[162:165], v144
	ds_read_b128 v[170:173], v144 offset:1024
	ds_read_b128 v[174:177], v144 offset:2048
	ds_read_b128 v[178:181], v144 offset:3072
	v_lshl_add_u64 v[144:145], s[52:53], 0, v[138:139]
	s_add_i32 m0, s16, 0xc000
	ds_read_b128 v[182:185], v149
	ds_read_b128 v[186:189], v149 offset:1024
	ds_read_b128 v[190:193], v149 offset:2048
	ds_read_b128 v[194:197], v149 offset:3072
	ds_read_b128 v[198:201], v149 offset:4096
	ds_read_b128 v[202:205], v149 offset:5120
	ds_read_b128 v[206:209], v149 offset:6144
	ds_read_b128 v[210:213], v149 offset:7168
	global_load_lds_dwordx4 v[144:145], off
	v_lshl_add_u64 v[144:145], s[52:53], 0, v[136:137]
	s_add_i32 m0, s16, 0xe000
	s_nop 0
	global_load_lds_dwordx4 v[144:145], off
	s_waitcnt vmcnt(8)
	s_waitcnt lgkmcnt(0)
	s_barrier
	s_setprio 1
	v_mfma_f32_16x16x32_bf16 v[126:129], v[140:143], v[182:185], v[126:129]
	v_mfma_f32_16x16x32_bf16 v[122:125], v[154:157], v[182:185], v[122:125]
	v_mfma_f32_16x16x32_bf16 v[110:113], v[140:143], v[190:193], v[110:113]
	v_mfma_f32_16x16x32_bf16 v[106:109], v[154:157], v[190:193], v[106:109]
	v_mfma_f32_16x16x32_bf16 v[94:97], v[140:143], v[198:201], v[94:97]
	v_mfma_f32_16x16x32_bf16 v[90:93], v[154:157], v[198:201], v[90:93]
	v_mfma_f32_16x16x32_bf16 v[78:81], v[140:143], v[206:209], v[78:81]
	v_mfma_f32_16x16x32_bf16 v[74:77], v[154:157], v[206:209], v[74:77]
	v_mfma_f32_16x16x32_bf16 v[126:129], v[150:153], v[186:189], v[126:129]
	v_mfma_f32_16x16x32_bf16 v[122:125], v[158:161], v[186:189], v[122:125]
	v_mfma_f32_16x16x32_bf16 v[110:113], v[150:153], v[194:197], v[110:113]
	v_mfma_f32_16x16x32_bf16 v[106:109], v[158:161], v[194:197], v[106:109]
	v_mfma_f32_16x16x32_bf16 v[94:97], v[150:153], v[202:205], v[94:97]
	v_mfma_f32_16x16x32_bf16 v[90:93], v[158:161], v[202:205], v[90:93]
	v_mfma_f32_16x16x32_bf16 v[78:81], v[150:153], v[210:213], v[78:81]
	v_mfma_f32_16x16x32_bf16 v[74:77], v[158:161], v[210:213], v[74:77]
	s_setprio 0
	s_setprio 1
	v_mfma_f32_16x16x32_bf16 v[118:121], v[162:165], v[182:185], v[118:121]
	v_mfma_f32_16x16x32_bf16 v[114:117], v[174:177], v[182:185], v[114:117]
	v_mfma_f32_16x16x32_bf16 v[102:105], v[162:165], v[190:193], v[102:105]
	v_mfma_f32_16x16x32_bf16 v[98:101], v[174:177], v[190:193], v[98:101]
	v_mfma_f32_16x16x32_bf16 v[86:89], v[162:165], v[198:201], v[86:89]
	v_mfma_f32_16x16x32_bf16 v[82:85], v[174:177], v[198:201], v[82:85]
	v_mfma_f32_16x16x32_bf16 v[70:73], v[162:165], v[206:209], v[70:73]
	v_mfma_f32_16x16x32_bf16 v[66:69], v[174:177], v[206:209], v[66:69]
	v_mfma_f32_16x16x32_bf16 v[118:121], v[170:173], v[186:189], v[118:121]
	v_mfma_f32_16x16x32_bf16 v[114:117], v[178:181], v[186:189], v[114:117]
	v_mfma_f32_16x16x32_bf16 v[102:105], v[170:173], v[194:197], v[102:105]
	v_mfma_f32_16x16x32_bf16 v[98:101], v[178:181], v[194:197], v[98:101]
	v_mfma_f32_16x16x32_bf16 v[86:89], v[170:173], v[202:205], v[86:89]
	v_mfma_f32_16x16x32_bf16 v[82:85], v[178:181], v[202:205], v[82:85]
	v_mfma_f32_16x16x32_bf16 v[70:73], v[170:173], v[210:213], v[70:73]
	v_mfma_f32_16x16x32_bf16 v[66:69], v[178:181], v[210:213], v[66:69]
	s_setprio 0
	s_barrier
	s_add_i32 s68, s68, s15
	v_lshl_add_u64 v[144:145], s[54:55], 0, v[166:167]
	s_mov_b32 m0, s68
	ds_read_b128 v[182:185], v149 offset:16384
	ds_read_b128 v[186:189], v149 offset:17408
	ds_read_b128 v[190:193], v149 offset:18432
	ds_read_b128 v[194:197], v149 offset:19456
	ds_read_b128 v[198:201], v149 offset:20480
	ds_read_b128 v[202:205], v149 offset:21504
	ds_read_b128 v[206:209], v149 offset:22528
	ds_read_b128 v[210:213], v149 offset:23552
	global_load_lds_dwordx4 v[144:145], off
	s_add_i32 m0, s68, 0x2000
	s_add_u32 s68, s54, 0x40000
	v_lshl_add_u64 v[214:215], s[54:55], 0, v[130:131]
	s_addc_u32 s69, s55, 0
	s_add_i32 s70, s70, s15
	global_load_lds_dwordx4 v[214:215], off
	v_lshl_add_u64 v[216:217], s[68:69], 0, v[166:167]
	s_mov_b32 m0, s70
	v_lshl_add_u64 v[218:219], s[58:59], 0, v[134:135]
	global_load_lds_dwordx4 v[216:217], off
	v_lshl_add_u64 v[216:217], s[68:69], 0, v[130:131]
	s_add_i32 m0, s70, 0x2000
	s_nop 0
	global_load_lds_dwordx4 v[216:217], off
	v_lshl_add_u64 v[216:217], s[58:59], 0, v[132:133]
	s_mov_b32 m0, s16
	s_nop 0
	global_load_lds_dwordx4 v[216:217], off
	s_mov_b32 m0, s20
	s_nop 0
	global_load_lds_dwordx4 v[218:219], off
	s_waitcnt vmcnt(8)
	s_waitcnt lgkmcnt(0)
	s_barrier
	s_setprio 1
	v_mfma_f32_16x16x32_bf16 v[62:65], v[140:143], v[182:185], v[62:65]
	v_mfma_f32_16x16x32_bf16 v[58:61], v[154:157], v[182:185], v[58:61]
	v_mfma_f32_16x16x32_bf16 v[46:49], v[140:143], v[190:193], v[46:49]
	v_mfma_f32_16x16x32_bf16 v[42:45], v[154:157], v[190:193], v[42:45]
	v_mfma_f32_16x16x32_bf16 v[30:33], v[140:143], v[198:201], v[30:33]
	v_mfma_f32_16x16x32_bf16 v[26:29], v[154:157], v[198:201], v[26:29]
	v_mfma_f32_16x16x32_bf16 v[14:17], v[140:143], v[206:209], v[14:17]
	v_mfma_f32_16x16x32_bf16 v[10:13], v[154:157], v[206:209], v[10:13]
	v_mfma_f32_16x16x32_bf16 v[62:65], v[150:153], v[186:189], v[62:65]
	v_mfma_f32_16x16x32_bf16 v[58:61], v[158:161], v[186:189], v[58:61]
	v_mfma_f32_16x16x32_bf16 v[46:49], v[150:153], v[194:197], v[46:49]
	v_mfma_f32_16x16x32_bf16 v[42:45], v[158:161], v[194:197], v[42:45]
	v_mfma_f32_16x16x32_bf16 v[30:33], v[150:153], v[202:205], v[30:33]
	v_mfma_f32_16x16x32_bf16 v[26:29], v[158:161], v[202:205], v[26:29]
	v_mfma_f32_16x16x32_bf16 v[14:17], v[150:153], v[210:213], v[14:17]
	v_mfma_f32_16x16x32_bf16 v[10:13], v[158:161], v[210:213], v[10:13]
	s_setprio 0
	s_setprio 1
	v_mfma_f32_16x16x32_bf16 v[54:57], v[162:165], v[182:185], v[54:57]
	v_mfma_f32_16x16x32_bf16 v[50:53], v[174:177], v[182:185], v[50:53]
	v_mfma_f32_16x16x32_bf16 v[38:41], v[162:165], v[190:193], v[38:41]
	v_mfma_f32_16x16x32_bf16 v[34:37], v[174:177], v[190:193], v[34:37]
	v_mfma_f32_16x16x32_bf16 v[22:25], v[162:165], v[198:201], v[22:25]
	v_mfma_f32_16x16x32_bf16 v[18:21], v[174:177], v[198:201], v[18:21]
	v_mfma_f32_16x16x32_bf16 v[6:9], v[162:165], v[206:209], v[6:9]
	v_mfma_f32_16x16x32_bf16 v[2:5], v[174:177], v[206:209], v[2:5]
	v_mfma_f32_16x16x32_bf16 v[54:57], v[170:173], v[186:189], v[54:57]
	v_mfma_f32_16x16x32_bf16 v[50:53], v[178:181], v[186:189], v[50:53]
	v_mfma_f32_16x16x32_bf16 v[38:41], v[170:173], v[194:197], v[38:41]
	v_mfma_f32_16x16x32_bf16 v[34:37], v[178:181], v[194:197], v[34:37]
	v_mfma_f32_16x16x32_bf16 v[22:25], v[170:173], v[202:205], v[22:25]
	v_mfma_f32_16x16x32_bf16 v[18:21], v[178:181], v[202:205], v[18:21]
	v_mfma_f32_16x16x32_bf16 v[6:9], v[170:173], v[210:213], v[6:9]
	v_mfma_f32_16x16x32_bf16 v[2:5], v[178:181], v[210:213], v[2:5]
	s_setprio 0
	s_barrier
	s_add_i32 s68, 0, 0x18000
	s_add_i32 s69, 0, 0x1c000
	v_add_u32_e32 v158, s68, v147
	v_add_u32_e32 v169, s69, v147
	ds_read_b128 v[140:143], v158
	ds_read_b128 v[150:153], v158 offset:1024
	ds_read_b128 v[154:157], v158 offset:2048
	ds_read_b128 v[158:161], v158 offset:3072
	ds_read_b128 v[162:165], v169
	ds_read_b128 v[170:173], v169 offset:1024
	ds_read_b128 v[174:177], v169 offset:2048
	ds_read_b128 v[178:181], v169 offset:3072
	s_add_u32 s58, s58, 0x40000
	s_addc_u32 s59, s59, 0
	s_mov_b32 m0, s21
	v_lshl_add_u64 v[220:221], s[58:59], 0, v[132:133]
	ds_read_b128 v[182:185], v149 offset:32768
	ds_read_b128 v[186:189], v149 offset:33792
	ds_read_b128 v[190:193], v149 offset:34816
	ds_read_b128 v[194:197], v149 offset:35840
	ds_read_b128 v[198:201], v149 offset:36864
	ds_read_b128 v[202:205], v149 offset:37888
	ds_read_b128 v[206:209], v149 offset:38912
	ds_read_b128 v[210:213], v149 offset:39936
	global_load_lds_dwordx4 v[220:221], off
	v_lshl_add_u64 v[220:221], s[58:59], 0, v[134:135]
	s_mov_b32 m0, s22
	s_nop 0
	global_load_lds_dwordx4 v[220:221], off
	s_waitcnt vmcnt(8)
	s_waitcnt lgkmcnt(0)
	s_barrier
	s_setprio 1
	v_mfma_f32_16x16x32_bf16 v[126:129], v[140:143], v[182:185], v[126:129]
	v_mfma_f32_16x16x32_bf16 v[122:125], v[154:157], v[182:185], v[122:125]
	v_mfma_f32_16x16x32_bf16 v[110:113], v[140:143], v[190:193], v[110:113]
	v_mfma_f32_16x16x32_bf16 v[106:109], v[154:157], v[190:193], v[106:109]
	v_mfma_f32_16x16x32_bf16 v[94:97], v[140:143], v[198:201], v[94:97]
	v_mfma_f32_16x16x32_bf16 v[90:93], v[154:157], v[198:201], v[90:93]
	v_mfma_f32_16x16x32_bf16 v[78:81], v[140:143], v[206:209], v[78:81]
	v_mfma_f32_16x16x32_bf16 v[74:77], v[154:157], v[206:209], v[74:77]
	v_mfma_f32_16x16x32_bf16 v[126:129], v[150:153], v[186:189], v[126:129]
	v_mfma_f32_16x16x32_bf16 v[122:125], v[158:161], v[186:189], v[122:125]
	v_mfma_f32_16x16x32_bf16 v[110:113], v[150:153], v[194:197], v[110:113]
	v_mfma_f32_16x16x32_bf16 v[106:109], v[158:161], v[194:197], v[106:109]
	v_mfma_f32_16x16x32_bf16 v[94:97], v[150:153], v[202:205], v[94:97]
	v_mfma_f32_16x16x32_bf16 v[90:93], v[158:161], v[202:205], v[90:93]
	v_mfma_f32_16x16x32_bf16 v[78:81], v[150:153], v[210:213], v[78:81]
	v_mfma_f32_16x16x32_bf16 v[74:77], v[158:161], v[210:213], v[74:77]
	s_setprio 0
	s_setprio 1
	v_mfma_f32_16x16x32_bf16 v[118:121], v[162:165], v[182:185], v[118:121]
	v_mfma_f32_16x16x32_bf16 v[114:117], v[174:177], v[182:185], v[114:117]
	v_mfma_f32_16x16x32_bf16 v[102:105], v[162:165], v[190:193], v[102:105]
	v_mfma_f32_16x16x32_bf16 v[98:101], v[174:177], v[190:193], v[98:101]
	v_mfma_f32_16x16x32_bf16 v[86:89], v[162:165], v[198:201], v[86:89]
	v_mfma_f32_16x16x32_bf16 v[82:85], v[174:177], v[198:201], v[82:85]
	v_mfma_f32_16x16x32_bf16 v[70:73], v[162:165], v[206:209], v[70:73]
	v_mfma_f32_16x16x32_bf16 v[66:69], v[174:177], v[206:209], v[66:69]
	v_mfma_f32_16x16x32_bf16 v[118:121], v[170:173], v[186:189], v[118:121]
	v_mfma_f32_16x16x32_bf16 v[114:117], v[178:181], v[186:189], v[114:117]
	v_mfma_f32_16x16x32_bf16 v[102:105], v[170:173], v[194:197], v[102:105]
	v_mfma_f32_16x16x32_bf16 v[98:101], v[178:181], v[194:197], v[98:101]
	v_mfma_f32_16x16x32_bf16 v[86:89], v[170:173], v[202:205], v[86:89]
	v_mfma_f32_16x16x32_bf16 v[82:85], v[178:181], v[202:205], v[82:85]
	v_mfma_f32_16x16x32_bf16 v[70:73], v[170:173], v[210:213], v[70:73]
	v_mfma_f32_16x16x32_bf16 v[66:69], v[178:181], v[210:213], v[66:69]
	s_setprio 0
	s_barrier
	s_add_i32 s58, s68, s15
	v_lshl_add_u64 v[144:145], v[144:145], 0, s[56:57]
	s_mov_b32 m0, s58
	ds_read_b128 v[182:185], v149 offset:49152
	ds_read_b128 v[186:189], v149 offset:50176
	ds_read_b128 v[190:193], v149 offset:51200
	ds_read_b128 v[194:197], v149 offset:52224
	ds_read_b128 v[198:201], v149 offset:53248
	ds_read_b128 v[202:205], v149 offset:54272
	ds_read_b128 v[206:209], v149 offset:55296
	ds_read_b128 v[210:213], v149 offset:56320
	global_load_lds_dwordx4 v[144:145], off
	s_add_i32 m0, s58, 0x2000
	s_add_u32 s54, s54, 0x40080
	v_lshl_add_u64 v[144:145], v[214:215], 0, s[56:57]
	s_addc_u32 s55, s55, 0
	s_add_i32 s58, s69, s15
	global_load_lds_dwordx4 v[144:145], off
	v_lshl_add_u64 v[144:145], s[54:55], 0, v[166:167]
	s_mov_b32 m0, s58
	s_nop 0
	global_load_lds_dwordx4 v[144:145], off
	v_lshl_add_u64 v[144:145], s[54:55], 0, v[130:131]
	s_add_i32 m0, s58, 0x2000
	s_nop 0
	global_load_lds_dwordx4 v[144:145], off
	v_lshl_add_u64 v[144:145], v[216:217], 0, s[56:57]
	s_mov_b32 m0, s23
	s_nop 0
	global_load_lds_dwordx4 v[144:145], off
	v_lshl_add_u64 v[144:145], v[218:219], 0, s[56:57]
	s_mov_b32 m0, s24
	s_nop 0
	global_load_lds_dwordx4 v[144:145], off
	s_waitcnt vmcnt(8)
	s_waitcnt lgkmcnt(0)
	s_barrier
	s_setprio 1
	v_mfma_f32_16x16x32_bf16 v[62:65], v[140:143], v[182:185], v[62:65]
	v_mfma_f32_16x16x32_bf16 v[58:61], v[154:157], v[182:185], v[58:61]
	v_mfma_f32_16x16x32_bf16 v[46:49], v[140:143], v[190:193], v[46:49]
	v_mfma_f32_16x16x32_bf16 v[42:45], v[154:157], v[190:193], v[42:45]
	v_mfma_f32_16x16x32_bf16 v[30:33], v[140:143], v[198:201], v[30:33]
	v_mfma_f32_16x16x32_bf16 v[26:29], v[154:157], v[198:201], v[26:29]
	v_mfma_f32_16x16x32_bf16 v[14:17], v[140:143], v[206:209], v[14:17]
	v_mfma_f32_16x16x32_bf16 v[10:13], v[154:157], v[206:209], v[10:13]
	v_mfma_f32_16x16x32_bf16 v[62:65], v[150:153], v[186:189], v[62:65]
	v_mfma_f32_16x16x32_bf16 v[58:61], v[158:161], v[186:189], v[58:61]
	v_mfma_f32_16x16x32_bf16 v[46:49], v[150:153], v[194:197], v[46:49]
	v_mfma_f32_16x16x32_bf16 v[42:45], v[158:161], v[194:197], v[42:45]
	v_mfma_f32_16x16x32_bf16 v[30:33], v[150:153], v[202:205], v[30:33]
	v_mfma_f32_16x16x32_bf16 v[26:29], v[158:161], v[202:205], v[26:29]
	v_mfma_f32_16x16x32_bf16 v[14:17], v[150:153], v[210:213], v[14:17]
	v_mfma_f32_16x16x32_bf16 v[10:13], v[158:161], v[210:213], v[10:13]
	s_setprio 0
	s_setprio 1
	v_mfma_f32_16x16x32_bf16 v[54:57], v[162:165], v[182:185], v[54:57]
	v_mfma_f32_16x16x32_bf16 v[50:53], v[174:177], v[182:185], v[50:53]
	v_mfma_f32_16x16x32_bf16 v[38:41], v[162:165], v[190:193], v[38:41]
	v_mfma_f32_16x16x32_bf16 v[34:37], v[174:177], v[190:193], v[34:37]
	v_mfma_f32_16x16x32_bf16 v[22:25], v[162:165], v[198:201], v[22:25]
	v_mfma_f32_16x16x32_bf16 v[18:21], v[174:177], v[198:201], v[18:21]
	v_mfma_f32_16x16x32_bf16 v[6:9], v[162:165], v[206:209], v[6:9]
	v_mfma_f32_16x16x32_bf16 v[2:5], v[174:177], v[206:209], v[2:5]
	v_mfma_f32_16x16x32_bf16 v[54:57], v[170:173], v[186:189], v[54:57]
	v_mfma_f32_16x16x32_bf16 v[50:53], v[178:181], v[186:189], v[50:53]
	v_mfma_f32_16x16x32_bf16 v[38:41], v[170:173], v[194:197], v[38:41]
	v_mfma_f32_16x16x32_bf16 v[34:37], v[178:181], v[194:197], v[34:37]
	v_mfma_f32_16x16x32_bf16 v[22:25], v[170:173], v[202:205], v[22:25]
	v_mfma_f32_16x16x32_bf16 v[18:21], v[178:181], v[202:205], v[18:21]
	v_mfma_f32_16x16x32_bf16 v[6:9], v[170:173], v[210:213], v[6:9]
	v_mfma_f32_16x16x32_bf16 v[2:5], v[178:181], v[210:213], v[2:5]
	s_setprio 0
	s_barrier
	s_add_u32 s64, s64, 0x100
	s_addc_u32 s65, s65, 0
	s_add_u32 s52, s52, 0x100
	s_addc_u32 s53, s53, 0
	s_cmp_ge_i32 s66, s1
	s_mov_b32 s54, s66
	s_cbranch_scc0 .LBB0_1438

.Lpeelph15_1:
	s_add_i32 s91, s91, 2
	s_add_u32 s64, s70, 0x100
	s_addc_u32 s65, s71, 0
	s_and_b64 s[74:75], s[68:69], exec
	s_cselect_b32 s74, 0, s64
	s_cselect_b32 s75, 0, s65
	s_add_u32 s74, s28, s74
	s_addc_u32 s75, s29, s75
	s_add_u32 s92, s51, s70
	s_addc_u32 s93, s53, s71
	s_and_b64 s[68:69], s[68:69], exec
	s_cselect_b32 s69, s55, s93
	s_cselect_b32 s68, s54, s92
	s_add_i32 s93, 0, 0x10000
	s_add_i32 s92, 0, 0x14000
	v_add_u32_e32 v2, s93, v210
	v_add_u32_e32 v6, s92, v210
	ds_read_b128 v[26:29], v2
	ds_read_b128 v[30:33], v2 offset:1024
	ds_read_b128 v[18:21], v2 offset:2048
	ds_read_b128 v[22:25], v2 offset:3072
	ds_read_b128 v[10:13], v6
	ds_read_b128 v[14:17], v6 offset:1024
	ds_read_b128 v[2:5], v6 offset:2048
	ds_read_b128 v[6:9], v6 offset:3072
	v_lshl_add_u64 v[170:171], v[194:195], 0, s[70:71]
	s_add_i32 m0, s59, 0xc000
	ds_read_b128 v[196:199], v212
	ds_read_b128 v[200:203], v212 offset:1024
	ds_read_b128 v[214:217], v212 offset:2048
	ds_read_b128 v[218:221], v212 offset:3072
	ds_read_b128 v[236:239], v212 offset:4096
	ds_read_b128 v[240:243], v212 offset:5120
	ds_read_b128 v[244:247], v212 offset:6144
	ds_read_b128 v[248:251], v212 offset:7168
	global_load_lds_dwordx4 v[170:171], off
	v_lshl_add_u64 v[170:171], v[192:193], 0, s[70:71]
	s_add_i32 m0, s59, 0xe000
	s_nop 0
	global_load_lds_dwordx4 v[170:171], off
	s_waitcnt vmcnt(8)
	s_waitcnt lgkmcnt(0)
	s_barrier
	s_setprio 1
	v_mfma_scale_f32_16x16x128_f8f6f4 v[154:157], v[26:33], v[196:203], 0, v208, v207 op_sel_hi:[0,0,0]
	v_mfma_scale_f32_16x16x128_f8f6f4 v[150:153], v[18:25], v[196:203], 0, v208, v207 op_sel_hi:[0,0,0]
	v_mfma_scale_f32_16x16x128_f8f6f4 v[142:145], v[26:33], v[214:221], 0, v208, v207 op_sel_hi:[0,0,0]
	v_mfma_scale_f32_16x16x128_f8f6f4 v[134:137], v[18:25], v[214:221], 0, v208, v207 op_sel_hi:[0,0,0]
	v_mfma_scale_f32_16x16x128_f8f6f4 v[126:129], v[26:33], v[236:243], 0, v208, v207 op_sel_hi:[0,0,0]
	v_mfma_scale_f32_16x16x128_f8f6f4 v[118:121], v[18:25], v[236:243], 0, v208, v207 op_sel_hi:[0,0,0]
	v_mfma_scale_f32_16x16x128_f8f6f4 v[110:113], v[26:33], v[244:251], 0, v208, v207 op_sel_hi:[0,0,0]
	v_mfma_scale_f32_16x16x128_f8f6f4 v[102:105], v[18:25], v[244:251], 0, v208, v207 op_sel_hi:[0,0,0]
	s_setprio 0
	s_setprio 1
	v_mfma_scale_f32_16x16x128_f8f6f4 v[158:161], v[10:17], v[196:203], 0, v208, v207 op_sel_hi:[0,0,0]
	v_mfma_scale_f32_16x16x128_f8f6f4 v[146:149], v[2:9], v[196:203], 0, v208, v207 op_sel_hi:[0,0,0]
	v_mfma_scale_f32_16x16x128_f8f6f4 v[138:141], v[10:17], v[214:221], 0, v208, v207 op_sel_hi:[0,0,0]
	v_mfma_scale_f32_16x16x128_f8f6f4 v[130:133], v[2:9], v[214:221], 0, v208, v207 op_sel_hi:[0,0,0]
	v_mfma_scale_f32_16x16x128_f8f6f4 v[122:125], v[10:17], v[236:243], 0, v208, v207 op_sel_hi:[0,0,0]
	v_mfma_scale_f32_16x16x128_f8f6f4 v[114:117], v[2:9], v[236:243], 0, v208, v207 op_sel_hi:[0,0,0]
	v_mfma_scale_f32_16x16x128_f8f6f4 v[106:109], v[10:17], v[244:251], 0, v208, v207 op_sel_hi:[0,0,0]
	v_mfma_scale_f32_16x16x128_f8f6f4 v[98:101], v[2:9], v[244:251], 0, v208, v207 op_sel_hi:[0,0,0]
	s_setprio 0
	s_barrier
	s_add_i32 s70, s93, s72
	v_lshl_add_u64 v[196:197], s[68:69], 0, v[162:163]
	s_mov_b32 m0, s70
	ds_read_b128 v[214:217], v212 offset:16384
	ds_read_b128 v[218:221], v212 offset:17408
	ds_read_b128 v[236:239], v212 offset:18432
	ds_read_b128 v[240:243], v212 offset:19456
	ds_read_b128 v[244:247], v212 offset:20480
	ds_read_b128 v[248:251], v212 offset:21504
	ds_read_b128 v[170:173], v212 offset:22528
	ds_read_b128 v[174:177], v212 offset:23552
	global_load_lds_dwordx4 v[196:197], off
	s_add_i32 m0, s70, 0x2000
	s_add_u32 s70, s68, 0x20000
	v_lshl_add_u64 v[198:199], s[68:69], 0, v[164:165]
	s_addc_u32 s71, s69, 0
	s_add_i32 s92, s92, s72
	global_load_lds_dwordx4 v[198:199], off
	v_lshl_add_u64 v[200:201], s[70:71], 0, v[162:163]
	s_mov_b32 m0, s92
	v_mov_b32_e32 v179, v167
	global_load_lds_dwordx4 v[200:201], off
	v_lshl_add_u64 v[200:201], s[70:71], 0, v[164:165]
	s_add_i32 m0, s92, 0x2000
	v_lshl_add_u64 v[202:203], s[74:75], 0, v[166:167]
	global_load_lds_dwordx4 v[200:201], off
	s_mov_b32 m0, s59
	v_lshl_add_u64 v[200:201], s[74:75], 0, v[178:179]
	global_load_lds_dwordx4 v166, s[74:75]
	s_mov_b32 m0, s61
	s_nop 0
	global_load_lds_dwordx4 v178, s[74:75]
	s_waitcnt vmcnt(8)
	s_waitcnt lgkmcnt(0)
	s_barrier
	s_setprio 1
	v_mfma_scale_f32_16x16x128_f8f6f4 v[94:97], v[26:33], v[214:221], 0, v208, v207 op_sel_hi:[0,0,0]
	v_mfma_scale_f32_16x16x128_f8f6f4 v[86:89], v[18:25], v[214:221], 0, v208, v207 op_sel_hi:[0,0,0]
	v_mfma_scale_f32_16x16x128_f8f6f4 v[78:81], v[26:33], v[236:243], 0, v208, v207 op_sel_hi:[0,0,0]
	v_mfma_scale_f32_16x16x128_f8f6f4 v[70:73], v[18:25], v[236:243], 0, v208, v207 op_sel_hi:[0,0,0]
	v_mfma_scale_f32_16x16x128_f8f6f4 v[62:65], v[26:33], v[244:251], 0, v208, v207 op_sel_hi:[0,0,0]
	v_mfma_scale_f32_16x16x128_f8f6f4 v[54:57], v[18:25], v[244:251], 0, v208, v207 op_sel_hi:[0,0,0]
	v_mfma_scale_f32_16x16x128_f8f6f4 v[46:49], v[26:33], v[170:177], 0, v208, v207 op_sel_hi:[0,0,0]
	v_mfma_scale_f32_16x16x128_f8f6f4 v[38:41], v[18:25], v[170:177], 0, v208, v207 op_sel_hi:[0,0,0]
	s_setprio 0
	s_setprio 1
	v_mfma_scale_f32_16x16x128_f8f6f4 v[90:93], v[10:17], v[214:221], 0, v208, v207 op_sel_hi:[0,0,0]
	v_mfma_scale_f32_16x16x128_f8f6f4 v[82:85], v[2:9], v[214:221], 0, v208, v207 op_sel_hi:[0,0,0]
	v_mfma_scale_f32_16x16x128_f8f6f4 v[74:77], v[10:17], v[236:243], 0, v208, v207 op_sel_hi:[0,0,0]
	v_mfma_scale_f32_16x16x128_f8f6f4 v[66:69], v[2:9], v[236:243], 0, v208, v207 op_sel_hi:[0,0,0]
	v_mfma_scale_f32_16x16x128_f8f6f4 v[58:61], v[10:17], v[244:251], 0, v208, v207 op_sel_hi:[0,0,0]
	v_mfma_scale_f32_16x16x128_f8f6f4 v[50:53], v[2:9], v[244:251], 0, v208, v207 op_sel_hi:[0,0,0]
	v_mfma_scale_f32_16x16x128_f8f6f4 v[42:45], v[10:17], v[170:177], 0, v208, v207 op_sel_hi:[0,0,0]
	v_mfma_scale_f32_16x16x128_f8f6f4 v[34:37], v[2:9], v[170:177], 0, v208, v207 op_sel_hi:[0,0,0]
	s_setprio 0
	s_barrier
	s_add_i32 s70, 0, 0x18000
	s_add_i32 s71, 0, 0x1c000
	v_add_u32_e32 v2, s70, v210
	v_add_u32_e32 v6, s71, v210
	ds_read_b128 v[26:29], v2
	ds_read_b128 v[30:33], v2 offset:1024
	ds_read_b128 v[18:21], v2 offset:2048
	ds_read_b128 v[22:25], v2 offset:3072
	ds_read_b128 v[10:13], v6
	ds_read_b128 v[14:17], v6 offset:1024
	ds_read_b128 v[2:5], v6 offset:2048
	ds_read_b128 v[6:9], v6 offset:3072
	s_mov_b32 m0, s73
	ds_read_b128 v[170:173], v212 offset:32768
	ds_read_b128 v[174:177], v212 offset:33792
	ds_read_b128 v[214:217], v212 offset:34816
	ds_read_b128 v[218:221], v212 offset:35840
	ds_read_b128 v[236:239], v212 offset:36864
	ds_read_b128 v[240:243], v212 offset:37888
	ds_read_b128 v[244:247], v212 offset:38912
	ds_read_b128 v[248:251], v212 offset:39936
	global_load_lds_dwordx4 v180, s[74:75]
	s_mov_b32 m0, s76
	s_nop 0
	global_load_lds_dwordx4 v182, s[74:75]
	s_waitcnt vmcnt(8)
	s_waitcnt lgkmcnt(0)
	s_barrier
	s_setprio 1
	v_mfma_scale_f32_16x16x128_f8f6f4 v[154:157], v[26:33], v[170:177], v[154:157], v208, v207 op_sel_hi:[0,0,0]
	v_mfma_scale_f32_16x16x128_f8f6f4 v[150:153], v[18:25], v[170:177], v[150:153], v208, v207 op_sel_hi:[0,0,0]
	v_mfma_scale_f32_16x16x128_f8f6f4 v[142:145], v[26:33], v[214:221], v[142:145], v208, v207 op_sel_hi:[0,0,0]
	v_mfma_scale_f32_16x16x128_f8f6f4 v[134:137], v[18:25], v[214:221], v[134:137], v208, v207 op_sel_hi:[0,0,0]
	v_mfma_scale_f32_16x16x128_f8f6f4 v[126:129], v[26:33], v[236:243], v[126:129], v208, v207 op_sel_hi:[0,0,0]
	v_mfma_scale_f32_16x16x128_f8f6f4 v[118:121], v[18:25], v[236:243], v[118:121], v208, v207 op_sel_hi:[0,0,0]
	v_mfma_scale_f32_16x16x128_f8f6f4 v[110:113], v[26:33], v[244:251], v[110:113], v208, v207 op_sel_hi:[0,0,0]
	v_mfma_scale_f32_16x16x128_f8f6f4 v[102:105], v[18:25], v[244:251], v[102:105], v208, v207 op_sel_hi:[0,0,0]
	s_setprio 0
	s_setprio 1
	v_mfma_scale_f32_16x16x128_f8f6f4 v[158:161], v[10:17], v[170:177], v[158:161], v208, v207 op_sel_hi:[0,0,0]
	v_mfma_scale_f32_16x16x128_f8f6f4 v[146:149], v[2:9], v[170:177], v[146:149], v208, v207 op_sel_hi:[0,0,0]
	v_mfma_scale_f32_16x16x128_f8f6f4 v[138:141], v[10:17], v[214:221], v[138:141], v208, v207 op_sel_hi:[0,0,0]
	v_mfma_scale_f32_16x16x128_f8f6f4 v[130:133], v[2:9], v[214:221], v[130:133], v208, v207 op_sel_hi:[0,0,0]
	v_mfma_scale_f32_16x16x128_f8f6f4 v[122:125], v[10:17], v[236:243], v[122:125], v208, v207 op_sel_hi:[0,0,0]
	v_mfma_scale_f32_16x16x128_f8f6f4 v[114:117], v[2:9], v[236:243], v[114:117], v208, v207 op_sel_hi:[0,0,0]
	v_mfma_scale_f32_16x16x128_f8f6f4 v[106:109], v[10:17], v[244:251], v[106:109], v208, v207 op_sel_hi:[0,0,0]
	v_mfma_scale_f32_16x16x128_f8f6f4 v[98:101], v[2:9], v[244:251], v[98:101], v208, v207 op_sel_hi:[0,0,0]
	s_setprio 0
	s_barrier
	s_add_i32 s70, s70, s72
	v_lshl_add_u64 v[196:197], v[196:197], 0, s[56:57]
	s_mov_b32 m0, s70
	ds_read_b128 v[170:173], v212 offset:49152
	ds_read_b128 v[174:177], v212 offset:50176
	ds_read_b128 v[214:217], v212 offset:51200
	ds_read_b128 v[218:221], v212 offset:52224
	ds_read_b128 v[236:239], v212 offset:53248
	ds_read_b128 v[240:243], v212 offset:54272
	ds_read_b128 v[244:247], v212 offset:55296
	ds_read_b128 v[248:251], v212 offset:56320
	global_load_lds_dwordx4 v[196:197], off
	s_add_i32 m0, s70, 0x2000
	s_add_u32 s68, s68, 0x20080
	v_lshl_add_u64 v[196:197], v[198:199], 0, s[56:57]
	s_addc_u32 s69, s69, 0
	s_add_i32 s70, s71, s72
	global_load_lds_dwordx4 v[196:197], off
	v_lshl_add_u64 v[196:197], s[68:69], 0, v[162:163]
	s_mov_b32 m0, s70
	s_nop 0
	global_load_lds_dwordx4 v[196:197], off
	v_lshl_add_u64 v[196:197], s[68:69], 0, v[164:165]
	s_add_i32 m0, s70, 0x2000
	s_nop 0
	global_load_lds_dwordx4 v[196:197], off
	v_lshl_add_u64 v[196:197], v[202:203], 0, s[56:57]
	s_mov_b32 m0, s77
	s_nop 0
	global_load_lds_dwordx4 v[196:197], off
	v_lshl_add_u64 v[196:197], v[200:201], 0, s[56:57]
	s_mov_b32 m0, s79
	s_nop 0
	global_load_lds_dwordx4 v[196:197], off
	s_waitcnt vmcnt(8)
	s_waitcnt lgkmcnt(0)
	s_barrier
	s_setprio 1
	v_mfma_scale_f32_16x16x128_f8f6f4 v[94:97], v[26:33], v[170:177], v[94:97], v208, v207 op_sel_hi:[0,0,0]
	v_mfma_scale_f32_16x16x128_f8f6f4 v[86:89], v[18:25], v[170:177], v[86:89], v208, v207 op_sel_hi:[0,0,0]
	v_mfma_scale_f32_16x16x128_f8f6f4 v[78:81], v[26:33], v[214:221], v[78:81], v208, v207 op_sel_hi:[0,0,0]
	v_mfma_scale_f32_16x16x128_f8f6f4 v[70:73], v[18:25], v[214:221], v[70:73], v208, v207 op_sel_hi:[0,0,0]
	v_mfma_scale_f32_16x16x128_f8f6f4 v[62:65], v[26:33], v[236:243], v[62:65], v208, v207 op_sel_hi:[0,0,0]
	v_mfma_scale_f32_16x16x128_f8f6f4 v[54:57], v[18:25], v[236:243], v[54:57], v208, v207 op_sel_hi:[0,0,0]
	v_mfma_scale_f32_16x16x128_f8f6f4 v[46:49], v[26:33], v[244:251], v[46:49], v208, v207 op_sel_hi:[0,0,0]
	v_mfma_scale_f32_16x16x128_f8f6f4 v[38:41], v[18:25], v[244:251], v[38:41], v208, v207 op_sel_hi:[0,0,0]
	s_setprio 0
	s_setprio 1
	v_mfma_scale_f32_16x16x128_f8f6f4 v[90:93], v[10:17], v[170:177], v[90:93], v208, v207 op_sel_hi:[0,0,0]
	v_mfma_scale_f32_16x16x128_f8f6f4 v[82:85], v[2:9], v[170:177], v[82:85], v208, v207 op_sel_hi:[0,0,0]
	v_mfma_scale_f32_16x16x128_f8f6f4 v[74:77], v[10:17], v[214:221], v[74:77], v208, v207 op_sel_hi:[0,0,0]
	v_mfma_scale_f32_16x16x128_f8f6f4 v[66:69], v[2:9], v[214:221], v[66:69], v208, v207 op_sel_hi:[0,0,0]
	v_mfma_scale_f32_16x16x128_f8f6f4 v[58:61], v[10:17], v[236:243], v[58:61], v208, v207 op_sel_hi:[0,0,0]
	v_mfma_scale_f32_16x16x128_f8f6f4 v[50:53], v[2:9], v[236:243], v[50:53], v208, v207 op_sel_hi:[0,0,0]
	v_mfma_scale_f32_16x16x128_f8f6f4 v[42:45], v[10:17], v[244:251], v[42:45], v208, v207 op_sel_hi:[0,0,0]
	v_mfma_scale_f32_16x16x128_f8f6f4 v[34:37], v[2:9], v[244:251], v[34:37], v208, v207 op_sel_hi:[0,0,0]
	s_setprio 0
	s_barrier
	s_cmp_ge_i32 s91, s11
	s_cbranch_scc1 .LBB0_1695
	s_mov_b64 s[70:71], s[64:65]
	s_branch .LBB0_1691

.LBB0_1693:
	s_add_i32 s91, s91, 2
	s_add_u32 s64, s70, 0x100
	s_addc_u32 s65, s71, 0
	s_and_b64 s[74:75], s[68:69], exec
	s_cselect_b32 s74, 0, s64
	s_cselect_b32 s75, 0, s65
	s_add_u32 s74, s28, s74
	s_addc_u32 s75, s29, s75
	s_add_u32 s92, s51, s70
	s_addc_u32 s93, s53, s71
	s_and_b64 s[68:69], s[68:69], exec
	s_cselect_b32 s69, s55, s93
	s_cselect_b32 s68, s54, s92
	s_add_i32 s93, 0, 0x10000
	s_add_i32 s92, 0, 0x14000
	v_add_u32_e32 v2, s93, v210
	v_add_u32_e32 v6, s92, v210
	ds_read_b128 v[26:29], v2
	ds_read_b128 v[30:33], v2 offset:1024
	ds_read_b128 v[18:21], v2 offset:2048
	ds_read_b128 v[22:25], v2 offset:3072
	ds_read_b128 v[10:13], v6
	ds_read_b128 v[14:17], v6 offset:1024
	ds_read_b128 v[2:5], v6 offset:2048
	ds_read_b128 v[6:9], v6 offset:3072
	v_lshl_add_u64 v[170:171], v[194:195], 0, s[70:71]
	s_add_i32 m0, s59, 0xc000
	ds_read_b128 v[196:199], v212
	ds_read_b128 v[200:203], v212 offset:1024
	ds_read_b128 v[214:217], v212 offset:2048
	ds_read_b128 v[218:221], v212 offset:3072
	ds_read_b128 v[236:239], v212 offset:4096
	ds_read_b128 v[240:243], v212 offset:5120
	ds_read_b128 v[244:247], v212 offset:6144
	ds_read_b128 v[248:251], v212 offset:7168
	global_load_lds_dwordx4 v[170:171], off
	v_lshl_add_u64 v[170:171], v[192:193], 0, s[70:71]
	s_add_i32 m0, s59, 0xe000
	s_nop 0
	global_load_lds_dwordx4 v[170:171], off
	s_waitcnt vmcnt(8)
	s_waitcnt lgkmcnt(0)
	s_barrier
	s_setprio 1
	v_mfma_scale_f32_16x16x128_f8f6f4 v[154:157], v[26:33], v[196:203], v[154:157], v208, v207 op_sel_hi:[0,0,0]
	v_mfma_scale_f32_16x16x128_f8f6f4 v[150:153], v[18:25], v[196:203], v[150:153], v208, v207 op_sel_hi:[0,0,0]
	v_mfma_scale_f32_16x16x128_f8f6f4 v[142:145], v[26:33], v[214:221], v[142:145], v208, v207 op_sel_hi:[0,0,0]
	v_mfma_scale_f32_16x16x128_f8f6f4 v[134:137], v[18:25], v[214:221], v[134:137], v208, v207 op_sel_hi:[0,0,0]
	v_mfma_scale_f32_16x16x128_f8f6f4 v[126:129], v[26:33], v[236:243], v[126:129], v208, v207 op_sel_hi:[0,0,0]
	v_mfma_scale_f32_16x16x128_f8f6f4 v[118:121], v[18:25], v[236:243], v[118:121], v208, v207 op_sel_hi:[0,0,0]
	v_mfma_scale_f32_16x16x128_f8f6f4 v[110:113], v[26:33], v[244:251], v[110:113], v208, v207 op_sel_hi:[0,0,0]
	v_mfma_scale_f32_16x16x128_f8f6f4 v[102:105], v[18:25], v[244:251], v[102:105], v208, v207 op_sel_hi:[0,0,0]
	s_setprio 0
	s_setprio 1
	v_mfma_scale_f32_16x16x128_f8f6f4 v[158:161], v[10:17], v[196:203], v[158:161], v208, v207 op_sel_hi:[0,0,0]
	v_mfma_scale_f32_16x16x128_f8f6f4 v[146:149], v[2:9], v[196:203], v[146:149], v208, v207 op_sel_hi:[0,0,0]
	v_mfma_scale_f32_16x16x128_f8f6f4 v[138:141], v[10:17], v[214:221], v[138:141], v208, v207 op_sel_hi:[0,0,0]
	v_mfma_scale_f32_16x16x128_f8f6f4 v[130:133], v[2:9], v[214:221], v[130:133], v208, v207 op_sel_hi:[0,0,0]
	v_mfma_scale_f32_16x16x128_f8f6f4 v[122:125], v[10:17], v[236:243], v[122:125], v208, v207 op_sel_hi:[0,0,0]
	v_mfma_scale_f32_16x16x128_f8f6f4 v[114:117], v[2:9], v[236:243], v[114:117], v208, v207 op_sel_hi:[0,0,0]
	v_mfma_scale_f32_16x16x128_f8f6f4 v[106:109], v[10:17], v[244:251], v[106:109], v208, v207 op_sel_hi:[0,0,0]
	v_mfma_scale_f32_16x16x128_f8f6f4 v[98:101], v[2:9], v[244:251], v[98:101], v208, v207 op_sel_hi:[0,0,0]
	s_setprio 0
	s_barrier
	s_add_i32 s70, s93, s72
	v_lshl_add_u64 v[196:197], s[68:69], 0, v[162:163]
	s_mov_b32 m0, s70
	ds_read_b128 v[214:217], v212 offset:16384
	ds_read_b128 v[218:221], v212 offset:17408
	ds_read_b128 v[236:239], v212 offset:18432
	ds_read_b128 v[240:243], v212 offset:19456
	ds_read_b128 v[244:247], v212 offset:20480
	ds_read_b128 v[248:251], v212 offset:21504
	ds_read_b128 v[170:173], v212 offset:22528
	ds_read_b128 v[174:177], v212 offset:23552
	global_load_lds_dwordx4 v[196:197], off
	s_add_i32 m0, s70, 0x2000
	s_add_u32 s70, s68, 0x20000
	v_lshl_add_u64 v[198:199], s[68:69], 0, v[164:165]
	s_addc_u32 s71, s69, 0
	s_add_i32 s92, s92, s72
	global_load_lds_dwordx4 v[198:199], off
	v_lshl_add_u64 v[200:201], s[70:71], 0, v[162:163]
	s_mov_b32 m0, s92
	v_mov_b32_e32 v179, v167
	global_load_lds_dwordx4 v[200:201], off
	v_lshl_add_u64 v[200:201], s[70:71], 0, v[164:165]
	s_add_i32 m0, s92, 0x2000
	v_lshl_add_u64 v[202:203], s[74:75], 0, v[166:167]
	global_load_lds_dwordx4 v[200:201], off
	s_mov_b32 m0, s59
	v_lshl_add_u64 v[200:201], s[74:75], 0, v[178:179]
	global_load_lds_dwordx4 v166, s[74:75]
	s_mov_b32 m0, s61
	s_nop 0
	global_load_lds_dwordx4 v178, s[74:75]
	s_waitcnt vmcnt(8)
	s_waitcnt lgkmcnt(0)
	s_barrier
	s_setprio 1
	v_mfma_scale_f32_16x16x128_f8f6f4 v[94:97], v[26:33], v[214:221], v[94:97], v208, v207 op_sel_hi:[0,0,0]
	v_mfma_scale_f32_16x16x128_f8f6f4 v[86:89], v[18:25], v[214:221], v[86:89], v208, v207 op_sel_hi:[0,0,0]
	v_mfma_scale_f32_16x16x128_f8f6f4 v[78:81], v[26:33], v[236:243], v[78:81], v208, v207 op_sel_hi:[0,0,0]
	v_mfma_scale_f32_16x16x128_f8f6f4 v[70:73], v[18:25], v[236:243], v[70:73], v208, v207 op_sel_hi:[0,0,0]
	v_mfma_scale_f32_16x16x128_f8f6f4 v[62:65], v[26:33], v[244:251], v[62:65], v208, v207 op_sel_hi:[0,0,0]
	v_mfma_scale_f32_16x16x128_f8f6f4 v[54:57], v[18:25], v[244:251], v[54:57], v208, v207 op_sel_hi:[0,0,0]
	v_mfma_scale_f32_16x16x128_f8f6f4 v[46:49], v[26:33], v[170:177], v[46:49], v208, v207 op_sel_hi:[0,0,0]
	v_mfma_scale_f32_16x16x128_f8f6f4 v[38:41], v[18:25], v[170:177], v[38:41], v208, v207 op_sel_hi:[0,0,0]
	s_setprio 0
	s_setprio 1
	v_mfma_scale_f32_16x16x128_f8f6f4 v[90:93], v[10:17], v[214:221], v[90:93], v208, v207 op_sel_hi:[0,0,0]
	v_mfma_scale_f32_16x16x128_f8f6f4 v[82:85], v[2:9], v[214:221], v[82:85], v208, v207 op_sel_hi:[0,0,0]
	v_mfma_scale_f32_16x16x128_f8f6f4 v[74:77], v[10:17], v[236:243], v[74:77], v208, v207 op_sel_hi:[0,0,0]
	v_mfma_scale_f32_16x16x128_f8f6f4 v[66:69], v[2:9], v[236:243], v[66:69], v208, v207 op_sel_hi:[0,0,0]
	v_mfma_scale_f32_16x16x128_f8f6f4 v[58:61], v[10:17], v[244:251], v[58:61], v208, v207 op_sel_hi:[0,0,0]
	v_mfma_scale_f32_16x16x128_f8f6f4 v[50:53], v[2:9], v[244:251], v[50:53], v208, v207 op_sel_hi:[0,0,0]
	v_mfma_scale_f32_16x16x128_f8f6f4 v[42:45], v[10:17], v[170:177], v[42:45], v208, v207 op_sel_hi:[0,0,0]
	v_mfma_scale_f32_16x16x128_f8f6f4 v[34:37], v[2:9], v[170:177], v[34:37], v208, v207 op_sel_hi:[0,0,0]
	s_setprio 0
	s_barrier
	s_add_i32 s70, 0, 0x18000
	s_add_i32 s71, 0, 0x1c000
	v_add_u32_e32 v2, s70, v210
	v_add_u32_e32 v6, s71, v210
	ds_read_b128 v[26:29], v2
	ds_read_b128 v[30:33], v2 offset:1024
	ds_read_b128 v[18:21], v2 offset:2048
	ds_read_b128 v[22:25], v2 offset:3072
	ds_read_b128 v[10:13], v6
	ds_read_b128 v[14:17], v6 offset:1024
	ds_read_b128 v[2:5], v6 offset:2048
	ds_read_b128 v[6:9], v6 offset:3072
	s_mov_b32 m0, s73
	ds_read_b128 v[170:173], v212 offset:32768
	ds_read_b128 v[174:177], v212 offset:33792
	ds_read_b128 v[214:217], v212 offset:34816
	ds_read_b128 v[218:221], v212 offset:35840
	ds_read_b128 v[236:239], v212 offset:36864
	ds_read_b128 v[240:243], v212 offset:37888
	ds_read_b128 v[244:247], v212 offset:38912
	ds_read_b128 v[248:251], v212 offset:39936
	global_load_lds_dwordx4 v180, s[74:75]
	s_mov_b32 m0, s76
	s_nop 0
	global_load_lds_dwordx4 v182, s[74:75]
	s_waitcnt vmcnt(8)
	s_waitcnt lgkmcnt(0)
	s_barrier
	s_setprio 1
	v_mfma_scale_f32_16x16x128_f8f6f4 v[154:157], v[26:33], v[170:177], v[154:157], v208, v207 op_sel_hi:[0,0,0]
	v_mfma_scale_f32_16x16x128_f8f6f4 v[150:153], v[18:25], v[170:177], v[150:153], v208, v207 op_sel_hi:[0,0,0]
	v_mfma_scale_f32_16x16x128_f8f6f4 v[142:145], v[26:33], v[214:221], v[142:145], v208, v207 op_sel_hi:[0,0,0]
	v_mfma_scale_f32_16x16x128_f8f6f4 v[134:137], v[18:25], v[214:221], v[134:137], v208, v207 op_sel_hi:[0,0,0]
	v_mfma_scale_f32_16x16x128_f8f6f4 v[126:129], v[26:33], v[236:243], v[126:129], v208, v207 op_sel_hi:[0,0,0]
	v_mfma_scale_f32_16x16x128_f8f6f4 v[118:121], v[18:25], v[236:243], v[118:121], v208, v207 op_sel_hi:[0,0,0]
	v_mfma_scale_f32_16x16x128_f8f6f4 v[110:113], v[26:33], v[244:251], v[110:113], v208, v207 op_sel_hi:[0,0,0]
	v_mfma_scale_f32_16x16x128_f8f6f4 v[102:105], v[18:25], v[244:251], v[102:105], v208, v207 op_sel_hi:[0,0,0]
	s_setprio 0
	s_setprio 1
	v_mfma_scale_f32_16x16x128_f8f6f4 v[158:161], v[10:17], v[170:177], v[158:161], v208, v207 op_sel_hi:[0,0,0]
	v_mfma_scale_f32_16x16x128_f8f6f4 v[146:149], v[2:9], v[170:177], v[146:149], v208, v207 op_sel_hi:[0,0,0]
	v_mfma_scale_f32_16x16x128_f8f6f4 v[138:141], v[10:17], v[214:221], v[138:141], v208, v207 op_sel_hi:[0,0,0]
	v_mfma_scale_f32_16x16x128_f8f6f4 v[130:133], v[2:9], v[214:221], v[130:133], v208, v207 op_sel_hi:[0,0,0]
	v_mfma_scale_f32_16x16x128_f8f6f4 v[122:125], v[10:17], v[236:243], v[122:125], v208, v207 op_sel_hi:[0,0,0]
	v_mfma_scale_f32_16x16x128_f8f6f4 v[114:117], v[2:9], v[236:243], v[114:117], v208, v207 op_sel_hi:[0,0,0]
	v_mfma_scale_f32_16x16x128_f8f6f4 v[106:109], v[10:17], v[244:251], v[106:109], v208, v207 op_sel_hi:[0,0,0]
	v_mfma_scale_f32_16x16x128_f8f6f4 v[98:101], v[2:9], v[244:251], v[98:101], v208, v207 op_sel_hi:[0,0,0]
	s_setprio 0
	s_barrier
	s_add_i32 s70, s70, s72
	v_lshl_add_u64 v[196:197], v[196:197], 0, s[56:57]
	s_mov_b32 m0, s70
	ds_read_b128 v[170:173], v212 offset:49152
	ds_read_b128 v[174:177], v212 offset:50176
	ds_read_b128 v[214:217], v212 offset:51200
	ds_read_b128 v[218:221], v212 offset:52224
	ds_read_b128 v[236:239], v212 offset:53248
	ds_read_b128 v[240:243], v212 offset:54272
	ds_read_b128 v[244:247], v212 offset:55296
	ds_read_b128 v[248:251], v212 offset:56320
	global_load_lds_dwordx4 v[196:197], off
	s_add_i32 m0, s70, 0x2000
	s_add_u32 s68, s68, 0x20080
	v_lshl_add_u64 v[196:197], v[198:199], 0, s[56:57]
	s_addc_u32 s69, s69, 0
	s_add_i32 s70, s71, s72
	global_load_lds_dwordx4 v[196:197], off
	v_lshl_add_u64 v[196:197], s[68:69], 0, v[162:163]
	s_mov_b32 m0, s70
	s_nop 0
	global_load_lds_dwordx4 v[196:197], off
	v_lshl_add_u64 v[196:197], s[68:69], 0, v[164:165]
	s_add_i32 m0, s70, 0x2000
	s_nop 0
	global_load_lds_dwordx4 v[196:197], off
	v_lshl_add_u64 v[196:197], v[202:203], 0, s[56:57]
	s_mov_b32 m0, s77
	s_nop 0
	global_load_lds_dwordx4 v[196:197], off
	v_lshl_add_u64 v[196:197], v[200:201], 0, s[56:57]
	s_mov_b32 m0, s79
	s_nop 0
	global_load_lds_dwordx4 v[196:197], off
	s_waitcnt vmcnt(8)
	s_waitcnt lgkmcnt(0)
	s_barrier
	s_setprio 1
	v_mfma_scale_f32_16x16x128_f8f6f4 v[94:97], v[26:33], v[170:177], v[94:97], v208, v207 op_sel_hi:[0,0,0]
	v_mfma_scale_f32_16x16x128_f8f6f4 v[86:89], v[18:25], v[170:177], v[86:89], v208, v207 op_sel_hi:[0,0,0]
	v_mfma_scale_f32_16x16x128_f8f6f4 v[78:81], v[26:33], v[214:221], v[78:81], v208, v207 op_sel_hi:[0,0,0]
	v_mfma_scale_f32_16x16x128_f8f6f4 v[70:73], v[18:25], v[214:221], v[70:73], v208, v207 op_sel_hi:[0,0,0]
	v_mfma_scale_f32_16x16x128_f8f6f4 v[62:65], v[26:33], v[236:243], v[62:65], v208, v207 op_sel_hi:[0,0,0]
	v_mfma_scale_f32_16x16x128_f8f6f4 v[54:57], v[18:25], v[236:243], v[54:57], v208, v207 op_sel_hi:[0,0,0]
	v_mfma_scale_f32_16x16x128_f8f6f4 v[46:49], v[26:33], v[244:251], v[46:49], v208, v207 op_sel_hi:[0,0,0]
	v_mfma_scale_f32_16x16x128_f8f6f4 v[38:41], v[18:25], v[244:251], v[38:41], v208, v207 op_sel_hi:[0,0,0]
	s_setprio 0
	s_setprio 1
	v_mfma_scale_f32_16x16x128_f8f6f4 v[90:93], v[10:17], v[170:177], v[90:93], v208, v207 op_sel_hi:[0,0,0]
	v_mfma_scale_f32_16x16x128_f8f6f4 v[82:85], v[2:9], v[170:177], v[82:85], v208, v207 op_sel_hi:[0,0,0]
	v_mfma_scale_f32_16x16x128_f8f6f4 v[74:77], v[10:17], v[214:221], v[74:77], v208, v207 op_sel_hi:[0,0,0]
	v_mfma_scale_f32_16x16x128_f8f6f4 v[66:69], v[2:9], v[214:221], v[66:69], v208, v207 op_sel_hi:[0,0,0]
	v_mfma_scale_f32_16x16x128_f8f6f4 v[58:61], v[10:17], v[236:243], v[58:61], v208, v207 op_sel_hi:[0,0,0]
	v_mfma_scale_f32_16x16x128_f8f6f4 v[50:53], v[2:9], v[236:243], v[50:53], v208, v207 op_sel_hi:[0,0,0]
	v_mfma_scale_f32_16x16x128_f8f6f4 v[42:45], v[10:17], v[244:251], v[42:45], v208, v207 op_sel_hi:[0,0,0]
	v_mfma_scale_f32_16x16x128_f8f6f4 v[34:37], v[2:9], v[244:251], v[34:37], v208, v207 op_sel_hi:[0,0,0]
	s_setprio 0
	s_barrier
	s_cmp_ge_i32 s91, s11
	s_cbranch_scc1 .LBB0_1695
	s_mov_b64 s[70:71], s[64:65]
	s_branch .LBB0_1691

.Lpeelph16_0:
	s_add_i32 s91, s64, 2
	s_add_u32 s62, s60, 0x100
	s_addc_u32 s63, s61, 0
	s_add_i32 s92, 0, 0x10000
	s_cmp_eq_u32 s74, s64
	s_cselect_b32 s69, s53, s63
	s_cselect_b32 s68, s52, s62
	s_cselect_b32 s65, s55, s59
	s_cselect_b32 s64, s54, s51
	s_add_i32 s93, 0, 0x14000
	v_add_u32_e32 v2, s92, v196
	v_add_u32_e32 v6, s93, v196
	ds_read_b128 v[26:29], v2
	ds_read_b128 v[30:33], v2 offset:1024
	ds_read_b128 v[18:21], v2 offset:2048
	ds_read_b128 v[22:25], v2 offset:3072
	ds_read_b128 v[10:13], v6
	ds_read_b128 v[14:17], v6 offset:1024
	ds_read_b128 v[2:5], v6 offset:2048
	ds_read_b128 v[6:9], v6 offset:3072
	v_lshl_add_u64 v[216:217], s[60:61], 0, v[184:185]
	s_add_i32 m0, s21, 0xc000
	ds_read_b128 v[170:173], v198
	ds_read_b128 v[174:177], v198 offset:1024
	ds_read_b128 v[186:189], v198 offset:2048
	ds_read_b128 v[190:193], v198 offset:3072
	ds_read_b128 v[200:203], v198 offset:4096
	ds_read_b128 v[204:207], v198 offset:5120
	ds_read_b128 v[208:211], v198 offset:6144
	ds_read_b128 v[212:215], v198 offset:7168
	global_load_lds_dwordx4 v[216:217], off
	v_lshl_add_u64 v[216:217], s[60:61], 0, v[182:183]
	s_add_i32 m0, s21, 0xe000
	s_nop 0
	global_load_lds_dwordx4 v[216:217], off
	s_waitcnt vmcnt(8)
	s_waitcnt lgkmcnt(0)
	s_barrier
	s_setprio 1
	v_mfma_scale_f32_16x16x128_f8f6f4 v[154:157], v[26:33], v[170:177], 0, v194, v169 op_sel_hi:[0,0,0]
	v_mfma_scale_f32_16x16x128_f8f6f4 v[158:161], v[18:25], v[170:177], 0, v194, v169 op_sel_hi:[0,0,0]
	v_mfma_scale_f32_16x16x128_f8f6f4 v[138:141], v[26:33], v[186:193], 0, v194, v169 op_sel_hi:[0,0,0]
	v_mfma_scale_f32_16x16x128_f8f6f4 v[142:145], v[18:25], v[186:193], 0, v194, v169 op_sel_hi:[0,0,0]
	v_mfma_scale_f32_16x16x128_f8f6f4 v[122:125], v[26:33], v[200:207], 0, v194, v169 op_sel_hi:[0,0,0]
	v_mfma_scale_f32_16x16x128_f8f6f4 v[126:129], v[18:25], v[200:207], 0, v194, v169 op_sel_hi:[0,0,0]
	v_mfma_scale_f32_16x16x128_f8f6f4 v[106:109], v[26:33], v[208:215], 0, v194, v169 op_sel_hi:[0,0,0]
	v_mfma_scale_f32_16x16x128_f8f6f4 v[110:113], v[18:25], v[208:215], 0, v194, v169 op_sel_hi:[0,0,0]
	s_setprio 0
	s_setprio 1
	v_mfma_scale_f32_16x16x128_f8f6f4 v[146:149], v[10:17], v[170:177], 0, v194, v169 op_sel_hi:[0,0,0]
	v_mfma_scale_f32_16x16x128_f8f6f4 v[150:153], v[2:9], v[170:177], 0, v194, v169 op_sel_hi:[0,0,0]
	v_mfma_scale_f32_16x16x128_f8f6f4 v[130:133], v[10:17], v[186:193], 0, v194, v169 op_sel_hi:[0,0,0]
	v_mfma_scale_f32_16x16x128_f8f6f4 v[134:137], v[2:9], v[186:193], 0, v194, v169 op_sel_hi:[0,0,0]
	v_mfma_scale_f32_16x16x128_f8f6f4 v[114:117], v[10:17], v[200:207], 0, v194, v169 op_sel_hi:[0,0,0]
	v_mfma_scale_f32_16x16x128_f8f6f4 v[118:121], v[2:9], v[200:207], 0, v194, v169 op_sel_hi:[0,0,0]
	v_mfma_scale_f32_16x16x128_f8f6f4 v[98:101], v[10:17], v[208:215], 0, v194, v169 op_sel_hi:[0,0,0]
	v_mfma_scale_f32_16x16x128_f8f6f4 v[102:105], v[2:9], v[208:215], 0, v194, v169 op_sel_hi:[0,0,0]
	s_setprio 0
	s_barrier
	s_add_i32 s60, s92, s20
	v_lshl_add_u64 v[186:187], s[64:65], 0, v[164:165]
	s_mov_b32 m0, s60
	ds_read_b128 v[170:173], v198 offset:16384
	ds_read_b128 v[174:177], v198 offset:17408
	ds_read_b128 v[200:203], v198 offset:18432
	ds_read_b128 v[204:207], v198 offset:19456
	ds_read_b128 v[208:211], v198 offset:20480
	ds_read_b128 v[212:215], v198 offset:21504
	ds_read_b128 v[216:219], v198 offset:22528
	ds_read_b128 v[220:223], v198 offset:23552
	global_load_lds_dwordx4 v[186:187], off
	s_add_i32 m0, s60, 0x2000
	s_add_u32 s60, s64, 0x70000
	v_lshl_add_u64 v[188:189], s[64:65], 0, v[180:181]
	s_addc_u32 s61, s65, 0
	s_add_i32 s92, s93, s20
	global_load_lds_dwordx4 v[188:189], off
	v_lshl_add_u64 v[190:191], s[60:61], 0, v[164:165]
	s_mov_b32 m0, s92
	v_lshl_add_u64 v[192:193], s[68:69], 0, v[178:179]
	global_load_lds_dwordx4 v[190:191], off
	v_lshl_add_u64 v[190:191], s[60:61], 0, v[180:181]
	s_add_i32 m0, s92, 0x2000
	s_nop 0
	global_load_lds_dwordx4 v[190:191], off
	v_lshl_add_u64 v[190:191], s[68:69], 0, v[162:163]
	s_mov_b32 m0, s21
	s_nop 0
	global_load_lds_dwordx4 v[190:191], off
	s_mov_b32 m0, s22
	s_nop 0
	global_load_lds_dwordx4 v[192:193], off
	s_waitcnt vmcnt(8)
	s_waitcnt lgkmcnt(0)
	s_barrier
	s_setprio 1
	v_mfma_scale_f32_16x16x128_f8f6f4 v[90:93], v[26:33], v[170:177], 0, v194, v169 op_sel_hi:[0,0,0]
	v_mfma_scale_f32_16x16x128_f8f6f4 v[94:97], v[18:25], v[170:177], 0, v194, v169 op_sel_hi:[0,0,0]
	v_mfma_scale_f32_16x16x128_f8f6f4 v[74:77], v[26:33], v[200:207], 0, v194, v169 op_sel_hi:[0,0,0]
	v_mfma_scale_f32_16x16x128_f8f6f4 v[78:81], v[18:25], v[200:207], 0, v194, v169 op_sel_hi:[0,0,0]
	v_mfma_scale_f32_16x16x128_f8f6f4 v[58:61], v[26:33], v[208:215], 0, v194, v169 op_sel_hi:[0,0,0]
	v_mfma_scale_f32_16x16x128_f8f6f4 v[62:65], v[18:25], v[208:215], 0, v194, v169 op_sel_hi:[0,0,0]
	v_mfma_scale_f32_16x16x128_f8f6f4 v[42:45], v[26:33], v[216:223], 0, v194, v169 op_sel_hi:[0,0,0]
	v_mfma_scale_f32_16x16x128_f8f6f4 v[46:49], v[18:25], v[216:223], 0, v194, v169 op_sel_hi:[0,0,0]
	s_setprio 0
	s_setprio 1
	v_mfma_scale_f32_16x16x128_f8f6f4 v[82:85], v[10:17], v[170:177], 0, v194, v169 op_sel_hi:[0,0,0]
	v_mfma_scale_f32_16x16x128_f8f6f4 v[86:89], v[2:9], v[170:177], 0, v194, v169 op_sel_hi:[0,0,0]
	v_mfma_scale_f32_16x16x128_f8f6f4 v[66:69], v[10:17], v[200:207], 0, v194, v169 op_sel_hi:[0,0,0]
	v_mfma_scale_f32_16x16x128_f8f6f4 v[70:73], v[2:9], v[200:207], 0, v194, v169 op_sel_hi:[0,0,0]
	v_mfma_scale_f32_16x16x128_f8f6f4 v[50:53], v[10:17], v[208:215], 0, v194, v169 op_sel_hi:[0,0,0]
	v_mfma_scale_f32_16x16x128_f8f6f4 v[54:57], v[2:9], v[208:215], 0, v194, v169 op_sel_hi:[0,0,0]
	v_mfma_scale_f32_16x16x128_f8f6f4 v[34:37], v[10:17], v[216:223], 0, v194, v169 op_sel_hi:[0,0,0]
	v_mfma_scale_f32_16x16x128_f8f6f4 v[38:41], v[2:9], v[216:223], 0, v194, v169 op_sel_hi:[0,0,0]
	s_setprio 0
	s_barrier
	s_add_i32 s92, 0, 0x18000
	s_add_i32 s93, 0, 0x1c000
	v_add_u32_e32 v2, s92, v196
	v_add_u32_e32 v6, s93, v196
	ds_read_b128 v[26:29], v2
	ds_read_b128 v[30:33], v2 offset:1024
	ds_read_b128 v[18:21], v2 offset:2048
	ds_read_b128 v[22:25], v2 offset:3072
	ds_read_b128 v[10:13], v6
	ds_read_b128 v[14:17], v6 offset:1024
	ds_read_b128 v[2:5], v6 offset:2048
	ds_read_b128 v[6:9], v6 offset:3072
	s_add_u32 s60, s68, 0x70000
	s_addc_u32 s61, s69, 0
	s_mov_b32 m0, s23
	v_lshl_add_u64 v[232:233], s[60:61], 0, v[162:163]
	ds_read_b128 v[170:173], v198 offset:32768
	ds_read_b128 v[174:177], v198 offset:33792
	ds_read_b128 v[200:203], v198 offset:34816
	ds_read_b128 v[204:207], v198 offset:35840
	ds_read_b128 v[208:211], v198 offset:36864
	ds_read_b128 v[212:215], v198 offset:37888
	ds_read_b128 v[216:219], v198 offset:38912
	ds_read_b128 v[220:223], v198 offset:39936
	global_load_lds_dwordx4 v[232:233], off
	v_lshl_add_u64 v[232:233], s[60:61], 0, v[178:179]
	s_mov_b32 m0, s70
	s_nop 0
	global_load_lds_dwordx4 v[232:233], off
	s_waitcnt vmcnt(8)
	s_waitcnt lgkmcnt(0)
	s_barrier
	s_setprio 1
	v_mfma_scale_f32_16x16x128_f8f6f4 v[154:157], v[26:33], v[170:177], v[154:157], v194, v169 op_sel_hi:[0,0,0]
	v_mfma_scale_f32_16x16x128_f8f6f4 v[158:161], v[18:25], v[170:177], v[158:161], v194, v169 op_sel_hi:[0,0,0]
	v_mfma_scale_f32_16x16x128_f8f6f4 v[138:141], v[26:33], v[200:207], v[138:141], v194, v169 op_sel_hi:[0,0,0]
	v_mfma_scale_f32_16x16x128_f8f6f4 v[142:145], v[18:25], v[200:207], v[142:145], v194, v169 op_sel_hi:[0,0,0]
	v_mfma_scale_f32_16x16x128_f8f6f4 v[122:125], v[26:33], v[208:215], v[122:125], v194, v169 op_sel_hi:[0,0,0]
	v_mfma_scale_f32_16x16x128_f8f6f4 v[126:129], v[18:25], v[208:215], v[126:129], v194, v169 op_sel_hi:[0,0,0]
	v_mfma_scale_f32_16x16x128_f8f6f4 v[106:109], v[26:33], v[216:223], v[106:109], v194, v169 op_sel_hi:[0,0,0]
	v_mfma_scale_f32_16x16x128_f8f6f4 v[110:113], v[18:25], v[216:223], v[110:113], v194, v169 op_sel_hi:[0,0,0]
	s_setprio 0
	s_setprio 1
	v_mfma_scale_f32_16x16x128_f8f6f4 v[146:149], v[10:17], v[170:177], v[146:149], v194, v169 op_sel_hi:[0,0,0]
	v_mfma_scale_f32_16x16x128_f8f6f4 v[150:153], v[2:9], v[170:177], v[150:153], v194, v169 op_sel_hi:[0,0,0]
	v_mfma_scale_f32_16x16x128_f8f6f4 v[130:133], v[10:17], v[200:207], v[130:133], v194, v169 op_sel_hi:[0,0,0]
	v_mfma_scale_f32_16x16x128_f8f6f4 v[134:137], v[2:9], v[200:207], v[134:137], v194, v169 op_sel_hi:[0,0,0]
	v_mfma_scale_f32_16x16x128_f8f6f4 v[114:117], v[10:17], v[208:215], v[114:117], v194, v169 op_sel_hi:[0,0,0]
	v_mfma_scale_f32_16x16x128_f8f6f4 v[118:121], v[2:9], v[208:215], v[118:121], v194, v169 op_sel_hi:[0,0,0]
	v_mfma_scale_f32_16x16x128_f8f6f4 v[98:101], v[10:17], v[216:223], v[98:101], v194, v169 op_sel_hi:[0,0,0]
	v_mfma_scale_f32_16x16x128_f8f6f4 v[102:105], v[2:9], v[216:223], v[102:105], v194, v169 op_sel_hi:[0,0,0]
	s_setprio 0
	s_barrier
	s_add_i32 s60, s92, s20
	v_lshl_add_u64 v[186:187], v[186:187], 0, s[56:57]
	s_mov_b32 m0, s60
	ds_read_b128 v[170:173], v198 offset:49152
	ds_read_b128 v[174:177], v198 offset:50176
	ds_read_b128 v[200:203], v198 offset:51200
	ds_read_b128 v[204:207], v198 offset:52224
	ds_read_b128 v[208:211], v198 offset:53248
	ds_read_b128 v[212:215], v198 offset:54272
	ds_read_b128 v[216:219], v198 offset:55296
	ds_read_b128 v[220:223], v198 offset:56320
	global_load_lds_dwordx4 v[186:187], off
	s_add_i32 m0, s60, 0x2000
	s_add_u32 s60, s64, 0x70080
	v_lshl_add_u64 v[186:187], v[188:189], 0, s[56:57]
	s_addc_u32 s61, s65, 0
	s_add_i32 s64, s93, s20
	global_load_lds_dwordx4 v[186:187], off
	v_lshl_add_u64 v[186:187], s[60:61], 0, v[164:165]
	s_mov_b32 m0, s64
	s_nop 0
	global_load_lds_dwordx4 v[186:187], off
	v_lshl_add_u64 v[186:187], s[60:61], 0, v[180:181]
	s_add_i32 m0, s64, 0x2000
	s_nop 0
	global_load_lds_dwordx4 v[186:187], off
	v_lshl_add_u64 v[186:187], v[190:191], 0, s[56:57]
	s_mov_b32 m0, s71
	s_nop 0
	global_load_lds_dwordx4 v[186:187], off
	v_lshl_add_u64 v[186:187], v[192:193], 0, s[56:57]
	s_mov_b32 m0, s72
	s_nop 0
	global_load_lds_dwordx4 v[186:187], off
	s_waitcnt vmcnt(8)
	s_waitcnt lgkmcnt(0)
	s_barrier
	s_setprio 1
	v_mfma_scale_f32_16x16x128_f8f6f4 v[90:93], v[26:33], v[170:177], v[90:93], v194, v169 op_sel_hi:[0,0,0]
	v_mfma_scale_f32_16x16x128_f8f6f4 v[94:97], v[18:25], v[170:177], v[94:97], v194, v169 op_sel_hi:[0,0,0]
	v_mfma_scale_f32_16x16x128_f8f6f4 v[74:77], v[26:33], v[200:207], v[74:77], v194, v169 op_sel_hi:[0,0,0]
	v_mfma_scale_f32_16x16x128_f8f6f4 v[78:81], v[18:25], v[200:207], v[78:81], v194, v169 op_sel_hi:[0,0,0]
	v_mfma_scale_f32_16x16x128_f8f6f4 v[58:61], v[26:33], v[208:215], v[58:61], v194, v169 op_sel_hi:[0,0,0]
	v_mfma_scale_f32_16x16x128_f8f6f4 v[62:65], v[18:25], v[208:215], v[62:65], v194, v169 op_sel_hi:[0,0,0]
	v_mfma_scale_f32_16x16x128_f8f6f4 v[42:45], v[26:33], v[216:223], v[42:45], v194, v169 op_sel_hi:[0,0,0]
	v_mfma_scale_f32_16x16x128_f8f6f4 v[46:49], v[18:25], v[216:223], v[46:49], v194, v169 op_sel_hi:[0,0,0]
	s_setprio 0
	s_setprio 1
	v_mfma_scale_f32_16x16x128_f8f6f4 v[82:85], v[10:17], v[170:177], v[82:85], v194, v169 op_sel_hi:[0,0,0]
	v_mfma_scale_f32_16x16x128_f8f6f4 v[86:89], v[2:9], v[170:177], v[86:89], v194, v169 op_sel_hi:[0,0,0]
	v_mfma_scale_f32_16x16x128_f8f6f4 v[66:69], v[10:17], v[200:207], v[66:69], v194, v169 op_sel_hi:[0,0,0]
	v_mfma_scale_f32_16x16x128_f8f6f4 v[70:73], v[2:9], v[200:207], v[70:73], v194, v169 op_sel_hi:[0,0,0]
	v_mfma_scale_f32_16x16x128_f8f6f4 v[50:53], v[10:17], v[208:215], v[50:53], v194, v169 op_sel_hi:[0,0,0]
	v_mfma_scale_f32_16x16x128_f8f6f4 v[54:57], v[2:9], v[208:215], v[54:57], v194, v169 op_sel_hi:[0,0,0]
	v_mfma_scale_f32_16x16x128_f8f6f4 v[34:37], v[10:17], v[216:223], v[34:37], v194, v169 op_sel_hi:[0,0,0]
	v_mfma_scale_f32_16x16x128_f8f6f4 v[38:41], v[2:9], v[216:223], v[38:41], v194, v169 op_sel_hi:[0,0,0]
	s_setprio 0
	s_barrier
	s_add_u32 s51, s51, 0x100
	s_addc_u32 s59, s59, 0
	s_cmp_ge_i32 s91, s8
	s_mov_b64 s[60:61], s[62:63]
	s_mov_b32 s64, s91
	s_cbranch_scc0 .LBB0_1777
	s_branch .Lpeelexitph16
.LBB0_1777:
	s_add_i32 s91, s64, 2
	s_add_u32 s62, s60, 0x100
	s_addc_u32 s63, s61, 0
	s_add_i32 s92, 0, 0x10000
	s_cmp_eq_u32 s74, s64
	s_cselect_b32 s69, s53, s63
	s_cselect_b32 s68, s52, s62
	s_cselect_b32 s65, s55, s59
	s_cselect_b32 s64, s54, s51
	s_add_i32 s93, 0, 0x14000
	v_add_u32_e32 v2, s92, v196
	v_add_u32_e32 v6, s93, v196
	ds_read_b128 v[26:29], v2
	ds_read_b128 v[30:33], v2 offset:1024
	ds_read_b128 v[18:21], v2 offset:2048
	ds_read_b128 v[22:25], v2 offset:3072
	ds_read_b128 v[10:13], v6
	ds_read_b128 v[14:17], v6 offset:1024
	ds_read_b128 v[2:5], v6 offset:2048
	ds_read_b128 v[6:9], v6 offset:3072
	v_lshl_add_u64 v[216:217], s[60:61], 0, v[184:185]
	s_add_i32 m0, s21, 0xc000
	ds_read_b128 v[170:173], v198
	ds_read_b128 v[174:177], v198 offset:1024
	ds_read_b128 v[186:189], v198 offset:2048
	ds_read_b128 v[190:193], v198 offset:3072
	ds_read_b128 v[200:203], v198 offset:4096
	ds_read_b128 v[204:207], v198 offset:5120
	ds_read_b128 v[208:211], v198 offset:6144
	ds_read_b128 v[212:215], v198 offset:7168
	global_load_lds_dwordx4 v[216:217], off
	v_lshl_add_u64 v[216:217], s[60:61], 0, v[182:183]
	s_add_i32 m0, s21, 0xe000
	s_nop 0
	global_load_lds_dwordx4 v[216:217], off
	s_waitcnt vmcnt(8)
	s_waitcnt lgkmcnt(0)
	s_barrier
	s_setprio 1
	v_mfma_scale_f32_16x16x128_f8f6f4 v[154:157], v[26:33], v[170:177], v[154:157], v194, v169 op_sel_hi:[0,0,0]
	v_mfma_scale_f32_16x16x128_f8f6f4 v[158:161], v[18:25], v[170:177], v[158:161], v194, v169 op_sel_hi:[0,0,0]
	v_mfma_scale_f32_16x16x128_f8f6f4 v[138:141], v[26:33], v[186:193], v[138:141], v194, v169 op_sel_hi:[0,0,0]
	v_mfma_scale_f32_16x16x128_f8f6f4 v[142:145], v[18:25], v[186:193], v[142:145], v194, v169 op_sel_hi:[0,0,0]
	v_mfma_scale_f32_16x16x128_f8f6f4 v[122:125], v[26:33], v[200:207], v[122:125], v194, v169 op_sel_hi:[0,0,0]
	v_mfma_scale_f32_16x16x128_f8f6f4 v[126:129], v[18:25], v[200:207], v[126:129], v194, v169 op_sel_hi:[0,0,0]
	v_mfma_scale_f32_16x16x128_f8f6f4 v[106:109], v[26:33], v[208:215], v[106:109], v194, v169 op_sel_hi:[0,0,0]
	v_mfma_scale_f32_16x16x128_f8f6f4 v[110:113], v[18:25], v[208:215], v[110:113], v194, v169 op_sel_hi:[0,0,0]
	s_setprio 0
	s_setprio 1
	v_mfma_scale_f32_16x16x128_f8f6f4 v[146:149], v[10:17], v[170:177], v[146:149], v194, v169 op_sel_hi:[0,0,0]
	v_mfma_scale_f32_16x16x128_f8f6f4 v[150:153], v[2:9], v[170:177], v[150:153], v194, v169 op_sel_hi:[0,0,0]
	v_mfma_scale_f32_16x16x128_f8f6f4 v[130:133], v[10:17], v[186:193], v[130:133], v194, v169 op_sel_hi:[0,0,0]
	v_mfma_scale_f32_16x16x128_f8f6f4 v[134:137], v[2:9], v[186:193], v[134:137], v194, v169 op_sel_hi:[0,0,0]
	v_mfma_scale_f32_16x16x128_f8f6f4 v[114:117], v[10:17], v[200:207], v[114:117], v194, v169 op_sel_hi:[0,0,0]
	v_mfma_scale_f32_16x16x128_f8f6f4 v[118:121], v[2:9], v[200:207], v[118:121], v194, v169 op_sel_hi:[0,0,0]
	v_mfma_scale_f32_16x16x128_f8f6f4 v[98:101], v[10:17], v[208:215], v[98:101], v194, v169 op_sel_hi:[0,0,0]
	v_mfma_scale_f32_16x16x128_f8f6f4 v[102:105], v[2:9], v[208:215], v[102:105], v194, v169 op_sel_hi:[0,0,0]
	s_setprio 0
	s_barrier
	s_add_i32 s60, s92, s20
	v_lshl_add_u64 v[186:187], s[64:65], 0, v[164:165]
	s_mov_b32 m0, s60
	ds_read_b128 v[170:173], v198 offset:16384
	ds_read_b128 v[174:177], v198 offset:17408
	ds_read_b128 v[200:203], v198 offset:18432
	ds_read_b128 v[204:207], v198 offset:19456
	ds_read_b128 v[208:211], v198 offset:20480
	ds_read_b128 v[212:215], v198 offset:21504
	ds_read_b128 v[216:219], v198 offset:22528
	ds_read_b128 v[220:223], v198 offset:23552
	global_load_lds_dwordx4 v[186:187], off
	s_add_i32 m0, s60, 0x2000
	s_add_u32 s60, s64, 0x70000
	v_lshl_add_u64 v[188:189], s[64:65], 0, v[180:181]
	s_addc_u32 s61, s65, 0
	s_add_i32 s92, s93, s20
	global_load_lds_dwordx4 v[188:189], off
	v_lshl_add_u64 v[190:191], s[60:61], 0, v[164:165]
	s_mov_b32 m0, s92
	v_lshl_add_u64 v[192:193], s[68:69], 0, v[178:179]
	global_load_lds_dwordx4 v[190:191], off
	v_lshl_add_u64 v[190:191], s[60:61], 0, v[180:181]
	s_add_i32 m0, s92, 0x2000
	s_nop 0
	global_load_lds_dwordx4 v[190:191], off
	v_lshl_add_u64 v[190:191], s[68:69], 0, v[162:163]
	s_mov_b32 m0, s21
	s_nop 0
	global_load_lds_dwordx4 v[190:191], off
	s_mov_b32 m0, s22
	s_nop 0
	global_load_lds_dwordx4 v[192:193], off
	s_waitcnt vmcnt(8)
	s_waitcnt lgkmcnt(0)
	s_barrier
	s_setprio 1
	v_mfma_scale_f32_16x16x128_f8f6f4 v[90:93], v[26:33], v[170:177], v[90:93], v194, v169 op_sel_hi:[0,0,0]
	v_mfma_scale_f32_16x16x128_f8f6f4 v[94:97], v[18:25], v[170:177], v[94:97], v194, v169 op_sel_hi:[0,0,0]
	v_mfma_scale_f32_16x16x128_f8f6f4 v[74:77], v[26:33], v[200:207], v[74:77], v194, v169 op_sel_hi:[0,0,0]
	v_mfma_scale_f32_16x16x128_f8f6f4 v[78:81], v[18:25], v[200:207], v[78:81], v194, v169 op_sel_hi:[0,0,0]
	v_mfma_scale_f32_16x16x128_f8f6f4 v[58:61], v[26:33], v[208:215], v[58:61], v194, v169 op_sel_hi:[0,0,0]
	v_mfma_scale_f32_16x16x128_f8f6f4 v[62:65], v[18:25], v[208:215], v[62:65], v194, v169 op_sel_hi:[0,0,0]
	v_mfma_scale_f32_16x16x128_f8f6f4 v[42:45], v[26:33], v[216:223], v[42:45], v194, v169 op_sel_hi:[0,0,0]
	v_mfma_scale_f32_16x16x128_f8f6f4 v[46:49], v[18:25], v[216:223], v[46:49], v194, v169 op_sel_hi:[0,0,0]
	s_setprio 0
	s_setprio 1
	v_mfma_scale_f32_16x16x128_f8f6f4 v[82:85], v[10:17], v[170:177], v[82:85], v194, v169 op_sel_hi:[0,0,0]
	v_mfma_scale_f32_16x16x128_f8f6f4 v[86:89], v[2:9], v[170:177], v[86:89], v194, v169 op_sel_hi:[0,0,0]
	v_mfma_scale_f32_16x16x128_f8f6f4 v[66:69], v[10:17], v[200:207], v[66:69], v194, v169 op_sel_hi:[0,0,0]
	v_mfma_scale_f32_16x16x128_f8f6f4 v[70:73], v[2:9], v[200:207], v[70:73], v194, v169 op_sel_hi:[0,0,0]
	v_mfma_scale_f32_16x16x128_f8f6f4 v[50:53], v[10:17], v[208:215], v[50:53], v194, v169 op_sel_hi:[0,0,0]
	v_mfma_scale_f32_16x16x128_f8f6f4 v[54:57], v[2:9], v[208:215], v[54:57], v194, v169 op_sel_hi:[0,0,0]
	v_mfma_scale_f32_16x16x128_f8f6f4 v[34:37], v[10:17], v[216:223], v[34:37], v194, v169 op_sel_hi:[0,0,0]
	v_mfma_scale_f32_16x16x128_f8f6f4 v[38:41], v[2:9], v[216:223], v[38:41], v194, v169 op_sel_hi:[0,0,0]
	s_setprio 0
	s_barrier
	s_add_i32 s92, 0, 0x18000
	s_add_i32 s93, 0, 0x1c000
	v_add_u32_e32 v2, s92, v196
	v_add_u32_e32 v6, s93, v196
	ds_read_b128 v[26:29], v2
	ds_read_b128 v[30:33], v2 offset:1024
	ds_read_b128 v[18:21], v2 offset:2048
	ds_read_b128 v[22:25], v2 offset:3072
	ds_read_b128 v[10:13], v6
	ds_read_b128 v[14:17], v6 offset:1024
	ds_read_b128 v[2:5], v6 offset:2048
	ds_read_b128 v[6:9], v6 offset:3072
	s_add_u32 s60, s68, 0x70000
	s_addc_u32 s61, s69, 0
	s_mov_b32 m0, s23
	v_lshl_add_u64 v[232:233], s[60:61], 0, v[162:163]
	ds_read_b128 v[170:173], v198 offset:32768
	ds_read_b128 v[174:177], v198 offset:33792
	ds_read_b128 v[200:203], v198 offset:34816
	ds_read_b128 v[204:207], v198 offset:35840
	ds_read_b128 v[208:211], v198 offset:36864
	ds_read_b128 v[212:215], v198 offset:37888
	ds_read_b128 v[216:219], v198 offset:38912
	ds_read_b128 v[220:223], v198 offset:39936
	global_load_lds_dwordx4 v[232:233], off
	v_lshl_add_u64 v[232:233], s[60:61], 0, v[178:179]
	s_mov_b32 m0, s70
	s_nop 0
	global_load_lds_dwordx4 v[232:233], off
	s_waitcnt vmcnt(8)
	s_waitcnt lgkmcnt(0)
	s_barrier
	s_setprio 1
	v_mfma_scale_f32_16x16x128_f8f6f4 v[154:157], v[26:33], v[170:177], v[154:157], v194, v169 op_sel_hi:[0,0,0]
	v_mfma_scale_f32_16x16x128_f8f6f4 v[158:161], v[18:25], v[170:177], v[158:161], v194, v169 op_sel_hi:[0,0,0]
	v_mfma_scale_f32_16x16x128_f8f6f4 v[138:141], v[26:33], v[200:207], v[138:141], v194, v169 op_sel_hi:[0,0,0]
	v_mfma_scale_f32_16x16x128_f8f6f4 v[142:145], v[18:25], v[200:207], v[142:145], v194, v169 op_sel_hi:[0,0,0]
	v_mfma_scale_f32_16x16x128_f8f6f4 v[122:125], v[26:33], v[208:215], v[122:125], v194, v169 op_sel_hi:[0,0,0]
	v_mfma_scale_f32_16x16x128_f8f6f4 v[126:129], v[18:25], v[208:215], v[126:129], v194, v169 op_sel_hi:[0,0,0]
	v_mfma_scale_f32_16x16x128_f8f6f4 v[106:109], v[26:33], v[216:223], v[106:109], v194, v169 op_sel_hi:[0,0,0]
	v_mfma_scale_f32_16x16x128_f8f6f4 v[110:113], v[18:25], v[216:223], v[110:113], v194, v169 op_sel_hi:[0,0,0]
	s_setprio 0
	s_setprio 1
	v_mfma_scale_f32_16x16x128_f8f6f4 v[146:149], v[10:17], v[170:177], v[146:149], v194, v169 op_sel_hi:[0,0,0]
	v_mfma_scale_f32_16x16x128_f8f6f4 v[150:153], v[2:9], v[170:177], v[150:153], v194, v169 op_sel_hi:[0,0,0]
	v_mfma_scale_f32_16x16x128_f8f6f4 v[130:133], v[10:17], v[200:207], v[130:133], v194, v169 op_sel_hi:[0,0,0]
	v_mfma_scale_f32_16x16x128_f8f6f4 v[134:137], v[2:9], v[200:207], v[134:137], v194, v169 op_sel_hi:[0,0,0]
	v_mfma_scale_f32_16x16x128_f8f6f4 v[114:117], v[10:17], v[208:215], v[114:117], v194, v169 op_sel_hi:[0,0,0]
	v_mfma_scale_f32_16x16x128_f8f6f4 v[118:121], v[2:9], v[208:215], v[118:121], v194, v169 op_sel_hi:[0,0,0]
	v_mfma_scale_f32_16x16x128_f8f6f4 v[98:101], v[10:17], v[216:223], v[98:101], v194, v169 op_sel_hi:[0,0,0]
	v_mfma_scale_f32_16x16x128_f8f6f4 v[102:105], v[2:9], v[216:223], v[102:105], v194, v169 op_sel_hi:[0,0,0]
	s_setprio 0
	s_barrier
	s_add_i32 s60, s92, s20
	v_lshl_add_u64 v[186:187], v[186:187], 0, s[56:57]
	s_mov_b32 m0, s60
	ds_read_b128 v[170:173], v198 offset:49152
	ds_read_b128 v[174:177], v198 offset:50176
	ds_read_b128 v[200:203], v198 offset:51200
	ds_read_b128 v[204:207], v198 offset:52224
	ds_read_b128 v[208:211], v198 offset:53248
	ds_read_b128 v[212:215], v198 offset:54272
	ds_read_b128 v[216:219], v198 offset:55296
	ds_read_b128 v[220:223], v198 offset:56320
	global_load_lds_dwordx4 v[186:187], off
	s_add_i32 m0, s60, 0x2000
	s_add_u32 s60, s64, 0x70080
	v_lshl_add_u64 v[186:187], v[188:189], 0, s[56:57]
	s_addc_u32 s61, s65, 0
	s_add_i32 s64, s93, s20
	global_load_lds_dwordx4 v[186:187], off
	v_lshl_add_u64 v[186:187], s[60:61], 0, v[164:165]
	s_mov_b32 m0, s64
	s_nop 0
	global_load_lds_dwordx4 v[186:187], off
	v_lshl_add_u64 v[186:187], s[60:61], 0, v[180:181]
	s_add_i32 m0, s64, 0x2000
	s_nop 0
	global_load_lds_dwordx4 v[186:187], off
	v_lshl_add_u64 v[186:187], v[190:191], 0, s[56:57]
	s_mov_b32 m0, s71
	s_nop 0
	global_load_lds_dwordx4 v[186:187], off
	v_lshl_add_u64 v[186:187], v[192:193], 0, s[56:57]
	s_mov_b32 m0, s72
	s_nop 0
	global_load_lds_dwordx4 v[186:187], off
	s_waitcnt vmcnt(8)
	s_waitcnt lgkmcnt(0)
	s_barrier
	s_setprio 1
	v_mfma_scale_f32_16x16x128_f8f6f4 v[90:93], v[26:33], v[170:177], v[90:93], v194, v169 op_sel_hi:[0,0,0]
	v_mfma_scale_f32_16x16x128_f8f6f4 v[94:97], v[18:25], v[170:177], v[94:97], v194, v169 op_sel_hi:[0,0,0]
	v_mfma_scale_f32_16x16x128_f8f6f4 v[74:77], v[26:33], v[200:207], v[74:77], v194, v169 op_sel_hi:[0,0,0]
	v_mfma_scale_f32_16x16x128_f8f6f4 v[78:81], v[18:25], v[200:207], v[78:81], v194, v169 op_sel_hi:[0,0,0]
	v_mfma_scale_f32_16x16x128_f8f6f4 v[58:61], v[26:33], v[208:215], v[58:61], v194, v169 op_sel_hi:[0,0,0]
	v_mfma_scale_f32_16x16x128_f8f6f4 v[62:65], v[18:25], v[208:215], v[62:65], v194, v169 op_sel_hi:[0,0,0]
	v_mfma_scale_f32_16x16x128_f8f6f4 v[42:45], v[26:33], v[216:223], v[42:45], v194, v169 op_sel_hi:[0,0,0]
	v_mfma_scale_f32_16x16x128_f8f6f4 v[46:49], v[18:25], v[216:223], v[46:49], v194, v169 op_sel_hi:[0,0,0]
	s_setprio 0
	s_setprio 1
	v_mfma_scale_f32_16x16x128_f8f6f4 v[82:85], v[10:17], v[170:177], v[82:85], v194, v169 op_sel_hi:[0,0,0]
	v_mfma_scale_f32_16x16x128_f8f6f4 v[86:89], v[2:9], v[170:177], v[86:89], v194, v169 op_sel_hi:[0,0,0]
	v_mfma_scale_f32_16x16x128_f8f6f4 v[66:69], v[10:17], v[200:207], v[66:69], v194, v169 op_sel_hi:[0,0,0]
	v_mfma_scale_f32_16x16x128_f8f6f4 v[70:73], v[2:9], v[200:207], v[70:73], v194, v169 op_sel_hi:[0,0,0]
	v_mfma_scale_f32_16x16x128_f8f6f4 v[50:53], v[10:17], v[208:215], v[50:53], v194, v169 op_sel_hi:[0,0,0]
	v_mfma_scale_f32_16x16x128_f8f6f4 v[54:57], v[2:9], v[208:215], v[54:57], v194, v169 op_sel_hi:[0,0,0]
	v_mfma_scale_f32_16x16x128_f8f6f4 v[34:37], v[10:17], v[216:223], v[34:37], v194, v169 op_sel_hi:[0,0,0]
	v_mfma_scale_f32_16x16x128_f8f6f4 v[38:41], v[2:9], v[216:223], v[38:41], v194, v169 op_sel_hi:[0,0,0]
	s_setprio 0
	s_barrier
	s_add_u32 s51, s51, 0x100
	s_addc_u32 s59, s59, 0
	s_cmp_ge_i32 s91, s8
	s_mov_b64 s[60:61], s[62:63]
	s_mov_b32 s64, s91
	s_cbranch_scc0 .LBB0_1777

.Lpeelph17_1:
	s_add_i32 s55, s55, 2
	s_add_u32 s60, s64, 0x100
	s_addc_u32 s61, s65, 0
	s_and_b64 s[68:69], s[62:63], exec
	s_cselect_b32 s68, 0, s60
	s_cselect_b32 s69, 0, s61
	s_add_u32 s68, s30, s68
	s_addc_u32 s69, s31, s69
	s_add_u32 s91, s47, s64
	s_addc_u32 s92, s49, s65
	s_and_b64 s[62:63], s[62:63], exec
	s_cselect_b32 s63, s53, s92
	s_cselect_b32 s62, s52, s91
	s_add_i32 s92, 0, 0x10000
	s_add_i32 s91, 0, 0x14000
	v_add_u32_e32 v2, s92, v210
	v_add_u32_e32 v6, s91, v210
	ds_read_b128 v[26:29], v2
	ds_read_b128 v[30:33], v2 offset:1024
	ds_read_b128 v[18:21], v2 offset:2048
	ds_read_b128 v[22:25], v2 offset:3072
	ds_read_b128 v[10:13], v6
	ds_read_b128 v[14:17], v6 offset:1024
	ds_read_b128 v[2:5], v6 offset:2048
	ds_read_b128 v[6:9], v6 offset:3072
	v_lshl_add_u64 v[222:223], v[194:195], 0, s[64:65]
	s_add_i32 m0, s59, 0xc000
	ds_read_b128 v[170:173], v212
	ds_read_b128 v[174:177], v212 offset:1024
	ds_read_b128 v[196:199], v212 offset:2048
	ds_read_b128 v[200:203], v212 offset:3072
	ds_read_b128 v[214:217], v212 offset:4096
	ds_read_b128 v[218:221], v212 offset:5120
	ds_read_b128 v[236:239], v212 offset:6144
	ds_read_b128 v[240:243], v212 offset:7168
	global_load_lds_dwordx4 v[222:223], off
	v_lshl_add_u64 v[222:223], v[192:193], 0, s[64:65]
	s_add_i32 m0, s59, 0xe000
	s_nop 0
	global_load_lds_dwordx4 v[222:223], off
	s_waitcnt vmcnt(8)
	s_waitcnt lgkmcnt(0)
	s_barrier
	s_setprio 1
	v_mfma_scale_f32_16x16x128_f8f6f4 v[154:157], v[26:33], v[170:177], 0, v208, v207 op_sel_hi:[0,0,0]
	v_mfma_scale_f32_16x16x128_f8f6f4 v[150:153], v[18:25], v[170:177], 0, v208, v207 op_sel_hi:[0,0,0]
	v_mfma_scale_f32_16x16x128_f8f6f4 v[142:145], v[26:33], v[196:203], 0, v208, v207 op_sel_hi:[0,0,0]
	v_mfma_scale_f32_16x16x128_f8f6f4 v[134:137], v[18:25], v[196:203], 0, v208, v207 op_sel_hi:[0,0,0]
	v_mfma_scale_f32_16x16x128_f8f6f4 v[126:129], v[26:33], v[214:221], 0, v208, v207 op_sel_hi:[0,0,0]
	v_mfma_scale_f32_16x16x128_f8f6f4 v[118:121], v[18:25], v[214:221], 0, v208, v207 op_sel_hi:[0,0,0]
	v_mfma_scale_f32_16x16x128_f8f6f4 v[110:113], v[26:33], v[236:243], 0, v208, v207 op_sel_hi:[0,0,0]
	v_mfma_scale_f32_16x16x128_f8f6f4 v[102:105], v[18:25], v[236:243], 0, v208, v207 op_sel_hi:[0,0,0]
	s_setprio 0
	s_setprio 1
	v_mfma_scale_f32_16x16x128_f8f6f4 v[158:161], v[10:17], v[170:177], 0, v208, v207 op_sel_hi:[0,0,0]
	v_mfma_scale_f32_16x16x128_f8f6f4 v[146:149], v[2:9], v[170:177], 0, v208, v207 op_sel_hi:[0,0,0]
	v_mfma_scale_f32_16x16x128_f8f6f4 v[138:141], v[10:17], v[196:203], 0, v208, v207 op_sel_hi:[0,0,0]
	v_mfma_scale_f32_16x16x128_f8f6f4 v[130:133], v[2:9], v[196:203], 0, v208, v207 op_sel_hi:[0,0,0]
	v_mfma_scale_f32_16x16x128_f8f6f4 v[122:125], v[10:17], v[214:221], 0, v208, v207 op_sel_hi:[0,0,0]
	v_mfma_scale_f32_16x16x128_f8f6f4 v[114:117], v[2:9], v[214:221], 0, v208, v207 op_sel_hi:[0,0,0]
	v_mfma_scale_f32_16x16x128_f8f6f4 v[106:109], v[10:17], v[236:243], 0, v208, v207 op_sel_hi:[0,0,0]
	v_mfma_scale_f32_16x16x128_f8f6f4 v[98:101], v[2:9], v[236:243], 0, v208, v207 op_sel_hi:[0,0,0]
	s_setprio 0
	s_barrier
	s_add_i32 s64, s92, s22
	v_lshl_add_u64 v[196:197], s[62:63], 0, v[162:163]
	s_mov_b32 m0, s64
	ds_read_b128 v[170:173], v212 offset:16384
	ds_read_b128 v[174:177], v212 offset:17408
	ds_read_b128 v[214:217], v212 offset:18432
	ds_read_b128 v[218:221], v212 offset:19456
	ds_read_b128 v[236:239], v212 offset:20480
	ds_read_b128 v[240:243], v212 offset:21504
	ds_read_b128 v[244:247], v212 offset:22528
	ds_read_b128 v[248:251], v212 offset:23552
	global_load_lds_dwordx4 v[196:197], off
	s_add_i32 m0, s64, 0x2000
	s_add_u32 s64, s62, 0x20000
	v_lshl_add_u64 v[198:199], s[62:63], 0, v[164:165]
	s_addc_u32 s65, s63, 0
	s_add_i32 s91, s91, s22
	global_load_lds_dwordx4 v[198:199], off
	v_lshl_add_u64 v[200:201], s[64:65], 0, v[162:163]
	s_mov_b32 m0, s91
	v_mov_b32_e32 v179, v167
	global_load_lds_dwordx4 v[200:201], off
	v_lshl_add_u64 v[200:201], s[64:65], 0, v[164:165]
	s_add_i32 m0, s91, 0x2000
	v_lshl_add_u64 v[202:203], s[68:69], 0, v[166:167]
	global_load_lds_dwordx4 v[200:201], off
	s_mov_b32 m0, s59
	v_lshl_add_u64 v[200:201], s[68:69], 0, v[178:179]
	global_load_lds_dwordx4 v166, s[68:69]
	s_mov_b32 m0, s71
	s_nop 0
	global_load_lds_dwordx4 v178, s[68:69]
	s_waitcnt vmcnt(8)
	s_waitcnt lgkmcnt(0)
	s_barrier
	s_setprio 1
	v_mfma_scale_f32_16x16x128_f8f6f4 v[94:97], v[26:33], v[170:177], 0, v208, v207 op_sel_hi:[0,0,0]
	v_mfma_scale_f32_16x16x128_f8f6f4 v[86:89], v[18:25], v[170:177], 0, v208, v207 op_sel_hi:[0,0,0]
	v_mfma_scale_f32_16x16x128_f8f6f4 v[78:81], v[26:33], v[214:221], 0, v208, v207 op_sel_hi:[0,0,0]
	v_mfma_scale_f32_16x16x128_f8f6f4 v[70:73], v[18:25], v[214:221], 0, v208, v207 op_sel_hi:[0,0,0]
	v_mfma_scale_f32_16x16x128_f8f6f4 v[62:65], v[26:33], v[236:243], 0, v208, v207 op_sel_hi:[0,0,0]
	v_mfma_scale_f32_16x16x128_f8f6f4 v[54:57], v[18:25], v[236:243], 0, v208, v207 op_sel_hi:[0,0,0]
	v_mfma_scale_f32_16x16x128_f8f6f4 v[46:49], v[26:33], v[244:251], 0, v208, v207 op_sel_hi:[0,0,0]
	v_mfma_scale_f32_16x16x128_f8f6f4 v[38:41], v[18:25], v[244:251], 0, v208, v207 op_sel_hi:[0,0,0]
	s_setprio 0
	s_setprio 1
	v_mfma_scale_f32_16x16x128_f8f6f4 v[90:93], v[10:17], v[170:177], 0, v208, v207 op_sel_hi:[0,0,0]
	v_mfma_scale_f32_16x16x128_f8f6f4 v[82:85], v[2:9], v[170:177], 0, v208, v207 op_sel_hi:[0,0,0]
	v_mfma_scale_f32_16x16x128_f8f6f4 v[74:77], v[10:17], v[214:221], 0, v208, v207 op_sel_hi:[0,0,0]
	v_mfma_scale_f32_16x16x128_f8f6f4 v[66:69], v[2:9], v[214:221], 0, v208, v207 op_sel_hi:[0,0,0]
	v_mfma_scale_f32_16x16x128_f8f6f4 v[58:61], v[10:17], v[236:243], 0, v208, v207 op_sel_hi:[0,0,0]
	v_mfma_scale_f32_16x16x128_f8f6f4 v[50:53], v[2:9], v[236:243], 0, v208, v207 op_sel_hi:[0,0,0]
	v_mfma_scale_f32_16x16x128_f8f6f4 v[42:45], v[10:17], v[244:251], 0, v208, v207 op_sel_hi:[0,0,0]
	v_mfma_scale_f32_16x16x128_f8f6f4 v[34:37], v[2:9], v[244:251], 0, v208, v207 op_sel_hi:[0,0,0]
	s_setprio 0
	s_barrier
	s_add_i32 s64, 0, 0x18000
	s_add_i32 s65, 0, 0x1c000
	v_add_u32_e32 v2, s64, v210
	v_add_u32_e32 v6, s65, v210
	ds_read_b128 v[26:29], v2
	ds_read_b128 v[30:33], v2 offset:1024
	ds_read_b128 v[18:21], v2 offset:2048
	ds_read_b128 v[22:25], v2 offset:3072
	ds_read_b128 v[10:13], v6
	ds_read_b128 v[14:17], v6 offset:1024
	ds_read_b128 v[2:5], v6 offset:2048
	ds_read_b128 v[6:9], v6 offset:3072
	s_mov_b32 m0, s72
	ds_read_b128 v[170:173], v212 offset:32768
	ds_read_b128 v[174:177], v212 offset:33792
	ds_read_b128 v[214:217], v212 offset:34816
	ds_read_b128 v[218:221], v212 offset:35840
	ds_read_b128 v[236:239], v212 offset:36864
	ds_read_b128 v[240:243], v212 offset:37888
	ds_read_b128 v[244:247], v212 offset:38912
	ds_read_b128 v[248:251], v212 offset:39936
	global_load_lds_dwordx4 v180, s[68:69]
	s_mov_b32 m0, s73
	s_nop 0
	global_load_lds_dwordx4 v182, s[68:69]
	s_waitcnt vmcnt(8)
	s_waitcnt lgkmcnt(0)
	s_barrier
	s_setprio 1
	v_mfma_scale_f32_16x16x128_f8f6f4 v[154:157], v[26:33], v[170:177], v[154:157], v208, v207 op_sel_hi:[0,0,0]
	v_mfma_scale_f32_16x16x128_f8f6f4 v[150:153], v[18:25], v[170:177], v[150:153], v208, v207 op_sel_hi:[0,0,0]
	v_mfma_scale_f32_16x16x128_f8f6f4 v[142:145], v[26:33], v[214:221], v[142:145], v208, v207 op_sel_hi:[0,0,0]
	v_mfma_scale_f32_16x16x128_f8f6f4 v[134:137], v[18:25], v[214:221], v[134:137], v208, v207 op_sel_hi:[0,0,0]
	v_mfma_scale_f32_16x16x128_f8f6f4 v[126:129], v[26:33], v[236:243], v[126:129], v208, v207 op_sel_hi:[0,0,0]
	v_mfma_scale_f32_16x16x128_f8f6f4 v[118:121], v[18:25], v[236:243], v[118:121], v208, v207 op_sel_hi:[0,0,0]
	v_mfma_scale_f32_16x16x128_f8f6f4 v[110:113], v[26:33], v[244:251], v[110:113], v208, v207 op_sel_hi:[0,0,0]
	v_mfma_scale_f32_16x16x128_f8f6f4 v[102:105], v[18:25], v[244:251], v[102:105], v208, v207 op_sel_hi:[0,0,0]
	s_setprio 0
	s_setprio 1
	v_mfma_scale_f32_16x16x128_f8f6f4 v[158:161], v[10:17], v[170:177], v[158:161], v208, v207 op_sel_hi:[0,0,0]
	v_mfma_scale_f32_16x16x128_f8f6f4 v[146:149], v[2:9], v[170:177], v[146:149], v208, v207 op_sel_hi:[0,0,0]
	v_mfma_scale_f32_16x16x128_f8f6f4 v[138:141], v[10:17], v[214:221], v[138:141], v208, v207 op_sel_hi:[0,0,0]
	v_mfma_scale_f32_16x16x128_f8f6f4 v[130:133], v[2:9], v[214:221], v[130:133], v208, v207 op_sel_hi:[0,0,0]
	v_mfma_scale_f32_16x16x128_f8f6f4 v[122:125], v[10:17], v[236:243], v[122:125], v208, v207 op_sel_hi:[0,0,0]
	v_mfma_scale_f32_16x16x128_f8f6f4 v[114:117], v[2:9], v[236:243], v[114:117], v208, v207 op_sel_hi:[0,0,0]
	v_mfma_scale_f32_16x16x128_f8f6f4 v[106:109], v[10:17], v[244:251], v[106:109], v208, v207 op_sel_hi:[0,0,0]
	v_mfma_scale_f32_16x16x128_f8f6f4 v[98:101], v[2:9], v[244:251], v[98:101], v208, v207 op_sel_hi:[0,0,0]
	s_setprio 0
	s_barrier
	s_add_i32 s64, s64, s22
	v_lshl_add_u64 v[196:197], v[196:197], 0, s[56:57]
	s_mov_b32 m0, s64
	ds_read_b128 v[170:173], v212 offset:49152
	ds_read_b128 v[174:177], v212 offset:50176
	ds_read_b128 v[214:217], v212 offset:51200
	ds_read_b128 v[218:221], v212 offset:52224
	ds_read_b128 v[236:239], v212 offset:53248
	ds_read_b128 v[240:243], v212 offset:54272
	ds_read_b128 v[244:247], v212 offset:55296
	ds_read_b128 v[248:251], v212 offset:56320
	global_load_lds_dwordx4 v[196:197], off
	s_add_i32 m0, s64, 0x2000
	s_add_u32 s62, s62, 0x20080
	v_lshl_add_u64 v[196:197], v[198:199], 0, s[56:57]
	s_addc_u32 s63, s63, 0
	s_add_i32 s64, s65, s22
	global_load_lds_dwordx4 v[196:197], off
	v_lshl_add_u64 v[196:197], s[62:63], 0, v[162:163]
	s_mov_b32 m0, s64
	s_nop 0
	global_load_lds_dwordx4 v[196:197], off
	v_lshl_add_u64 v[196:197], s[62:63], 0, v[164:165]
	s_add_i32 m0, s64, 0x2000
	s_nop 0
	global_load_lds_dwordx4 v[196:197], off
	v_lshl_add_u64 v[196:197], v[202:203], 0, s[56:57]
	s_mov_b32 m0, s74
	s_nop 0
	global_load_lds_dwordx4 v[196:197], off
	v_lshl_add_u64 v[196:197], v[200:201], 0, s[56:57]
	s_mov_b32 m0, s75
	s_nop 0
	global_load_lds_dwordx4 v[196:197], off
	s_waitcnt vmcnt(8)
	s_waitcnt lgkmcnt(0)
	s_barrier
	s_setprio 1
	v_mfma_scale_f32_16x16x128_f8f6f4 v[94:97], v[26:33], v[170:177], v[94:97], v208, v207 op_sel_hi:[0,0,0]
	v_mfma_scale_f32_16x16x128_f8f6f4 v[86:89], v[18:25], v[170:177], v[86:89], v208, v207 op_sel_hi:[0,0,0]
	v_mfma_scale_f32_16x16x128_f8f6f4 v[78:81], v[26:33], v[214:221], v[78:81], v208, v207 op_sel_hi:[0,0,0]
	v_mfma_scale_f32_16x16x128_f8f6f4 v[70:73], v[18:25], v[214:221], v[70:73], v208, v207 op_sel_hi:[0,0,0]
	v_mfma_scale_f32_16x16x128_f8f6f4 v[62:65], v[26:33], v[236:243], v[62:65], v208, v207 op_sel_hi:[0,0,0]
	v_mfma_scale_f32_16x16x128_f8f6f4 v[54:57], v[18:25], v[236:243], v[54:57], v208, v207 op_sel_hi:[0,0,0]
	v_mfma_scale_f32_16x16x128_f8f6f4 v[46:49], v[26:33], v[244:251], v[46:49], v208, v207 op_sel_hi:[0,0,0]
	v_mfma_scale_f32_16x16x128_f8f6f4 v[38:41], v[18:25], v[244:251], v[38:41], v208, v207 op_sel_hi:[0,0,0]
	s_setprio 0
	s_setprio 1
	v_mfma_scale_f32_16x16x128_f8f6f4 v[90:93], v[10:17], v[170:177], v[90:93], v208, v207 op_sel_hi:[0,0,0]
	v_mfma_scale_f32_16x16x128_f8f6f4 v[82:85], v[2:9], v[170:177], v[82:85], v208, v207 op_sel_hi:[0,0,0]
	v_mfma_scale_f32_16x16x128_f8f6f4 v[74:77], v[10:17], v[214:221], v[74:77], v208, v207 op_sel_hi:[0,0,0]
	v_mfma_scale_f32_16x16x128_f8f6f4 v[66:69], v[2:9], v[214:221], v[66:69], v208, v207 op_sel_hi:[0,0,0]
	v_mfma_scale_f32_16x16x128_f8f6f4 v[58:61], v[10:17], v[236:243], v[58:61], v208, v207 op_sel_hi:[0,0,0]
	v_mfma_scale_f32_16x16x128_f8f6f4 v[50:53], v[2:9], v[236:243], v[50:53], v208, v207 op_sel_hi:[0,0,0]
	v_mfma_scale_f32_16x16x128_f8f6f4 v[42:45], v[10:17], v[244:251], v[42:45], v208, v207 op_sel_hi:[0,0,0]
	v_mfma_scale_f32_16x16x128_f8f6f4 v[34:37], v[2:9], v[244:251], v[34:37], v208, v207 op_sel_hi:[0,0,0]
	s_setprio 0
	s_barrier
	s_cmp_lt_i32 s55, s11
	s_cbranch_scc0 .LBB0_1841
	s_mov_b64 s[64:65], s[60:61]
	s_branch .LBB0_1836

.LBB0_1838:
	s_add_i32 s55, s55, 2
	s_add_u32 s60, s64, 0x100
	s_addc_u32 s61, s65, 0
	s_and_b64 s[68:69], s[62:63], exec
	s_cselect_b32 s68, 0, s60
	s_cselect_b32 s69, 0, s61
	s_add_u32 s68, s30, s68
	s_addc_u32 s69, s31, s69
	s_add_u32 s91, s47, s64
	s_addc_u32 s92, s49, s65
	s_and_b64 s[62:63], s[62:63], exec
	s_cselect_b32 s63, s53, s92
	s_cselect_b32 s62, s52, s91
	s_add_i32 s92, 0, 0x10000
	s_add_i32 s91, 0, 0x14000
	v_add_u32_e32 v2, s92, v210
	v_add_u32_e32 v6, s91, v210
	ds_read_b128 v[26:29], v2
	ds_read_b128 v[30:33], v2 offset:1024
	ds_read_b128 v[18:21], v2 offset:2048
	ds_read_b128 v[22:25], v2 offset:3072
	ds_read_b128 v[10:13], v6
	ds_read_b128 v[14:17], v6 offset:1024
	ds_read_b128 v[2:5], v6 offset:2048
	ds_read_b128 v[6:9], v6 offset:3072
	v_lshl_add_u64 v[222:223], v[194:195], 0, s[64:65]
	s_add_i32 m0, s59, 0xc000
	ds_read_b128 v[170:173], v212
	ds_read_b128 v[174:177], v212 offset:1024
	ds_read_b128 v[196:199], v212 offset:2048
	ds_read_b128 v[200:203], v212 offset:3072
	ds_read_b128 v[214:217], v212 offset:4096
	ds_read_b128 v[218:221], v212 offset:5120
	ds_read_b128 v[236:239], v212 offset:6144
	ds_read_b128 v[240:243], v212 offset:7168
	global_load_lds_dwordx4 v[222:223], off
	v_lshl_add_u64 v[222:223], v[192:193], 0, s[64:65]
	s_add_i32 m0, s59, 0xe000
	s_nop 0
	global_load_lds_dwordx4 v[222:223], off
	s_waitcnt vmcnt(8)
	s_waitcnt lgkmcnt(0)
	s_barrier
	s_setprio 1
	v_mfma_scale_f32_16x16x128_f8f6f4 v[154:157], v[26:33], v[170:177], v[154:157], v208, v207 op_sel_hi:[0,0,0]
	v_mfma_scale_f32_16x16x128_f8f6f4 v[150:153], v[18:25], v[170:177], v[150:153], v208, v207 op_sel_hi:[0,0,0]
	v_mfma_scale_f32_16x16x128_f8f6f4 v[142:145], v[26:33], v[196:203], v[142:145], v208, v207 op_sel_hi:[0,0,0]
	v_mfma_scale_f32_16x16x128_f8f6f4 v[134:137], v[18:25], v[196:203], v[134:137], v208, v207 op_sel_hi:[0,0,0]
	v_mfma_scale_f32_16x16x128_f8f6f4 v[126:129], v[26:33], v[214:221], v[126:129], v208, v207 op_sel_hi:[0,0,0]
	v_mfma_scale_f32_16x16x128_f8f6f4 v[118:121], v[18:25], v[214:221], v[118:121], v208, v207 op_sel_hi:[0,0,0]
	v_mfma_scale_f32_16x16x128_f8f6f4 v[110:113], v[26:33], v[236:243], v[110:113], v208, v207 op_sel_hi:[0,0,0]
	v_mfma_scale_f32_16x16x128_f8f6f4 v[102:105], v[18:25], v[236:243], v[102:105], v208, v207 op_sel_hi:[0,0,0]
	s_setprio 0
	s_setprio 1
	v_mfma_scale_f32_16x16x128_f8f6f4 v[158:161], v[10:17], v[170:177], v[158:161], v208, v207 op_sel_hi:[0,0,0]
	v_mfma_scale_f32_16x16x128_f8f6f4 v[146:149], v[2:9], v[170:177], v[146:149], v208, v207 op_sel_hi:[0,0,0]
	v_mfma_scale_f32_16x16x128_f8f6f4 v[138:141], v[10:17], v[196:203], v[138:141], v208, v207 op_sel_hi:[0,0,0]
	v_mfma_scale_f32_16x16x128_f8f6f4 v[130:133], v[2:9], v[196:203], v[130:133], v208, v207 op_sel_hi:[0,0,0]
	v_mfma_scale_f32_16x16x128_f8f6f4 v[122:125], v[10:17], v[214:221], v[122:125], v208, v207 op_sel_hi:[0,0,0]
	v_mfma_scale_f32_16x16x128_f8f6f4 v[114:117], v[2:9], v[214:221], v[114:117], v208, v207 op_sel_hi:[0,0,0]
	v_mfma_scale_f32_16x16x128_f8f6f4 v[106:109], v[10:17], v[236:243], v[106:109], v208, v207 op_sel_hi:[0,0,0]
	v_mfma_scale_f32_16x16x128_f8f6f4 v[98:101], v[2:9], v[236:243], v[98:101], v208, v207 op_sel_hi:[0,0,0]
	s_setprio 0
	s_barrier
	s_add_i32 s64, s92, s22
	v_lshl_add_u64 v[196:197], s[62:63], 0, v[162:163]
	s_mov_b32 m0, s64
	ds_read_b128 v[170:173], v212 offset:16384
	ds_read_b128 v[174:177], v212 offset:17408
	ds_read_b128 v[214:217], v212 offset:18432
	ds_read_b128 v[218:221], v212 offset:19456
	ds_read_b128 v[236:239], v212 offset:20480
	ds_read_b128 v[240:243], v212 offset:21504
	ds_read_b128 v[244:247], v212 offset:22528
	ds_read_b128 v[248:251], v212 offset:23552
	global_load_lds_dwordx4 v[196:197], off
	s_add_i32 m0, s64, 0x2000
	s_add_u32 s64, s62, 0x20000
	v_lshl_add_u64 v[198:199], s[62:63], 0, v[164:165]
	s_addc_u32 s65, s63, 0
	s_add_i32 s91, s91, s22
	global_load_lds_dwordx4 v[198:199], off
	v_lshl_add_u64 v[200:201], s[64:65], 0, v[162:163]
	s_mov_b32 m0, s91
	v_mov_b32_e32 v179, v167
	global_load_lds_dwordx4 v[200:201], off
	v_lshl_add_u64 v[200:201], s[64:65], 0, v[164:165]
	s_add_i32 m0, s91, 0x2000
	v_lshl_add_u64 v[202:203], s[68:69], 0, v[166:167]
	global_load_lds_dwordx4 v[200:201], off
	s_mov_b32 m0, s59
	v_lshl_add_u64 v[200:201], s[68:69], 0, v[178:179]
	global_load_lds_dwordx4 v166, s[68:69]
	s_mov_b32 m0, s71
	s_nop 0
	global_load_lds_dwordx4 v178, s[68:69]
	s_waitcnt vmcnt(8)
	s_waitcnt lgkmcnt(0)
	s_barrier
	s_setprio 1
	v_mfma_scale_f32_16x16x128_f8f6f4 v[94:97], v[26:33], v[170:177], v[94:97], v208, v207 op_sel_hi:[0,0,0]
	v_mfma_scale_f32_16x16x128_f8f6f4 v[86:89], v[18:25], v[170:177], v[86:89], v208, v207 op_sel_hi:[0,0,0]
	v_mfma_scale_f32_16x16x128_f8f6f4 v[78:81], v[26:33], v[214:221], v[78:81], v208, v207 op_sel_hi:[0,0,0]
	v_mfma_scale_f32_16x16x128_f8f6f4 v[70:73], v[18:25], v[214:221], v[70:73], v208, v207 op_sel_hi:[0,0,0]
	v_mfma_scale_f32_16x16x128_f8f6f4 v[62:65], v[26:33], v[236:243], v[62:65], v208, v207 op_sel_hi:[0,0,0]
	v_mfma_scale_f32_16x16x128_f8f6f4 v[54:57], v[18:25], v[236:243], v[54:57], v208, v207 op_sel_hi:[0,0,0]
	v_mfma_scale_f32_16x16x128_f8f6f4 v[46:49], v[26:33], v[244:251], v[46:49], v208, v207 op_sel_hi:[0,0,0]
	v_mfma_scale_f32_16x16x128_f8f6f4 v[38:41], v[18:25], v[244:251], v[38:41], v208, v207 op_sel_hi:[0,0,0]
	s_setprio 0
	s_setprio 1
	v_mfma_scale_f32_16x16x128_f8f6f4 v[90:93], v[10:17], v[170:177], v[90:93], v208, v207 op_sel_hi:[0,0,0]
	v_mfma_scale_f32_16x16x128_f8f6f4 v[82:85], v[2:9], v[170:177], v[82:85], v208, v207 op_sel_hi:[0,0,0]
	v_mfma_scale_f32_16x16x128_f8f6f4 v[74:77], v[10:17], v[214:221], v[74:77], v208, v207 op_sel_hi:[0,0,0]
	v_mfma_scale_f32_16x16x128_f8f6f4 v[66:69], v[2:9], v[214:221], v[66:69], v208, v207 op_sel_hi:[0,0,0]
	v_mfma_scale_f32_16x16x128_f8f6f4 v[58:61], v[10:17], v[236:243], v[58:61], v208, v207 op_sel_hi:[0,0,0]
	v_mfma_scale_f32_16x16x128_f8f6f4 v[50:53], v[2:9], v[236:243], v[50:53], v208, v207 op_sel_hi:[0,0,0]
	v_mfma_scale_f32_16x16x128_f8f6f4 v[42:45], v[10:17], v[244:251], v[42:45], v208, v207 op_sel_hi:[0,0,0]
	v_mfma_scale_f32_16x16x128_f8f6f4 v[34:37], v[2:9], v[244:251], v[34:37], v208, v207 op_sel_hi:[0,0,0]
	s_setprio 0
	s_barrier
	s_add_i32 s64, 0, 0x18000
	s_add_i32 s65, 0, 0x1c000
	v_add_u32_e32 v2, s64, v210
	v_add_u32_e32 v6, s65, v210
	ds_read_b128 v[26:29], v2
	ds_read_b128 v[30:33], v2 offset:1024
	ds_read_b128 v[18:21], v2 offset:2048
	ds_read_b128 v[22:25], v2 offset:3072
	ds_read_b128 v[10:13], v6
	ds_read_b128 v[14:17], v6 offset:1024
	ds_read_b128 v[2:5], v6 offset:2048
	ds_read_b128 v[6:9], v6 offset:3072
	s_mov_b32 m0, s72
	ds_read_b128 v[170:173], v212 offset:32768
	ds_read_b128 v[174:177], v212 offset:33792
	ds_read_b128 v[214:217], v212 offset:34816
	ds_read_b128 v[218:221], v212 offset:35840
	ds_read_b128 v[236:239], v212 offset:36864
	ds_read_b128 v[240:243], v212 offset:37888
	ds_read_b128 v[244:247], v212 offset:38912
	ds_read_b128 v[248:251], v212 offset:39936
	global_load_lds_dwordx4 v180, s[68:69]
	s_mov_b32 m0, s73
	s_nop 0
	global_load_lds_dwordx4 v182, s[68:69]
	s_waitcnt vmcnt(8)
	s_waitcnt lgkmcnt(0)
	s_barrier
	s_setprio 1
	v_mfma_scale_f32_16x16x128_f8f6f4 v[154:157], v[26:33], v[170:177], v[154:157], v208, v207 op_sel_hi:[0,0,0]
	v_mfma_scale_f32_16x16x128_f8f6f4 v[150:153], v[18:25], v[170:177], v[150:153], v208, v207 op_sel_hi:[0,0,0]
	v_mfma_scale_f32_16x16x128_f8f6f4 v[142:145], v[26:33], v[214:221], v[142:145], v208, v207 op_sel_hi:[0,0,0]
	v_mfma_scale_f32_16x16x128_f8f6f4 v[134:137], v[18:25], v[214:221], v[134:137], v208, v207 op_sel_hi:[0,0,0]
	v_mfma_scale_f32_16x16x128_f8f6f4 v[126:129], v[26:33], v[236:243], v[126:129], v208, v207 op_sel_hi:[0,0,0]
	v_mfma_scale_f32_16x16x128_f8f6f4 v[118:121], v[18:25], v[236:243], v[118:121], v208, v207 op_sel_hi:[0,0,0]
	v_mfma_scale_f32_16x16x128_f8f6f4 v[110:113], v[26:33], v[244:251], v[110:113], v208, v207 op_sel_hi:[0,0,0]
	v_mfma_scale_f32_16x16x128_f8f6f4 v[102:105], v[18:25], v[244:251], v[102:105], v208, v207 op_sel_hi:[0,0,0]
	s_setprio 0
	s_setprio 1
	v_mfma_scale_f32_16x16x128_f8f6f4 v[158:161], v[10:17], v[170:177], v[158:161], v208, v207 op_sel_hi:[0,0,0]
	v_mfma_scale_f32_16x16x128_f8f6f4 v[146:149], v[2:9], v[170:177], v[146:149], v208, v207 op_sel_hi:[0,0,0]
	v_mfma_scale_f32_16x16x128_f8f6f4 v[138:141], v[10:17], v[214:221], v[138:141], v208, v207 op_sel_hi:[0,0,0]
	v_mfma_scale_f32_16x16x128_f8f6f4 v[130:133], v[2:9], v[214:221], v[130:133], v208, v207 op_sel_hi:[0,0,0]
	v_mfma_scale_f32_16x16x128_f8f6f4 v[122:125], v[10:17], v[236:243], v[122:125], v208, v207 op_sel_hi:[0,0,0]
	v_mfma_scale_f32_16x16x128_f8f6f4 v[114:117], v[2:9], v[236:243], v[114:117], v208, v207 op_sel_hi:[0,0,0]
	v_mfma_scale_f32_16x16x128_f8f6f4 v[106:109], v[10:17], v[244:251], v[106:109], v208, v207 op_sel_hi:[0,0,0]
	v_mfma_scale_f32_16x16x128_f8f6f4 v[98:101], v[2:9], v[244:251], v[98:101], v208, v207 op_sel_hi:[0,0,0]
	s_setprio 0
	s_barrier
	s_add_i32 s64, s64, s22
	v_lshl_add_u64 v[196:197], v[196:197], 0, s[56:57]
	s_mov_b32 m0, s64
	ds_read_b128 v[170:173], v212 offset:49152
	ds_read_b128 v[174:177], v212 offset:50176
	ds_read_b128 v[214:217], v212 offset:51200
	ds_read_b128 v[218:221], v212 offset:52224
	ds_read_b128 v[236:239], v212 offset:53248
	ds_read_b128 v[240:243], v212 offset:54272
	ds_read_b128 v[244:247], v212 offset:55296
	ds_read_b128 v[248:251], v212 offset:56320
	global_load_lds_dwordx4 v[196:197], off
	s_add_i32 m0, s64, 0x2000
	s_add_u32 s62, s62, 0x20080
	v_lshl_add_u64 v[196:197], v[198:199], 0, s[56:57]
	s_addc_u32 s63, s63, 0
	s_add_i32 s64, s65, s22
	global_load_lds_dwordx4 v[196:197], off
	v_lshl_add_u64 v[196:197], s[62:63], 0, v[162:163]
	s_mov_b32 m0, s64
	s_nop 0
	global_load_lds_dwordx4 v[196:197], off
	v_lshl_add_u64 v[196:197], s[62:63], 0, v[164:165]
	s_add_i32 m0, s64, 0x2000
	s_nop 0
	global_load_lds_dwordx4 v[196:197], off
	v_lshl_add_u64 v[196:197], v[202:203], 0, s[56:57]
	s_mov_b32 m0, s74
	s_nop 0
	global_load_lds_dwordx4 v[196:197], off
	v_lshl_add_u64 v[196:197], v[200:201], 0, s[56:57]
	s_mov_b32 m0, s75
	s_nop 0
	global_load_lds_dwordx4 v[196:197], off
	s_waitcnt vmcnt(8)
	s_waitcnt lgkmcnt(0)
	s_barrier
	s_setprio 1
	v_mfma_scale_f32_16x16x128_f8f6f4 v[94:97], v[26:33], v[170:177], v[94:97], v208, v207 op_sel_hi:[0,0,0]
	v_mfma_scale_f32_16x16x128_f8f6f4 v[86:89], v[18:25], v[170:177], v[86:89], v208, v207 op_sel_hi:[0,0,0]
	v_mfma_scale_f32_16x16x128_f8f6f4 v[78:81], v[26:33], v[214:221], v[78:81], v208, v207 op_sel_hi:[0,0,0]
	v_mfma_scale_f32_16x16x128_f8f6f4 v[70:73], v[18:25], v[214:221], v[70:73], v208, v207 op_sel_hi:[0,0,0]
	v_mfma_scale_f32_16x16x128_f8f6f4 v[62:65], v[26:33], v[236:243], v[62:65], v208, v207 op_sel_hi:[0,0,0]
	v_mfma_scale_f32_16x16x128_f8f6f4 v[54:57], v[18:25], v[236:243], v[54:57], v208, v207 op_sel_hi:[0,0,0]
	v_mfma_scale_f32_16x16x128_f8f6f4 v[46:49], v[26:33], v[244:251], v[46:49], v208, v207 op_sel_hi:[0,0,0]
	v_mfma_scale_f32_16x16x128_f8f6f4 v[38:41], v[18:25], v[244:251], v[38:41], v208, v207 op_sel_hi:[0,0,0]
	s_setprio 0
	s_setprio 1
	v_mfma_scale_f32_16x16x128_f8f6f4 v[90:93], v[10:17], v[170:177], v[90:93], v208, v207 op_sel_hi:[0,0,0]
	v_mfma_scale_f32_16x16x128_f8f6f4 v[82:85], v[2:9], v[170:177], v[82:85], v208, v207 op_sel_hi:[0,0,0]
	v_mfma_scale_f32_16x16x128_f8f6f4 v[74:77], v[10:17], v[214:221], v[74:77], v208, v207 op_sel_hi:[0,0,0]
	v_mfma_scale_f32_16x16x128_f8f6f4 v[66:69], v[2:9], v[214:221], v[66:69], v208, v207 op_sel_hi:[0,0,0]
	v_mfma_scale_f32_16x16x128_f8f6f4 v[58:61], v[10:17], v[236:243], v[58:61], v208, v207 op_sel_hi:[0,0,0]
	v_mfma_scale_f32_16x16x128_f8f6f4 v[50:53], v[2:9], v[236:243], v[50:53], v208, v207 op_sel_hi:[0,0,0]
	v_mfma_scale_f32_16x16x128_f8f6f4 v[42:45], v[10:17], v[244:251], v[42:45], v208, v207 op_sel_hi:[0,0,0]
	v_mfma_scale_f32_16x16x128_f8f6f4 v[34:37], v[2:9], v[244:251], v[34:37], v208, v207 op_sel_hi:[0,0,0]
	s_setprio 0
	s_barrier
	s_cmp_lt_i32 s55, s11
	s_cbranch_scc0 .LBB0_1841
	s_mov_b64 s[64:65], s[60:61]
	s_branch .LBB0_1836

.Lpeelph18_0:
	s_add_i32 s75, s70, 2
	s_add_u32 s42, s18, 0x100
	s_addc_u32 s43, s19, 0
	s_add_i32 s46, 0, 0x10000
	s_cmp_eq_u32 s14, s70
	s_cselect_b32 vcc_hi, s69, s43
	s_cselect_b32 vcc_lo, s68, s42
	s_cselect_b32 s71, s37, s45
	s_cselect_b32 s70, s36, s35
	s_add_i32 s47, 0, 0x14000
	v_add_u32_e32 v2, s46, v196
	v_add_u32_e32 v6, s47, v196
	ds_read_b128 v[26:29], v2
	ds_read_b128 v[30:33], v2 offset:1024
	ds_read_b128 v[18:21], v2 offset:2048
	ds_read_b128 v[22:25], v2 offset:3072
	ds_read_b128 v[10:13], v6
	ds_read_b128 v[14:17], v6 offset:1024
	ds_read_b128 v[2:5], v6 offset:2048
	ds_read_b128 v[6:9], v6 offset:3072
	v_lshl_add_u64 v[218:219], s[18:19], 0, v[184:185]
	s_add_i32 m0, s73, 0xc000
	ds_read_b128 v[170:173], v201
	ds_read_b128 v[174:177], v201 offset:1024
	ds_read_b128 v[186:189], v201 offset:2048
	ds_read_b128 v[190:193], v201 offset:3072
	ds_read_b128 v[202:205], v201 offset:4096
	ds_read_b128 v[206:209], v201 offset:5120
	ds_read_b128 v[210:213], v201 offset:6144
	ds_read_b128 v[214:217], v201 offset:7168
	global_load_lds_dwordx4 v[218:219], off
	v_lshl_add_u64 v[218:219], s[18:19], 0, v[182:183]
	s_add_i32 m0, s73, 0xe000
	s_nop 0
	global_load_lds_dwordx4 v[218:219], off
	s_waitcnt vmcnt(8)
	s_waitcnt lgkmcnt(0)
	s_barrier
	s_setprio 1
	v_mfma_scale_f32_16x16x128_f8f6f4 v[158:161], v[26:33], v[170:177], 0, v194, v169 op_sel_hi:[0,0,0]
	v_mfma_scale_f32_16x16x128_f8f6f4 v[154:157], v[18:25], v[170:177], 0, v194, v169 op_sel_hi:[0,0,0]
	v_mfma_scale_f32_16x16x128_f8f6f4 v[142:145], v[26:33], v[186:193], 0, v194, v169 op_sel_hi:[0,0,0]
	v_mfma_scale_f32_16x16x128_f8f6f4 v[138:141], v[18:25], v[186:193], 0, v194, v169 op_sel_hi:[0,0,0]
	v_mfma_scale_f32_16x16x128_f8f6f4 v[126:129], v[26:33], v[202:209], 0, v194, v169 op_sel_hi:[0,0,0]
	v_mfma_scale_f32_16x16x128_f8f6f4 v[122:125], v[18:25], v[202:209], 0, v194, v169 op_sel_hi:[0,0,0]
	v_mfma_scale_f32_16x16x128_f8f6f4 v[110:113], v[26:33], v[210:217], 0, v194, v169 op_sel_hi:[0,0,0]
	v_mfma_scale_f32_16x16x128_f8f6f4 v[106:109], v[18:25], v[210:217], 0, v194, v169 op_sel_hi:[0,0,0]
	s_setprio 0
	s_setprio 1
	v_mfma_scale_f32_16x16x128_f8f6f4 v[150:153], v[10:17], v[170:177], 0, v194, v169 op_sel_hi:[0,0,0]
	v_mfma_scale_f32_16x16x128_f8f6f4 v[146:149], v[2:9], v[170:177], 0, v194, v169 op_sel_hi:[0,0,0]
	v_mfma_scale_f32_16x16x128_f8f6f4 v[134:137], v[10:17], v[186:193], 0, v194, v169 op_sel_hi:[0,0,0]
	v_mfma_scale_f32_16x16x128_f8f6f4 v[130:133], v[2:9], v[186:193], 0, v194, v169 op_sel_hi:[0,0,0]
	v_mfma_scale_f32_16x16x128_f8f6f4 v[118:121], v[10:17], v[202:209], 0, v194, v169 op_sel_hi:[0,0,0]
	v_mfma_scale_f32_16x16x128_f8f6f4 v[114:117], v[2:9], v[202:209], 0, v194, v169 op_sel_hi:[0,0,0]
	v_mfma_scale_f32_16x16x128_f8f6f4 v[102:105], v[10:17], v[210:217], 0, v194, v169 op_sel_hi:[0,0,0]
	v_mfma_scale_f32_16x16x128_f8f6f4 v[98:101], v[2:9], v[210:217], 0, v194, v169 op_sel_hi:[0,0,0]
	s_setprio 0
	s_barrier
	s_add_i32 s18, s46, s95
	v_lshl_add_u64 v[186:187], s[70:71], 0, v[164:165]
	s_mov_b32 m0, s18
	ds_read_b128 v[170:173], v201 offset:16384
	ds_read_b128 v[174:177], v201 offset:17408
	ds_read_b128 v[202:205], v201 offset:18432
	ds_read_b128 v[206:209], v201 offset:19456
	ds_read_b128 v[210:213], v201 offset:20480
	ds_read_b128 v[214:217], v201 offset:21504
	ds_read_b128 v[236:239], v201 offset:22528
	ds_read_b128 v[240:243], v201 offset:23552
	global_load_lds_dwordx4 v[186:187], off
	s_add_i32 m0, s18, 0x2000
	s_add_u32 s18, s70, 0x70000
	v_lshl_add_u64 v[188:189], s[70:71], 0, v[180:181]
	s_addc_u32 s19, s71, 0
	s_add_i32 s46, s47, s95
	global_load_lds_dwordx4 v[188:189], off
	v_lshl_add_u64 v[190:191], s[18:19], 0, v[164:165]
	s_mov_b32 m0, s46
	v_lshl_add_u64 v[192:193], vcc, 0, v[178:179]
	global_load_lds_dwordx4 v[190:191], off
	v_lshl_add_u64 v[190:191], s[18:19], 0, v[180:181]
	s_add_i32 m0, s46, 0x2000
	s_nop 0
	global_load_lds_dwordx4 v[190:191], off
	v_lshl_add_u64 v[190:191], vcc, 0, v[162:163]
	s_mov_b32 m0, s73
	s_nop 0
	global_load_lds_dwordx4 v[190:191], off
	s_mov_b32 m0, s8
	s_nop 0
	global_load_lds_dwordx4 v[192:193], off
	s_waitcnt vmcnt(8)
	s_waitcnt lgkmcnt(0)
	s_barrier
	s_setprio 1
	v_mfma_scale_f32_16x16x128_f8f6f4 v[94:97], v[26:33], v[170:177], 0, v194, v169 op_sel_hi:[0,0,0]
	v_mfma_scale_f32_16x16x128_f8f6f4 v[90:93], v[18:25], v[170:177], 0, v194, v169 op_sel_hi:[0,0,0]
	v_mfma_scale_f32_16x16x128_f8f6f4 v[78:81], v[26:33], v[202:209], 0, v194, v169 op_sel_hi:[0,0,0]
	v_mfma_scale_f32_16x16x128_f8f6f4 v[74:77], v[18:25], v[202:209], 0, v194, v169 op_sel_hi:[0,0,0]
	v_mfma_scale_f32_16x16x128_f8f6f4 v[62:65], v[26:33], v[210:217], 0, v194, v169 op_sel_hi:[0,0,0]
	v_mfma_scale_f32_16x16x128_f8f6f4 v[58:61], v[18:25], v[210:217], 0, v194, v169 op_sel_hi:[0,0,0]
	v_mfma_scale_f32_16x16x128_f8f6f4 v[46:49], v[26:33], v[236:243], 0, v194, v169 op_sel_hi:[0,0,0]
	v_mfma_scale_f32_16x16x128_f8f6f4 v[42:45], v[18:25], v[236:243], 0, v194, v169 op_sel_hi:[0,0,0]
	s_setprio 0
	s_setprio 1
	v_mfma_scale_f32_16x16x128_f8f6f4 v[86:89], v[10:17], v[170:177], 0, v194, v169 op_sel_hi:[0,0,0]
	v_mfma_scale_f32_16x16x128_f8f6f4 v[82:85], v[2:9], v[170:177], 0, v194, v169 op_sel_hi:[0,0,0]
	v_mfma_scale_f32_16x16x128_f8f6f4 v[70:73], v[10:17], v[202:209], 0, v194, v169 op_sel_hi:[0,0,0]
	v_mfma_scale_f32_16x16x128_f8f6f4 v[66:69], v[2:9], v[202:209], 0, v194, v169 op_sel_hi:[0,0,0]
	v_mfma_scale_f32_16x16x128_f8f6f4 v[54:57], v[10:17], v[210:217], 0, v194, v169 op_sel_hi:[0,0,0]
	v_mfma_scale_f32_16x16x128_f8f6f4 v[50:53], v[2:9], v[210:217], 0, v194, v169 op_sel_hi:[0,0,0]
	v_mfma_scale_f32_16x16x128_f8f6f4 v[38:41], v[10:17], v[236:243], 0, v194, v169 op_sel_hi:[0,0,0]
	v_mfma_scale_f32_16x16x128_f8f6f4 v[34:37], v[2:9], v[236:243], 0, v194, v169 op_sel_hi:[0,0,0]
	s_setprio 0
	s_barrier
	s_add_i32 s46, 0, 0x18000
	s_add_i32 s47, 0, 0x1c000
	v_add_u32_e32 v2, s46, v196
	v_add_u32_e32 v6, s47, v196
	ds_read_b128 v[26:29], v2
	ds_read_b128 v[30:33], v2 offset:1024
	ds_read_b128 v[18:21], v2 offset:2048
	ds_read_b128 v[22:25], v2 offset:3072
	ds_read_b128 v[10:13], v6
	ds_read_b128 v[14:17], v6 offset:1024
	ds_read_b128 v[2:5], v6 offset:2048
	ds_read_b128 v[6:9], v6 offset:3072
	s_add_u32 s18, vcc_lo, 0x70000
	s_addc_u32 s19, vcc_hi, 0
	s_mov_b32 m0, s11
	v_lshl_add_u64 v[218:219], s[18:19], 0, v[162:163]
	ds_read_b128 v[170:173], v201 offset:32768
	ds_read_b128 v[174:177], v201 offset:33792
	ds_read_b128 v[202:205], v201 offset:34816
	ds_read_b128 v[206:209], v201 offset:35840
	ds_read_b128 v[210:213], v201 offset:36864
	ds_read_b128 v[214:217], v201 offset:37888
	ds_read_b128 v[236:239], v201 offset:38912
	ds_read_b128 v[240:243], v201 offset:39936
	global_load_lds_dwordx4 v[218:219], off
	v_lshl_add_u64 v[218:219], s[18:19], 0, v[178:179]
	s_mov_b32 m0, s84
	s_nop 0
	global_load_lds_dwordx4 v[218:219], off
	s_waitcnt vmcnt(8)
	s_waitcnt lgkmcnt(0)
	s_barrier
	s_setprio 1
	v_mfma_scale_f32_16x16x128_f8f6f4 v[158:161], v[26:33], v[170:177], v[158:161], v194, v169 op_sel_hi:[0,0,0]
	v_mfma_scale_f32_16x16x128_f8f6f4 v[154:157], v[18:25], v[170:177], v[154:157], v194, v169 op_sel_hi:[0,0,0]
	v_mfma_scale_f32_16x16x128_f8f6f4 v[142:145], v[26:33], v[202:209], v[142:145], v194, v169 op_sel_hi:[0,0,0]
	v_mfma_scale_f32_16x16x128_f8f6f4 v[138:141], v[18:25], v[202:209], v[138:141], v194, v169 op_sel_hi:[0,0,0]
	v_mfma_scale_f32_16x16x128_f8f6f4 v[126:129], v[26:33], v[210:217], v[126:129], v194, v169 op_sel_hi:[0,0,0]
	v_mfma_scale_f32_16x16x128_f8f6f4 v[122:125], v[18:25], v[210:217], v[122:125], v194, v169 op_sel_hi:[0,0,0]
	v_mfma_scale_f32_16x16x128_f8f6f4 v[110:113], v[26:33], v[236:243], v[110:113], v194, v169 op_sel_hi:[0,0,0]
	v_mfma_scale_f32_16x16x128_f8f6f4 v[106:109], v[18:25], v[236:243], v[106:109], v194, v169 op_sel_hi:[0,0,0]
	s_setprio 0
	s_setprio 1
	v_mfma_scale_f32_16x16x128_f8f6f4 v[150:153], v[10:17], v[170:177], v[150:153], v194, v169 op_sel_hi:[0,0,0]
	v_mfma_scale_f32_16x16x128_f8f6f4 v[146:149], v[2:9], v[170:177], v[146:149], v194, v169 op_sel_hi:[0,0,0]
	v_mfma_scale_f32_16x16x128_f8f6f4 v[134:137], v[10:17], v[202:209], v[134:137], v194, v169 op_sel_hi:[0,0,0]
	v_mfma_scale_f32_16x16x128_f8f6f4 v[130:133], v[2:9], v[202:209], v[130:133], v194, v169 op_sel_hi:[0,0,0]
	v_mfma_scale_f32_16x16x128_f8f6f4 v[118:121], v[10:17], v[210:217], v[118:121], v194, v169 op_sel_hi:[0,0,0]
	v_mfma_scale_f32_16x16x128_f8f6f4 v[114:117], v[2:9], v[210:217], v[114:117], v194, v169 op_sel_hi:[0,0,0]
	v_mfma_scale_f32_16x16x128_f8f6f4 v[102:105], v[10:17], v[236:243], v[102:105], v194, v169 op_sel_hi:[0,0,0]
	v_mfma_scale_f32_16x16x128_f8f6f4 v[98:101], v[2:9], v[236:243], v[98:101], v194, v169 op_sel_hi:[0,0,0]
	s_setprio 0
	s_barrier
	s_add_i32 s18, s46, s95
	v_lshl_add_u64 v[186:187], v[186:187], 0, s[56:57]
	s_mov_b32 m0, s18
	ds_read_b128 v[170:173], v201 offset:49152
	ds_read_b128 v[174:177], v201 offset:50176
	ds_read_b128 v[202:205], v201 offset:51200
	ds_read_b128 v[206:209], v201 offset:52224
	ds_read_b128 v[210:213], v201 offset:53248
	ds_read_b128 v[214:217], v201 offset:54272
	ds_read_b128 v[236:239], v201 offset:55296
	ds_read_b128 v[240:243], v201 offset:56320
	global_load_lds_dwordx4 v[186:187], off
	s_add_i32 m0, s18, 0x2000
	s_add_u32 s18, s70, 0x70080
	v_lshl_add_u64 v[186:187], v[188:189], 0, s[56:57]
	s_addc_u32 s19, s71, 0
	s_add_i32 s46, s47, s95
	global_load_lds_dwordx4 v[186:187], off
	v_lshl_add_u64 v[186:187], s[18:19], 0, v[164:165]
	s_mov_b32 m0, s46
	s_nop 0
	global_load_lds_dwordx4 v[186:187], off
	v_lshl_add_u64 v[186:187], s[18:19], 0, v[180:181]
	s_add_i32 m0, s46, 0x2000
	s_nop 0
	global_load_lds_dwordx4 v[186:187], off
	v_lshl_add_u64 v[186:187], v[190:191], 0, s[56:57]
	s_mov_b32 m0, s0
	s_nop 0
	global_load_lds_dwordx4 v[186:187], off
	v_lshl_add_u64 v[186:187], v[192:193], 0, s[56:57]
	s_mov_b32 m0, s88
	s_nop 0
	global_load_lds_dwordx4 v[186:187], off
	s_waitcnt vmcnt(8)
	s_waitcnt lgkmcnt(0)
	s_barrier
	s_setprio 1
	v_mfma_scale_f32_16x16x128_f8f6f4 v[94:97], v[26:33], v[170:177], v[94:97], v194, v169 op_sel_hi:[0,0,0]
	v_mfma_scale_f32_16x16x128_f8f6f4 v[90:93], v[18:25], v[170:177], v[90:93], v194, v169 op_sel_hi:[0,0,0]
	v_mfma_scale_f32_16x16x128_f8f6f4 v[78:81], v[26:33], v[202:209], v[78:81], v194, v169 op_sel_hi:[0,0,0]
	v_mfma_scale_f32_16x16x128_f8f6f4 v[74:77], v[18:25], v[202:209], v[74:77], v194, v169 op_sel_hi:[0,0,0]
	v_mfma_scale_f32_16x16x128_f8f6f4 v[62:65], v[26:33], v[210:217], v[62:65], v194, v169 op_sel_hi:[0,0,0]
	v_mfma_scale_f32_16x16x128_f8f6f4 v[58:61], v[18:25], v[210:217], v[58:61], v194, v169 op_sel_hi:[0,0,0]
	v_mfma_scale_f32_16x16x128_f8f6f4 v[46:49], v[26:33], v[236:243], v[46:49], v194, v169 op_sel_hi:[0,0,0]
	v_mfma_scale_f32_16x16x128_f8f6f4 v[42:45], v[18:25], v[236:243], v[42:45], v194, v169 op_sel_hi:[0,0,0]
	s_setprio 0
	s_setprio 1
	v_mfma_scale_f32_16x16x128_f8f6f4 v[86:89], v[10:17], v[170:177], v[86:89], v194, v169 op_sel_hi:[0,0,0]
	v_mfma_scale_f32_16x16x128_f8f6f4 v[82:85], v[2:9], v[170:177], v[82:85], v194, v169 op_sel_hi:[0,0,0]
	v_mfma_scale_f32_16x16x128_f8f6f4 v[70:73], v[10:17], v[202:209], v[70:73], v194, v169 op_sel_hi:[0,0,0]
	v_mfma_scale_f32_16x16x128_f8f6f4 v[66:69], v[2:9], v[202:209], v[66:69], v194, v169 op_sel_hi:[0,0,0]
	v_mfma_scale_f32_16x16x128_f8f6f4 v[54:57], v[10:17], v[210:217], v[54:57], v194, v169 op_sel_hi:[0,0,0]
	v_mfma_scale_f32_16x16x128_f8f6f4 v[50:53], v[2:9], v[210:217], v[50:53], v194, v169 op_sel_hi:[0,0,0]
	v_mfma_scale_f32_16x16x128_f8f6f4 v[38:41], v[10:17], v[236:243], v[38:41], v194, v169 op_sel_hi:[0,0,0]
	v_mfma_scale_f32_16x16x128_f8f6f4 v[34:37], v[2:9], v[236:243], v[34:37], v194, v169 op_sel_hi:[0,0,0]
	s_setprio 0
	s_barrier
	s_add_u32 s35, s35, 0x100
	s_addc_u32 s45, s45, 0
	s_cmp_lt_i32 s75, s16
	s_mov_b64 s[18:19], s[42:43]
	s_mov_b32 s70, s75
	s_cbranch_scc1 .LBB0_1923
	s_branch .Lpeelexitph18
.LBB0_1923:
	s_add_i32 s75, s70, 2
	s_add_u32 s42, s18, 0x100
	s_addc_u32 s43, s19, 0
	s_add_i32 s46, 0, 0x10000
	s_cmp_eq_u32 s14, s70
	s_cselect_b32 vcc_hi, s69, s43
	s_cselect_b32 vcc_lo, s68, s42
	s_cselect_b32 s71, s37, s45
	s_cselect_b32 s70, s36, s35
	s_add_i32 s47, 0, 0x14000
	v_add_u32_e32 v2, s46, v196
	v_add_u32_e32 v6, s47, v196
	ds_read_b128 v[26:29], v2
	ds_read_b128 v[30:33], v2 offset:1024
	ds_read_b128 v[18:21], v2 offset:2048
	ds_read_b128 v[22:25], v2 offset:3072
	ds_read_b128 v[10:13], v6
	ds_read_b128 v[14:17], v6 offset:1024
	ds_read_b128 v[2:5], v6 offset:2048
	ds_read_b128 v[6:9], v6 offset:3072
	v_lshl_add_u64 v[218:219], s[18:19], 0, v[184:185]
	s_add_i32 m0, s73, 0xc000
	ds_read_b128 v[170:173], v201
	ds_read_b128 v[174:177], v201 offset:1024
	ds_read_b128 v[186:189], v201 offset:2048
	ds_read_b128 v[190:193], v201 offset:3072
	ds_read_b128 v[202:205], v201 offset:4096
	ds_read_b128 v[206:209], v201 offset:5120
	ds_read_b128 v[210:213], v201 offset:6144
	ds_read_b128 v[214:217], v201 offset:7168
	global_load_lds_dwordx4 v[218:219], off
	v_lshl_add_u64 v[218:219], s[18:19], 0, v[182:183]
	s_add_i32 m0, s73, 0xe000
	s_nop 0
	global_load_lds_dwordx4 v[218:219], off
	s_waitcnt vmcnt(8)
	s_waitcnt lgkmcnt(0)
	s_barrier
	s_setprio 1
	v_mfma_scale_f32_16x16x128_f8f6f4 v[158:161], v[26:33], v[170:177], v[158:161], v194, v169 op_sel_hi:[0,0,0]
	v_mfma_scale_f32_16x16x128_f8f6f4 v[154:157], v[18:25], v[170:177], v[154:157], v194, v169 op_sel_hi:[0,0,0]
	v_mfma_scale_f32_16x16x128_f8f6f4 v[142:145], v[26:33], v[186:193], v[142:145], v194, v169 op_sel_hi:[0,0,0]
	v_mfma_scale_f32_16x16x128_f8f6f4 v[138:141], v[18:25], v[186:193], v[138:141], v194, v169 op_sel_hi:[0,0,0]
	v_mfma_scale_f32_16x16x128_f8f6f4 v[126:129], v[26:33], v[202:209], v[126:129], v194, v169 op_sel_hi:[0,0,0]
	v_mfma_scale_f32_16x16x128_f8f6f4 v[122:125], v[18:25], v[202:209], v[122:125], v194, v169 op_sel_hi:[0,0,0]
	v_mfma_scale_f32_16x16x128_f8f6f4 v[110:113], v[26:33], v[210:217], v[110:113], v194, v169 op_sel_hi:[0,0,0]
	v_mfma_scale_f32_16x16x128_f8f6f4 v[106:109], v[18:25], v[210:217], v[106:109], v194, v169 op_sel_hi:[0,0,0]
	s_setprio 0
	s_setprio 1
	v_mfma_scale_f32_16x16x128_f8f6f4 v[150:153], v[10:17], v[170:177], v[150:153], v194, v169 op_sel_hi:[0,0,0]
	v_mfma_scale_f32_16x16x128_f8f6f4 v[146:149], v[2:9], v[170:177], v[146:149], v194, v169 op_sel_hi:[0,0,0]
	v_mfma_scale_f32_16x16x128_f8f6f4 v[134:137], v[10:17], v[186:193], v[134:137], v194, v169 op_sel_hi:[0,0,0]
	v_mfma_scale_f32_16x16x128_f8f6f4 v[130:133], v[2:9], v[186:193], v[130:133], v194, v169 op_sel_hi:[0,0,0]
	v_mfma_scale_f32_16x16x128_f8f6f4 v[118:121], v[10:17], v[202:209], v[118:121], v194, v169 op_sel_hi:[0,0,0]
	v_mfma_scale_f32_16x16x128_f8f6f4 v[114:117], v[2:9], v[202:209], v[114:117], v194, v169 op_sel_hi:[0,0,0]
	v_mfma_scale_f32_16x16x128_f8f6f4 v[102:105], v[10:17], v[210:217], v[102:105], v194, v169 op_sel_hi:[0,0,0]
	v_mfma_scale_f32_16x16x128_f8f6f4 v[98:101], v[2:9], v[210:217], v[98:101], v194, v169 op_sel_hi:[0,0,0]
	s_setprio 0
	s_barrier
	s_add_i32 s18, s46, s95
	v_lshl_add_u64 v[186:187], s[70:71], 0, v[164:165]
	s_mov_b32 m0, s18
	ds_read_b128 v[170:173], v201 offset:16384
	ds_read_b128 v[174:177], v201 offset:17408
	ds_read_b128 v[202:205], v201 offset:18432
	ds_read_b128 v[206:209], v201 offset:19456
	ds_read_b128 v[210:213], v201 offset:20480
	ds_read_b128 v[214:217], v201 offset:21504
	ds_read_b128 v[236:239], v201 offset:22528
	ds_read_b128 v[240:243], v201 offset:23552
	global_load_lds_dwordx4 v[186:187], off
	s_add_i32 m0, s18, 0x2000
	s_add_u32 s18, s70, 0x70000
	v_lshl_add_u64 v[188:189], s[70:71], 0, v[180:181]
	s_addc_u32 s19, s71, 0
	s_add_i32 s46, s47, s95
	global_load_lds_dwordx4 v[188:189], off
	v_lshl_add_u64 v[190:191], s[18:19], 0, v[164:165]
	s_mov_b32 m0, s46
	v_lshl_add_u64 v[192:193], vcc, 0, v[178:179]
	global_load_lds_dwordx4 v[190:191], off
	v_lshl_add_u64 v[190:191], s[18:19], 0, v[180:181]
	s_add_i32 m0, s46, 0x2000
	s_nop 0
	global_load_lds_dwordx4 v[190:191], off
	v_lshl_add_u64 v[190:191], vcc, 0, v[162:163]
	s_mov_b32 m0, s73
	s_nop 0
	global_load_lds_dwordx4 v[190:191], off
	s_mov_b32 m0, s8
	s_nop 0
	global_load_lds_dwordx4 v[192:193], off
	s_waitcnt vmcnt(8)
	s_waitcnt lgkmcnt(0)
	s_barrier
	s_setprio 1
	v_mfma_scale_f32_16x16x128_f8f6f4 v[94:97], v[26:33], v[170:177], v[94:97], v194, v169 op_sel_hi:[0,0,0]
	v_mfma_scale_f32_16x16x128_f8f6f4 v[90:93], v[18:25], v[170:177], v[90:93], v194, v169 op_sel_hi:[0,0,0]
	v_mfma_scale_f32_16x16x128_f8f6f4 v[78:81], v[26:33], v[202:209], v[78:81], v194, v169 op_sel_hi:[0,0,0]
	v_mfma_scale_f32_16x16x128_f8f6f4 v[74:77], v[18:25], v[202:209], v[74:77], v194, v169 op_sel_hi:[0,0,0]
	v_mfma_scale_f32_16x16x128_f8f6f4 v[62:65], v[26:33], v[210:217], v[62:65], v194, v169 op_sel_hi:[0,0,0]
	v_mfma_scale_f32_16x16x128_f8f6f4 v[58:61], v[18:25], v[210:217], v[58:61], v194, v169 op_sel_hi:[0,0,0]
	v_mfma_scale_f32_16x16x128_f8f6f4 v[46:49], v[26:33], v[236:243], v[46:49], v194, v169 op_sel_hi:[0,0,0]
	v_mfma_scale_f32_16x16x128_f8f6f4 v[42:45], v[18:25], v[236:243], v[42:45], v194, v169 op_sel_hi:[0,0,0]
	s_setprio 0
	s_setprio 1
	v_mfma_scale_f32_16x16x128_f8f6f4 v[86:89], v[10:17], v[170:177], v[86:89], v194, v169 op_sel_hi:[0,0,0]
	v_mfma_scale_f32_16x16x128_f8f6f4 v[82:85], v[2:9], v[170:177], v[82:85], v194, v169 op_sel_hi:[0,0,0]
	v_mfma_scale_f32_16x16x128_f8f6f4 v[70:73], v[10:17], v[202:209], v[70:73], v194, v169 op_sel_hi:[0,0,0]
	v_mfma_scale_f32_16x16x128_f8f6f4 v[66:69], v[2:9], v[202:209], v[66:69], v194, v169 op_sel_hi:[0,0,0]
	v_mfma_scale_f32_16x16x128_f8f6f4 v[54:57], v[10:17], v[210:217], v[54:57], v194, v169 op_sel_hi:[0,0,0]
	v_mfma_scale_f32_16x16x128_f8f6f4 v[50:53], v[2:9], v[210:217], v[50:53], v194, v169 op_sel_hi:[0,0,0]
	v_mfma_scale_f32_16x16x128_f8f6f4 v[38:41], v[10:17], v[236:243], v[38:41], v194, v169 op_sel_hi:[0,0,0]
	v_mfma_scale_f32_16x16x128_f8f6f4 v[34:37], v[2:9], v[236:243], v[34:37], v194, v169 op_sel_hi:[0,0,0]
	s_setprio 0
	s_barrier
	s_add_i32 s46, 0, 0x18000
	s_add_i32 s47, 0, 0x1c000
	v_add_u32_e32 v2, s46, v196
	v_add_u32_e32 v6, s47, v196
	ds_read_b128 v[26:29], v2
	ds_read_b128 v[30:33], v2 offset:1024
	ds_read_b128 v[18:21], v2 offset:2048
	ds_read_b128 v[22:25], v2 offset:3072
	ds_read_b128 v[10:13], v6
	ds_read_b128 v[14:17], v6 offset:1024
	ds_read_b128 v[2:5], v6 offset:2048
	ds_read_b128 v[6:9], v6 offset:3072
	s_add_u32 s18, vcc_lo, 0x70000
	s_addc_u32 s19, vcc_hi, 0
	s_mov_b32 m0, s11
	v_lshl_add_u64 v[218:219], s[18:19], 0, v[162:163]
	ds_read_b128 v[170:173], v201 offset:32768
	ds_read_b128 v[174:177], v201 offset:33792
	ds_read_b128 v[202:205], v201 offset:34816
	ds_read_b128 v[206:209], v201 offset:35840
	ds_read_b128 v[210:213], v201 offset:36864
	ds_read_b128 v[214:217], v201 offset:37888
	ds_read_b128 v[236:239], v201 offset:38912
	ds_read_b128 v[240:243], v201 offset:39936
	global_load_lds_dwordx4 v[218:219], off
	v_lshl_add_u64 v[218:219], s[18:19], 0, v[178:179]
	s_mov_b32 m0, s84
	s_nop 0
	global_load_lds_dwordx4 v[218:219], off
	s_waitcnt vmcnt(8)
	s_waitcnt lgkmcnt(0)
	s_barrier
	s_setprio 1
	v_mfma_scale_f32_16x16x128_f8f6f4 v[158:161], v[26:33], v[170:177], v[158:161], v194, v169 op_sel_hi:[0,0,0]
	v_mfma_scale_f32_16x16x128_f8f6f4 v[154:157], v[18:25], v[170:177], v[154:157], v194, v169 op_sel_hi:[0,0,0]
	v_mfma_scale_f32_16x16x128_f8f6f4 v[142:145], v[26:33], v[202:209], v[142:145], v194, v169 op_sel_hi:[0,0,0]
	v_mfma_scale_f32_16x16x128_f8f6f4 v[138:141], v[18:25], v[202:209], v[138:141], v194, v169 op_sel_hi:[0,0,0]
	v_mfma_scale_f32_16x16x128_f8f6f4 v[126:129], v[26:33], v[210:217], v[126:129], v194, v169 op_sel_hi:[0,0,0]
	v_mfma_scale_f32_16x16x128_f8f6f4 v[122:125], v[18:25], v[210:217], v[122:125], v194, v169 op_sel_hi:[0,0,0]
	v_mfma_scale_f32_16x16x128_f8f6f4 v[110:113], v[26:33], v[236:243], v[110:113], v194, v169 op_sel_hi:[0,0,0]
	v_mfma_scale_f32_16x16x128_f8f6f4 v[106:109], v[18:25], v[236:243], v[106:109], v194, v169 op_sel_hi:[0,0,0]
	s_setprio 0
	s_setprio 1
	v_mfma_scale_f32_16x16x128_f8f6f4 v[150:153], v[10:17], v[170:177], v[150:153], v194, v169 op_sel_hi:[0,0,0]
	v_mfma_scale_f32_16x16x128_f8f6f4 v[146:149], v[2:9], v[170:177], v[146:149], v194, v169 op_sel_hi:[0,0,0]
	v_mfma_scale_f32_16x16x128_f8f6f4 v[134:137], v[10:17], v[202:209], v[134:137], v194, v169 op_sel_hi:[0,0,0]
	v_mfma_scale_f32_16x16x128_f8f6f4 v[130:133], v[2:9], v[202:209], v[130:133], v194, v169 op_sel_hi:[0,0,0]
	v_mfma_scale_f32_16x16x128_f8f6f4 v[118:121], v[10:17], v[210:217], v[118:121], v194, v169 op_sel_hi:[0,0,0]
	v_mfma_scale_f32_16x16x128_f8f6f4 v[114:117], v[2:9], v[210:217], v[114:117], v194, v169 op_sel_hi:[0,0,0]
	v_mfma_scale_f32_16x16x128_f8f6f4 v[102:105], v[10:17], v[236:243], v[102:105], v194, v169 op_sel_hi:[0,0,0]
	v_mfma_scale_f32_16x16x128_f8f6f4 v[98:101], v[2:9], v[236:243], v[98:101], v194, v169 op_sel_hi:[0,0,0]
	s_setprio 0
	s_barrier
	s_add_i32 s18, s46, s95
	v_lshl_add_u64 v[186:187], v[186:187], 0, s[56:57]
	s_mov_b32 m0, s18
	ds_read_b128 v[170:173], v201 offset:49152
	ds_read_b128 v[174:177], v201 offset:50176
	ds_read_b128 v[202:205], v201 offset:51200
	ds_read_b128 v[206:209], v201 offset:52224
	ds_read_b128 v[210:213], v201 offset:53248
	ds_read_b128 v[214:217], v201 offset:54272
	ds_read_b128 v[236:239], v201 offset:55296
	ds_read_b128 v[240:243], v201 offset:56320
	global_load_lds_dwordx4 v[186:187], off
	s_add_i32 m0, s18, 0x2000
	s_add_u32 s18, s70, 0x70080
	v_lshl_add_u64 v[186:187], v[188:189], 0, s[56:57]
	s_addc_u32 s19, s71, 0
	s_add_i32 s46, s47, s95
	global_load_lds_dwordx4 v[186:187], off
	v_lshl_add_u64 v[186:187], s[18:19], 0, v[164:165]
	s_mov_b32 m0, s46
	s_nop 0
	global_load_lds_dwordx4 v[186:187], off
	v_lshl_add_u64 v[186:187], s[18:19], 0, v[180:181]
	s_add_i32 m0, s46, 0x2000
	s_nop 0
	global_load_lds_dwordx4 v[186:187], off
	v_lshl_add_u64 v[186:187], v[190:191], 0, s[56:57]
	s_mov_b32 m0, s0
	s_nop 0
	global_load_lds_dwordx4 v[186:187], off
	v_lshl_add_u64 v[186:187], v[192:193], 0, s[56:57]
	s_mov_b32 m0, s88
	s_nop 0
	global_load_lds_dwordx4 v[186:187], off
	s_waitcnt vmcnt(8)
	s_waitcnt lgkmcnt(0)
	s_barrier
	s_setprio 1
	v_mfma_scale_f32_16x16x128_f8f6f4 v[94:97], v[26:33], v[170:177], v[94:97], v194, v169 op_sel_hi:[0,0,0]
	v_mfma_scale_f32_16x16x128_f8f6f4 v[90:93], v[18:25], v[170:177], v[90:93], v194, v169 op_sel_hi:[0,0,0]
	v_mfma_scale_f32_16x16x128_f8f6f4 v[78:81], v[26:33], v[202:209], v[78:81], v194, v169 op_sel_hi:[0,0,0]
	v_mfma_scale_f32_16x16x128_f8f6f4 v[74:77], v[18:25], v[202:209], v[74:77], v194, v169 op_sel_hi:[0,0,0]
	v_mfma_scale_f32_16x16x128_f8f6f4 v[62:65], v[26:33], v[210:217], v[62:65], v194, v169 op_sel_hi:[0,0,0]
	v_mfma_scale_f32_16x16x128_f8f6f4 v[58:61], v[18:25], v[210:217], v[58:61], v194, v169 op_sel_hi:[0,0,0]
	v_mfma_scale_f32_16x16x128_f8f6f4 v[46:49], v[26:33], v[236:243], v[46:49], v194, v169 op_sel_hi:[0,0,0]
	v_mfma_scale_f32_16x16x128_f8f6f4 v[42:45], v[18:25], v[236:243], v[42:45], v194, v169 op_sel_hi:[0,0,0]
	s_setprio 0
	s_setprio 1
	v_mfma_scale_f32_16x16x128_f8f6f4 v[86:89], v[10:17], v[170:177], v[86:89], v194, v169 op_sel_hi:[0,0,0]
	v_mfma_scale_f32_16x16x128_f8f6f4 v[82:85], v[2:9], v[170:177], v[82:85], v194, v169 op_sel_hi:[0,0,0]
	v_mfma_scale_f32_16x16x128_f8f6f4 v[70:73], v[10:17], v[202:209], v[70:73], v194, v169 op_sel_hi:[0,0,0]
	v_mfma_scale_f32_16x16x128_f8f6f4 v[66:69], v[2:9], v[202:209], v[66:69], v194, v169 op_sel_hi:[0,0,0]
	v_mfma_scale_f32_16x16x128_f8f6f4 v[54:57], v[10:17], v[210:217], v[54:57], v194, v169 op_sel_hi:[0,0,0]
	v_mfma_scale_f32_16x16x128_f8f6f4 v[50:53], v[2:9], v[210:217], v[50:53], v194, v169 op_sel_hi:[0,0,0]
	v_mfma_scale_f32_16x16x128_f8f6f4 v[38:41], v[10:17], v[236:243], v[38:41], v194, v169 op_sel_hi:[0,0,0]
	v_mfma_scale_f32_16x16x128_f8f6f4 v[34:37], v[2:9], v[236:243], v[34:37], v194, v169 op_sel_hi:[0,0,0]
	s_setprio 0
	s_barrier
	s_add_u32 s35, s35, 0x100
	s_addc_u32 s45, s45, 0
	s_cmp_lt_i32 s75, s16
	s_mov_b64 s[18:19], s[42:43]
	s_mov_b32 s70, s75
	s_cbranch_scc1 .LBB0_1923
